# baseline (speedup 1.0000x reference)
_Z16closed_form_mainPKfS0_PKiPf:
	s_load_dwordx8 s[16:23], s[0:1], 0x0
	s_lshr_b32 s6, s2, 3
	v_readfirstlane_b32 s0, v0
	s_mul_hi_u32 s7, s6, 0x24924925
	s_lshr_b32 s4, s0, 6
	s_and_b32 s0, s2, 7
	s_mul_i32 s1, s7, 7
	s_bfe_u32 s5, s2, 0x10003
	s_sub_i32 s1, s6, s1
	s_mul_i32 s36, s0, 7
	s_xor_b32 s3, s4, s5
	s_add_i32 s36, s36, s1
	s_waitcnt lgkmcnt(0)
	s_mov_b64 s[28:29], s[22:23]
	v_and_b32_e32 v19, 63, v0
	s_cmp_lt_u32 s36, 52
	s_mov_b64 s[0:1], -1
	s_cbranch_scc0 .LBB0_32
	s_mul_hi_u32 s0, s6, 0x20820821
	s_lshr_b32 s38, s0, 3
	s_mul_hi_u32 s0, s7, 0x1c71c71d
	s_mul_i32 s0, s0, 9
	s_sub_i32 s0, s7, s0
	v_add_u32_e32 v2, -3, v19
	v_mad_u64_u32 v[0:1], s[0:1], s0, 57, v[2:3]
	s_mov_b64 s[24:25], s[18:19]
	v_mov_b32_e32 v1, 0x200
	v_med3_i32 v1, v0, 0, v1
	s_mul_i32 s34, s36, 10
	s_and_b32 s17, s17, 0xffff
	s_and_b32 s25, s25, 0xffff
	v_cmp_gt_u32_e64 s[0:1], 57, v2
	s_mov_b32 s19, 0x20000
	s_mov_b32 s18, 0xe0e038
	s_mov_b32 s26, 0x606018
	s_mul_i32 s35, s38, 0x70701c
	s_mul_i32 s33, s38, 0x30300c
	v_lshlrev_b32_e32 v28, 2, v1
	v_mul_u32_u24_e32 v27, 12, v1
	v_lshlrev_b32_e32 v23, 4, v19
	s_cmp_lg_u32 s4, s5
	v_sub_u32_e64 v29, s34, 2 clamp
	s_cbranch_scc0 .LBB0_15
	s_mov_b32 s27, s19
	s_and_b32 s21, s21, 0xffff
	s_mov_b32 s22, 0x202008
	s_mov_b32 s23, s19
	s_mul_i32 s38, s38, 0x101004
	s_movk_i32 s37, 0x80
	v_add_u32_e32 v18, -1, v0
	s_movk_i32 s4, 0x201
	s_movk_i32 s5, 0x1ff
	v_cmp_gt_u32_e64 s[40:41], s4, v0
	v_cmp_gt_u32_e64 s[42:43], s5, v18
	v_mov_b32_e32 v18, 0x42c80000
	v_mov_b32_e32 v22, 0x3de38e39
	v_mov_b32_e32 v26, 0x3a3d6628
	v_mov_b32_e32 v1, 0
	s_add_i32 s4, s34, -3
	s_max_i32 s4, s4, 0
	s_mul_i32 s4, s4, 0x804
	s_add_i32 s4, s4, s38
	buffer_load_dword v29, v28, s[20:23], s4 offen nt
	s_add_i32 s4, s34, -2
	s_max_i32 s4, s4, 0
	s_mul_i32 s4, s4, 0x804
	s_add_i32 s4, s4, s38
	buffer_load_dword v2, v28, s[20:23], s4 offen nt
	s_add_i32 s5, s34, -2
	s_max_i32 s5, s5, 0
	s_mul_i32 s6, s5, 0x804
	s_add_i32 s6, s6, s35
	s_add_i32 s7, s6, 0x505014
	s_add_i32 s8, s6, 0x606018
	s_mul_i32 s9, s5, 0x180c
	s_add_i32 s9, s9, s33
	s_add_i32 s4, s34, -1
	s_max_i32 s4, s4, 0
	s_mul_i32 s4, s4, 0x804
	s_add_i32 s4, s4, s38
	buffer_load_dword v3, v28, s[20:23], s4 offen nt
	buffer_load_dwordx3 v[8:10], v27, s[24:27], s9 offen nt
	buffer_load_dword v4, v28, s[16:19], s7 offen nt
	buffer_load_dword v5, v28, s[16:19], s8 offen nt
	s_add_i32 s5, s34, -1
	s_max_i32 s5, s5, 0
	s_mul_i32 s6, s5, 0x804
	s_add_i32 s6, s6, s35
	s_add_i32 s7, s6, 0x505014
	s_add_i32 s8, s6, 0x606018
	s_mul_i32 s9, s5, 0x180c
	s_add_i32 s9, s9, s33
	s_add_i32 s4, s34, 0
	s_min_i32 s4, s4, 0x200
	s_mul_i32 s4, s4, 0x804
	s_add_i32 s4, s4, s38
	buffer_load_dword v16, v28, s[20:23], s4 offen nt
	buffer_load_dwordx3 v[12:14], v27, s[24:27], s9 offen nt
	buffer_load_dword v6, v28, s[16:19], s7 offen nt
	buffer_load_dword v7, v28, s[16:19], s8 offen nt
	s_waitcnt vmcnt(8)
	s_add_i32 s4, s34, -3
	s_cmpk_lt_u32 s4, 0x201
	s_cselect_b64 s[12:13], s[40:41], 0
	v_cmp_eq_u32_e64 s[14:15], s37, v29
	s_and_b64 s[14:15], s[14:15], s[12:13]
	v_cndmask_b32_e64 v17, 0, 1, s[14:15]
	s_add_i32 s4, s34, -2
	s_cmpk_lt_u32 s4, 0x201
	s_cselect_b64 s[12:13], s[40:41], 0
	v_cmp_eq_u32_e64 s[14:15], s37, v2
	s_and_b64 s[14:15], s[14:15], s[12:13]
	v_cndmask_b32_e64 v20, 0, 1, s[14:15]
	s_nop 0
	v_or_b32_dpp v21, v17, v17 wave_shr:1 row_mask:0xf bank_mask:0xf bound_ctrl:1
	v_or_b32_dpp v24, v20, v20 wave_shr:1 row_mask:0xf bank_mask:0xf bound_ctrl:1
	s_nop 1
	v_or_b32_dpp v21, v17, v21 wave_shl:1 row_mask:0xf bank_mask:0xf bound_ctrl:1
	v_or_b32_dpp v24, v20, v24 wave_shl:1 row_mask:0xf bank_mask:0xf bound_ctrl:1
	s_nop 1
	v_or_b32_dpp v25, v21, v21 wave_shr:1 row_mask:0xf bank_mask:0xf bound_ctrl:1
	v_or_b32_dpp v30, v24, v24 wave_shr:1 row_mask:0xf bank_mask:0xf bound_ctrl:1
	s_nop 1
	v_or_b32_dpp v25, v21, v25 wave_shl:1 row_mask:0xf bank_mask:0xf bound_ctrl:1
	v_or_b32_dpp v30, v24, v30 wave_shl:1 row_mask:0xf bank_mask:0xf bound_ctrl:1
	v_mov_b32_e32 v17, 0
	v_mov_b32_e32 v24, 0
	s_add_i32 s5, s34, 0
	s_min_i32 s5, s5, 0x200
	s_mul_i32 s6, s5, 0x804
	s_add_i32 s6, s6, s35
	s_add_i32 s7, s6, 0x505014
	s_add_i32 s8, s6, 0x606018
	s_mul_i32 s9, s5, 0x180c
	s_add_i32 s9, s9, s33
	s_add_i32 s4, s34, 1
	s_min_i32 s4, s4, 0x200
	s_mul_i32 s4, s4, 0x804
	s_add_i32 s4, s4, s38
	buffer_load_dword v31, v28, s[20:23], s4 offen nt
	buffer_load_dwordx3 v[32:34], v27, s[24:27], s9 offen nt
	buffer_load_dword v20, v28, s[16:19], s7 offen nt
	buffer_load_dword v21, v28, s[16:19], s8 offen nt
	s_waitcnt vmcnt(8)
	v_mov_b32_dpp v36, v8 wave_shr:1 row_mask:0xf bank_mask:0xf bound_ctrl:1
	v_mov_b32_dpp v37, v9 wave_shr:1 row_mask:0xf bank_mask:0xf bound_ctrl:1
	v_mov_b32_dpp v38, v10 wave_shr:1 row_mask:0xf bank_mask:0xf bound_ctrl:1
	v_mov_b32_dpp v40, v8 wave_shl:1 row_mask:0xf bank_mask:0xf bound_ctrl:1
	v_mov_b32_dpp v41, v9 wave_shl:1 row_mask:0xf bank_mask:0xf bound_ctrl:1
	v_mov_b32_dpp v42, v10 wave_shl:1 row_mask:0xf bank_mask:0xf bound_ctrl:1
	s_add_i32 s4, s34, -1
	s_cmpk_lt_u32 s4, 0x201
	s_cselect_b64 s[12:13], s[40:41], 0
	v_cmp_eq_u32_e64 s[14:15], s37, v3
	s_and_b64 s[14:15], s[14:15], s[12:13]
	v_cndmask_b32_e64 v44, 0, 1, s[14:15]
	v_mul_f32_e32 v46, v8, v8
	v_mul_f32_e32 v47, v8, v9
	v_mul_f32_e32 v48, v8, v10
	v_mul_f32_e32 v49, v9, v9
	v_mul_f32_e32 v50, v9, v10
	v_mul_f32_e32 v51, v10, v10
	v_or_b32_dpp v45, v44, v44 wave_shr:1 row_mask:0xf bank_mask:0xf bound_ctrl:1
	s_nop 1
	v_or_b32_dpp v45, v44, v45 wave_shl:1 row_mask:0xf bank_mask:0xf bound_ctrl:1
	s_nop 1
	v_or_b32_dpp v52, v45, v45 wave_shr:1 row_mask:0xf bank_mask:0xf bound_ctrl:1
	s_nop 1
	v_or_b32_dpp v52, v45, v52 wave_shl:1 row_mask:0xf bank_mask:0xf bound_ctrl:1
	v_or3_b32 v53, v52, v30, v25
	v_or3_b32 v53, v53, v17, v24
	s_add_i32 s4, s34, -4
	s_cmpk_lt_u32 s4, 0x1ff
	s_cselect_b64 s[12:13], s[42:43], 0
	v_cmp_ne_u32_e64 s[30:31], 0, v53
	s_and_b64 s[30:31], s[30:31], s[12:13]
	v_cndmask_b32_e64 v53, 0, 1.0, s[30:31]
	v_add_f32_e32 v44, v8, v36
	v_add_f32_e32 v45, v9, v37
	v_add_f32_e32 v54, v10, v38
	v_fmac_f32_e32 v46, v36, v36
	v_fmac_f32_e32 v47, v36, v37
	v_fmac_f32_e32 v48, v36, v38
	v_fmac_f32_e32 v49, v37, v37
	v_fmac_f32_e32 v50, v37, v38
	v_fmac_f32_e32 v51, v38, v38
	v_add_f32_dpp v61, v53, v53 wave_shr:1 row_mask:0xf bank_mask:0xf bound_ctrl:1
	v_add_f32_e32 v44, v44, v40
	v_add_f32_e32 v45, v45, v41
	v_add_f32_e32 v54, v54, v42
	v_fma_f32 v55, v40, v40, v46
	v_fma_f32 v56, v40, v41, v47
	v_fma_f32 v57, v40, v42, v48
	v_fma_f32 v58, v41, v41, v49
	v_fma_f32 v59, v41, v42, v50
	v_fma_f32 v60, v42, v42, v51
	v_add_f32_dpp v61, v53, v61 wave_shl:1 row_mask:0xf bank_mask:0xf bound_ctrl:1
	s_barrier
	v_mov_b32_dpp v46, v4 wave_shr:1 row_mask:0xf bank_mask:0xf bound_ctrl:1
	v_mov_b32_dpp v47, v5 wave_shr:1 row_mask:0xf bank_mask:0xf bound_ctrl:1
	v_mov_b32_dpp v50, v4 wave_shl:1 row_mask:0xf bank_mask:0xf bound_ctrl:1
	v_mov_b32_dpp v51, v5 wave_shl:1 row_mask:0xf bank_mask:0xf bound_ctrl:1
	v_pk_mul_f32 v[48:49], v[4:5], v[8:9] op_sel_hi:[1,0]
	v_pk_mul_f32 v[64:65], v[4:5], v[8:9] op_sel:[0,1]
	v_pk_mul_f32 v[68:69], v[4:5], v[10:11] op_sel_hi:[1,0]
	v_pk_add_f32 v[72:73], v[4:5], v[46:47]
	v_pk_fma_f32 v[48:49], v[46:47], v[36:37], v[48:49] op_sel_hi:[1,0,1]
	v_pk_fma_f32 v[64:65], v[46:47], v[36:37], v[64:65] op_sel:[0,1,0]
	v_pk_fma_f32 v[68:69], v[46:47], v[38:39], v[68:69] op_sel_hi:[1,0,1]
	v_pk_add_f32 v[72:73], v[72:73], v[50:51]
	v_pk_fma_f32 v[48:49], v[50:51], v[40:41], v[48:49] op_sel_hi:[1,0,1]
	v_pk_fma_f32 v[64:65], v[50:51], v[40:41], v[64:65] op_sel:[0,1,0]
	v_pk_fma_f32 v[68:69], v[50:51], v[42:43], v[68:69] op_sel_hi:[1,0,1]
	s_add_i32 s5, s34, 1
	s_min_i32 s5, s5, 0x200
	s_mul_i32 s6, s5, 0x804
	s_add_i32 s6, s6, s35
	s_add_i32 s7, s6, 0x505014
	s_add_i32 s8, s6, 0x606018
	s_mul_i32 s9, s5, 0x180c
	s_add_i32 s9, s9, s33
	s_add_i32 s4, s34, 2
	s_min_i32 s4, s4, 0x200
	s_mul_i32 s4, s4, 0x804
	s_add_i32 s4, s4, s38
	buffer_load_dword v24, v28, s[20:23], s4 offen nt
	buffer_load_dwordx3 v[76:78], v27, s[24:27], s9 offen nt
	buffer_load_dword v46, v28, s[16:19], s7 offen nt
	buffer_load_dword v47, v28, s[16:19], s8 offen nt
	s_waitcnt vmcnt(8)
	v_mov_b32_dpp v80, v12 wave_shr:1 row_mask:0xf bank_mask:0xf bound_ctrl:1
	v_mov_b32_dpp v81, v13 wave_shr:1 row_mask:0xf bank_mask:0xf bound_ctrl:1
	v_mov_b32_dpp v82, v14 wave_shr:1 row_mask:0xf bank_mask:0xf bound_ctrl:1
	v_mov_b32_dpp v84, v12 wave_shl:1 row_mask:0xf bank_mask:0xf bound_ctrl:1
	v_mov_b32_dpp v85, v13 wave_shl:1 row_mask:0xf bank_mask:0xf bound_ctrl:1
	v_mov_b32_dpp v86, v14 wave_shl:1 row_mask:0xf bank_mask:0xf bound_ctrl:1
	s_add_i32 s4, s34, 0
	s_cmpk_lt_u32 s4, 0x201
	s_cselect_b64 s[12:13], s[40:41], 0
	v_cmp_eq_u32_e64 s[14:15], s37, v16
	s_and_b64 s[14:15], s[14:15], s[12:13]
	v_cndmask_b32_e64 v53, 0, 1, s[14:15]
	v_mul_f32_e32 v50, v12, v12
	v_mul_f32_e32 v51, v12, v13
	v_mul_f32_e32 v62, v12, v14
	v_mul_f32_e32 v63, v13, v13
	v_mul_f32_e32 v66, v13, v14
	v_mul_f32_e32 v67, v14, v14
	v_or_b32_dpp v70, v53, v53 wave_shr:1 row_mask:0xf bank_mask:0xf bound_ctrl:1
	s_nop 1
	v_or_b32_dpp v70, v53, v70 wave_shl:1 row_mask:0xf bank_mask:0xf bound_ctrl:1
	s_nop 1
	v_or_b32_dpp v71, v70, v70 wave_shr:1 row_mask:0xf bank_mask:0xf bound_ctrl:1
	s_nop 1
	v_or_b32_dpp v71, v70, v71 wave_shl:1 row_mask:0xf bank_mask:0xf bound_ctrl:1
	v_or3_b32 v53, v71, v52, v30
	v_or3_b32 v53, v53, v25, v17
	s_add_i32 s4, s34, -3
	s_cmpk_lt_u32 s4, 0x1ff
	s_cselect_b64 s[12:13], s[42:43], 0
	v_cmp_ne_u32_e64 s[30:31], 0, v53
	s_and_b64 s[30:31], s[30:31], s[12:13]
	v_cndmask_b32_e64 v53, 0, 1.0, s[30:31]
	v_add_f32_e32 v74, v12, v80
	v_add_f32_e32 v75, v13, v81
	v_add_f32_e32 v88, v14, v82
	v_fmac_f32_e32 v50, v80, v80
	v_fmac_f32_e32 v51, v80, v81
	v_fmac_f32_e32 v62, v80, v82
	v_fmac_f32_e32 v63, v81, v81
	v_fmac_f32_e32 v66, v81, v82
	v_fmac_f32_e32 v67, v82, v82
	v_add_f32_dpp v95, v53, v53 wave_shr:1 row_mask:0xf bank_mask:0xf bound_ctrl:1
	v_add_f32_e32 v74, v74, v84
	v_add_f32_e32 v75, v75, v85
	v_add_f32_e32 v88, v88, v86
	v_fma_f32 v89, v84, v84, v50
	v_fma_f32 v90, v84, v85, v51
	v_fma_f32 v91, v84, v86, v62
	v_fma_f32 v92, v85, v85, v63
	v_fma_f32 v93, v85, v86, v66
	v_fma_f32 v94, v86, v86, v67
	v_add_f32_dpp v95, v53, v95 wave_shl:1 row_mask:0xf bank_mask:0xf bound_ctrl:1
	s_barrier
	v_mov_b32_dpp v96, v6 wave_shr:1 row_mask:0xf bank_mask:0xf bound_ctrl:1
	v_mov_b32_dpp v97, v7 wave_shr:1 row_mask:0xf bank_mask:0xf bound_ctrl:1
	v_mov_b32_dpp v100, v6 wave_shl:1 row_mask:0xf bank_mask:0xf bound_ctrl:1
	v_mov_b32_dpp v101, v7 wave_shl:1 row_mask:0xf bank_mask:0xf bound_ctrl:1
	v_pk_mul_f32 v[50:51], v[6:7], v[12:13] op_sel_hi:[1,0]
	v_pk_mul_f32 v[62:63], v[6:7], v[12:13] op_sel:[0,1]
	v_pk_mul_f32 v[66:67], v[6:7], v[14:15] op_sel_hi:[1,0]
	v_pk_add_f32 v[98:99], v[6:7], v[96:97]
	v_pk_fma_f32 v[50:51], v[96:97], v[80:81], v[50:51] op_sel_hi:[1,0,1]
	v_pk_fma_f32 v[62:63], v[96:97], v[80:81], v[62:63] op_sel:[0,1,0]
	v_pk_fma_f32 v[66:67], v[96:97], v[82:83], v[66:67] op_sel_hi:[1,0,1]
	v_pk_add_f32 v[98:99], v[98:99], v[100:101]
	v_pk_fma_f32 v[50:51], v[100:101], v[84:85], v[50:51] op_sel_hi:[1,0,1]
	v_pk_fma_f32 v[62:63], v[100:101], v[84:85], v[62:63] op_sel:[0,1,0]
	v_pk_fma_f32 v[66:67], v[100:101], v[86:87], v[66:67] op_sel_hi:[1,0,1]
	s_add_i32 s5, s34, 2
	s_min_i32 s5, s5, 0x200
	s_mul_i32 s6, s5, 0x804
	s_add_i32 s6, s6, s35
	s_add_i32 s7, s6, 0x505014
	s_add_i32 s8, s6, 0x606018
	s_mul_i32 s9, s5, 0x180c
	s_add_i32 s9, s9, s33
	s_add_i32 s4, s34, 3
	s_min_i32 s4, s4, 0x200
	s_mul_i32 s4, s4, 0x804
	s_add_i32 s4, s4, s38
	buffer_load_dword v17, v28, s[20:23], s4 offen nt
	buffer_load_dwordx3 v[100:102], v27, s[24:27], s9 offen nt
	buffer_load_dword v96, v28, s[16:19], s7 offen nt
	buffer_load_dword v97, v28, s[16:19], s8 offen nt
	s_waitcnt vmcnt(8)
	v_mov_b32_dpp v104, v32 wave_shr:1 row_mask:0xf bank_mask:0xf bound_ctrl:1
	v_mov_b32_dpp v105, v33 wave_shr:1 row_mask:0xf bank_mask:0xf bound_ctrl:1
	v_mov_b32_dpp v106, v34 wave_shr:1 row_mask:0xf bank_mask:0xf bound_ctrl:1
	v_mov_b32_dpp v108, v32 wave_shl:1 row_mask:0xf bank_mask:0xf bound_ctrl:1
	v_mov_b32_dpp v109, v33 wave_shl:1 row_mask:0xf bank_mask:0xf bound_ctrl:1
	v_mov_b32_dpp v110, v34 wave_shl:1 row_mask:0xf bank_mask:0xf bound_ctrl:1
	s_add_i32 s4, s34, 1
	s_cmpk_lt_u32 s4, 0x201
	s_cselect_b64 s[12:13], s[40:41], 0
	v_cmp_eq_u32_e64 s[14:15], s37, v31
	s_and_b64 s[14:15], s[14:15], s[12:13]
	v_cndmask_b32_e64 v29, 0, 1, s[14:15]
	v_mul_f32_e32 v112, v32, v32
	v_mul_f32_e32 v113, v32, v33
	v_mul_f32_e32 v114, v32, v34
	v_mul_f32_e32 v115, v33, v33
	v_mul_f32_e32 v116, v33, v34
	v_mul_f32_e32 v117, v34, v34
	v_or_b32_dpp v53, v29, v29 wave_shr:1 row_mask:0xf bank_mask:0xf bound_ctrl:1
	s_nop 1
	v_or_b32_dpp v53, v29, v53 wave_shl:1 row_mask:0xf bank_mask:0xf bound_ctrl:1
	s_nop 1
	v_or_b32_dpp v70, v53, v53 wave_shr:1 row_mask:0xf bank_mask:0xf bound_ctrl:1
	s_nop 1
	v_or_b32_dpp v70, v53, v70 wave_shl:1 row_mask:0xf bank_mask:0xf bound_ctrl:1
	v_or3_b32 v29, v70, v71, v52
	v_or3_b32 v29, v29, v30, v25
	s_add_i32 s4, s34, -2
	s_cmpk_lt_u32 s4, 0x1ff
	s_cselect_b64 s[12:13], s[42:43], 0
	v_cmp_ne_u32_e64 s[30:31], 0, v29
	s_and_b64 s[30:31], s[30:31], s[12:13]
	v_cndmask_b32_e64 v29, 0, 1.0, s[30:31]
	v_add_f32_e32 v118, v32, v104
	v_add_f32_e32 v119, v33, v105
	v_add_f32_e32 v120, v34, v106
	v_fmac_f32_e32 v112, v104, v104
	v_fmac_f32_e32 v113, v104, v105
	v_fmac_f32_e32 v114, v104, v106
	v_fmac_f32_e32 v115, v105, v105
	v_fmac_f32_e32 v116, v105, v106
	v_fmac_f32_e32 v117, v106, v106
	v_add_f32_dpp v127, v29, v29 wave_shr:1 row_mask:0xf bank_mask:0xf bound_ctrl:1
	v_add_f32_e32 v118, v118, v108
	v_add_f32_e32 v119, v119, v109
	v_add_f32_e32 v120, v120, v110
	v_fma_f32 v121, v108, v108, v112
	v_fma_f32 v122, v108, v109, v113
	v_fma_f32 v123, v108, v110, v114
	v_fma_f32 v124, v109, v109, v115
	v_fma_f32 v125, v109, v110, v116
	v_fma_f32 v126, v110, v110, v117
	v_add_f32_dpp v127, v29, v127 wave_shl:1 row_mask:0xf bank_mask:0xf bound_ctrl:1
	v_pk_add_f32 v[114:115], v[74:75], v[118:119]
	v_pk_add_f32 v[112:113], v[44:45], v[114:115]
	v_pk_add_f32 v[44:45], v[88:89], v[120:121]
	v_pk_add_f32 v[74:75], v[54:55], v[44:45]
	v_pk_add_f32 v[54:55], v[90:91], v[122:123]
	v_pk_add_f32 v[88:89], v[56:57], v[54:55]
	v_pk_add_f32 v[56:57], v[92:93], v[124:125]
	v_pk_add_f32 v[90:91], v[58:59], v[56:57]
	v_pk_add_f32 v[58:59], v[94:95], v[126:127]
	v_pk_add_f32 v[92:93], v[60:61], v[58:59]
	v_mul_f32_e32 v128, v112, v22
	v_mul_f32_e32 v129, v113, v22
	v_mul_f32_e32 v130, v74, v22
	v_fma_f32 v29, v75, v22, v26
	v_mul_f32_e32 v53, v88, v22
	v_mul_f32_e32 v60, v89, v22
	v_fma_f32 v61, v90, v22, v26
	v_mul_f32_e32 v94, v91, v22
	v_fma_f32 v95, v92, v22, v26
	v_fma_f32 v29, -v128, v128, v29
	v_fma_f32 v53, -v128, v129, v53
	v_fma_f32 v60, -v128, v130, v60
	v_fma_f32 v61, -v129, v129, v61
	v_fma_f32 v94, -v129, v130, v94
	v_fma_f32 v95, -v130, v130, v95
	v_mul_f32_e32 v116, v94, v94
	v_mul_f32_e32 v117, v53, v95
	v_mul_f32_e32 v140, v60, v61
	v_mul_f32_e32 v141, v60, v60
	v_mul_f32_e32 v142, v29, v94
	v_mul_f32_e32 v143, v53, v53
	v_fma_f32 v116, v61, v95, -v116
	v_fma_f32 v117, v60, v94, -v117
	v_fma_f32 v140, v53, v94, -v140
	v_fma_f32 v141, v29, v95, -v141
	v_fma_f32 v142, v53, v60, -v142
	v_fma_f32 v143, v29, v61, -v143
	v_mul_f32_e32 v144, v29, v116
	v_fmac_f32_e32 v144, v53, v117
	v_fmac_f32_e32 v144, v60, v140
	v_rcp_f32_e32 v144, v144
	v_cmp_ne_u32_e64 vcc, s37, v2
	v_mul_f32_e32 v144, v144, v22
	v_cndmask_b32_e64 v144, 0, v144, s[30:31]
	v_cndmask_b32_e64 v29, 0, v18, vcc
	v_cndmask_b32_e64 v137, 0, v22, s[30:31]
	v_mul_f32_e32 v131, v116, v144
	v_mul_f32_e32 v132, v117, v144
	v_mul_f32_e32 v133, v140, v144
	v_mul_f32_e32 v134, v141, v144
	v_mul_f32_e32 v135, v142, v144
	v_mul_f32_e32 v136, v143, v144
	v_add_f32_e32 v138, v93, v29
	v_mov_b32_e32 v139, v2
	ds_write_b128 v23, v[128:131]
	ds_write_b128 v23, v[132:135] offset:1024
	ds_write_b128 v23, v[136:139] offset:2048
	s_waitcnt lgkmcnt(0)
	s_barrier
	v_mov_b32_dpp v74, v20 wave_shr:1 row_mask:0xf bank_mask:0xf bound_ctrl:1
	v_mov_b32_dpp v75, v21 wave_shr:1 row_mask:0xf bank_mask:0xf bound_ctrl:1
	v_mov_b32_dpp v90, v20 wave_shl:1 row_mask:0xf bank_mask:0xf bound_ctrl:1
	v_mov_b32_dpp v91, v21 wave_shl:1 row_mask:0xf bank_mask:0xf bound_ctrl:1
	v_pk_mul_f32 v[60:61], v[20:21], v[32:33] op_sel_hi:[1,0]
	v_pk_mul_f32 v[88:89], v[20:21], v[32:33] op_sel:[0,1]
	v_pk_mul_f32 v[92:93], v[20:21], v[34:35] op_sel_hi:[1,0]
	v_pk_add_f32 v[112:113], v[20:21], v[74:75]
	v_pk_fma_f32 v[60:61], v[74:75], v[104:105], v[60:61] op_sel_hi:[1,0,1]
	v_pk_fma_f32 v[88:89], v[74:75], v[104:105], v[88:89] op_sel:[0,1,0]
	v_pk_fma_f32 v[92:93], v[74:75], v[106:107], v[92:93] op_sel_hi:[1,0,1]
	v_pk_add_f32 v[112:113], v[112:113], v[90:91]
	v_pk_fma_f32 v[60:61], v[90:91], v[108:109], v[60:61] op_sel_hi:[1,0,1]
	v_pk_fma_f32 v[88:89], v[90:91], v[108:109], v[88:89] op_sel:[0,1,0]
	v_pk_fma_f32 v[92:93], v[90:91], v[110:111], v[92:93] op_sel_hi:[1,0,1]
	v_pk_add_f32 v[74:75], v[98:99], v[112:113]
	v_pk_add_f32 v[90:91], v[72:73], v[74:75]
	v_pk_add_f32 v[94:95], v[50:51], v[60:61]
	v_pk_add_f32 v[72:73], v[48:49], v[94:95]
	v_pk_add_f32 v[50:51], v[62:63], v[88:89]
	v_pk_add_f32 v[48:49], v[64:65], v[50:51]
	v_pk_add_f32 v[62:63], v[66:67], v[92:93]
	v_pk_add_f32 v[64:65], v[68:69], v[62:63]
	v_pk_fma_f32 v[72:73], v[128:129], v[90:91], v[72:73] op_sel_hi:[0,1,1] neg_lo:[1,0,0] neg_hi:[1,0,0]
	v_pk_fma_f32 v[48:49], v[128:129], v[90:91], v[48:49] op_sel:[1,0,0] neg_lo:[1,0,0] neg_hi:[1,0,0]
	v_pk_fma_f32 v[64:65], v[130:131], v[90:91], v[64:65] op_sel_hi:[0,1,1] neg_lo:[1,0,0] neg_hi:[1,0,0]
	v_pk_mul_f32 v[66:67], v[130:131], v[72:73] op_sel:[1,0]
	v_pk_mul_f32 v[98:99], v[132:133], v[72:73] op_sel_hi:[0,1]
	v_pk_mul_f32 v[142:143], v[132:133], v[72:73] op_sel:[1,0]
	v_pk_fma_f32 v[66:67], v[132:133], v[48:49], v[66:67] op_sel_hi:[0,1,1]
	v_pk_fma_f32 v[98:99], v[134:135], v[48:49], v[98:99] op_sel_hi:[0,1,1]
	v_pk_fma_f32 v[142:143], v[134:135], v[48:49], v[142:143] op_sel:[1,0,0]
	v_pk_fma_f32 v[66:67], v[132:133], v[64:65], v[66:67] op_sel:[1,0,0]
	v_pk_fma_f32 v[98:99], v[134:135], v[64:65], v[98:99] op_sel:[1,0,0]
	v_pk_fma_f32 v[142:143], v[136:137], v[64:65], v[142:143] op_sel_hi:[0,1,1]
	v_pk_mul_f32 v[68:69], v[128:129], v[66:67] op_sel_hi:[0,1]
	v_pk_fma_f32 v[68:69], v[128:129], v[98:99], v[68:69] op_sel:[1,0,0]
	v_pk_fma_f32 v[68:69], v[130:131], v[142:143], v[68:69] op_sel_hi:[0,1,1]
	v_pk_fma_f32 v[68:69], v[136:137], v[90:91], v[68:69] op_sel:[1,0,0] neg_lo:[0,0,1] neg_hi:[0,0,1]
	s_add_i32 s5, s34, 3
	s_min_i32 s5, s5, 0x200
	s_mul_i32 s6, s5, 0x804
	s_add_i32 s6, s6, s35
	s_add_i32 s7, s6, 0x505014
	s_add_i32 s8, s6, 0x606018
	s_mul_i32 s9, s5, 0x180c
	s_add_i32 s9, s9, s33
	s_add_i32 s4, s34, 4
	s_min_i32 s4, s4, 0x200
	s_mul_i32 s4, s4, 0x804
	s_add_i32 s4, s4, s38
	buffer_load_dword v2, v28, s[20:23], s4 offen nt
	buffer_load_dwordx3 v[8:10], v27, s[24:27], s9 offen nt
	buffer_load_dword v4, v28, s[16:19], s7 offen nt
	buffer_load_dword v5, v28, s[16:19], s8 offen nt
	s_waitcnt vmcnt(8)
	v_mov_b32_dpp v36, v76 wave_shr:1 row_mask:0xf bank_mask:0xf bound_ctrl:1
	v_mov_b32_dpp v37, v77 wave_shr:1 row_mask:0xf bank_mask:0xf bound_ctrl:1
	v_mov_b32_dpp v38, v78 wave_shr:1 row_mask:0xf bank_mask:0xf bound_ctrl:1
	v_mov_b32_dpp v40, v76 wave_shl:1 row_mask:0xf bank_mask:0xf bound_ctrl:1
	v_mov_b32_dpp v41, v77 wave_shl:1 row_mask:0xf bank_mask:0xf bound_ctrl:1
	v_mov_b32_dpp v42, v78 wave_shl:1 row_mask:0xf bank_mask:0xf bound_ctrl:1
	s_add_i32 s4, s34, 2
	s_cmpk_lt_u32 s4, 0x201
	s_cselect_b64 s[12:13], s[40:41], 0
	v_cmp_eq_u32_e64 s[14:15], s37, v24
	s_and_b64 s[14:15], s[14:15], s[12:13]
	v_cndmask_b32_e64 v25, 0, 1, s[14:15]
	v_mul_f32_e32 v48, v76, v76
	v_mul_f32_e32 v49, v76, v77
	v_mul_f32_e32 v64, v76, v78
	v_mul_f32_e32 v65, v77, v77
	v_mul_f32_e32 v72, v77, v78
	v_mul_f32_e32 v73, v78, v78
	v_or_b32_dpp v29, v25, v25 wave_shr:1 row_mask:0xf bank_mask:0xf bound_ctrl:1
	s_nop 1
	v_or_b32_dpp v29, v25, v29 wave_shl:1 row_mask:0xf bank_mask:0xf bound_ctrl:1
	s_nop 1
	v_or_b32_dpp v53, v29, v29 wave_shr:1 row_mask:0xf bank_mask:0xf bound_ctrl:1
	s_nop 1
	v_or_b32_dpp v53, v29, v53 wave_shl:1 row_mask:0xf bank_mask:0xf bound_ctrl:1
	v_or3_b32 v25, v53, v70, v71
	v_or3_b32 v25, v25, v52, v30
	s_add_i32 s4, s34, -1
	s_cmpk_lt_u32 s4, 0x1ff
	s_cselect_b64 s[12:13], s[42:43], 0
	v_cmp_ne_u32_e64 s[30:31], 0, v25
	s_and_b64 s[30:31], s[30:31], s[12:13]
	v_cndmask_b32_e64 v25, 0, 1.0, s[30:31]
	v_add_f32_e32 v90, v76, v36
	v_add_f32_e32 v91, v77, v37
	v_add_f32_e32 v116, v78, v38
	v_fmac_f32_e32 v48, v36, v36
	v_fmac_f32_e32 v49, v36, v37
	v_fmac_f32_e32 v64, v36, v38
	v_fmac_f32_e32 v65, v37, v37
	v_fmac_f32_e32 v72, v37, v38
	v_fmac_f32_e32 v73, v38, v38
	v_add_f32_dpp v133, v25, v25 wave_shr:1 row_mask:0xf bank_mask:0xf bound_ctrl:1
	v_add_f32_e32 v90, v90, v40
	v_add_f32_e32 v91, v91, v41
	v_add_f32_e32 v116, v116, v42
	v_fma_f32 v117, v40, v40, v48
	v_fma_f32 v128, v40, v41, v49
	v_fma_f32 v129, v40, v42, v64
	v_fma_f32 v130, v41, v41, v65
	v_fma_f32 v131, v41, v42, v72
	v_fma_f32 v132, v42, v42, v73
	v_add_f32_dpp v133, v25, v133 wave_shl:1 row_mask:0xf bank_mask:0xf bound_ctrl:1
	v_pk_add_f32 v[48:49], v[114:115], v[90:91]
	v_pk_add_f32 v[64:65], v[44:45], v[116:117]
	v_pk_add_f32 v[44:45], v[54:55], v[128:129]
	v_pk_add_f32 v[54:55], v[56:57], v[130:131]
	v_pk_add_f32 v[56:57], v[58:59], v[132:133]
	v_mul_f32_e32 v136, v48, v22
	v_mul_f32_e32 v137, v49, v22
	v_mul_f32_e32 v138, v64, v22
	v_fma_f32 v25, v65, v22, v26
	v_mul_f32_e32 v29, v44, v22
	v_mul_f32_e32 v58, v45, v22
	v_fma_f32 v59, v54, v22, v26
	v_mul_f32_e32 v72, v55, v22
	v_fma_f32 v73, v56, v22, v26
	v_fma_f32 v25, -v136, v136, v25
	v_fma_f32 v29, -v136, v137, v29
	v_fma_f32 v58, -v136, v138, v58
	v_fma_f32 v59, -v137, v137, v59
	v_fma_f32 v72, -v137, v138, v72
	v_fma_f32 v73, -v138, v138, v73
	v_mul_f32_e32 v114, v72, v72
	v_mul_f32_e32 v115, v29, v73
	v_mul_f32_e32 v134, v58, v59
	v_mul_f32_e32 v135, v58, v58
	v_mul_f32_e32 v140, v25, v72
	v_mul_f32_e32 v141, v29, v29
	v_fma_f32 v114, v59, v73, -v114
	v_fma_f32 v115, v58, v72, -v115
	v_fma_f32 v134, v29, v72, -v134
	v_fma_f32 v135, v25, v73, -v135
	v_fma_f32 v140, v29, v58, -v140
	v_fma_f32 v141, v25, v59, -v141
	v_mul_f32_e32 v152, v25, v114
	v_fmac_f32_e32 v152, v29, v115
	v_fmac_f32_e32 v152, v58, v134
	v_rcp_f32_e32 v152, v152
	v_cmp_ne_u32_e64 vcc, s37, v3
	v_mul_f32_e32 v152, v152, v22
	v_cndmask_b32_e64 v152, 0, v152, s[30:31]
	v_cndmask_b32_e64 v25, 0, v18, vcc
	v_cndmask_b32_e64 v149, 0, v22, s[30:31]
	v_mul_f32_e32 v139, v114, v152
	v_mul_f32_e32 v144, v115, v152
	v_mul_f32_e32 v145, v134, v152
	v_mul_f32_e32 v146, v135, v152
	v_mul_f32_e32 v147, v140, v152
	v_mul_f32_e32 v148, v141, v152
	v_add_f32_e32 v150, v57, v25
	v_mov_b32_e32 v151, v3
	ds_write_b128 v23, v[136:139] offset:3072
	ds_write_b128 v23, v[144:147] offset:4096
	ds_write_b128 v23, v[148:151] offset:5120
	s_waitcnt lgkmcnt(0)
	s_barrier
	v_mov_b32_dpp v44, v46 wave_shr:1 row_mask:0xf bank_mask:0xf bound_ctrl:1
	v_mov_b32_dpp v45, v47 wave_shr:1 row_mask:0xf bank_mask:0xf bound_ctrl:1
	v_mov_b32_dpp v48, v46 wave_shl:1 row_mask:0xf bank_mask:0xf bound_ctrl:1
	v_mov_b32_dpp v49, v47 wave_shl:1 row_mask:0xf bank_mask:0xf bound_ctrl:1
	v_pk_mul_f32 v[54:55], v[46:47], v[76:77] op_sel_hi:[1,0]
	v_pk_mul_f32 v[58:59], v[46:47], v[76:77] op_sel:[0,1]
	v_pk_mul_f32 v[114:115], v[46:47], v[78:79] op_sel_hi:[1,0]
	v_pk_add_f32 v[134:135], v[46:47], v[44:45]
	v_pk_fma_f32 v[54:55], v[44:45], v[36:37], v[54:55] op_sel_hi:[1,0,1]
	v_pk_fma_f32 v[58:59], v[44:45], v[36:37], v[58:59] op_sel:[0,1,0]
	v_pk_fma_f32 v[114:115], v[44:45], v[38:39], v[114:115] op_sel_hi:[1,0,1]
	v_pk_add_f32 v[134:135], v[134:135], v[48:49]
	v_pk_fma_f32 v[54:55], v[48:49], v[40:41], v[54:55] op_sel_hi:[1,0,1]
	v_pk_fma_f32 v[58:59], v[48:49], v[40:41], v[58:59] op_sel:[0,1,0]
	v_pk_fma_f32 v[114:115], v[48:49], v[42:43], v[114:115] op_sel_hi:[1,0,1]
	v_pk_add_f32 v[44:45], v[74:75], v[134:135]
	v_pk_add_f32 v[74:75], v[94:95], v[54:55]
	v_pk_add_f32 v[94:95], v[50:51], v[58:59]
	v_pk_add_f32 v[50:51], v[62:63], v[114:115]
	v_pk_fma_f32 v[74:75], v[136:137], v[44:45], v[74:75] op_sel_hi:[0,1,1] neg_lo:[1,0,0] neg_hi:[1,0,0]
	v_pk_fma_f32 v[94:95], v[136:137], v[44:45], v[94:95] op_sel:[1,0,0] neg_lo:[1,0,0] neg_hi:[1,0,0]
	v_pk_fma_f32 v[50:51], v[138:139], v[44:45], v[50:51] op_sel_hi:[0,1,1] neg_lo:[1,0,0] neg_hi:[1,0,0]
	v_pk_mul_f32 v[48:49], v[138:139], v[74:75] op_sel:[1,0]
	v_pk_mul_f32 v[56:57], v[144:145], v[74:75] op_sel_hi:[0,1]
	v_pk_mul_f32 v[64:65], v[144:145], v[74:75] op_sel:[1,0]
	v_pk_fma_f32 v[48:49], v[144:145], v[94:95], v[48:49] op_sel_hi:[0,1,1]
	v_pk_fma_f32 v[56:57], v[146:147], v[94:95], v[56:57] op_sel_hi:[0,1,1]
	v_pk_fma_f32 v[64:65], v[146:147], v[94:95], v[64:65] op_sel:[1,0,0]
	v_pk_fma_f32 v[48:49], v[144:145], v[50:51], v[48:49] op_sel:[1,0,0]
	v_pk_fma_f32 v[56:57], v[146:147], v[50:51], v[56:57] op_sel:[1,0,0]
	v_pk_fma_f32 v[64:65], v[148:149], v[50:51], v[64:65] op_sel_hi:[0,1,1]
	v_pk_mul_f32 v[62:63], v[136:137], v[48:49] op_sel_hi:[0,1]
	v_pk_fma_f32 v[62:63], v[136:137], v[56:57], v[62:63] op_sel:[1,0,0]
	v_pk_fma_f32 v[62:63], v[138:139], v[64:65], v[62:63] op_sel_hi:[0,1,1]
	v_pk_fma_f32 v[62:63], v[148:149], v[44:45], v[62:63] op_sel:[1,0,0] neg_lo:[0,0,1] neg_hi:[0,0,1]
	s_add_i32 s5, s34, 4
	s_min_i32 s5, s5, 0x200
	s_mul_i32 s6, s5, 0x804
	s_add_i32 s6, s6, s35
	s_add_i32 s7, s6, 0x505014
	s_add_i32 s8, s6, 0x606018
	s_mul_i32 s9, s5, 0x180c
	s_add_i32 s9, s9, s33
	s_add_i32 s4, s34, 5
	s_min_i32 s4, s4, 0x200
	s_mul_i32 s4, s4, 0x804
	s_add_i32 s4, s4, s38
	buffer_load_dword v3, v28, s[20:23], s4 offen nt
	buffer_load_dwordx3 v[12:14], v27, s[24:27], s9 offen nt
	buffer_load_dword v6, v28, s[16:19], s7 offen nt
	buffer_load_dword v7, v28, s[16:19], s8 offen nt
	s_waitcnt vmcnt(8)
	v_mov_b32_dpp v72, v100 wave_shr:1 row_mask:0xf bank_mask:0xf bound_ctrl:1
	v_mov_b32_dpp v73, v101 wave_shr:1 row_mask:0xf bank_mask:0xf bound_ctrl:1
	v_mov_b32_dpp v74, v102 wave_shr:1 row_mask:0xf bank_mask:0xf bound_ctrl:1
	v_mov_b32_dpp v80, v100 wave_shl:1 row_mask:0xf bank_mask:0xf bound_ctrl:1
	v_mov_b32_dpp v81, v101 wave_shl:1 row_mask:0xf bank_mask:0xf bound_ctrl:1
	v_mov_b32_dpp v82, v102 wave_shl:1 row_mask:0xf bank_mask:0xf bound_ctrl:1
	s_add_i32 s4, s34, 3
	s_cmpk_lt_u32 s4, 0x201
	s_cselect_b64 s[12:13], s[40:41], 0
	v_cmp_eq_u32_e64 s[14:15], s37, v17
	s_and_b64 s[14:15], s[14:15], s[12:13]
	v_cndmask_b32_e64 v25, 0, 1, s[14:15]
	v_mul_f32_e32 v44, v100, v100
	v_mul_f32_e32 v45, v100, v101
	v_mul_f32_e32 v50, v100, v102
	v_mul_f32_e32 v51, v101, v101
	v_mul_f32_e32 v84, v101, v102
	v_mul_f32_e32 v85, v102, v102
	v_or_b32_dpp v29, v25, v25 wave_shr:1 row_mask:0xf bank_mask:0xf bound_ctrl:1
	s_nop 1
	v_or_b32_dpp v29, v25, v29 wave_shl:1 row_mask:0xf bank_mask:0xf bound_ctrl:1
	s_nop 1
	v_or_b32_dpp v30, v29, v29 wave_shr:1 row_mask:0xf bank_mask:0xf bound_ctrl:1
	s_nop 1
	v_or_b32_dpp v30, v29, v30 wave_shl:1 row_mask:0xf bank_mask:0xf bound_ctrl:1
	v_or3_b32 v25, v30, v53, v70
	v_or3_b32 v25, v25, v71, v52
	s_add_i32 s4, s34, 0
	s_cmpk_lt_u32 s4, 0x1ff
	s_cselect_b64 s[12:13], s[42:43], 0
	v_cmp_ne_u32_e64 s[30:31], 0, v25
	s_and_b64 s[30:31], s[30:31], s[12:13]
	v_cndmask_b32_e64 v25, 0, 1.0, s[30:31]
	v_add_f32_e32 v86, v100, v72
	v_add_f32_e32 v87, v101, v73
	v_add_f32_e32 v94, v102, v74
	v_fmac_f32_e32 v44, v72, v72
	v_fmac_f32_e32 v45, v72, v73
	v_fmac_f32_e32 v50, v72, v74
	v_fmac_f32_e32 v51, v73, v73
	v_fmac_f32_e32 v84, v73, v74
	v_fmac_f32_e32 v85, v74, v74
	v_add_f32_dpp v141, v25, v25 wave_shr:1 row_mask:0xf bank_mask:0xf bound_ctrl:1
	v_add_f32_e32 v86, v86, v80
	v_add_f32_e32 v87, v87, v81
	v_add_f32_e32 v94, v94, v82
	v_fma_f32 v95, v80, v80, v44
	v_fma_f32 v136, v80, v81, v45
	v_fma_f32 v137, v80, v82, v50
	v_fma_f32 v138, v81, v81, v51
	v_fma_f32 v139, v81, v82, v84
	v_fma_f32 v140, v82, v82, v85
	v_add_f32_dpp v141, v25, v141 wave_shl:1 row_mask:0xf bank_mask:0xf bound_ctrl:1
	v_pk_add_f32 v[44:45], v[90:91], v[86:87]
	v_pk_add_f32 v[50:51], v[118:119], v[44:45]
	v_pk_add_f32 v[90:91], v[116:117], v[94:95]
	v_pk_add_f32 v[84:85], v[120:121], v[90:91]
	v_pk_add_f32 v[116:117], v[128:129], v[136:137]
	v_pk_add_f32 v[118:119], v[122:123], v[116:117]
	v_pk_add_f32 v[122:123], v[130:131], v[138:139]
	v_pk_add_f32 v[120:121], v[124:125], v[122:123]
	v_pk_add_f32 v[124:125], v[132:133], v[140:141]
	v_pk_add_f32 v[128:129], v[126:127], v[124:125]
	v_mul_f32_e32 v144, v50, v22
	v_mul_f32_e32 v145, v51, v22
	v_mul_f32_e32 v146, v84, v22
	v_fma_f32 v25, v85, v22, v26
	v_mul_f32_e32 v29, v118, v22
	v_mul_f32_e32 v126, v119, v22
	v_fma_f32 v127, v120, v22, v26
	v_mul_f32_e32 v130, v121, v22
	v_fma_f32 v131, v128, v22, v26
	v_fma_f32 v25, -v144, v144, v25
	v_fma_f32 v29, -v144, v145, v29
	v_fma_f32 v126, -v144, v146, v126
	v_fma_f32 v127, -v145, v145, v127
	v_fma_f32 v130, -v145, v146, v130
	v_fma_f32 v131, -v146, v146, v131
	v_mul_f32_e32 v132, v130, v130
	v_mul_f32_e32 v133, v29, v131
	v_mul_f32_e32 v156, v126, v127
	v_mul_f32_e32 v157, v126, v126
	v_mul_f32_e32 v158, v25, v130
	v_mul_f32_e32 v159, v29, v29
	v_fma_f32 v132, v127, v131, -v132
	v_fma_f32 v133, v126, v130, -v133
	v_fma_f32 v156, v29, v130, -v156
	v_fma_f32 v157, v25, v131, -v157
	v_fma_f32 v158, v29, v126, -v158
	v_fma_f32 v159, v25, v127, -v159
	v_mul_f32_e32 v160, v25, v132
	v_fmac_f32_e32 v160, v29, v133
	v_fmac_f32_e32 v160, v126, v156
	v_rcp_f32_e32 v160, v160
	v_cmp_ne_u32_e64 vcc, s37, v16
	v_mul_f32_e32 v160, v160, v22
	v_cndmask_b32_e64 v160, 0, v160, s[30:31]
	v_cndmask_b32_e64 v25, 0, v18, vcc
	v_cndmask_b32_e64 v153, 0, v22, s[30:31]
	v_mul_f32_e32 v147, v132, v160
	v_mul_f32_e32 v148, v133, v160
	v_mul_f32_e32 v149, v156, v160
	v_mul_f32_e32 v150, v157, v160
	v_mul_f32_e32 v151, v158, v160
	v_mul_f32_e32 v152, v159, v160
	v_add_f32_e32 v154, v129, v25
	v_mov_b32_e32 v155, v16
	ds_write_b128 v23, v[144:147]
	ds_write_b128 v23, v[148:151] offset:1024
	ds_write_b128 v23, v[152:155] offset:2048
	s_waitcnt lgkmcnt(0)
	s_barrier
	v_mov_b32_dpp v50, v96 wave_shr:1 row_mask:0xf bank_mask:0xf bound_ctrl:1
	v_mov_b32_dpp v51, v97 wave_shr:1 row_mask:0xf bank_mask:0xf bound_ctrl:1
	v_mov_b32_dpp v118, v96 wave_shl:1 row_mask:0xf bank_mask:0xf bound_ctrl:1
	v_mov_b32_dpp v119, v97 wave_shl:1 row_mask:0xf bank_mask:0xf bound_ctrl:1
	v_pk_mul_f32 v[84:85], v[96:97], v[100:101] op_sel_hi:[1,0]
	v_pk_mul_f32 v[120:121], v[96:97], v[100:101] op_sel:[0,1]
	v_pk_mul_f32 v[128:129], v[96:97], v[102:103] op_sel_hi:[1,0]
	v_pk_add_f32 v[132:133], v[96:97], v[50:51]
	v_pk_fma_f32 v[84:85], v[50:51], v[72:73], v[84:85] op_sel_hi:[1,0,1]
	v_pk_fma_f32 v[120:121], v[50:51], v[72:73], v[120:121] op_sel:[0,1,0]
	v_pk_fma_f32 v[128:129], v[50:51], v[74:75], v[128:129] op_sel_hi:[1,0,1]
	v_pk_add_f32 v[132:133], v[132:133], v[118:119]
	v_pk_fma_f32 v[84:85], v[118:119], v[80:81], v[84:85] op_sel_hi:[1,0,1]
	v_pk_fma_f32 v[120:121], v[118:119], v[80:81], v[120:121] op_sel:[0,1,0]
	v_pk_fma_f32 v[128:129], v[118:119], v[82:83], v[128:129] op_sel_hi:[1,0,1]
	v_pk_add_f32 v[50:51], v[134:135], v[132:133]
	v_pk_add_f32 v[118:119], v[112:113], v[50:51]
	v_pk_add_f32 v[126:127], v[54:55], v[84:85]
	v_pk_add_f32 v[112:113], v[60:61], v[126:127]
	v_pk_add_f32 v[54:55], v[58:59], v[120:121]
	v_pk_add_f32 v[60:61], v[88:89], v[54:55]
	v_pk_add_f32 v[58:59], v[114:115], v[128:129]
	v_pk_add_f32 v[88:89], v[92:93], v[58:59]
	v_pk_fma_f32 v[112:113], v[144:145], v[118:119], v[112:113] op_sel_hi:[0,1,1] neg_lo:[1,0,0] neg_hi:[1,0,0]
	v_pk_fma_f32 v[60:61], v[144:145], v[118:119], v[60:61] op_sel:[1,0,0] neg_lo:[1,0,0] neg_hi:[1,0,0]
	v_pk_fma_f32 v[88:89], v[146:147], v[118:119], v[88:89] op_sel_hi:[0,1,1] neg_lo:[1,0,0] neg_hi:[1,0,0]
	v_pk_mul_f32 v[114:115], v[146:147], v[112:113] op_sel:[1,0]
	v_pk_mul_f32 v[130:131], v[148:149], v[112:113] op_sel_hi:[0,1]
	v_pk_mul_f32 v[134:135], v[148:149], v[112:113] op_sel:[1,0]
	v_pk_fma_f32 v[114:115], v[148:149], v[60:61], v[114:115] op_sel_hi:[0,1,1]
	v_pk_fma_f32 v[130:131], v[150:151], v[60:61], v[130:131] op_sel_hi:[0,1,1]
	v_pk_fma_f32 v[134:135], v[150:151], v[60:61], v[134:135] op_sel:[1,0,0]
	v_pk_fma_f32 v[114:115], v[148:149], v[88:89], v[114:115] op_sel:[1,0,0]
	v_pk_fma_f32 v[130:131], v[150:151], v[88:89], v[130:131] op_sel:[1,0,0]
	v_pk_fma_f32 v[134:135], v[152:153], v[88:89], v[134:135] op_sel_hi:[0,1,1]
	v_pk_mul_f32 v[92:93], v[144:145], v[114:115] op_sel_hi:[0,1]
	v_pk_fma_f32 v[92:93], v[144:145], v[130:131], v[92:93] op_sel:[1,0,0]
	v_pk_fma_f32 v[92:93], v[146:147], v[134:135], v[92:93] op_sel_hi:[0,1,1]
	v_pk_fma_f32 v[92:93], v[152:153], v[118:119], v[92:93] op_sel:[1,0,0] neg_lo:[0,0,1] neg_hi:[0,0,1]
	v_cmp_eq_u32_e64 s[10:11], 6, v155
	v_cmp_eq_u32_e64 s[14:15], 7, v155
	v_pk_add_f32 v[60:61], v[48:49], v[114:115]
	v_pk_add_f32 v[88:89], v[66:67], v[60:61]
	v_pk_add_f32 v[48:49], v[56:57], v[130:131]
	v_pk_add_f32 v[66:67], v[98:99], v[48:49]
	v_pk_add_f32 v[56:57], v[64:65], v[134:135]
	v_pk_add_f32 v[98:99], v[142:143], v[56:57]
	v_pk_add_f32 v[118:119], v[62:63], v[92:93]
	v_pk_add_f32 v[64:65], v[68:69], v[118:119]
	v_pk_fma_f32 v[68:69], v[104:105], v[88:89], v[64:65] op_sel_hi:[0,1,1]
	v_pk_fma_f32 v[112:113], v[108:109], v[88:89], v[64:65] op_sel_hi:[0,1,1]
	v_pk_fma_f32 v[68:69], v[104:105], v[66:67], v[68:69] op_sel:[1,0,0]
	v_pk_fma_f32 v[112:113], v[108:109], v[66:67], v[112:113] op_sel:[1,0,0]
	v_pk_fma_f32 v[68:69], v[106:107], v[98:99], v[68:69] op_sel_hi:[0,1,1]
	v_pk_fma_f32 v[112:113], v[110:111], v[98:99], v[112:113] op_sel_hi:[0,1,1]
	v_pk_fma_f32 v[64:65], v[32:33], v[88:89], v[64:65] op_sel_hi:[0,1,1]
	v_pk_fma_f32 v[64:65], v[32:33], v[66:67], v[64:65] op_sel:[1,0,0]
	v_pk_fma_f32 v[64:65], v[34:35], v[98:99], v[64:65] op_sel_hi:[0,1,1]
	v_cndmask_b32_e64 v62, 0, v18, s[10:11]
	v_cndmask_b32_e64 v63, 0, v18, s[14:15]
	v_add_f32_dpp v64, v68, v64 wave_shl:1 row_mask:0xf bank_mask:0xf bound_ctrl:1
	v_add_f32_dpp v65, v69, v65 wave_shl:1 row_mask:0xf bank_mask:0xf bound_ctrl:1
	s_add_i32 s4, s34, 0
	s_cmpk_lt_i32 s4, 0x201
	s_cselect_b64 s[12:13], s[0:1], 0
	v_add_f32_dpp v64, v112, v64 wave_shr:1 row_mask:0xf bank_mask:0xf bound_ctrl:1
	v_add_f32_dpp v65, v113, v65 wave_shr:1 row_mask:0xf bank_mask:0xf bound_ctrl:1
	v_pk_fma_f32 v[64:65], v[20:21], v[154:155], v[64:65] op_sel_hi:[1,0,1] neg_lo:[0,0,1] neg_hi:[0,0,1]
	v_pk_add_f32 v[64:65], v[64:65], v[62:63] neg_lo:[0,1] neg_hi:[0,1]
	v_pk_mul_f32 v[142:143], v[64:65], v[64:65]
	v_add_f32_e32 v142, v142, v143
	v_cndmask_b32_e64 v143, 0, v142, s[12:13]
	v_add_f32_e32 v1, v1, v143
	s_add_i32 s5, s34, 5
	s_min_i32 s5, s5, 0x200
	s_mul_i32 s6, s5, 0x804
	s_add_i32 s6, s6, s35
	s_add_i32 s7, s6, 0x505014
	s_add_i32 s8, s6, 0x606018
	s_mul_i32 s9, s5, 0x180c
	s_add_i32 s9, s9, s33
	s_add_i32 s4, s34, 6
	s_min_i32 s4, s4, 0x200
	s_mul_i32 s4, s4, 0x804
	s_add_i32 s4, s4, s38
	buffer_load_dword v16, v28, s[20:23], s4 offen nt
	buffer_load_dwordx3 v[32:34], v27, s[24:27], s9 offen nt
	buffer_load_dword v20, v28, s[16:19], s7 offen nt
	buffer_load_dword v21, v28, s[16:19], s8 offen nt
	s_waitcnt vmcnt(8)
	v_mov_b32_dpp v64, v8 wave_shr:1 row_mask:0xf bank_mask:0xf bound_ctrl:1
	v_mov_b32_dpp v65, v9 wave_shr:1 row_mask:0xf bank_mask:0xf bound_ctrl:1
	v_mov_b32_dpp v66, v10 wave_shr:1 row_mask:0xf bank_mask:0xf bound_ctrl:1
	v_mov_b32_dpp v104, v8 wave_shl:1 row_mask:0xf bank_mask:0xf bound_ctrl:1
	v_mov_b32_dpp v105, v9 wave_shl:1 row_mask:0xf bank_mask:0xf bound_ctrl:1
	v_mov_b32_dpp v106, v10 wave_shl:1 row_mask:0xf bank_mask:0xf bound_ctrl:1
	s_add_i32 s4, s34, 4
	s_cmpk_lt_u32 s4, 0x201
	s_cselect_b64 s[12:13], s[40:41], 0
	v_cmp_eq_u32_e64 s[14:15], s37, v2
	s_and_b64 s[14:15], s[14:15], s[12:13]
	v_cndmask_b32_e64 v25, 0, 1, s[14:15]
	v_mul_f32_e32 v62, v8, v8
	v_mul_f32_e32 v63, v8, v9
	v_mul_f32_e32 v68, v8, v10
	v_mul_f32_e32 v69, v9, v9
	v_mul_f32_e32 v88, v9, v10
	v_mul_f32_e32 v89, v10, v10
	v_or_b32_dpp v29, v25, v25 wave_shr:1 row_mask:0xf bank_mask:0xf bound_ctrl:1
	s_nop 1
	v_or_b32_dpp v29, v25, v29 wave_shl:1 row_mask:0xf bank_mask:0xf bound_ctrl:1
	s_nop 1
	v_or_b32_dpp v52, v29, v29 wave_shr:1 row_mask:0xf bank_mask:0xf bound_ctrl:1
	s_nop 1
	v_or_b32_dpp v52, v29, v52 wave_shl:1 row_mask:0xf bank_mask:0xf bound_ctrl:1
	v_or3_b32 v25, v52, v30, v53
	v_or3_b32 v25, v25, v70, v71
	s_add_i32 s4, s34, 1
	s_cmpk_lt_u32 s4, 0x1ff
	s_cselect_b64 s[12:13], s[42:43], 0
	v_cmp_ne_u32_e64 s[30:31], 0, v25
	s_and_b64 s[30:31], s[30:31], s[12:13]
	v_cndmask_b32_e64 v25, 0, 1.0, s[30:31]
	v_add_f32_e32 v98, v8, v64
	v_add_f32_e32 v99, v9, v65
	v_add_f32_e32 v108, v10, v66
	v_fmac_f32_e32 v62, v64, v64
	v_fmac_f32_e32 v63, v64, v65
	v_fmac_f32_e32 v68, v64, v66
	v_fmac_f32_e32 v69, v65, v65
	v_fmac_f32_e32 v88, v65, v66
	v_fmac_f32_e32 v89, v66, v66
	v_add_f32_dpp v143, v25, v25 wave_shr:1 row_mask:0xf bank_mask:0xf bound_ctrl:1
	v_add_f32_e32 v98, v98, v104
	v_add_f32_e32 v99, v99, v105
	v_add_f32_e32 v108, v108, v106
	v_fma_f32 v109, v104, v104, v62
	v_fma_f32 v110, v104, v105, v63
	v_fma_f32 v111, v104, v106, v68
	v_fma_f32 v112, v105, v105, v69
	v_fma_f32 v113, v105, v106, v88
	v_fma_f32 v142, v106, v106, v89
	v_add_f32_dpp v143, v25, v143 wave_shl:1 row_mask:0xf bank_mask:0xf bound_ctrl:1
	v_pk_add_f32 v[62:63], v[44:45], v[98:99]
	v_pk_add_f32 v[44:45], v[90:91], v[108:109]
	v_pk_add_f32 v[68:69], v[116:117], v[110:111]
	v_pk_add_f32 v[88:89], v[122:123], v[112:113]
	v_pk_add_f32 v[90:91], v[124:125], v[142:143]
	v_mul_f32_e32 v144, v62, v22
	v_mul_f32_e32 v145, v63, v22
	v_mul_f32_e32 v146, v44, v22
	v_fma_f32 v25, v45, v22, v26
	v_mul_f32_e32 v29, v68, v22
	v_mul_f32_e32 v116, v69, v22
	v_fma_f32 v117, v88, v22, v26
	v_mul_f32_e32 v122, v89, v22
	v_fma_f32 v123, v90, v22, v26
	v_fma_f32 v25, -v144, v144, v25
	v_fma_f32 v29, -v144, v145, v29
	v_fma_f32 v116, -v144, v146, v116
	v_fma_f32 v117, -v145, v145, v117
	v_fma_f32 v122, -v145, v146, v122
	v_fma_f32 v123, -v146, v146, v123
	v_mul_f32_e32 v124, v122, v122
	v_mul_f32_e32 v125, v29, v123
	v_mul_f32_e32 v156, v116, v117
	v_mul_f32_e32 v157, v116, v116
	v_mul_f32_e32 v158, v25, v122
	v_mul_f32_e32 v159, v29, v29
	v_fma_f32 v124, v117, v123, -v124
	v_fma_f32 v125, v116, v122, -v125
	v_fma_f32 v156, v29, v122, -v156
	v_fma_f32 v157, v25, v123, -v157
	v_fma_f32 v158, v29, v116, -v158
	v_fma_f32 v159, v25, v117, -v159
	v_mul_f32_e32 v160, v25, v124
	v_fmac_f32_e32 v160, v29, v125
	v_fmac_f32_e32 v160, v116, v156
	v_rcp_f32_e32 v160, v160
	v_cmp_ne_u32_e64 vcc, s37, v31
	v_mul_f32_e32 v160, v160, v22
	v_cndmask_b32_e64 v160, 0, v160, s[30:31]
	v_cndmask_b32_e64 v25, 0, v18, vcc
	v_cndmask_b32_e64 v153, 0, v22, s[30:31]
	v_mul_f32_e32 v147, v124, v160
	v_mul_f32_e32 v148, v125, v160
	v_mul_f32_e32 v149, v156, v160
	v_mul_f32_e32 v150, v157, v160
	v_mul_f32_e32 v151, v158, v160
	v_mul_f32_e32 v152, v159, v160
	v_add_f32_e32 v154, v91, v25
	v_mov_b32_e32 v155, v31
	ds_write_b128 v23, v[144:147] offset:3072
	ds_write_b128 v23, v[148:151] offset:4096
	ds_write_b128 v23, v[152:155] offset:5120
	s_waitcnt lgkmcnt(0)
	s_barrier
	v_mov_b32_dpp v62, v4 wave_shr:1 row_mask:0xf bank_mask:0xf bound_ctrl:1
	v_mov_b32_dpp v63, v5 wave_shr:1 row_mask:0xf bank_mask:0xf bound_ctrl:1
	v_mov_b32_dpp v90, v4 wave_shl:1 row_mask:0xf bank_mask:0xf bound_ctrl:1
	v_mov_b32_dpp v91, v5 wave_shl:1 row_mask:0xf bank_mask:0xf bound_ctrl:1
	v_pk_mul_f32 v[44:45], v[4:5], v[8:9] op_sel_hi:[1,0]
	v_pk_mul_f32 v[68:69], v[4:5], v[8:9] op_sel:[0,1]
	v_pk_mul_f32 v[88:89], v[4:5], v[10:11] op_sel_hi:[1,0]
	v_pk_add_f32 v[116:117], v[4:5], v[62:63]
	v_pk_fma_f32 v[44:45], v[62:63], v[64:65], v[44:45] op_sel_hi:[1,0,1]
	v_pk_fma_f32 v[68:69], v[62:63], v[64:65], v[68:69] op_sel:[0,1,0]
	v_pk_fma_f32 v[88:89], v[62:63], v[66:67], v[88:89] op_sel_hi:[1,0,1]
	v_pk_add_f32 v[116:117], v[116:117], v[90:91]
	v_pk_fma_f32 v[44:45], v[90:91], v[104:105], v[44:45] op_sel_hi:[1,0,1]
	v_pk_fma_f32 v[68:69], v[90:91], v[104:105], v[68:69] op_sel:[0,1,0]
	v_pk_fma_f32 v[88:89], v[90:91], v[106:107], v[88:89] op_sel_hi:[1,0,1]
	v_pk_add_f32 v[62:63], v[50:51], v[116:117]
	v_pk_add_f32 v[124:125], v[126:127], v[44:45]
	v_pk_add_f32 v[156:157], v[54:55], v[68:69]
	v_pk_add_f32 v[160:161], v[58:59], v[88:89]
	v_pk_fma_f32 v[124:125], v[144:145], v[62:63], v[124:125] op_sel_hi:[0,1,1] neg_lo:[1,0,0] neg_hi:[1,0,0]
	v_pk_fma_f32 v[156:157], v[144:145], v[62:63], v[156:157] op_sel:[1,0,0] neg_lo:[1,0,0] neg_hi:[1,0,0]
	v_pk_fma_f32 v[160:161], v[146:147], v[62:63], v[160:161] op_sel_hi:[0,1,1] neg_lo:[1,0,0] neg_hi:[1,0,0]
	v_pk_mul_f32 v[50:51], v[146:147], v[124:125] op_sel:[1,0]
	v_pk_mul_f32 v[54:55], v[148:149], v[124:125] op_sel_hi:[0,1]
	v_pk_mul_f32 v[58:59], v[148:149], v[124:125] op_sel:[1,0]
	v_pk_fma_f32 v[50:51], v[148:149], v[156:157], v[50:51] op_sel_hi:[0,1,1]
	v_pk_fma_f32 v[54:55], v[150:151], v[156:157], v[54:55] op_sel_hi:[0,1,1]
	v_pk_fma_f32 v[58:59], v[150:151], v[156:157], v[58:59] op_sel:[1,0,0]
	v_pk_fma_f32 v[50:51], v[148:149], v[160:161], v[50:51] op_sel:[1,0,0]
	v_pk_fma_f32 v[54:55], v[150:151], v[160:161], v[54:55] op_sel:[1,0,0]
	v_pk_fma_f32 v[58:59], v[152:153], v[160:161], v[58:59] op_sel_hi:[0,1,1]
	v_pk_mul_f32 v[164:165], v[144:145], v[50:51] op_sel_hi:[0,1]
	v_pk_fma_f32 v[164:165], v[144:145], v[54:55], v[164:165] op_sel:[1,0,0]
	v_pk_fma_f32 v[164:165], v[146:147], v[58:59], v[164:165] op_sel_hi:[0,1,1]
	v_pk_fma_f32 v[164:165], v[152:153], v[62:63], v[164:165] op_sel:[1,0,0] neg_lo:[0,0,1] neg_hi:[0,0,1]
	v_cmp_eq_u32_e64 s[10:11], 6, v155
	v_cmp_eq_u32_e64 s[14:15], 7, v155
	v_pk_add_f32 v[62:63], v[60:61], v[50:51]
	v_pk_add_f32 v[60:61], v[48:49], v[54:55]
	v_pk_add_f32 v[48:49], v[56:57], v[58:59]
	v_pk_add_f32 v[90:91], v[118:119], v[164:165]
	v_pk_fma_f32 v[118:119], v[36:37], v[62:63], v[90:91] op_sel_hi:[0,1,1]
	v_pk_fma_f32 v[122:123], v[40:41], v[62:63], v[90:91] op_sel_hi:[0,1,1]
	v_pk_fma_f32 v[118:119], v[36:37], v[60:61], v[118:119] op_sel:[1,0,0]
	v_pk_fma_f32 v[122:123], v[40:41], v[60:61], v[122:123] op_sel:[1,0,0]
	v_pk_fma_f32 v[118:119], v[38:39], v[48:49], v[118:119] op_sel_hi:[0,1,1]
	v_pk_fma_f32 v[122:123], v[42:43], v[48:49], v[122:123] op_sel_hi:[0,1,1]
	v_pk_fma_f32 v[90:91], v[76:77], v[62:63], v[90:91] op_sel_hi:[0,1,1]
	v_pk_fma_f32 v[90:91], v[76:77], v[60:61], v[90:91] op_sel:[1,0,0]
	v_pk_fma_f32 v[90:91], v[78:79], v[48:49], v[90:91] op_sel_hi:[0,1,1]
	v_cndmask_b32_e64 v56, 0, v18, s[10:11]
	v_cndmask_b32_e64 v57, 0, v18, s[14:15]
	v_add_f32_dpp v90, v118, v90 wave_shl:1 row_mask:0xf bank_mask:0xf bound_ctrl:1
	v_add_f32_dpp v91, v119, v91 wave_shl:1 row_mask:0xf bank_mask:0xf bound_ctrl:1
	s_add_i32 s4, s34, 1
	s_cmpk_lt_i32 s4, 0x201
	s_cselect_b64 s[12:13], s[0:1], 0
	v_add_f32_dpp v90, v122, v90 wave_shr:1 row_mask:0xf bank_mask:0xf bound_ctrl:1
	v_add_f32_dpp v91, v123, v91 wave_shr:1 row_mask:0xf bank_mask:0xf bound_ctrl:1
	v_pk_fma_f32 v[90:91], v[46:47], v[154:155], v[90:91] op_sel_hi:[1,0,1] neg_lo:[0,0,1] neg_hi:[0,0,1]
	v_pk_add_f32 v[90:91], v[90:91], v[56:57] neg_lo:[0,1] neg_hi:[0,1]
	v_pk_mul_f32 v[124:125], v[90:91], v[90:91]
	v_add_f32_e32 v124, v124, v125
	v_cndmask_b32_e64 v125, 0, v124, s[12:13]
	v_add_f32_e32 v1, v1, v125
	s_add_i32 s5, s34, 6
	s_min_i32 s5, s5, 0x200
	s_mul_i32 s6, s5, 0x804
	s_add_i32 s6, s6, s35
	s_add_i32 s7, s6, 0x505014
	s_add_i32 s8, s6, 0x606018
	s_mul_i32 s9, s5, 0x180c
	s_add_i32 s9, s9, s33
	s_add_i32 s4, s34, 7
	s_min_i32 s4, s4, 0x200
	s_mul_i32 s4, s4, 0x804
	s_add_i32 s4, s4, s38
	buffer_load_dword v25, v28, s[20:23], s4 offen nt
	buffer_load_dwordx3 v[40:42], v27, s[24:27], s9 offen nt
	buffer_load_dword v36, v28, s[16:19], s7 offen nt
	buffer_load_dword v37, v28, s[16:19], s8 offen nt
	s_waitcnt vmcnt(8)
	v_mov_b32_dpp v60, v12 wave_shr:1 row_mask:0xf bank_mask:0xf bound_ctrl:1
	v_mov_b32_dpp v61, v13 wave_shr:1 row_mask:0xf bank_mask:0xf bound_ctrl:1
	v_mov_b32_dpp v62, v14 wave_shr:1 row_mask:0xf bank_mask:0xf bound_ctrl:1
	v_mov_b32_dpp v76, v12 wave_shl:1 row_mask:0xf bank_mask:0xf bound_ctrl:1
	v_mov_b32_dpp v77, v13 wave_shl:1 row_mask:0xf bank_mask:0xf bound_ctrl:1
	v_mov_b32_dpp v78, v14 wave_shl:1 row_mask:0xf bank_mask:0xf bound_ctrl:1
	s_add_i32 s4, s34, 5
	s_cmpk_lt_u32 s4, 0x201
	s_cselect_b64 s[12:13], s[40:41], 0
	v_cmp_eq_u32_e64 s[14:15], s37, v3
	s_and_b64 s[14:15], s[14:15], s[12:13]
	v_cndmask_b32_e64 v29, 0, 1, s[14:15]
	v_mul_f32_e32 v38, v12, v12
	v_mul_f32_e32 v39, v12, v13
	v_mul_f32_e32 v46, v12, v14
	v_mul_f32_e32 v47, v13, v13
	v_mul_f32_e32 v48, v13, v14
	v_mul_f32_e32 v49, v14, v14
	v_or_b32_dpp v31, v29, v29 wave_shr:1 row_mask:0xf bank_mask:0xf bound_ctrl:1
	s_nop 1
	v_or_b32_dpp v31, v29, v31 wave_shl:1 row_mask:0xf bank_mask:0xf bound_ctrl:1
	s_nop 1
	v_or_b32_dpp v71, v31, v31 wave_shr:1 row_mask:0xf bank_mask:0xf bound_ctrl:1
	s_nop 1
	v_or_b32_dpp v71, v31, v71 wave_shl:1 row_mask:0xf bank_mask:0xf bound_ctrl:1
	v_or3_b32 v29, v71, v52, v30
	v_or3_b32 v29, v29, v53, v70
	s_add_i32 s4, s34, 2
	s_cmpk_lt_u32 s4, 0x1ff
	s_cselect_b64 s[12:13], s[42:43], 0
	v_cmp_ne_u32_e64 s[30:31], 0, v29
	s_and_b64 s[30:31], s[30:31], s[12:13]
	v_cndmask_b32_e64 v29, 0, 1.0, s[30:31]
	v_add_f32_e32 v56, v12, v60
	v_add_f32_e32 v57, v13, v61
	v_add_f32_e32 v90, v14, v62
	v_fmac_f32_e32 v38, v60, v60
	v_fmac_f32_e32 v39, v60, v61
	v_fmac_f32_e32 v46, v60, v62
	v_fmac_f32_e32 v47, v61, v61
	v_fmac_f32_e32 v48, v61, v62
	v_fmac_f32_e32 v49, v62, v62
	v_add_f32_dpp v125, v29, v29 wave_shr:1 row_mask:0xf bank_mask:0xf bound_ctrl:1
	v_add_f32_e32 v56, v56, v76
	v_add_f32_e32 v57, v57, v77
	v_add_f32_e32 v90, v90, v78
	v_fma_f32 v91, v76, v76, v38
	v_fma_f32 v118, v76, v77, v39
	v_fma_f32 v119, v76, v78, v46
	v_fma_f32 v122, v77, v77, v47
	v_fma_f32 v123, v77, v78, v48
	v_fma_f32 v124, v78, v78, v49
	v_add_f32_dpp v125, v29, v125 wave_shl:1 row_mask:0xf bank_mask:0xf bound_ctrl:1
	v_pk_add_f32 v[48:49], v[98:99], v[56:57]
	v_pk_add_f32 v[38:39], v[86:87], v[48:49]
	v_pk_add_f32 v[144:145], v[108:109], v[90:91]
	v_pk_add_f32 v[46:47], v[94:95], v[144:145]
	v_pk_add_f32 v[86:87], v[110:111], v[118:119]
	v_pk_add_f32 v[94:95], v[136:137], v[86:87]
	v_pk_add_f32 v[108:109], v[112:113], v[122:123]
	v_pk_add_f32 v[98:99], v[138:139], v[108:109]
	v_pk_add_f32 v[110:111], v[142:143], v[124:125]
	v_pk_add_f32 v[112:113], v[140:141], v[110:111]
	v_mul_f32_e32 v136, v38, v22
	v_mul_f32_e32 v137, v39, v22
	v_mul_f32_e32 v138, v46, v22
	v_fma_f32 v29, v47, v22, v26
	v_mul_f32_e32 v31, v94, v22
	v_mul_f32_e32 v126, v95, v22
	v_fma_f32 v127, v98, v22, v26
	v_mul_f32_e32 v146, v99, v22
	v_fma_f32 v147, v112, v22, v26
	v_fma_f32 v29, -v136, v136, v29
	v_fma_f32 v31, -v136, v137, v31
	v_fma_f32 v126, -v136, v138, v126
	v_fma_f32 v127, -v137, v137, v127
	v_fma_f32 v146, -v137, v138, v146
	v_fma_f32 v147, -v138, v138, v147
	v_mul_f32_e32 v152, v146, v146
	v_mul_f32_e32 v153, v31, v147
	v_mul_f32_e32 v154, v126, v127
	v_mul_f32_e32 v155, v126, v126
	v_mul_f32_e32 v156, v29, v146
	v_mul_f32_e32 v157, v31, v31
	v_fma_f32 v152, v127, v147, -v152
	v_fma_f32 v153, v126, v146, -v153
	v_fma_f32 v154, v31, v146, -v154
	v_fma_f32 v155, v29, v147, -v155
	v_fma_f32 v156, v31, v126, -v156
	v_fma_f32 v157, v29, v127, -v157
	v_mul_f32_e32 v158, v29, v152
	v_fmac_f32_e32 v158, v31, v153
	v_fmac_f32_e32 v158, v126, v154
	v_rcp_f32_e32 v158, v158
	v_cmp_ne_u32_e64 vcc, s37, v24
	v_mul_f32_e32 v158, v158, v22
	v_cndmask_b32_e64 v158, 0, v158, s[30:31]
	v_cndmask_b32_e64 v29, 0, v18, vcc
	v_cndmask_b32_e64 v149, 0, v22, s[30:31]
	v_mul_f32_e32 v139, v152, v158
	v_mul_f32_e32 v140, v153, v158
	v_mul_f32_e32 v141, v154, v158
	v_mul_f32_e32 v142, v155, v158
	v_mul_f32_e32 v143, v156, v158
	v_mul_f32_e32 v148, v157, v158
	v_add_f32_e32 v150, v113, v29
	v_mov_b32_e32 v151, v24
	ds_write_b128 v23, v[136:139]
	ds_write_b128 v23, v[140:143] offset:1024
	ds_write_b128 v23, v[148:151] offset:2048
	s_waitcnt lgkmcnt(0)
	s_barrier
	v_mov_b32_dpp v112, v6 wave_shr:1 row_mask:0xf bank_mask:0xf bound_ctrl:1
	v_mov_b32_dpp v113, v7 wave_shr:1 row_mask:0xf bank_mask:0xf bound_ctrl:1
	v_mov_b32_dpp v152, v6 wave_shl:1 row_mask:0xf bank_mask:0xf bound_ctrl:1
	v_mov_b32_dpp v153, v7 wave_shl:1 row_mask:0xf bank_mask:0xf bound_ctrl:1
	v_pk_mul_f32 v[38:39], v[6:7], v[12:13] op_sel_hi:[1,0]
	v_pk_mul_f32 v[46:47], v[6:7], v[12:13] op_sel:[0,1]
	v_pk_mul_f32 v[94:95], v[6:7], v[14:15] op_sel_hi:[1,0]
	v_pk_add_f32 v[98:99], v[6:7], v[112:113]
	v_pk_fma_f32 v[38:39], v[112:113], v[60:61], v[38:39] op_sel_hi:[1,0,1]
	v_pk_fma_f32 v[46:47], v[112:113], v[60:61], v[46:47] op_sel:[0,1,0]
	v_pk_fma_f32 v[94:95], v[112:113], v[62:63], v[94:95] op_sel_hi:[1,0,1]
	v_pk_add_f32 v[98:99], v[98:99], v[152:153]
	v_pk_fma_f32 v[38:39], v[152:153], v[76:77], v[38:39] op_sel_hi:[1,0,1]
	v_pk_fma_f32 v[46:47], v[152:153], v[76:77], v[46:47] op_sel:[0,1,0]
	v_pk_fma_f32 v[94:95], v[152:153], v[78:79], v[94:95] op_sel_hi:[1,0,1]
	v_pk_add_f32 v[126:127], v[116:117], v[98:99]
	v_pk_add_f32 v[112:113], v[132:133], v[126:127]
	v_pk_add_f32 v[146:147], v[44:45], v[38:39]
	v_pk_add_f32 v[154:155], v[84:85], v[146:147]
	v_pk_add_f32 v[158:159], v[68:69], v[46:47]
	v_pk_add_f32 v[162:163], v[120:121], v[158:159]
	v_pk_add_f32 v[166:167], v[88:89], v[94:95]
	v_pk_add_f32 v[170:171], v[128:129], v[166:167]
	v_pk_fma_f32 v[154:155], v[136:137], v[112:113], v[154:155] op_sel_hi:[0,1,1] neg_lo:[1,0,0] neg_hi:[1,0,0]
	v_pk_fma_f32 v[162:163], v[136:137], v[112:113], v[162:163] op_sel:[1,0,0] neg_lo:[1,0,0] neg_hi:[1,0,0]
	v_pk_fma_f32 v[170:171], v[138:139], v[112:113], v[170:171] op_sel_hi:[0,1,1] neg_lo:[1,0,0] neg_hi:[1,0,0]
	v_pk_mul_f32 v[44:45], v[138:139], v[154:155] op_sel:[1,0]
	v_pk_mul_f32 v[68:69], v[140:141], v[154:155] op_sel_hi:[0,1]
	v_pk_mul_f32 v[84:85], v[140:141], v[154:155] op_sel:[1,0]
	v_pk_fma_f32 v[44:45], v[140:141], v[162:163], v[44:45] op_sel_hi:[0,1,1]
	v_pk_fma_f32 v[68:69], v[142:143], v[162:163], v[68:69] op_sel_hi:[0,1,1]
	v_pk_fma_f32 v[84:85], v[142:143], v[162:163], v[84:85] op_sel:[1,0,0]
	v_pk_fma_f32 v[44:45], v[140:141], v[170:171], v[44:45] op_sel:[1,0,0]
	v_pk_fma_f32 v[68:69], v[142:143], v[170:171], v[68:69] op_sel:[1,0,0]
	v_pk_fma_f32 v[84:85], v[148:149], v[170:171], v[84:85] op_sel_hi:[0,1,1]
	v_pk_mul_f32 v[174:175], v[136:137], v[44:45] op_sel_hi:[0,1]
	v_pk_fma_f32 v[174:175], v[136:137], v[68:69], v[174:175] op_sel:[1,0,0]
	v_pk_fma_f32 v[174:175], v[138:139], v[84:85], v[174:175] op_sel_hi:[0,1,1]
	v_pk_fma_f32 v[174:175], v[148:149], v[112:113], v[174:175] op_sel:[1,0,0] neg_lo:[0,0,1] neg_hi:[0,0,1]
	v_cmp_eq_u32_e64 s[10:11], 6, v151
	v_cmp_eq_u32_e64 s[14:15], 7, v151
	v_pk_add_f32 v[88:89], v[50:51], v[44:45]
	v_pk_add_f32 v[112:113], v[114:115], v[88:89]
	v_pk_add_f32 v[116:117], v[54:55], v[68:69]
	v_pk_add_f32 v[50:51], v[130:131], v[116:117]
	v_pk_add_f32 v[120:121], v[58:59], v[84:85]
	v_pk_add_f32 v[54:55], v[134:135], v[120:121]
	v_pk_add_f32 v[58:59], v[164:165], v[174:175]
	v_pk_add_f32 v[128:129], v[92:93], v[58:59]
	v_pk_fma_f32 v[92:93], v[72:73], v[112:113], v[128:129] op_sel_hi:[0,1,1]
	v_pk_fma_f32 v[132:133], v[80:81], v[112:113], v[128:129] op_sel_hi:[0,1,1]
	v_pk_fma_f32 v[92:93], v[72:73], v[50:51], v[92:93] op_sel:[1,0,0]
	v_pk_fma_f32 v[132:133], v[80:81], v[50:51], v[132:133] op_sel:[1,0,0]
	v_pk_fma_f32 v[92:93], v[74:75], v[54:55], v[92:93] op_sel_hi:[0,1,1]
	v_pk_fma_f32 v[132:133], v[82:83], v[54:55], v[132:133] op_sel_hi:[0,1,1]
	v_pk_fma_f32 v[128:129], v[100:101], v[112:113], v[128:129] op_sel_hi:[0,1,1]
	v_pk_fma_f32 v[128:129], v[100:101], v[50:51], v[128:129] op_sel:[1,0,0]
	v_pk_fma_f32 v[128:129], v[102:103], v[54:55], v[128:129] op_sel_hi:[0,1,1]
	v_cndmask_b32_e64 v114, 0, v18, s[10:11]
	v_cndmask_b32_e64 v115, 0, v18, s[14:15]
	v_add_f32_dpp v128, v92, v128 wave_shl:1 row_mask:0xf bank_mask:0xf bound_ctrl:1
	v_add_f32_dpp v129, v93, v129 wave_shl:1 row_mask:0xf bank_mask:0xf bound_ctrl:1
	s_add_i32 s4, s34, 2
	s_cmpk_lt_i32 s4, 0x201
	s_cselect_b64 s[12:13], s[0:1], 0
	v_add_f32_dpp v128, v132, v128 wave_shr:1 row_mask:0xf bank_mask:0xf bound_ctrl:1
	v_add_f32_dpp v129, v133, v129 wave_shr:1 row_mask:0xf bank_mask:0xf bound_ctrl:1
	v_pk_fma_f32 v[128:129], v[96:97], v[150:151], v[128:129] op_sel_hi:[1,0,1] neg_lo:[0,0,1] neg_hi:[0,0,1]
	v_pk_add_f32 v[128:129], v[128:129], v[114:115] neg_lo:[0,1] neg_hi:[0,1]
	v_pk_mul_f32 v[130:131], v[128:129], v[128:129]
	v_add_f32_e32 v130, v130, v131
	v_cndmask_b32_e64 v131, 0, v130, s[12:13]
	v_add_f32_e32 v1, v1, v131
	s_add_i32 s5, s34, 7
	s_min_i32 s5, s5, 0x200
	s_mul_i32 s6, s5, 0x804
	s_add_i32 s6, s6, s35
	s_add_i32 s7, s6, 0x505014
	s_add_i32 s8, s6, 0x606018
	s_mul_i32 s9, s5, 0x180c
	s_add_i32 s9, s9, s33
	s_add_i32 s4, s34, 8
	s_min_i32 s4, s4, 0x200
	s_mul_i32 s4, s4, 0x804
	s_add_i32 s4, s4, s38
	buffer_load_dword v24, v28, s[20:23], s4 offen nt
	buffer_load_dwordx3 v[72:74], v27, s[24:27], s9 offen nt
	buffer_load_dword v50, v28, s[16:19], s7 offen nt
	buffer_load_dword v51, v28, s[16:19], s8 offen nt
	s_waitcnt vmcnt(8)
	v_mov_b32_dpp v80, v32 wave_shr:1 row_mask:0xf bank_mask:0xf bound_ctrl:1
	v_mov_b32_dpp v81, v33 wave_shr:1 row_mask:0xf bank_mask:0xf bound_ctrl:1
	v_mov_b32_dpp v82, v34 wave_shr:1 row_mask:0xf bank_mask:0xf bound_ctrl:1
	v_mov_b32_dpp v100, v32 wave_shl:1 row_mask:0xf bank_mask:0xf bound_ctrl:1
	v_mov_b32_dpp v101, v33 wave_shl:1 row_mask:0xf bank_mask:0xf bound_ctrl:1
	v_mov_b32_dpp v102, v34 wave_shl:1 row_mask:0xf bank_mask:0xf bound_ctrl:1
	s_add_i32 s4, s34, 6
	s_cmpk_lt_u32 s4, 0x201
	s_cselect_b64 s[12:13], s[40:41], 0
	v_cmp_eq_u32_e64 s[14:15], s37, v16
	s_and_b64 s[14:15], s[14:15], s[12:13]
	v_cndmask_b32_e64 v29, 0, 1, s[14:15]
	v_mul_f32_e32 v54, v32, v32
	v_mul_f32_e32 v55, v32, v33
	v_mul_f32_e32 v92, v32, v34
	v_mul_f32_e32 v93, v33, v33
	v_mul_f32_e32 v96, v33, v34
	v_mul_f32_e32 v97, v34, v34
	v_or_b32_dpp v31, v29, v29 wave_shr:1 row_mask:0xf bank_mask:0xf bound_ctrl:1
	s_nop 1
	v_or_b32_dpp v31, v29, v31 wave_shl:1 row_mask:0xf bank_mask:0xf bound_ctrl:1
	s_nop 1
	v_or_b32_dpp v70, v31, v31 wave_shr:1 row_mask:0xf bank_mask:0xf bound_ctrl:1
	s_nop 1
	v_or_b32_dpp v70, v31, v70 wave_shl:1 row_mask:0xf bank_mask:0xf bound_ctrl:1
	v_or3_b32 v29, v70, v71, v52
	v_or3_b32 v29, v29, v30, v53
	s_add_i32 s4, s34, 3
	s_cmpk_lt_u32 s4, 0x1ff
	s_cselect_b64 s[12:13], s[42:43], 0
	v_cmp_ne_u32_e64 s[30:31], 0, v29
	s_and_b64 s[30:31], s[30:31], s[12:13]
	v_cndmask_b32_e64 v29, 0, 1.0, s[30:31]
	v_add_f32_e32 v112, v32, v80
	v_add_f32_e32 v113, v33, v81
	v_add_f32_e32 v114, v34, v82
	v_fmac_f32_e32 v54, v80, v80
	v_fmac_f32_e32 v55, v80, v81
	v_fmac_f32_e32 v92, v80, v82
	v_fmac_f32_e32 v93, v81, v81
	v_fmac_f32_e32 v96, v81, v82
	v_fmac_f32_e32 v97, v82, v82
	v_add_f32_dpp v133, v29, v29 wave_shr:1 row_mask:0xf bank_mask:0xf bound_ctrl:1
	v_add_f32_e32 v112, v112, v100
	v_add_f32_e32 v113, v113, v101
	v_add_f32_e32 v114, v114, v102
	v_fma_f32 v115, v100, v100, v54
	v_fma_f32 v128, v100, v101, v55
	v_fma_f32 v129, v100, v102, v92
	v_fma_f32 v130, v101, v101, v93
	v_fma_f32 v131, v101, v102, v96
	v_fma_f32 v132, v102, v102, v97
	v_add_f32_dpp v133, v29, v133 wave_shl:1 row_mask:0xf bank_mask:0xf bound_ctrl:1
	v_pk_add_f32 v[54:55], v[48:49], v[112:113]
	v_pk_add_f32 v[48:49], v[144:145], v[114:115]
	v_pk_add_f32 v[92:93], v[86:87], v[128:129]
	v_pk_add_f32 v[86:87], v[108:109], v[130:131]
	v_pk_add_f32 v[96:97], v[110:111], v[132:133]
	v_mul_f32_e32 v108, v54, v22
	v_mul_f32_e32 v109, v55, v22
	v_mul_f32_e32 v110, v48, v22
	v_fma_f32 v29, v49, v22, v26
	v_mul_f32_e32 v31, v92, v22
	v_mul_f32_e32 v134, v93, v22
	v_fma_f32 v135, v86, v22, v26
	v_mul_f32_e32 v144, v87, v22
	v_fma_f32 v145, v96, v22, v26
	v_fma_f32 v29, -v108, v108, v29
	v_fma_f32 v31, -v108, v109, v31
	v_fma_f32 v134, -v108, v110, v134
	v_fma_f32 v135, -v109, v109, v135
	v_fma_f32 v144, -v109, v110, v144
	v_fma_f32 v145, -v110, v110, v145
	v_mul_f32_e32 v148, v144, v144
	v_mul_f32_e32 v149, v31, v145
	v_mul_f32_e32 v150, v134, v135
	v_mul_f32_e32 v151, v134, v134
	v_mul_f32_e32 v152, v29, v144
	v_mul_f32_e32 v153, v31, v31
	v_fma_f32 v148, v135, v145, -v148
	v_fma_f32 v149, v134, v144, -v149
	v_fma_f32 v150, v31, v144, -v150
	v_fma_f32 v151, v29, v145, -v151
	v_fma_f32 v152, v31, v134, -v152
	v_fma_f32 v153, v29, v135, -v153
	v_mul_f32_e32 v154, v29, v148
	v_fmac_f32_e32 v154, v31, v149
	v_fmac_f32_e32 v154, v134, v150
	v_rcp_f32_e32 v154, v154
	v_cmp_ne_u32_e64 vcc, s37, v17
	v_mul_f32_e32 v154, v154, v22
	v_cndmask_b32_e64 v154, 0, v154, s[30:31]
	v_cndmask_b32_e64 v29, 0, v18, vcc
	v_cndmask_b32_e64 v141, 0, v22, s[30:31]
	v_mul_f32_e32 v111, v148, v154
	v_mul_f32_e32 v136, v149, v154
	v_mul_f32_e32 v137, v150, v154
	v_mul_f32_e32 v138, v151, v154
	v_mul_f32_e32 v139, v152, v154
	v_mul_f32_e32 v140, v153, v154
	v_add_f32_e32 v142, v97, v29
	v_mov_b32_e32 v143, v17
	ds_write_b128 v23, v[108:111] offset:3072
	ds_write_b128 v23, v[136:139] offset:4096
	ds_write_b128 v23, v[140:143] offset:5120
	s_waitcnt lgkmcnt(0)
	s_barrier
	v_mov_b32_dpp v54, v20 wave_shr:1 row_mask:0xf bank_mask:0xf bound_ctrl:1
	v_mov_b32_dpp v55, v21 wave_shr:1 row_mask:0xf bank_mask:0xf bound_ctrl:1
	v_mov_b32_dpp v86, v20 wave_shl:1 row_mask:0xf bank_mask:0xf bound_ctrl:1
	v_mov_b32_dpp v87, v21 wave_shl:1 row_mask:0xf bank_mask:0xf bound_ctrl:1
	v_pk_mul_f32 v[48:49], v[20:21], v[32:33] op_sel_hi:[1,0]
	v_pk_mul_f32 v[92:93], v[20:21], v[32:33] op_sel:[0,1]
	v_pk_mul_f32 v[96:97], v[20:21], v[34:35] op_sel_hi:[1,0]
	v_pk_add_f32 v[144:145], v[20:21], v[54:55]
	v_pk_fma_f32 v[48:49], v[54:55], v[80:81], v[48:49] op_sel_hi:[1,0,1]
	v_pk_fma_f32 v[92:93], v[54:55], v[80:81], v[92:93] op_sel:[0,1,0]
	v_pk_fma_f32 v[96:97], v[54:55], v[82:83], v[96:97] op_sel_hi:[1,0,1]
	v_pk_add_f32 v[144:145], v[144:145], v[86:87]
	v_pk_fma_f32 v[48:49], v[86:87], v[100:101], v[48:49] op_sel_hi:[1,0,1]
	v_pk_fma_f32 v[92:93], v[86:87], v[100:101], v[92:93] op_sel:[0,1,0]
	v_pk_fma_f32 v[96:97], v[86:87], v[102:103], v[96:97] op_sel_hi:[1,0,1]
	v_pk_add_f32 v[54:55], v[126:127], v[144:145]
	v_pk_add_f32 v[148:149], v[146:147], v[48:49]
	v_pk_add_f32 v[152:153], v[158:159], v[92:93]
	v_pk_add_f32 v[156:157], v[166:167], v[96:97]
	v_pk_fma_f32 v[148:149], v[108:109], v[54:55], v[148:149] op_sel_hi:[0,1,1] neg_lo:[1,0,0] neg_hi:[1,0,0]
	v_pk_fma_f32 v[152:153], v[108:109], v[54:55], v[152:153] op_sel:[1,0,0] neg_lo:[1,0,0] neg_hi:[1,0,0]
	v_pk_fma_f32 v[156:157], v[110:111], v[54:55], v[156:157] op_sel_hi:[0,1,1] neg_lo:[1,0,0] neg_hi:[1,0,0]
	v_pk_mul_f32 v[86:87], v[110:111], v[148:149] op_sel:[1,0]
	v_pk_mul_f32 v[126:127], v[136:137], v[148:149] op_sel_hi:[0,1]
	v_pk_mul_f32 v[134:135], v[136:137], v[148:149] op_sel:[1,0]
	v_pk_fma_f32 v[86:87], v[136:137], v[152:153], v[86:87] op_sel_hi:[0,1,1]
	v_pk_fma_f32 v[126:127], v[138:139], v[152:153], v[126:127] op_sel_hi:[0,1,1]
	v_pk_fma_f32 v[134:135], v[138:139], v[152:153], v[134:135] op_sel:[1,0,0]
	v_pk_fma_f32 v[86:87], v[136:137], v[156:157], v[86:87] op_sel:[1,0,0]
	v_pk_fma_f32 v[126:127], v[138:139], v[156:157], v[126:127] op_sel:[1,0,0]
	v_pk_fma_f32 v[134:135], v[140:141], v[156:157], v[134:135] op_sel_hi:[0,1,1]
	v_pk_mul_f32 v[160:161], v[108:109], v[86:87] op_sel_hi:[0,1]
	v_pk_fma_f32 v[160:161], v[108:109], v[126:127], v[160:161] op_sel:[1,0,0]
	v_pk_fma_f32 v[160:161], v[110:111], v[134:135], v[160:161] op_sel_hi:[0,1,1]
	v_pk_fma_f32 v[160:161], v[140:141], v[54:55], v[160:161] op_sel:[1,0,0] neg_lo:[0,0,1] neg_hi:[0,0,1]
	v_cmp_eq_u32_e64 s[10:11], 6, v143
	v_cmp_eq_u32_e64 s[14:15], 7, v143
	v_pk_add_f32 v[54:55], v[88:89], v[86:87]
	v_pk_add_f32 v[88:89], v[116:117], v[126:127]
	v_pk_add_f32 v[116:117], v[120:121], v[134:135]
	v_pk_add_f32 v[146:147], v[58:59], v[160:161]
	v_pk_fma_f32 v[58:59], v[64:65], v[54:55], v[146:147] op_sel_hi:[0,1,1]
	v_pk_fma_f32 v[150:151], v[104:105], v[54:55], v[146:147] op_sel_hi:[0,1,1]
	v_pk_fma_f32 v[58:59], v[64:65], v[88:89], v[58:59] op_sel:[1,0,0]
	v_pk_fma_f32 v[150:151], v[104:105], v[88:89], v[150:151] op_sel:[1,0,0]
	v_pk_fma_f32 v[58:59], v[66:67], v[116:117], v[58:59] op_sel_hi:[0,1,1]
	v_pk_fma_f32 v[150:151], v[106:107], v[116:117], v[150:151] op_sel_hi:[0,1,1]
	v_pk_fma_f32 v[146:147], v[8:9], v[54:55], v[146:147] op_sel_hi:[0,1,1]
	v_pk_fma_f32 v[146:147], v[8:9], v[88:89], v[146:147] op_sel:[1,0,0]
	v_pk_fma_f32 v[146:147], v[10:11], v[116:117], v[146:147] op_sel_hi:[0,1,1]
	v_cndmask_b32_e64 v120, 0, v18, s[10:11]
	v_cndmask_b32_e64 v121, 0, v18, s[14:15]
	v_add_f32_dpp v146, v58, v146 wave_shl:1 row_mask:0xf bank_mask:0xf bound_ctrl:1
	v_add_f32_dpp v147, v59, v147 wave_shl:1 row_mask:0xf bank_mask:0xf bound_ctrl:1
	s_add_i32 s4, s34, 3
	s_cmpk_lt_i32 s4, 0x201
	s_cselect_b64 s[12:13], s[0:1], 0
	v_add_f32_dpp v146, v150, v146 wave_shr:1 row_mask:0xf bank_mask:0xf bound_ctrl:1
	v_add_f32_dpp v147, v151, v147 wave_shr:1 row_mask:0xf bank_mask:0xf bound_ctrl:1
	v_pk_fma_f32 v[146:147], v[4:5], v[142:143], v[146:147] op_sel_hi:[1,0,1] neg_lo:[0,0,1] neg_hi:[0,0,1]
	v_pk_add_f32 v[146:147], v[146:147], v[120:121] neg_lo:[0,1] neg_hi:[0,1]
	v_pk_mul_f32 v[148:149], v[146:147], v[146:147]
	v_add_f32_e32 v148, v148, v149
	v_cndmask_b32_e64 v149, 0, v148, s[12:13]
	v_add_f32_e32 v1, v1, v149
	s_add_i32 s5, s34, 8
	s_min_i32 s5, s5, 0x200
	s_mul_i32 s6, s5, 0x804
	s_add_i32 s6, s6, s35
	s_add_i32 s7, s6, 0x505014
	s_add_i32 s8, s6, 0x606018
	s_mul_i32 s9, s5, 0x180c
	s_add_i32 s9, s9, s33
	s_add_i32 s4, s34, 9
	s_min_i32 s4, s4, 0x200
	s_mul_i32 s4, s4, 0x804
	s_add_i32 s4, s4, s38
	buffer_load_dword v17, v28, s[20:23], s4 offen nt
	buffer_load_dwordx3 v[8:10], v27, s[24:27], s9 offen nt
	buffer_load_dword v4, v28, s[16:19], s7 offen nt
	buffer_load_dword v5, v28, s[16:19], s8 offen nt
	s_waitcnt vmcnt(8)
	v_mov_b32_dpp v64, v40 wave_shr:1 row_mask:0xf bank_mask:0xf bound_ctrl:1
	v_mov_b32_dpp v65, v41 wave_shr:1 row_mask:0xf bank_mask:0xf bound_ctrl:1
	v_mov_b32_dpp v66, v42 wave_shr:1 row_mask:0xf bank_mask:0xf bound_ctrl:1
	v_mov_b32_dpp v104, v40 wave_shl:1 row_mask:0xf bank_mask:0xf bound_ctrl:1
	v_mov_b32_dpp v105, v41 wave_shl:1 row_mask:0xf bank_mask:0xf bound_ctrl:1
	v_mov_b32_dpp v106, v42 wave_shl:1 row_mask:0xf bank_mask:0xf bound_ctrl:1
	s_add_i32 s4, s34, 7
	s_cmpk_lt_u32 s4, 0x201
	s_cselect_b64 s[12:13], s[40:41], 0
	v_cmp_eq_u32_e64 s[14:15], s37, v25
	s_and_b64 s[14:15], s[14:15], s[12:13]
	v_cndmask_b32_e64 v29, 0, 1, s[14:15]
	v_mul_f32_e32 v54, v40, v40
	v_mul_f32_e32 v55, v40, v41
	v_mul_f32_e32 v58, v40, v42
	v_mul_f32_e32 v59, v41, v41
	v_mul_f32_e32 v88, v41, v42
	v_mul_f32_e32 v89, v42, v42
	v_or_b32_dpp v31, v29, v29 wave_shr:1 row_mask:0xf bank_mask:0xf bound_ctrl:1
	s_nop 1
	v_or_b32_dpp v31, v29, v31 wave_shl:1 row_mask:0xf bank_mask:0xf bound_ctrl:1
	s_nop 1
	v_or_b32_dpp v53, v31, v31 wave_shr:1 row_mask:0xf bank_mask:0xf bound_ctrl:1
	s_nop 1
	v_or_b32_dpp v53, v31, v53 wave_shl:1 row_mask:0xf bank_mask:0xf bound_ctrl:1
	v_or3_b32 v29, v53, v70, v71
	v_or3_b32 v29, v29, v52, v30
	s_add_i32 s4, s34, 4
	s_cmpk_lt_u32 s4, 0x1ff
	s_cselect_b64 s[12:13], s[42:43], 0
	v_cmp_ne_u32_e64 s[30:31], 0, v29
	s_and_b64 s[30:31], s[30:31], s[12:13]
	v_cndmask_b32_e64 v29, 0, 1.0, s[30:31]
	v_add_f32_e32 v108, v40, v64
	v_add_f32_e32 v109, v41, v65
	v_add_f32_e32 v110, v42, v66
	v_fmac_f32_e32 v54, v64, v64
	v_fmac_f32_e32 v55, v64, v65
	v_fmac_f32_e32 v58, v64, v66
	v_fmac_f32_e32 v59, v65, v65
	v_fmac_f32_e32 v88, v65, v66
	v_fmac_f32_e32 v89, v66, v66
	v_add_f32_dpp v137, v29, v29 wave_shr:1 row_mask:0xf bank_mask:0xf bound_ctrl:1
	v_add_f32_e32 v108, v108, v104
	v_add_f32_e32 v109, v109, v105
	v_add_f32_e32 v110, v110, v106
	v_fma_f32 v111, v104, v104, v54
	v_fma_f32 v116, v104, v105, v55
	v_fma_f32 v117, v104, v106, v58
	v_fma_f32 v120, v105, v105, v59
	v_fma_f32 v121, v105, v106, v88
	v_fma_f32 v136, v106, v106, v89
	v_add_f32_dpp v137, v29, v137 wave_shl:1 row_mask:0xf bank_mask:0xf bound_ctrl:1
	v_pk_add_f32 v[54:55], v[112:113], v[108:109]
	v_pk_add_f32 v[58:59], v[56:57], v[54:55]
	v_pk_add_f32 v[56:57], v[114:115], v[110:111]
	v_pk_add_f32 v[88:89], v[90:91], v[56:57]
	v_pk_add_f32 v[112:113], v[128:129], v[116:117]
	v_pk_add_f32 v[90:91], v[118:119], v[112:113]
	v_pk_add_f32 v[128:129], v[130:131], v[120:121]
	v_pk_add_f32 v[114:115], v[122:123], v[128:129]
	v_pk_add_f32 v[118:119], v[132:133], v[136:137]
	v_pk_add_f32 v[122:123], v[124:125], v[118:119]
	v_mul_f32_e32 v140, v58, v22
	v_mul_f32_e32 v141, v59, v22
	v_mul_f32_e32 v142, v88, v22
	v_fma_f32 v29, v89, v22, v26
	v_mul_f32_e32 v31, v90, v22
	v_mul_f32_e32 v124, v91, v22
	v_fma_f32 v125, v114, v22, v26
	v_mul_f32_e32 v130, v115, v22
	v_fma_f32 v131, v122, v22, v26
	v_fma_f32 v29, -v140, v140, v29
	v_fma_f32 v31, -v140, v141, v31
	v_fma_f32 v124, -v140, v142, v124
	v_fma_f32 v125, -v141, v141, v125
	v_fma_f32 v130, -v141, v142, v130
	v_fma_f32 v131, -v142, v142, v131
	v_mul_f32_e32 v132, v130, v130
	v_mul_f32_e32 v133, v31, v131
	v_mul_f32_e32 v138, v124, v125
	v_mul_f32_e32 v139, v124, v124
	v_mul_f32_e32 v146, v29, v130
	v_mul_f32_e32 v147, v31, v31
	v_fma_f32 v132, v125, v131, -v132
	v_fma_f32 v133, v124, v130, -v133
	v_fma_f32 v138, v31, v130, -v138
	v_fma_f32 v139, v29, v131, -v139
	v_fma_f32 v146, v31, v124, -v146
	v_fma_f32 v147, v29, v125, -v147
	v_mul_f32_e32 v156, v29, v132
	v_fmac_f32_e32 v156, v31, v133
	v_fmac_f32_e32 v156, v124, v138
	v_rcp_f32_e32 v156, v156
	v_cmp_ne_u32_e64 vcc, s37, v2
	v_mul_f32_e32 v156, v156, v22
	v_cndmask_b32_e64 v156, 0, v156, s[30:31]
	v_cndmask_b32_e64 v29, 0, v18, vcc
	v_cndmask_b32_e64 v153, 0, v22, s[30:31]
	v_mul_f32_e32 v143, v132, v156
	v_mul_f32_e32 v148, v133, v156
	v_mul_f32_e32 v149, v138, v156
	v_mul_f32_e32 v150, v139, v156
	v_mul_f32_e32 v151, v146, v156
	v_mul_f32_e32 v152, v147, v156
	v_add_f32_e32 v154, v123, v29
	v_mov_b32_e32 v155, v2
	ds_write_b128 v23, v[140:143]
	ds_write_b128 v23, v[148:151] offset:1024
	ds_write_b128 v23, v[152:155] offset:2048
	s_waitcnt lgkmcnt(0)
	s_barrier
	v_mov_b32_dpp v30, v36 wave_shr:1 row_mask:0xf bank_mask:0xf bound_ctrl:1
	v_mov_b32_dpp v31, v37 wave_shr:1 row_mask:0xf bank_mask:0xf bound_ctrl:1
	v_mov_b32_dpp v58, v36 wave_shl:1 row_mask:0xf bank_mask:0xf bound_ctrl:1
	v_mov_b32_dpp v59, v37 wave_shl:1 row_mask:0xf bank_mask:0xf bound_ctrl:1
	v_pk_mul_f32 v[88:89], v[36:37], v[40:41] op_sel_hi:[1,0]
	v_pk_mul_f32 v[124:125], v[36:37], v[40:41] op_sel:[0,1]
	v_pk_mul_f32 v[132:133], v[36:37], v[42:43] op_sel_hi:[1,0]
	v_pk_add_f32 v[156:157], v[36:37], v[30:31]
	v_pk_fma_f32 v[88:89], v[30:31], v[64:65], v[88:89] op_sel_hi:[1,0,1]
	v_pk_fma_f32 v[124:125], v[30:31], v[64:65], v[124:125] op_sel:[0,1,0]
	v_pk_fma_f32 v[132:133], v[30:31], v[66:67], v[132:133] op_sel_hi:[1,0,1]
	v_pk_add_f32 v[156:157], v[156:157], v[58:59]
	v_pk_fma_f32 v[88:89], v[58:59], v[104:105], v[88:89] op_sel_hi:[1,0,1]
	v_pk_fma_f32 v[124:125], v[58:59], v[104:105], v[124:125] op_sel:[0,1,0]
	v_pk_fma_f32 v[132:133], v[58:59], v[106:107], v[132:133] op_sel_hi:[1,0,1]
	v_pk_add_f32 v[164:165], v[144:145], v[156:157]
	v_pk_add_f32 v[30:31], v[98:99], v[164:165]
	v_pk_add_f32 v[144:145], v[48:49], v[88:89]
	v_pk_add_f32 v[168:169], v[38:39], v[144:145]
	v_pk_add_f32 v[48:49], v[92:93], v[124:125]
	v_pk_add_f32 v[172:173], v[46:47], v[48:49]
	v_pk_add_f32 v[92:93], v[96:97], v[132:133]
	v_pk_add_f32 v[176:177], v[94:95], v[92:93]
	v_pk_fma_f32 v[168:169], v[140:141], v[30:31], v[168:169] op_sel_hi:[0,1,1] neg_lo:[1,0,0] neg_hi:[1,0,0]
	v_pk_fma_f32 v[172:173], v[140:141], v[30:31], v[172:173] op_sel:[1,0,0] neg_lo:[1,0,0] neg_hi:[1,0,0]
	v_pk_fma_f32 v[176:177], v[142:143], v[30:31], v[176:177] op_sel_hi:[0,1,1] neg_lo:[1,0,0] neg_hi:[1,0,0]
	v_pk_mul_f32 v[38:39], v[142:143], v[168:169] op_sel:[1,0]
	v_pk_mul_f32 v[46:47], v[148:149], v[168:169] op_sel_hi:[0,1]
	v_pk_mul_f32 v[58:59], v[148:149], v[168:169] op_sel:[1,0]
	v_pk_fma_f32 v[38:39], v[148:149], v[172:173], v[38:39] op_sel_hi:[0,1,1]
	v_pk_fma_f32 v[46:47], v[150:151], v[172:173], v[46:47] op_sel_hi:[0,1,1]
	v_pk_fma_f32 v[58:59], v[150:151], v[172:173], v[58:59] op_sel:[1,0,0]
	v_pk_fma_f32 v[38:39], v[148:149], v[176:177], v[38:39] op_sel:[1,0,0]
	v_pk_fma_f32 v[46:47], v[150:151], v[176:177], v[46:47] op_sel:[1,0,0]
	v_pk_fma_f32 v[58:59], v[152:153], v[176:177], v[58:59] op_sel_hi:[0,1,1]
	v_pk_mul_f32 v[96:97], v[140:141], v[38:39] op_sel_hi:[0,1]
	v_pk_fma_f32 v[96:97], v[140:141], v[46:47], v[96:97] op_sel:[1,0,0]
	v_pk_fma_f32 v[96:97], v[142:143], v[58:59], v[96:97] op_sel_hi:[0,1,1]
	v_pk_fma_f32 v[96:97], v[152:153], v[30:31], v[96:97] op_sel:[1,0,0] neg_lo:[0,0,1] neg_hi:[0,0,1]
	v_cmp_eq_u32_e64 s[10:11], 6, v155
	v_cmp_eq_u32_e64 s[14:15], 7, v155
	v_pk_add_f32 v[30:31], v[86:87], v[38:39]
	v_pk_add_f32 v[90:91], v[44:45], v[30:31]
	v_pk_add_f32 v[86:87], v[126:127], v[46:47]
	v_pk_add_f32 v[44:45], v[68:69], v[86:87]
	v_pk_add_f32 v[94:95], v[134:135], v[58:59]
	v_pk_add_f32 v[68:69], v[84:85], v[94:95]
	v_pk_add_f32 v[84:85], v[160:161], v[96:97]
	v_pk_add_f32 v[98:99], v[174:175], v[84:85]
	v_pk_fma_f32 v[114:115], v[60:61], v[90:91], v[98:99] op_sel_hi:[0,1,1]
	v_pk_fma_f32 v[122:123], v[76:77], v[90:91], v[98:99] op_sel_hi:[0,1,1]
	v_pk_fma_f32 v[114:115], v[60:61], v[44:45], v[114:115] op_sel:[1,0,0]
	v_pk_fma_f32 v[122:123], v[76:77], v[44:45], v[122:123] op_sel:[1,0,0]
	v_pk_fma_f32 v[114:115], v[62:63], v[68:69], v[114:115] op_sel_hi:[0,1,1]
	v_pk_fma_f32 v[122:123], v[78:79], v[68:69], v[122:123] op_sel_hi:[0,1,1]
	v_pk_fma_f32 v[98:99], v[12:13], v[90:91], v[98:99] op_sel_hi:[0,1,1]
	v_pk_fma_f32 v[98:99], v[12:13], v[44:45], v[98:99] op_sel:[1,0,0]
	v_pk_fma_f32 v[98:99], v[14:15], v[68:69], v[98:99] op_sel_hi:[0,1,1]
	v_cndmask_b32_e64 v160, 0, v18, s[10:11]
	v_cndmask_b32_e64 v161, 0, v18, s[14:15]
	v_add_f32_dpp v98, v114, v98 wave_shl:1 row_mask:0xf bank_mask:0xf bound_ctrl:1
	v_add_f32_dpp v99, v115, v99 wave_shl:1 row_mask:0xf bank_mask:0xf bound_ctrl:1
	s_add_i32 s4, s34, 4
	s_cmpk_lt_i32 s4, 0x201
	s_cselect_b64 s[12:13], s[0:1], 0
	v_add_f32_dpp v98, v122, v98 wave_shr:1 row_mask:0xf bank_mask:0xf bound_ctrl:1
	v_add_f32_dpp v99, v123, v99 wave_shr:1 row_mask:0xf bank_mask:0xf bound_ctrl:1
	v_pk_fma_f32 v[98:99], v[6:7], v[154:155], v[98:99] op_sel_hi:[1,0,1] neg_lo:[0,0,1] neg_hi:[0,0,1]
	v_pk_add_f32 v[98:99], v[98:99], v[160:161] neg_lo:[0,1] neg_hi:[0,1]
	v_pk_mul_f32 v[126:127], v[98:99], v[98:99]
	v_add_f32_e32 v126, v126, v127
	v_cndmask_b32_e64 v127, 0, v126, s[12:13]
	v_add_f32_e32 v1, v1, v127
	s_add_i32 s5, s34, 9
	s_min_i32 s5, s5, 0x200
	s_mul_i32 s6, s5, 0x804
	s_add_i32 s6, s6, s35
	s_add_i32 s7, s6, 0x505014
	s_add_i32 s8, s6, 0x606018
	s_mul_i32 s9, s5, 0x180c
	s_add_i32 s9, s9, s33
	s_add_i32 s4, s34, 10
	s_min_i32 s4, s4, 0x200
	s_mul_i32 s4, s4, 0x804
	s_add_i32 s4, s4, s38
	buffer_load_dword v2, v28, s[20:23], s4 offen nt
	buffer_load_dwordx3 v[12:14], v27, s[24:27], s9 offen nt
	buffer_load_dword v6, v28, s[16:19], s7 offen nt
	buffer_load_dword v7, v28, s[16:19], s8 offen nt
	s_waitcnt vmcnt(8)
	v_mov_b32_dpp v60, v72 wave_shr:1 row_mask:0xf bank_mask:0xf bound_ctrl:1
	v_mov_b32_dpp v61, v73 wave_shr:1 row_mask:0xf bank_mask:0xf bound_ctrl:1
	v_mov_b32_dpp v62, v74 wave_shr:1 row_mask:0xf bank_mask:0xf bound_ctrl:1
	v_mov_b32_dpp v76, v72 wave_shl:1 row_mask:0xf bank_mask:0xf bound_ctrl:1
	v_mov_b32_dpp v77, v73 wave_shl:1 row_mask:0xf bank_mask:0xf bound_ctrl:1
	v_mov_b32_dpp v78, v74 wave_shl:1 row_mask:0xf bank_mask:0xf bound_ctrl:1
	s_add_i32 s4, s34, 8
	s_cmpk_lt_u32 s4, 0x201
	s_cselect_b64 s[12:13], s[40:41], 0
	v_cmp_eq_u32_e64 s[14:15], s37, v24
	s_and_b64 s[14:15], s[14:15], s[12:13]
	v_cndmask_b32_e64 v29, 0, 1, s[14:15]
	v_mul_f32_e32 v44, v72, v72
	v_mul_f32_e32 v45, v72, v73
	v_mul_f32_e32 v68, v72, v74
	v_mul_f32_e32 v69, v73, v73
	v_mul_f32_e32 v90, v73, v74
	v_mul_f32_e32 v91, v74, v74
	v_or_b32_dpp v98, v29, v29 wave_shr:1 row_mask:0xf bank_mask:0xf bound_ctrl:1
	s_nop 1
	v_or_b32_dpp v98, v29, v98 wave_shl:1 row_mask:0xf bank_mask:0xf bound_ctrl:1
	s_nop 1
	v_or_b32_dpp v99, v98, v98 wave_shr:1 row_mask:0xf bank_mask:0xf bound_ctrl:1
	s_nop 1
	v_or_b32_dpp v99, v98, v99 wave_shl:1 row_mask:0xf bank_mask:0xf bound_ctrl:1
	v_or3_b32 v29, v99, v53, v70
	v_or3_b32 v29, v29, v71, v52
	s_add_i32 s4, s34, 5
	s_cmpk_lt_u32 s4, 0x1ff
	s_cselect_b64 s[12:13], s[42:43], 0
	v_cmp_ne_u32_e64 s[30:31], 0, v29
	s_and_b64 s[30:31], s[30:31], s[12:13]
	v_cndmask_b32_e64 v29, 0, 1.0, s[30:31]
	v_add_f32_e32 v114, v72, v60
	v_add_f32_e32 v115, v73, v61
	v_add_f32_e32 v122, v74, v62
	v_fmac_f32_e32 v44, v60, v60
	v_fmac_f32_e32 v45, v60, v61
	v_fmac_f32_e32 v68, v60, v62
	v_fmac_f32_e32 v69, v61, v61
	v_fmac_f32_e32 v90, v61, v62
	v_fmac_f32_e32 v91, v62, v62
	v_add_f32_dpp v135, v29, v29 wave_shr:1 row_mask:0xf bank_mask:0xf bound_ctrl:1
	v_add_f32_e32 v114, v114, v76
	v_add_f32_e32 v115, v115, v77
	v_add_f32_e32 v122, v122, v78
	v_fma_f32 v123, v76, v76, v44
	v_fma_f32 v126, v76, v77, v45
	v_fma_f32 v127, v76, v78, v68
	v_fma_f32 v130, v77, v77, v69
	v_fma_f32 v131, v77, v78, v90
	v_fma_f32 v134, v78, v78, v91
	v_add_f32_dpp v135, v29, v135 wave_shl:1 row_mask:0xf bank_mask:0xf bound_ctrl:1
	v_pk_add_f32 v[44:45], v[54:55], v[114:115]
	v_pk_add_f32 v[54:55], v[56:57], v[122:123]
	v_pk_add_f32 v[56:57], v[112:113], v[126:127]
	v_pk_add_f32 v[68:69], v[128:129], v[130:131]
	v_pk_add_f32 v[90:91], v[118:119], v[134:135]
	v_mul_f32_e32 v140, v44, v22
	v_mul_f32_e32 v141, v45, v22
	v_mul_f32_e32 v142, v54, v22
	v_fma_f32 v29, v55, v22, v26
	v_mul_f32_e32 v98, v56, v22
	v_mul_f32_e32 v112, v57, v22
	v_fma_f32 v113, v68, v22, v26
	v_mul_f32_e32 v118, v69, v22
	v_fma_f32 v119, v90, v22, v26
	v_fma_f32 v29, -v140, v140, v29
	v_fma_f32 v98, -v140, v141, v98
	v_fma_f32 v112, -v140, v142, v112
	v_fma_f32 v113, -v141, v141, v113
	v_fma_f32 v118, -v141, v142, v118
	v_fma_f32 v119, -v142, v142, v119
	v_mul_f32_e32 v128, v118, v118
	v_mul_f32_e32 v129, v98, v119
	v_mul_f32_e32 v138, v112, v113
	v_mul_f32_e32 v139, v112, v112
	v_mul_f32_e32 v146, v29, v118
	v_mul_f32_e32 v147, v98, v98
	v_fma_f32 v128, v113, v119, -v128
	v_fma_f32 v129, v112, v118, -v129
	v_fma_f32 v138, v98, v118, -v138
	v_fma_f32 v139, v29, v119, -v139
	v_fma_f32 v146, v98, v112, -v146
	v_fma_f32 v147, v29, v113, -v147
	v_mul_f32_e32 v158, v29, v128
	v_fmac_f32_e32 v158, v98, v129
	v_fmac_f32_e32 v158, v112, v138
	v_rcp_f32_e32 v158, v158
	v_cmp_ne_u32_e64 vcc, s37, v3
	v_mul_f32_e32 v158, v158, v22
	v_cndmask_b32_e64 v158, 0, v158, s[30:31]
	v_cndmask_b32_e64 v29, 0, v18, vcc
	v_cndmask_b32_e64 v153, 0, v22, s[30:31]
	v_mul_f32_e32 v143, v128, v158
	v_mul_f32_e32 v148, v129, v158
	v_mul_f32_e32 v149, v138, v158
	v_mul_f32_e32 v150, v139, v158
	v_mul_f32_e32 v151, v146, v158
	v_mul_f32_e32 v152, v147, v158
	v_add_f32_e32 v154, v91, v29
	v_mov_b32_e32 v155, v3
	ds_write_b128 v23, v[140:143] offset:3072
	ds_write_b128 v23, v[148:151] offset:4096
	ds_write_b128 v23, v[152:155] offset:5120
	s_waitcnt lgkmcnt(0)
	s_barrier
	v_mov_b32_dpp v44, v50 wave_shr:1 row_mask:0xf bank_mask:0xf bound_ctrl:1
	v_mov_b32_dpp v45, v51 wave_shr:1 row_mask:0xf bank_mask:0xf bound_ctrl:1
	v_mov_b32_dpp v56, v50 wave_shl:1 row_mask:0xf bank_mask:0xf bound_ctrl:1
	v_mov_b32_dpp v57, v51 wave_shl:1 row_mask:0xf bank_mask:0xf bound_ctrl:1
	v_pk_mul_f32 v[54:55], v[50:51], v[72:73] op_sel_hi:[1,0]
	v_pk_mul_f32 v[90:91], v[50:51], v[72:73] op_sel:[0,1]
	v_pk_mul_f32 v[118:119], v[50:51], v[74:75] op_sel_hi:[1,0]
	v_pk_add_f32 v[138:139], v[50:51], v[44:45]
	v_pk_fma_f32 v[54:55], v[44:45], v[60:61], v[54:55] op_sel_hi:[1,0,1]
	v_pk_fma_f32 v[90:91], v[44:45], v[60:61], v[90:91] op_sel:[0,1,0]
	v_pk_fma_f32 v[118:119], v[44:45], v[62:63], v[118:119] op_sel_hi:[1,0,1]
	v_pk_add_f32 v[138:139], v[138:139], v[56:57]
	v_pk_fma_f32 v[54:55], v[56:57], v[76:77], v[54:55] op_sel_hi:[1,0,1]
	v_pk_fma_f32 v[90:91], v[56:57], v[76:77], v[90:91] op_sel:[0,1,0]
	v_pk_fma_f32 v[118:119], v[56:57], v[78:79], v[118:119] op_sel_hi:[1,0,1]
	v_pk_add_f32 v[44:45], v[164:165], v[138:139]
	v_pk_add_f32 v[146:147], v[144:145], v[54:55]
	v_pk_add_f32 v[158:159], v[48:49], v[90:91]
	v_pk_add_f32 v[162:163], v[92:93], v[118:119]
	v_pk_fma_f32 v[146:147], v[140:141], v[44:45], v[146:147] op_sel_hi:[0,1,1] neg_lo:[1,0,0] neg_hi:[1,0,0]
	v_pk_fma_f32 v[158:159], v[140:141], v[44:45], v[158:159] op_sel:[1,0,0] neg_lo:[1,0,0] neg_hi:[1,0,0]
	v_pk_fma_f32 v[162:163], v[142:143], v[44:45], v[162:163] op_sel_hi:[0,1,1] neg_lo:[1,0,0] neg_hi:[1,0,0]
	v_pk_mul_f32 v[48:49], v[142:143], v[146:147] op_sel:[1,0]
	v_pk_mul_f32 v[56:57], v[148:149], v[146:147] op_sel_hi:[0,1]
	v_pk_mul_f32 v[68:69], v[148:149], v[146:147] op_sel:[1,0]
	v_pk_fma_f32 v[48:49], v[148:149], v[158:159], v[48:49] op_sel_hi:[0,1,1]
	v_pk_fma_f32 v[56:57], v[150:151], v[158:159], v[56:57] op_sel_hi:[0,1,1]
	v_pk_fma_f32 v[68:69], v[150:151], v[158:159], v[68:69] op_sel:[1,0,0]
	v_pk_fma_f32 v[48:49], v[148:149], v[162:163], v[48:49] op_sel:[1,0,0]
	v_pk_fma_f32 v[56:57], v[150:151], v[162:163], v[56:57] op_sel:[1,0,0]
	v_pk_fma_f32 v[68:69], v[152:153], v[162:163], v[68:69] op_sel_hi:[0,1,1]
	v_pk_mul_f32 v[166:167], v[140:141], v[48:49] op_sel_hi:[0,1]
	v_pk_fma_f32 v[166:167], v[140:141], v[56:57], v[166:167] op_sel:[1,0,0]
	v_pk_fma_f32 v[166:167], v[142:143], v[68:69], v[166:167] op_sel_hi:[0,1,1]
	v_pk_fma_f32 v[166:167], v[152:153], v[44:45], v[166:167] op_sel:[1,0,0] neg_lo:[0,0,1] neg_hi:[0,0,1]
	v_cmp_eq_u32_e64 s[10:11], 6, v155
	v_cmp_eq_u32_e64 s[14:15], 7, v155
	v_pk_add_f32 v[44:45], v[30:31], v[48:49]
	v_pk_add_f32 v[30:31], v[86:87], v[56:57]
	v_pk_add_f32 v[86:87], v[94:95], v[68:69]
	v_pk_add_f32 v[92:93], v[84:85], v[166:167]
	v_pk_fma_f32 v[84:85], v[80:81], v[44:45], v[92:93] op_sel_hi:[0,1,1]
	v_pk_fma_f32 v[112:113], v[100:101], v[44:45], v[92:93] op_sel_hi:[0,1,1]
	v_pk_fma_f32 v[84:85], v[80:81], v[30:31], v[84:85] op_sel:[1,0,0]
	v_pk_fma_f32 v[112:113], v[100:101], v[30:31], v[112:113] op_sel:[1,0,0]
	v_pk_fma_f32 v[84:85], v[82:83], v[86:87], v[84:85] op_sel_hi:[0,1,1]
	v_pk_fma_f32 v[112:113], v[102:103], v[86:87], v[112:113] op_sel_hi:[0,1,1]
	v_pk_fma_f32 v[92:93], v[32:33], v[44:45], v[92:93] op_sel_hi:[0,1,1]
	v_pk_fma_f32 v[92:93], v[32:33], v[30:31], v[92:93] op_sel:[1,0,0]
	v_pk_fma_f32 v[92:93], v[34:35], v[86:87], v[92:93] op_sel_hi:[0,1,1]
	v_cndmask_b32_e64 v94, 0, v18, s[10:11]
	v_cndmask_b32_e64 v95, 0, v18, s[14:15]
	v_add_f32_dpp v92, v84, v92 wave_shl:1 row_mask:0xf bank_mask:0xf bound_ctrl:1
	v_add_f32_dpp v93, v85, v93 wave_shl:1 row_mask:0xf bank_mask:0xf bound_ctrl:1
	s_add_i32 s4, s34, 5
	s_cmpk_lt_i32 s4, 0x201
	s_cselect_b64 s[12:13], s[0:1], 0
	v_add_f32_dpp v92, v112, v92 wave_shr:1 row_mask:0xf bank_mask:0xf bound_ctrl:1
	v_add_f32_dpp v93, v113, v93 wave_shr:1 row_mask:0xf bank_mask:0xf bound_ctrl:1
	v_pk_fma_f32 v[92:93], v[20:21], v[154:155], v[92:93] op_sel_hi:[1,0,1] neg_lo:[0,0,1] neg_hi:[0,0,1]
	v_pk_add_f32 v[92:93], v[92:93], v[94:95] neg_lo:[0,1] neg_hi:[0,1]
	v_pk_mul_f32 v[128:129], v[92:93], v[92:93]
	v_add_f32_e32 v128, v128, v129
	v_cndmask_b32_e64 v129, 0, v128, s[12:13]
	v_add_f32_e32 v1, v1, v129
	s_add_i32 s5, s34, 10
	s_min_i32 s5, s5, 0x200
	s_mul_i32 s6, s5, 0x804
	s_add_i32 s6, s6, s35
	s_add_i32 s7, s6, 0x505014
	s_add_i32 s8, s6, 0x606018
	s_mul_i32 s9, s5, 0x180c
	s_add_i32 s9, s9, s33
	s_add_i32 s4, s34, 11
	s_min_i32 s4, s4, 0x200
	s_mul_i32 s4, s4, 0x804
	s_add_i32 s4, s4, s38
	buffer_load_dword v3, v28, s[20:23], s4 offen nt
	buffer_load_dwordx3 v[32:34], v27, s[24:27], s9 offen nt
	buffer_load_dword v20, v28, s[16:19], s7 offen nt
	buffer_load_dword v21, v28, s[16:19], s8 offen nt
	s_waitcnt vmcnt(8)
	v_mov_b32_dpp v80, v8 wave_shr:1 row_mask:0xf bank_mask:0xf bound_ctrl:1
	v_mov_b32_dpp v81, v9 wave_shr:1 row_mask:0xf bank_mask:0xf bound_ctrl:1
	v_mov_b32_dpp v82, v10 wave_shr:1 row_mask:0xf bank_mask:0xf bound_ctrl:1
	v_mov_b32_dpp v84, v8 wave_shl:1 row_mask:0xf bank_mask:0xf bound_ctrl:1
	v_mov_b32_dpp v85, v9 wave_shl:1 row_mask:0xf bank_mask:0xf bound_ctrl:1
	v_mov_b32_dpp v86, v10 wave_shl:1 row_mask:0xf bank_mask:0xf bound_ctrl:1
	s_add_i32 s4, s34, 9
	s_cmpk_lt_u32 s4, 0x201
	s_cselect_b64 s[12:13], s[40:41], 0
	v_cmp_eq_u32_e64 s[14:15], s37, v17
	s_and_b64 s[14:15], s[14:15], s[12:13]
	v_cndmask_b32_e64 v29, 0, 1, s[14:15]
	v_mul_f32_e32 v30, v8, v8
	v_mul_f32_e32 v31, v8, v9
	v_mul_f32_e32 v44, v8, v10
	v_mul_f32_e32 v45, v9, v9
	v_mul_f32_e32 v92, v9, v10
	v_mul_f32_e32 v93, v10, v10
	v_or_b32_dpp v52, v29, v29 wave_shr:1 row_mask:0xf bank_mask:0xf bound_ctrl:1
	s_nop 1
	v_or_b32_dpp v52, v29, v52 wave_shl:1 row_mask:0xf bank_mask:0xf bound_ctrl:1
	s_nop 1
	v_or_b32_dpp v98, v52, v52 wave_shr:1 row_mask:0xf bank_mask:0xf bound_ctrl:1
	s_nop 1
	v_or_b32_dpp v98, v52, v98 wave_shl:1 row_mask:0xf bank_mask:0xf bound_ctrl:1
	v_or3_b32 v29, v98, v99, v53
	v_or3_b32 v29, v29, v70, v71
	s_add_i32 s4, s34, 6
	s_cmpk_lt_u32 s4, 0x1ff
	s_cselect_b64 s[12:13], s[42:43], 0
	v_cmp_ne_u32_e64 s[30:31], 0, v29
	s_and_b64 s[30:31], s[30:31], s[12:13]
	v_cndmask_b32_e64 v29, 0, 1.0, s[30:31]
	v_add_f32_e32 v94, v8, v80
	v_add_f32_e32 v95, v9, v81
	v_add_f32_e32 v100, v10, v82
	v_fmac_f32_e32 v30, v80, v80
	v_fmac_f32_e32 v31, v80, v81
	v_fmac_f32_e32 v44, v80, v82
	v_fmac_f32_e32 v45, v81, v81
	v_fmac_f32_e32 v92, v81, v82
	v_fmac_f32_e32 v93, v82, v82
	v_add_f32_dpp v129, v29, v29 wave_shr:1 row_mask:0xf bank_mask:0xf bound_ctrl:1
	v_add_f32_e32 v94, v94, v84
	v_add_f32_e32 v95, v95, v85
	v_add_f32_e32 v100, v100, v86
	v_fma_f32 v101, v84, v84, v30
	v_fma_f32 v102, v84, v85, v31
	v_fma_f32 v103, v84, v86, v44
	v_fma_f32 v112, v85, v85, v45
	v_fma_f32 v113, v85, v86, v92
	v_fma_f32 v128, v86, v86, v93
	v_add_f32_dpp v129, v29, v129 wave_shl:1 row_mask:0xf bank_mask:0xf bound_ctrl:1
	v_pk_add_f32 v[30:31], v[114:115], v[94:95]
	v_pk_add_f32 v[44:45], v[108:109], v[30:31]
	v_pk_add_f32 v[92:93], v[122:123], v[100:101]
	v_pk_add_f32 v[108:109], v[110:111], v[92:93]
	v_pk_add_f32 v[110:111], v[126:127], v[102:103]
	v_pk_add_f32 v[114:115], v[116:117], v[110:111]
	v_pk_add_f32 v[122:123], v[130:131], v[112:113]
	v_pk_add_f32 v[116:117], v[120:121], v[122:123]
	v_pk_add_f32 v[126:127], v[134:135], v[128:129]
	v_pk_add_f32 v[120:121], v[136:137], v[126:127]
	v_mul_f32_e32 v140, v44, v22
	v_mul_f32_e32 v141, v45, v22
	v_mul_f32_e32 v142, v108, v22
	v_fma_f32 v29, v109, v22, v26
	v_mul_f32_e32 v52, v114, v22
	v_mul_f32_e32 v130, v115, v22
	v_fma_f32 v131, v116, v22, v26
	v_mul_f32_e32 v134, v117, v22
	v_fma_f32 v135, v120, v22, v26
	v_fma_f32 v29, -v140, v140, v29
	v_fma_f32 v52, -v140, v141, v52
	v_fma_f32 v130, -v140, v142, v130
	v_fma_f32 v131, -v141, v141, v131
	v_fma_f32 v134, -v141, v142, v134
	v_fma_f32 v135, -v142, v142, v135
	v_mul_f32_e32 v136, v134, v134
	v_mul_f32_e32 v137, v52, v135
	v_mul_f32_e32 v152, v130, v131
	v_mul_f32_e32 v153, v130, v130
	v_mul_f32_e32 v154, v29, v134
	v_mul_f32_e32 v155, v52, v52
	v_fma_f32 v136, v131, v135, -v136
	v_fma_f32 v137, v130, v134, -v137
	v_fma_f32 v152, v52, v134, -v152
	v_fma_f32 v153, v29, v135, -v153
	v_fma_f32 v154, v52, v130, -v154
	v_fma_f32 v155, v29, v131, -v155
	v_mul_f32_e32 v158, v29, v136
	v_fmac_f32_e32 v158, v52, v137
	v_fmac_f32_e32 v158, v130, v152
	v_rcp_f32_e32 v158, v158
	v_cmp_ne_u32_e64 vcc, s37, v16
	v_mul_f32_e32 v158, v158, v22
	v_cndmask_b32_e64 v158, 0, v158, s[30:31]
	v_cndmask_b32_e64 v29, 0, v18, vcc
	v_cndmask_b32_e64 v149, 0, v22, s[30:31]
	v_mul_f32_e32 v143, v136, v158
	v_mul_f32_e32 v144, v137, v158
	v_mul_f32_e32 v145, v152, v158
	v_mul_f32_e32 v146, v153, v158
	v_mul_f32_e32 v147, v154, v158
	v_mul_f32_e32 v148, v155, v158
	v_add_f32_e32 v150, v121, v29
	v_mov_b32_e32 v151, v16
	ds_write_b128 v23, v[140:143]
	ds_write_b128 v23, v[144:147] offset:1024
	ds_write_b128 v23, v[148:151] offset:2048
	s_waitcnt lgkmcnt(0)
	s_barrier
	v_mov_b32_dpp v114, v4 wave_shr:1 row_mask:0xf bank_mask:0xf bound_ctrl:1
	v_mov_b32_dpp v115, v5 wave_shr:1 row_mask:0xf bank_mask:0xf bound_ctrl:1
	v_mov_b32_dpp v130, v4 wave_shl:1 row_mask:0xf bank_mask:0xf bound_ctrl:1
	v_mov_b32_dpp v131, v5 wave_shl:1 row_mask:0xf bank_mask:0xf bound_ctrl:1
	v_pk_mul_f32 v[44:45], v[4:5], v[8:9] op_sel_hi:[1,0]
	v_pk_mul_f32 v[108:109], v[4:5], v[8:9] op_sel:[0,1]
	v_pk_mul_f32 v[116:117], v[4:5], v[10:11] op_sel_hi:[1,0]
	v_pk_add_f32 v[120:121], v[4:5], v[114:115]
	v_pk_fma_f32 v[44:45], v[114:115], v[80:81], v[44:45] op_sel_hi:[1,0,1]
	v_pk_fma_f32 v[108:109], v[114:115], v[80:81], v[108:109] op_sel:[0,1,0]
	v_pk_fma_f32 v[116:117], v[114:115], v[82:83], v[116:117] op_sel_hi:[1,0,1]
	v_pk_add_f32 v[120:121], v[120:121], v[130:131]
	v_pk_fma_f32 v[44:45], v[130:131], v[84:85], v[44:45] op_sel_hi:[1,0,1]
	v_pk_fma_f32 v[108:109], v[130:131], v[84:85], v[108:109] op_sel:[0,1,0]
	v_pk_fma_f32 v[116:117], v[130:131], v[86:87], v[116:117] op_sel_hi:[1,0,1]
	v_pk_add_f32 v[114:115], v[138:139], v[120:121]
	v_pk_add_f32 v[130:131], v[156:157], v[114:115]
	v_pk_add_f32 v[134:135], v[54:55], v[44:45]
	v_pk_add_f32 v[136:137], v[88:89], v[134:135]
	v_pk_add_f32 v[54:55], v[90:91], v[108:109]
	v_pk_add_f32 v[88:89], v[124:125], v[54:55]
	v_pk_add_f32 v[90:91], v[118:119], v[116:117]
	v_pk_add_f32 v[124:125], v[132:133], v[90:91]
	v_pk_fma_f32 v[136:137], v[140:141], v[130:131], v[136:137] op_sel_hi:[0,1,1] neg_lo:[1,0,0] neg_hi:[1,0,0]
	v_pk_fma_f32 v[88:89], v[140:141], v[130:131], v[88:89] op_sel:[1,0,0] neg_lo:[1,0,0] neg_hi:[1,0,0]
	v_pk_fma_f32 v[124:125], v[142:143], v[130:131], v[124:125] op_sel_hi:[0,1,1] neg_lo:[1,0,0] neg_hi:[1,0,0]
	v_pk_mul_f32 v[118:119], v[142:143], v[136:137] op_sel:[1,0]
	v_pk_mul_f32 v[138:139], v[144:145], v[136:137] op_sel_hi:[0,1]
	v_pk_mul_f32 v[154:155], v[144:145], v[136:137] op_sel:[1,0]
	v_pk_fma_f32 v[118:119], v[144:145], v[88:89], v[118:119] op_sel_hi:[0,1,1]
	v_pk_fma_f32 v[138:139], v[146:147], v[88:89], v[138:139] op_sel_hi:[0,1,1]
	v_pk_fma_f32 v[154:155], v[146:147], v[88:89], v[154:155] op_sel:[1,0,0]
	v_pk_fma_f32 v[118:119], v[144:145], v[124:125], v[118:119] op_sel:[1,0,0]
	v_pk_fma_f32 v[138:139], v[146:147], v[124:125], v[138:139] op_sel:[1,0,0]
	v_pk_fma_f32 v[154:155], v[148:149], v[124:125], v[154:155] op_sel_hi:[0,1,1]
	v_pk_mul_f32 v[132:133], v[140:141], v[118:119] op_sel_hi:[0,1]
	v_pk_fma_f32 v[132:133], v[140:141], v[138:139], v[132:133] op_sel:[1,0,0]
	v_pk_fma_f32 v[132:133], v[142:143], v[154:155], v[132:133] op_sel_hi:[0,1,1]
	v_pk_fma_f32 v[132:133], v[148:149], v[130:131], v[132:133] op_sel:[1,0,0] neg_lo:[0,0,1] neg_hi:[0,0,1]
	v_cmp_eq_u32_e64 s[10:11], 6, v151
	v_cmp_eq_u32_e64 s[14:15], 7, v151
	v_pk_add_f32 v[88:89], v[48:49], v[118:119]
	v_pk_add_f32 v[124:125], v[38:39], v[88:89]
	v_pk_add_f32 v[48:49], v[56:57], v[138:139]
	v_pk_add_f32 v[38:39], v[46:47], v[48:49]
	v_pk_add_f32 v[56:57], v[68:69], v[154:155]
	v_pk_add_f32 v[46:47], v[58:59], v[56:57]
	v_pk_add_f32 v[58:59], v[166:167], v[132:133]
	v_pk_add_f32 v[68:69], v[96:97], v[58:59]
	v_pk_fma_f32 v[96:97], v[64:65], v[124:125], v[68:69] op_sel_hi:[0,1,1]
	v_pk_fma_f32 v[136:137], v[104:105], v[124:125], v[68:69] op_sel_hi:[0,1,1]
	v_pk_fma_f32 v[96:97], v[64:65], v[38:39], v[96:97] op_sel:[1,0,0]
	v_pk_fma_f32 v[136:137], v[104:105], v[38:39], v[136:137] op_sel:[1,0,0]
	v_pk_fma_f32 v[96:97], v[66:67], v[46:47], v[96:97] op_sel_hi:[0,1,1]
	v_pk_fma_f32 v[136:137], v[106:107], v[46:47], v[136:137] op_sel_hi:[0,1,1]
	v_pk_fma_f32 v[68:69], v[40:41], v[124:125], v[68:69] op_sel_hi:[0,1,1]
	v_pk_fma_f32 v[68:69], v[40:41], v[38:39], v[68:69] op_sel:[1,0,0]
	v_pk_fma_f32 v[68:69], v[42:43], v[46:47], v[68:69] op_sel_hi:[0,1,1]
	v_cndmask_b32_e64 v130, 0, v18, s[10:11]
	v_cndmask_b32_e64 v131, 0, v18, s[14:15]
	v_add_f32_dpp v68, v96, v68 wave_shl:1 row_mask:0xf bank_mask:0xf bound_ctrl:1
	v_add_f32_dpp v69, v97, v69 wave_shl:1 row_mask:0xf bank_mask:0xf bound_ctrl:1
	s_add_i32 s4, s34, 6
	s_cmpk_lt_i32 s4, 0x201
	s_cselect_b64 s[12:13], s[0:1], 0
	v_add_f32_dpp v68, v136, v68 wave_shr:1 row_mask:0xf bank_mask:0xf bound_ctrl:1
	v_add_f32_dpp v69, v137, v69 wave_shr:1 row_mask:0xf bank_mask:0xf bound_ctrl:1
	v_pk_fma_f32 v[68:69], v[36:37], v[150:151], v[68:69] op_sel_hi:[1,0,1] neg_lo:[0,0,1] neg_hi:[0,0,1]
	v_pk_add_f32 v[68:69], v[68:69], v[130:131] neg_lo:[0,1] neg_hi:[0,1]
	v_pk_mul_f32 v[152:153], v[68:69], v[68:69]
	v_add_f32_e32 v152, v152, v153
	v_cndmask_b32_e64 v153, 0, v152, s[12:13]
	v_add_f32_e32 v1, v1, v153
	s_add_i32 s5, s34, 11
	s_min_i32 s5, s5, 0x200
	s_mul_i32 s6, s5, 0x804
	s_add_i32 s6, s6, s35
	s_add_i32 s7, s6, 0x505014
	s_add_i32 s8, s6, 0x606018
	s_mul_i32 s9, s5, 0x180c
	s_add_i32 s9, s9, s33
	s_add_i32 s4, s34, 12
	s_min_i32 s4, s4, 0x200
	s_mul_i32 s4, s4, 0x804
	s_add_i32 s4, s4, s38
	buffer_load_dword v16, v28, s[20:23], s4 offen nt
	buffer_load_dwordx3 v[40:42], v27, s[24:27], s9 offen nt
	buffer_load_dword v36, v28, s[16:19], s7 offen nt
	buffer_load_dword v37, v28, s[16:19], s8 offen nt
	s_waitcnt vmcnt(8)
	v_mov_b32_dpp v64, v12 wave_shr:1 row_mask:0xf bank_mask:0xf bound_ctrl:1
	v_mov_b32_dpp v65, v13 wave_shr:1 row_mask:0xf bank_mask:0xf bound_ctrl:1
	v_mov_b32_dpp v66, v14 wave_shr:1 row_mask:0xf bank_mask:0xf bound_ctrl:1
	v_mov_b32_dpp v104, v12 wave_shl:1 row_mask:0xf bank_mask:0xf bound_ctrl:1
	v_mov_b32_dpp v105, v13 wave_shl:1 row_mask:0xf bank_mask:0xf bound_ctrl:1
	v_mov_b32_dpp v106, v14 wave_shl:1 row_mask:0xf bank_mask:0xf bound_ctrl:1
	s_add_i32 s4, s34, 10
	s_cmpk_lt_u32 s4, 0x201
	s_cselect_b64 s[12:13], s[40:41], 0
	v_cmp_eq_u32_e64 s[14:15], s37, v2
	s_and_b64 s[14:15], s[14:15], s[12:13]
	v_cndmask_b32_e64 v29, 0, 1, s[14:15]
	v_mul_f32_e32 v38, v12, v12
	v_mul_f32_e32 v39, v12, v13
	v_mul_f32_e32 v46, v12, v14
	v_mul_f32_e32 v47, v13, v13
	v_mul_f32_e32 v68, v13, v14
	v_mul_f32_e32 v69, v14, v14
	v_or_b32_dpp v52, v29, v29 wave_shr:1 row_mask:0xf bank_mask:0xf bound_ctrl:1
	s_nop 1
	v_or_b32_dpp v52, v29, v52 wave_shl:1 row_mask:0xf bank_mask:0xf bound_ctrl:1
	s_nop 1
	v_or_b32_dpp v71, v52, v52 wave_shr:1 row_mask:0xf bank_mask:0xf bound_ctrl:1
	s_nop 1
	v_or_b32_dpp v71, v52, v71 wave_shl:1 row_mask:0xf bank_mask:0xf bound_ctrl:1
	v_or3_b32 v29, v71, v98, v99
	v_or3_b32 v29, v29, v53, v70
	s_add_i32 s4, s34, 7
	s_cmpk_lt_u32 s4, 0x1ff
	s_cselect_b64 s[12:13], s[42:43], 0
	v_cmp_ne_u32_e64 s[30:31], 0, v29
	s_and_b64 s[30:31], s[30:31], s[12:13]
	v_cndmask_b32_e64 v29, 0, 1.0, s[30:31]
	v_add_f32_e32 v96, v12, v64
	v_add_f32_e32 v97, v13, v65
	v_add_f32_e32 v124, v14, v66
	v_fmac_f32_e32 v38, v64, v64
	v_fmac_f32_e32 v39, v64, v65
	v_fmac_f32_e32 v46, v64, v66
	v_fmac_f32_e32 v47, v65, v65
	v_fmac_f32_e32 v68, v65, v66
	v_fmac_f32_e32 v69, v66, v66
	v_add_f32_dpp v141, v29, v29 wave_shr:1 row_mask:0xf bank_mask:0xf bound_ctrl:1
	v_add_f32_e32 v96, v96, v104
	v_add_f32_e32 v97, v97, v105
	v_add_f32_e32 v124, v124, v106
	v_fma_f32 v125, v104, v104, v38
	v_fma_f32 v130, v104, v105, v39
	v_fma_f32 v131, v104, v106, v46
	v_fma_f32 v136, v105, v105, v47
	v_fma_f32 v137, v105, v106, v68
	v_fma_f32 v140, v106, v106, v69
	v_add_f32_dpp v141, v29, v141 wave_shl:1 row_mask:0xf bank_mask:0xf bound_ctrl:1
	v_pk_add_f32 v[38:39], v[30:31], v[96:97]
	v_pk_add_f32 v[30:31], v[92:93], v[124:125]
	v_pk_add_f32 v[46:47], v[110:111], v[130:131]
	v_pk_add_f32 v[68:69], v[122:123], v[136:137]
	v_pk_add_f32 v[92:93], v[126:127], v[140:141]
	v_mul_f32_e32 v144, v38, v22
	v_mul_f32_e32 v145, v39, v22
	v_mul_f32_e32 v146, v30, v22
	v_fma_f32 v29, v31, v22, v26
	v_mul_f32_e32 v52, v46, v22
	v_mul_f32_e32 v110, v47, v22
	v_fma_f32 v111, v68, v22, v26
	v_mul_f32_e32 v122, v69, v22
	v_fma_f32 v123, v92, v22, v26
	v_fma_f32 v29, -v144, v144, v29
	v_fma_f32 v52, -v144, v145, v52
	v_fma_f32 v110, -v144, v146, v110
	v_fma_f32 v111, -v145, v145, v111
	v_fma_f32 v122, -v145, v146, v122
	v_fma_f32 v123, -v146, v146, v123
	v_mul_f32_e32 v126, v122, v122
	v_mul_f32_e32 v127, v52, v123
	v_mul_f32_e32 v142, v110, v111
	v_mul_f32_e32 v143, v110, v110
	v_mul_f32_e32 v152, v29, v122
	v_mul_f32_e32 v153, v52, v52
	v_fma_f32 v126, v111, v123, -v126
	v_fma_f32 v127, v110, v122, -v127
	v_fma_f32 v142, v52, v122, -v142
	v_fma_f32 v143, v29, v123, -v143
	v_fma_f32 v152, v52, v110, -v152
	v_fma_f32 v153, v29, v111, -v153
	v_mul_f32_e32 v160, v29, v126
	v_fmac_f32_e32 v160, v52, v127
	v_fmac_f32_e32 v160, v110, v142
	v_rcp_f32_e32 v160, v160
	v_cmp_ne_u32_e64 vcc, s37, v25
	v_mul_f32_e32 v160, v160, v22
	v_cndmask_b32_e64 v160, 0, v160, s[30:31]
	v_cndmask_b32_e64 v29, 0, v18, vcc
	v_cndmask_b32_e64 v157, 0, v22, s[30:31]
	v_mul_f32_e32 v147, v126, v160
	v_mul_f32_e32 v148, v127, v160
	v_mul_f32_e32 v149, v142, v160
	v_mul_f32_e32 v150, v143, v160
	v_mul_f32_e32 v151, v152, v160
	v_mul_f32_e32 v156, v153, v160
	v_add_f32_e32 v158, v93, v29
	v_mov_b32_e32 v159, v25
	ds_write_b128 v23, v[144:147] offset:3072
	ds_write_b128 v23, v[148:151] offset:4096
	ds_write_b128 v23, v[156:159] offset:5120
	s_waitcnt lgkmcnt(0)
	s_barrier
	v_mov_b32_dpp v68, v6 wave_shr:1 row_mask:0xf bank_mask:0xf bound_ctrl:1
	v_mov_b32_dpp v69, v7 wave_shr:1 row_mask:0xf bank_mask:0xf bound_ctrl:1
	v_mov_b32_dpp v92, v6 wave_shl:1 row_mask:0xf bank_mask:0xf bound_ctrl:1
	v_mov_b32_dpp v93, v7 wave_shl:1 row_mask:0xf bank_mask:0xf bound_ctrl:1
	v_pk_mul_f32 v[30:31], v[6:7], v[12:13] op_sel_hi:[1,0]
	v_pk_mul_f32 v[38:39], v[6:7], v[12:13] op_sel:[0,1]
	v_pk_mul_f32 v[46:47], v[6:7], v[14:15] op_sel_hi:[1,0]
	v_pk_add_f32 v[110:111], v[6:7], v[68:69]
	v_pk_fma_f32 v[30:31], v[68:69], v[64:65], v[30:31] op_sel_hi:[1,0,1]
	v_pk_fma_f32 v[38:39], v[68:69], v[64:65], v[38:39] op_sel:[0,1,0]
	v_pk_fma_f32 v[46:47], v[68:69], v[66:67], v[46:47] op_sel_hi:[1,0,1]
	v_pk_add_f32 v[110:111], v[110:111], v[92:93]
	v_pk_fma_f32 v[30:31], v[92:93], v[104:105], v[30:31] op_sel_hi:[1,0,1]
	v_pk_fma_f32 v[38:39], v[92:93], v[104:105], v[38:39] op_sel:[0,1,0]
	v_pk_fma_f32 v[46:47], v[92:93], v[106:107], v[46:47] op_sel_hi:[1,0,1]
	v_pk_add_f32 v[68:69], v[114:115], v[110:111]
	v_pk_add_f32 v[114:115], v[134:135], v[30:31]
	v_pk_add_f32 v[122:123], v[54:55], v[38:39]
	v_pk_add_f32 v[54:55], v[90:91], v[46:47]
	v_pk_fma_f32 v[114:115], v[144:145], v[68:69], v[114:115] op_sel_hi:[0,1,1] neg_lo:[1,0,0] neg_hi:[1,0,0]
	v_pk_fma_f32 v[122:123], v[144:145], v[68:69], v[122:123] op_sel:[1,0,0] neg_lo:[1,0,0] neg_hi:[1,0,0]
	v_pk_fma_f32 v[54:55], v[146:147], v[68:69], v[54:55] op_sel_hi:[0,1,1] neg_lo:[1,0,0] neg_hi:[1,0,0]
	v_pk_mul_f32 v[92:93], v[146:147], v[114:115] op_sel:[1,0]
	v_pk_mul_f32 v[152:153], v[148:149], v[114:115] op_sel_hi:[0,1]
	v_pk_mul_f32 v[160:161], v[148:149], v[114:115] op_sel:[1,0]
	v_pk_fma_f32 v[92:93], v[148:149], v[122:123], v[92:93] op_sel_hi:[0,1,1]
	v_pk_fma_f32 v[152:153], v[150:151], v[122:123], v[152:153] op_sel_hi:[0,1,1]
	v_pk_fma_f32 v[160:161], v[150:151], v[122:123], v[160:161] op_sel:[1,0,0]
	v_pk_fma_f32 v[92:93], v[148:149], v[54:55], v[92:93] op_sel:[1,0,0]
	v_pk_fma_f32 v[152:153], v[150:151], v[54:55], v[152:153] op_sel:[1,0,0]
	v_pk_fma_f32 v[160:161], v[156:157], v[54:55], v[160:161] op_sel_hi:[0,1,1]
	v_pk_mul_f32 v[90:91], v[144:145], v[92:93] op_sel_hi:[0,1]
	v_pk_fma_f32 v[90:91], v[144:145], v[152:153], v[90:91] op_sel:[1,0,0]
	v_pk_fma_f32 v[90:91], v[146:147], v[160:161], v[90:91] op_sel_hi:[0,1,1]
	v_pk_fma_f32 v[90:91], v[156:157], v[68:69], v[90:91] op_sel:[1,0,0] neg_lo:[0,0,1] neg_hi:[0,0,1]
	v_cmp_eq_u32_e64 s[10:11], 6, v159
	v_cmp_eq_u32_e64 s[14:15], 7, v159
	v_pk_add_f32 v[54:55], v[88:89], v[92:93]
	v_pk_add_f32 v[68:69], v[48:49], v[152:153]
	v_pk_add_f32 v[48:49], v[56:57], v[160:161]
	v_pk_add_f32 v[114:115], v[58:59], v[90:91]
	v_pk_fma_f32 v[58:59], v[60:61], v[54:55], v[114:115] op_sel_hi:[0,1,1]
	v_pk_fma_f32 v[122:123], v[76:77], v[54:55], v[114:115] op_sel_hi:[0,1,1]
	v_pk_fma_f32 v[58:59], v[60:61], v[68:69], v[58:59] op_sel:[1,0,0]
	v_pk_fma_f32 v[122:123], v[76:77], v[68:69], v[122:123] op_sel:[1,0,0]
	v_pk_fma_f32 v[58:59], v[62:63], v[48:49], v[58:59] op_sel_hi:[0,1,1]
	v_pk_fma_f32 v[122:123], v[78:79], v[48:49], v[122:123] op_sel_hi:[0,1,1]
	v_pk_fma_f32 v[114:115], v[72:73], v[54:55], v[114:115] op_sel_hi:[0,1,1]
	v_pk_fma_f32 v[114:115], v[72:73], v[68:69], v[114:115] op_sel:[1,0,0]
	v_pk_fma_f32 v[114:115], v[74:75], v[48:49], v[114:115] op_sel_hi:[0,1,1]
	v_cndmask_b32_e64 v56, 0, v18, s[10:11]
	v_cndmask_b32_e64 v57, 0, v18, s[14:15]
	v_add_f32_dpp v114, v58, v114 wave_shl:1 row_mask:0xf bank_mask:0xf bound_ctrl:1
	v_add_f32_dpp v115, v59, v115 wave_shl:1 row_mask:0xf bank_mask:0xf bound_ctrl:1
	s_add_i32 s4, s34, 7
	s_cmpk_lt_i32 s4, 0x201
	s_cselect_b64 s[12:13], s[0:1], 0
	v_add_f32_dpp v114, v122, v114 wave_shr:1 row_mask:0xf bank_mask:0xf bound_ctrl:1
	v_add_f32_dpp v115, v123, v115 wave_shr:1 row_mask:0xf bank_mask:0xf bound_ctrl:1
	v_pk_fma_f32 v[114:115], v[50:51], v[158:159], v[114:115] op_sel_hi:[1,0,1] neg_lo:[0,0,1] neg_hi:[0,0,1]
	v_pk_add_f32 v[114:115], v[114:115], v[56:57] neg_lo:[0,1] neg_hi:[0,1]
	v_pk_mul_f32 v[88:89], v[114:115], v[114:115]
	v_add_f32_e32 v88, v88, v89
	v_cndmask_b32_e64 v89, 0, v88, s[12:13]
	v_add_f32_e32 v1, v1, v89
	s_waitcnt vmcnt(4)
	v_mov_b32_dpp v48, v32 wave_shr:1 row_mask:0xf bank_mask:0xf bound_ctrl:1
	v_mov_b32_dpp v49, v33 wave_shr:1 row_mask:0xf bank_mask:0xf bound_ctrl:1
	v_mov_b32_dpp v50, v34 wave_shr:1 row_mask:0xf bank_mask:0xf bound_ctrl:1
	v_mov_b32_dpp v56, v32 wave_shl:1 row_mask:0xf bank_mask:0xf bound_ctrl:1
	v_mov_b32_dpp v57, v33 wave_shl:1 row_mask:0xf bank_mask:0xf bound_ctrl:1
	v_mov_b32_dpp v58, v34 wave_shl:1 row_mask:0xf bank_mask:0xf bound_ctrl:1
	s_add_i32 s4, s34, 11
	s_cmpk_lt_u32 s4, 0x201
	s_cselect_b64 s[12:13], s[40:41], 0
	v_cmp_eq_u32_e64 s[14:15], s37, v3
	s_and_b64 s[14:15], s[14:15], s[12:13]
	v_cndmask_b32_e64 v25, 0, 1, s[14:15]
	v_mul_f32_e32 v54, v32, v32
	v_mul_f32_e32 v55, v32, v33
	v_mul_f32_e32 v60, v32, v34
	v_mul_f32_e32 v61, v33, v33
	v_mul_f32_e32 v62, v33, v34
	v_mul_f32_e32 v63, v34, v34
	v_or_b32_dpp v29, v25, v25 wave_shr:1 row_mask:0xf bank_mask:0xf bound_ctrl:1
	s_nop 1
	v_or_b32_dpp v29, v25, v29 wave_shl:1 row_mask:0xf bank_mask:0xf bound_ctrl:1
	s_nop 1
	v_or_b32_dpp v52, v29, v29 wave_shr:1 row_mask:0xf bank_mask:0xf bound_ctrl:1
	s_nop 1
	v_or_b32_dpp v52, v29, v52 wave_shl:1 row_mask:0xf bank_mask:0xf bound_ctrl:1
	v_or3_b32 v25, v52, v71, v98
	v_or3_b32 v25, v25, v99, v53
	s_add_i32 s4, s34, 8
	s_cmpk_lt_u32 s4, 0x1ff
	s_cselect_b64 s[12:13], s[42:43], 0
	v_cmp_ne_u32_e64 s[30:31], 0, v25
	s_and_b64 s[30:31], s[30:31], s[12:13]
	v_cndmask_b32_e64 v25, 0, 1.0, s[30:31]
	v_add_f32_e32 v68, v32, v48
	v_add_f32_e32 v69, v33, v49
	v_add_f32_e32 v72, v34, v50
	v_fmac_f32_e32 v54, v48, v48
	v_fmac_f32_e32 v55, v48, v49
	v_fmac_f32_e32 v60, v48, v50
	v_fmac_f32_e32 v61, v49, v49
	v_fmac_f32_e32 v62, v49, v50
	v_fmac_f32_e32 v63, v50, v50
	v_add_f32_dpp v79, v25, v25 wave_shr:1 row_mask:0xf bank_mask:0xf bound_ctrl:1
	v_add_f32_e32 v68, v68, v56
	v_add_f32_e32 v69, v69, v57
	v_add_f32_e32 v72, v72, v58
	v_fma_f32 v73, v56, v56, v54
	v_fma_f32 v74, v56, v57, v55
	v_fma_f32 v75, v56, v58, v60
	v_fma_f32 v76, v57, v57, v61
	v_fma_f32 v77, v57, v58, v62
	v_fma_f32 v78, v58, v58, v63
	v_add_f32_dpp v79, v25, v79 wave_shl:1 row_mask:0xf bank_mask:0xf bound_ctrl:1
	v_pk_add_f32 v[60:61], v[96:97], v[68:69]
	v_pk_add_f32 v[54:55], v[94:95], v[60:61]
	v_pk_add_f32 v[62:63], v[124:125], v[72:73]
	v_pk_add_f32 v[88:89], v[100:101], v[62:63]
	v_pk_add_f32 v[96:97], v[130:131], v[74:75]
	v_pk_add_f32 v[94:95], v[102:103], v[96:97]
	v_pk_add_f32 v[102:103], v[136:137], v[76:77]
	v_pk_add_f32 v[100:101], v[112:113], v[102:103]
	v_pk_add_f32 v[114:115], v[140:141], v[78:79]
	v_pk_add_f32 v[112:113], v[128:129], v[114:115]
	v_mul_f32_e32 v124, v54, v22
	v_mul_f32_e32 v125, v55, v22
	v_mul_f32_e32 v126, v88, v22
	v_fma_f32 v25, v89, v22, v26
	v_mul_f32_e32 v29, v94, v22
	v_mul_f32_e32 v70, v95, v22
	v_fma_f32 v122, v100, v22, v26
	v_mul_f32_e32 v123, v101, v22
	v_fma_f32 v134, v112, v22, v26
	v_fma_f32 v25, -v124, v124, v25
	v_fma_f32 v29, -v124, v125, v29
	v_fma_f32 v70, -v124, v126, v70
	v_fma_f32 v122, -v125, v125, v122
	v_fma_f32 v123, -v125, v126, v123
	v_fma_f32 v134, -v126, v126, v134
	v_mul_f32_e32 v135, v123, v123
	v_mul_f32_e32 v136, v29, v134
	v_mul_f32_e32 v137, v70, v122
	v_mul_f32_e32 v144, v70, v70
	v_mul_f32_e32 v145, v25, v123
	v_mul_f32_e32 v146, v29, v29
	v_fma_f32 v135, v122, v134, -v135
	v_fma_f32 v136, v70, v123, -v136
	v_fma_f32 v137, v29, v123, -v137
	v_fma_f32 v144, v25, v134, -v144
	v_fma_f32 v145, v29, v70, -v145
	v_fma_f32 v146, v25, v122, -v146
	v_mul_f32_e32 v147, v25, v135
	v_fmac_f32_e32 v147, v29, v136
	v_fmac_f32_e32 v147, v70, v137
	v_rcp_f32_e32 v147, v147
	v_cmp_ne_u32_e64 vcc, s37, v24
	v_mul_f32_e32 v147, v147, v22
	v_cndmask_b32_e64 v147, 0, v147, s[30:31]
	v_cndmask_b32_e64 v25, 0, v18, vcc
	v_cndmask_b32_e64 v141, 0, v22, s[30:31]
	v_mul_f32_e32 v127, v135, v147
	v_mul_f32_e32 v128, v136, v147
	v_mul_f32_e32 v129, v137, v147
	v_mul_f32_e32 v130, v144, v147
	v_mul_f32_e32 v131, v145, v147
	v_mul_f32_e32 v140, v146, v147
	v_add_f32_e32 v142, v113, v25
	v_mov_b32_e32 v143, v24
	ds_write_b128 v23, v[124:127]
	ds_write_b128 v23, v[128:131] offset:1024
	ds_write_b128 v23, v[140:143] offset:2048
	s_waitcnt lgkmcnt(0)
	s_barrier
	v_mov_b32_dpp v54, v20 wave_shr:1 row_mask:0xf bank_mask:0xf bound_ctrl:1
	v_mov_b32_dpp v55, v21 wave_shr:1 row_mask:0xf bank_mask:0xf bound_ctrl:1
	v_mov_b32_dpp v94, v20 wave_shl:1 row_mask:0xf bank_mask:0xf bound_ctrl:1
	v_mov_b32_dpp v95, v21 wave_shl:1 row_mask:0xf bank_mask:0xf bound_ctrl:1
	v_pk_mul_f32 v[24:25], v[20:21], v[32:33] op_sel_hi:[1,0]
	v_pk_mul_f32 v[88:89], v[20:21], v[32:33] op_sel:[0,1]
	v_pk_mul_f32 v[100:101], v[20:21], v[34:35] op_sel_hi:[1,0]
	v_pk_add_f32 v[112:113], v[20:21], v[54:55]
	v_pk_fma_f32 v[24:25], v[54:55], v[48:49], v[24:25] op_sel_hi:[1,0,1]
	v_pk_fma_f32 v[88:89], v[54:55], v[48:49], v[88:89] op_sel:[0,1,0]
	v_pk_fma_f32 v[100:101], v[54:55], v[50:51], v[100:101] op_sel_hi:[1,0,1]
	v_pk_add_f32 v[112:113], v[112:113], v[94:95]
	v_pk_fma_f32 v[24:25], v[94:95], v[56:57], v[24:25] op_sel_hi:[1,0,1]
	v_pk_fma_f32 v[88:89], v[94:95], v[56:57], v[88:89] op_sel:[0,1,0]
	v_pk_fma_f32 v[100:101], v[94:95], v[58:59], v[100:101] op_sel_hi:[1,0,1]
	v_pk_add_f32 v[54:55], v[110:111], v[112:113]
	v_pk_add_f32 v[94:95], v[120:121], v[54:55]
	v_pk_add_f32 v[110:111], v[30:31], v[24:25]
	v_pk_add_f32 v[120:121], v[44:45], v[110:111]
	v_pk_add_f32 v[30:31], v[38:39], v[88:89]
	v_pk_add_f32 v[44:45], v[108:109], v[30:31]
	v_pk_add_f32 v[38:39], v[46:47], v[100:101]
	v_pk_add_f32 v[108:109], v[116:117], v[38:39]
	v_pk_fma_f32 v[120:121], v[124:125], v[94:95], v[120:121] op_sel_hi:[0,1,1] neg_lo:[1,0,0] neg_hi:[1,0,0]
	v_pk_fma_f32 v[44:45], v[124:125], v[94:95], v[44:45] op_sel:[1,0,0] neg_lo:[1,0,0] neg_hi:[1,0,0]
	v_pk_fma_f32 v[108:109], v[126:127], v[94:95], v[108:109] op_sel_hi:[0,1,1] neg_lo:[1,0,0] neg_hi:[1,0,0]
	v_pk_mul_f32 v[46:47], v[126:127], v[120:121] op_sel:[1,0]
	v_pk_mul_f32 v[122:123], v[128:129], v[120:121] op_sel_hi:[0,1]
	v_pk_mul_f32 v[134:135], v[128:129], v[120:121] op_sel:[1,0]
	v_pk_fma_f32 v[46:47], v[128:129], v[44:45], v[46:47] op_sel_hi:[0,1,1]
	v_pk_fma_f32 v[122:123], v[130:131], v[44:45], v[122:123] op_sel_hi:[0,1,1]
	v_pk_fma_f32 v[134:135], v[130:131], v[44:45], v[134:135] op_sel:[1,0,0]
	v_pk_fma_f32 v[46:47], v[128:129], v[108:109], v[46:47] op_sel:[1,0,0]
	v_pk_fma_f32 v[122:123], v[130:131], v[108:109], v[122:123] op_sel:[1,0,0]
	v_pk_fma_f32 v[134:135], v[140:141], v[108:109], v[134:135] op_sel_hi:[0,1,1]
	v_pk_mul_f32 v[116:117], v[124:125], v[46:47] op_sel_hi:[0,1]
	v_pk_fma_f32 v[116:117], v[124:125], v[122:123], v[116:117] op_sel:[1,0,0]
	v_pk_fma_f32 v[116:117], v[126:127], v[134:135], v[116:117] op_sel_hi:[0,1,1]
	v_pk_fma_f32 v[116:117], v[140:141], v[94:95], v[116:117] op_sel:[1,0,0] neg_lo:[0,0,1] neg_hi:[0,0,1]
	v_cmp_eq_u32_e64 s[10:11], 6, v143
	v_cmp_eq_u32_e64 s[14:15], 7, v143
	v_pk_add_f32 v[44:45], v[92:93], v[46:47]
	v_pk_add_f32 v[94:95], v[118:119], v[44:45]
	v_pk_add_f32 v[92:93], v[152:153], v[122:123]
	v_pk_add_f32 v[108:109], v[138:139], v[92:93]
	v_pk_add_f32 v[120:121], v[160:161], v[134:135]
	v_pk_add_f32 v[118:119], v[154:155], v[120:121]
	v_pk_add_f32 v[138:139], v[90:91], v[116:117]
	v_pk_add_f32 v[136:137], v[132:133], v[138:139]
	v_pk_fma_f32 v[132:133], v[80:81], v[94:95], v[136:137] op_sel_hi:[0,1,1]
	v_pk_fma_f32 v[144:145], v[84:85], v[94:95], v[136:137] op_sel_hi:[0,1,1]
	v_pk_fma_f32 v[132:133], v[80:81], v[108:109], v[132:133] op_sel:[1,0,0]
	v_pk_fma_f32 v[144:145], v[84:85], v[108:109], v[144:145] op_sel:[1,0,0]
	v_pk_fma_f32 v[132:133], v[82:83], v[118:119], v[132:133] op_sel_hi:[0,1,1]
	v_pk_fma_f32 v[144:145], v[86:87], v[118:119], v[144:145] op_sel_hi:[0,1,1]
	v_pk_fma_f32 v[136:137], v[8:9], v[94:95], v[136:137] op_sel_hi:[0,1,1]
	v_pk_fma_f32 v[136:137], v[8:9], v[108:109], v[136:137] op_sel:[1,0,0]
	v_pk_fma_f32 v[136:137], v[10:11], v[118:119], v[136:137] op_sel_hi:[0,1,1]
	v_cndmask_b32_e64 v90, 0, v18, s[10:11]
	v_cndmask_b32_e64 v91, 0, v18, s[14:15]
	v_add_f32_dpp v136, v132, v136 wave_shl:1 row_mask:0xf bank_mask:0xf bound_ctrl:1
	v_add_f32_dpp v137, v133, v137 wave_shl:1 row_mask:0xf bank_mask:0xf bound_ctrl:1
	s_add_i32 s4, s34, 8
	s_cmpk_lt_i32 s4, 0x201
	s_cselect_b64 s[12:13], s[0:1], 0
	v_add_f32_dpp v136, v144, v136 wave_shr:1 row_mask:0xf bank_mask:0xf bound_ctrl:1
	v_add_f32_dpp v137, v145, v137 wave_shr:1 row_mask:0xf bank_mask:0xf bound_ctrl:1
	v_pk_fma_f32 v[136:137], v[4:5], v[142:143], v[136:137] op_sel_hi:[1,0,1] neg_lo:[0,0,1] neg_hi:[0,0,1]
	v_pk_add_f32 v[136:137], v[136:137], v[90:91] neg_lo:[0,1] neg_hi:[0,1]
	v_pk_mul_f32 v[146:147], v[136:137], v[136:137]
	v_add_f32_e32 v146, v146, v147
	v_cndmask_b32_e64 v147, 0, v146, s[12:13]
	v_add_f32_e32 v1, v1, v147
	s_waitcnt vmcnt(0)
	v_mov_b32_dpp v8, v40 wave_shr:1 row_mask:0xf bank_mask:0xf bound_ctrl:1
	v_mov_b32_dpp v9, v41 wave_shr:1 row_mask:0xf bank_mask:0xf bound_ctrl:1
	v_mov_b32_dpp v10, v42 wave_shr:1 row_mask:0xf bank_mask:0xf bound_ctrl:1
	v_mov_b32_dpp v80, v40 wave_shl:1 row_mask:0xf bank_mask:0xf bound_ctrl:1
	v_mov_b32_dpp v81, v41 wave_shl:1 row_mask:0xf bank_mask:0xf bound_ctrl:1
	v_mov_b32_dpp v82, v42 wave_shl:1 row_mask:0xf bank_mask:0xf bound_ctrl:1
	s_add_i32 s4, s34, 12
	s_cmpk_lt_u32 s4, 0x201
	s_cselect_b64 s[12:13], s[40:41], 0
	v_cmp_eq_u32_e64 s[14:15], s37, v16
	s_and_b64 s[14:15], s[14:15], s[12:13]
	v_cndmask_b32_e64 v29, 0, 1, s[14:15]
	v_mul_f32_e32 v4, v40, v40
	v_mul_f32_e32 v5, v40, v41
	v_mul_f32_e32 v84, v40, v42
	v_mul_f32_e32 v85, v41, v41
	v_mul_f32_e32 v86, v41, v42
	v_mul_f32_e32 v87, v42, v42
	v_or_b32_dpp v53, v29, v29 wave_shr:1 row_mask:0xf bank_mask:0xf bound_ctrl:1
	s_nop 1
	v_or_b32_dpp v53, v29, v53 wave_shl:1 row_mask:0xf bank_mask:0xf bound_ctrl:1
	s_nop 1
	v_or_b32_dpp v70, v53, v53 wave_shr:1 row_mask:0xf bank_mask:0xf bound_ctrl:1
	s_nop 1
	v_or_b32_dpp v70, v53, v70 wave_shl:1 row_mask:0xf bank_mask:0xf bound_ctrl:1
	v_or3_b32 v29, v70, v52, v71
	v_or3_b32 v29, v29, v98, v99
	s_add_i32 s4, s34, 9
	s_cmpk_lt_u32 s4, 0x1ff
	s_cselect_b64 s[12:13], s[42:43], 0
	v_cmp_ne_u32_e64 s[30:31], 0, v29
	s_and_b64 s[30:31], s[30:31], s[12:13]
	v_cndmask_b32_e64 v29, 0, 1.0, s[30:31]
	v_add_f32_e32 v90, v40, v8
	v_add_f32_e32 v91, v41, v9
	v_add_f32_e32 v94, v42, v10
	v_fmac_f32_e32 v4, v8, v8
	v_fmac_f32_e32 v5, v8, v9
	v_fmac_f32_e32 v84, v8, v10
	v_fmac_f32_e32 v85, v9, v9
	v_fmac_f32_e32 v86, v9, v10
	v_fmac_f32_e32 v87, v10, v10
	v_add_f32_dpp v125, v29, v29 wave_shr:1 row_mask:0xf bank_mask:0xf bound_ctrl:1
	v_add_f32_e32 v90, v90, v80
	v_add_f32_e32 v91, v91, v81
	v_add_f32_e32 v94, v94, v82
	v_fma_f32 v95, v80, v80, v4
	v_fma_f32 v108, v80, v81, v5
	v_fma_f32 v109, v80, v82, v84
	v_fma_f32 v118, v81, v81, v85
	v_fma_f32 v119, v81, v82, v86
	v_fma_f32 v124, v82, v82, v87
	v_add_f32_dpp v125, v29, v125 wave_shl:1 row_mask:0xf bank_mask:0xf bound_ctrl:1
	v_pk_add_f32 v[4:5], v[60:61], v[90:91]
	v_pk_add_f32 v[60:61], v[62:63], v[94:95]
	v_pk_add_f32 v[62:63], v[96:97], v[108:109]
	v_pk_add_f32 v[84:85], v[102:103], v[118:119]
	v_pk_add_f32 v[86:87], v[114:115], v[124:125]
	v_mul_f32_e32 v128, v4, v22
	v_mul_f32_e32 v129, v5, v22
	v_mul_f32_e32 v130, v60, v22
	v_fma_f32 v29, v61, v22, v26
	v_mul_f32_e32 v53, v62, v22
	v_mul_f32_e32 v96, v63, v22
	v_fma_f32 v97, v84, v22, v26
	v_mul_f32_e32 v102, v85, v22
	v_fma_f32 v103, v86, v22, v26
	v_fma_f32 v29, -v128, v128, v29
	v_fma_f32 v53, -v128, v129, v53
	v_fma_f32 v96, -v128, v130, v96
	v_fma_f32 v97, -v129, v129, v97
	v_fma_f32 v102, -v129, v130, v102
	v_fma_f32 v103, -v130, v130, v103
	v_mul_f32_e32 v114, v102, v102
	v_mul_f32_e32 v115, v53, v103
	v_mul_f32_e32 v126, v96, v97
	v_mul_f32_e32 v127, v96, v96
	v_mul_f32_e32 v132, v29, v102
	v_mul_f32_e32 v133, v53, v53
	v_fma_f32 v114, v97, v103, -v114
	v_fma_f32 v115, v96, v102, -v115
	v_fma_f32 v126, v53, v102, -v126
	v_fma_f32 v127, v29, v103, -v127
	v_fma_f32 v132, v53, v96, -v132
	v_fma_f32 v133, v29, v97, -v133
	v_mul_f32_e32 v136, v29, v114
	v_fmac_f32_e32 v136, v53, v115
	v_fmac_f32_e32 v136, v96, v126
	v_rcp_f32_e32 v136, v136
	v_cmp_ne_u32_e64 vcc, s37, v17
	v_mul_f32_e32 v136, v136, v22
	v_cndmask_b32_e64 v136, 0, v136, s[30:31]
	v_cndmask_b32_e64 v29, 0, v18, vcc
	v_cndmask_b32_e64 v145, 0, v22, s[30:31]
	v_mul_f32_e32 v131, v114, v136
	v_mul_f32_e32 v140, v115, v136
	v_mul_f32_e32 v141, v126, v136
	v_mul_f32_e32 v142, v127, v136
	v_mul_f32_e32 v143, v132, v136
	v_mul_f32_e32 v144, v133, v136
	v_add_f32_e32 v146, v87, v29
	v_mov_b32_e32 v147, v17
	ds_write_b128 v23, v[128:131] offset:3072
	ds_write_b128 v23, v[140:143] offset:4096
	ds_write_b128 v23, v[144:147] offset:5120
	s_waitcnt lgkmcnt(0)
	s_barrier
	v_mov_b32_dpp v62, v36 wave_shr:1 row_mask:0xf bank_mask:0xf bound_ctrl:1
	v_mov_b32_dpp v63, v37 wave_shr:1 row_mask:0xf bank_mask:0xf bound_ctrl:1
	v_mov_b32_dpp v86, v36 wave_shl:1 row_mask:0xf bank_mask:0xf bound_ctrl:1
	v_mov_b32_dpp v87, v37 wave_shl:1 row_mask:0xf bank_mask:0xf bound_ctrl:1
	v_pk_mul_f32 v[4:5], v[36:37], v[40:41] op_sel_hi:[1,0]
	v_pk_mul_f32 v[60:61], v[36:37], v[40:41] op_sel:[0,1]
	v_pk_mul_f32 v[84:85], v[36:37], v[42:43] op_sel_hi:[1,0]
	v_pk_add_f32 v[96:97], v[36:37], v[62:63]
	v_pk_fma_f32 v[4:5], v[62:63], v[8:9], v[4:5] op_sel_hi:[1,0,1]
	v_pk_fma_f32 v[60:61], v[62:63], v[8:9], v[60:61] op_sel:[0,1,0]
	v_pk_fma_f32 v[84:85], v[62:63], v[10:11], v[84:85] op_sel_hi:[1,0,1]
	v_pk_add_f32 v[96:97], v[96:97], v[86:87]
	v_pk_fma_f32 v[4:5], v[86:87], v[80:81], v[4:5] op_sel_hi:[1,0,1]
	v_pk_fma_f32 v[60:61], v[86:87], v[80:81], v[60:61] op_sel:[0,1,0]
	v_pk_fma_f32 v[84:85], v[86:87], v[82:83], v[84:85] op_sel_hi:[1,0,1]
	v_pk_add_f32 v[62:63], v[54:55], v[96:97]
	v_pk_add_f32 v[132:133], v[110:111], v[4:5]
	v_pk_add_f32 v[136:137], v[30:31], v[60:61]
	v_pk_add_f32 v[148:149], v[38:39], v[84:85]
	v_pk_fma_f32 v[132:133], v[128:129], v[62:63], v[132:133] op_sel_hi:[0,1,1] neg_lo:[1,0,0] neg_hi:[1,0,0]
	v_pk_fma_f32 v[136:137], v[128:129], v[62:63], v[136:137] op_sel:[1,0,0] neg_lo:[1,0,0] neg_hi:[1,0,0]
	v_pk_fma_f32 v[148:149], v[130:131], v[62:63], v[148:149] op_sel_hi:[0,1,1] neg_lo:[1,0,0] neg_hi:[1,0,0]
	v_pk_mul_f32 v[30:31], v[130:131], v[132:133] op_sel:[1,0]
	v_pk_mul_f32 v[38:39], v[140:141], v[132:133] op_sel_hi:[0,1]
	v_pk_mul_f32 v[54:55], v[140:141], v[132:133] op_sel:[1,0]
	v_pk_fma_f32 v[30:31], v[140:141], v[136:137], v[30:31] op_sel_hi:[0,1,1]
	v_pk_fma_f32 v[38:39], v[142:143], v[136:137], v[38:39] op_sel_hi:[0,1,1]
	v_pk_fma_f32 v[54:55], v[142:143], v[136:137], v[54:55] op_sel:[1,0,0]
	v_pk_fma_f32 v[30:31], v[140:141], v[148:149], v[30:31] op_sel:[1,0,0]
	v_pk_fma_f32 v[38:39], v[142:143], v[148:149], v[38:39] op_sel:[1,0,0]
	v_pk_fma_f32 v[54:55], v[144:145], v[148:149], v[54:55] op_sel_hi:[0,1,1]
	v_pk_mul_f32 v[152:153], v[128:129], v[30:31] op_sel_hi:[0,1]
	v_pk_fma_f32 v[152:153], v[128:129], v[38:39], v[152:153] op_sel:[1,0,0]
	v_pk_fma_f32 v[152:153], v[130:131], v[54:55], v[152:153] op_sel_hi:[0,1,1]
	v_pk_fma_f32 v[152:153], v[144:145], v[62:63], v[152:153] op_sel:[1,0,0] neg_lo:[0,0,1] neg_hi:[0,0,1]
	v_cmp_eq_u32_e64 s[10:11], 6, v147
	v_cmp_eq_u32_e64 s[14:15], 7, v147
	v_pk_add_f32 v[62:63], v[44:45], v[30:31]
	v_pk_add_f32 v[44:45], v[92:93], v[38:39]
	v_pk_add_f32 v[86:87], v[120:121], v[54:55]
	v_pk_add_f32 v[92:93], v[138:139], v[152:153]
	v_pk_fma_f32 v[120:121], v[64:65], v[62:63], v[92:93] op_sel_hi:[0,1,1]
	v_pk_fma_f32 v[132:133], v[104:105], v[62:63], v[92:93] op_sel_hi:[0,1,1]
	v_pk_fma_f32 v[120:121], v[64:65], v[44:45], v[120:121] op_sel:[1,0,0]
	v_pk_fma_f32 v[132:133], v[104:105], v[44:45], v[132:133] op_sel:[1,0,0]
	v_pk_fma_f32 v[120:121], v[66:67], v[86:87], v[120:121] op_sel_hi:[0,1,1]
	v_pk_fma_f32 v[132:133], v[106:107], v[86:87], v[132:133] op_sel_hi:[0,1,1]
	v_pk_fma_f32 v[92:93], v[12:13], v[62:63], v[92:93] op_sel_hi:[0,1,1]
	v_pk_fma_f32 v[92:93], v[12:13], v[44:45], v[92:93] op_sel:[1,0,0]
	v_pk_fma_f32 v[92:93], v[14:15], v[86:87], v[92:93] op_sel_hi:[0,1,1]
	v_cndmask_b32_e64 v102, 0, v18, s[10:11]
	v_cndmask_b32_e64 v103, 0, v18, s[14:15]
	v_add_f32_dpp v92, v120, v92 wave_shl:1 row_mask:0xf bank_mask:0xf bound_ctrl:1
	v_add_f32_dpp v93, v121, v93 wave_shl:1 row_mask:0xf bank_mask:0xf bound_ctrl:1
	s_add_i32 s4, s34, 9
	s_cmpk_lt_i32 s4, 0x201
	s_cselect_b64 s[12:13], s[0:1], 0
	v_add_f32_dpp v92, v132, v92 wave_shr:1 row_mask:0xf bank_mask:0xf bound_ctrl:1
	v_add_f32_dpp v93, v133, v93 wave_shr:1 row_mask:0xf bank_mask:0xf bound_ctrl:1
	v_pk_fma_f32 v[92:93], v[6:7], v[146:147], v[92:93] op_sel_hi:[1,0,1] neg_lo:[0,0,1] neg_hi:[0,0,1]
	v_pk_add_f32 v[92:93], v[92:93], v[102:103] neg_lo:[0,1] neg_hi:[0,1]
	v_pk_mul_f32 v[110:111], v[92:93], v[92:93]
	v_add_f32_e32 v110, v110, v111
	v_cndmask_b32_e64 v111, 0, v110, s[12:13]
	v_add_f32_e32 v1, v1, v111
	v_mov_b32_e32 v0, v1
	s_branch .LBB0_29
.LBB0_15:
.LBB0_16:
	s_mov_b32 s27, s19
	v_mov_b32_e32 v1, 0x42c80000
	v_mov_b32_e32 v0, 0
	s_add_i32 s4, s34, -2
	s_max_i32 s4, s4, 0
	s_mul_i32 s5, s4, 0x804
	s_add_i32 s5, s5, s35
	s_add_i32 s6, s5, 0x0
	s_add_i32 s7, s5, 0x101004
	s_add_i32 s8, s5, 0x202008
	s_add_i32 s11, s5, 0x30300c
	s_add_i32 s15, s5, 0x404010
	s_mul_i32 s9, s4, 0x180c
	s_add_i32 s9, s9, s33
	buffer_load_dword v2, v28, s[16:19], s6 offen nt
	buffer_load_dword v3, v28, s[16:19], s7 offen nt
	buffer_load_dword v4, v28, s[16:19], s8 offen nt
	buffer_load_dword v5, v28, s[16:19], s11 offen nt
	buffer_load_dword v6, v28, s[16:19], s15 offen nt
	buffer_load_dwordx3 v[8:10], v27, s[24:27], s9 offen nt
	s_add_i32 s4, s34, -1
	s_max_i32 s4, s4, 0
	s_mul_i32 s5, s4, 0x804
	s_add_i32 s5, s5, s35
	s_add_i32 s6, s5, 0x0
	s_add_i32 s7, s5, 0x101004
	s_add_i32 s8, s5, 0x202008
	s_add_i32 s11, s5, 0x30300c
	s_add_i32 s15, s5, 0x404010
	s_mul_i32 s9, s4, 0x180c
	s_add_i32 s9, s9, s33
	buffer_load_dword v12, v28, s[16:19], s6 offen nt
	buffer_load_dword v13, v28, s[16:19], s7 offen nt
	buffer_load_dword v14, v28, s[16:19], s8 offen nt
	buffer_load_dword v15, v28, s[16:19], s11 offen nt
	buffer_load_dword v16, v28, s[16:19], s15 offen nt
	buffer_load_dwordx3 v[32:34], v27, s[24:27], s9 offen nt
	s_add_i32 s4, s34, 0
	s_min_i32 s4, s4, 0x200
	s_mul_i32 s5, s4, 0x804
	s_add_i32 s5, s5, s35
	s_add_i32 s6, s5, 0x0
	s_add_i32 s7, s5, 0x101004
	s_add_i32 s8, s5, 0x202008
	s_add_i32 s11, s5, 0x30300c
	s_add_i32 s15, s5, 0x404010
	s_mul_i32 s9, s4, 0x180c
	s_add_i32 s9, s9, s33
	buffer_load_dword v20, v28, s[16:19], s6 offen nt
	buffer_load_dword v21, v28, s[16:19], s7 offen nt
	buffer_load_dword v24, v28, s[16:19], s8 offen nt
	buffer_load_dword v25, v28, s[16:19], s11 offen nt
	buffer_load_dword v30, v28, s[16:19], s15 offen nt
	buffer_load_dwordx3 v[36:38], v27, s[24:27], s9 offen nt
	s_waitcnt vmcnt(12)
	v_mov_b32_dpp v40, v8 wave_shr:1 row_mask:0xf bank_mask:0xf bound_ctrl:1
	v_mov_b32_dpp v41, v9 wave_shr:1 row_mask:0xf bank_mask:0xf bound_ctrl:1
	v_mov_b32_dpp v42, v10 wave_shr:1 row_mask:0xf bank_mask:0xf bound_ctrl:1
	v_mov_b32_dpp v44, v8 wave_shl:1 row_mask:0xf bank_mask:0xf bound_ctrl:1
	v_mov_b32_dpp v45, v9 wave_shl:1 row_mask:0xf bank_mask:0xf bound_ctrl:1
	v_mov_b32_dpp v46, v10 wave_shl:1 row_mask:0xf bank_mask:0xf bound_ctrl:1
	v_mov_b32_dpp v48, v2 wave_shr:1 row_mask:0xf bank_mask:0xf bound_ctrl:1
	v_mov_b32_dpp v49, v3 wave_shr:1 row_mask:0xf bank_mask:0xf bound_ctrl:1
	v_mov_b32_dpp v50, v4 wave_shr:1 row_mask:0xf bank_mask:0xf bound_ctrl:1
	v_mov_b32_dpp v51, v5 wave_shr:1 row_mask:0xf bank_mask:0xf bound_ctrl:1
	v_mov_b32_dpp v52, v6 wave_shr:1 row_mask:0xf bank_mask:0xf bound_ctrl:1
	v_mov_b32_dpp v56, v2 wave_shl:1 row_mask:0xf bank_mask:0xf bound_ctrl:1
	v_mov_b32_dpp v57, v3 wave_shl:1 row_mask:0xf bank_mask:0xf bound_ctrl:1
	v_mov_b32_dpp v54, v4 wave_shl:1 row_mask:0xf bank_mask:0xf bound_ctrl:1
	v_mov_b32_dpp v55, v5 wave_shl:1 row_mask:0xf bank_mask:0xf bound_ctrl:1
	v_mov_b32_dpp v60, v6 wave_shl:1 row_mask:0xf bank_mask:0xf bound_ctrl:1
	v_pk_mul_f32 v[58:59], v[2:3], v[8:9] op_sel_hi:[1,0]
	v_pk_mul_f32 v[64:65], v[4:5], v[8:9] op_sel_hi:[1,0]
	v_mul_f32_e32 v62, v6, v8
	v_pk_mul_f32 v[66:67], v[2:3], v[8:9] op_sel:[0,1]
	v_pk_mul_f32 v[68:69], v[4:5], v[8:9] op_sel:[0,1]
	v_mul_f32_e32 v70, v6, v9
	v_pk_mul_f32 v[74:75], v[2:3], v[10:11] op_sel_hi:[1,0]
	v_pk_mul_f32 v[72:73], v[4:5], v[10:11] op_sel_hi:[1,0]
	v_mul_f32_e32 v78, v6, v10
	v_pk_add_f32 v[82:83], v[2:3], v[48:49]
	v_pk_add_f32 v[76:77], v[4:5], v[50:51]
	v_add_f32_e32 v86, v6, v52
	v_pk_fma_f32 v[58:59], v[48:49], v[40:41], v[58:59] op_sel_hi:[1,0,1]
	v_pk_fma_f32 v[64:65], v[50:51], v[40:41], v[64:65] op_sel_hi:[1,0,1]
	v_fmac_f32_e32 v62, v52, v40
	v_pk_fma_f32 v[66:67], v[48:49], v[40:41], v[66:67] op_sel:[0,1,0]
	v_pk_fma_f32 v[68:69], v[50:51], v[40:41], v[68:69] op_sel:[0,1,0]
	v_fmac_f32_e32 v70, v52, v41
	v_pk_fma_f32 v[74:75], v[48:49], v[42:43], v[74:75] op_sel_hi:[1,0,1]
	v_pk_fma_f32 v[72:73], v[50:51], v[42:43], v[72:73] op_sel_hi:[1,0,1]
	v_fmac_f32_e32 v78, v52, v42
	v_pk_add_f32 v[82:83], v[82:83], v[56:57]
	v_pk_add_f32 v[76:77], v[76:77], v[54:55]
	v_add_f32_e32 v86, v86, v60
	v_pk_fma_f32 v[58:59], v[56:57], v[44:45], v[58:59] op_sel_hi:[1,0,1]
	v_pk_fma_f32 v[64:65], v[54:55], v[44:45], v[64:65] op_sel_hi:[1,0,1]
	v_fmac_f32_e32 v62, v60, v44
	v_pk_fma_f32 v[66:67], v[56:57], v[44:45], v[66:67] op_sel:[0,1,0]
	v_pk_fma_f32 v[68:69], v[54:55], v[44:45], v[68:69] op_sel:[0,1,0]
	v_fmac_f32_e32 v70, v60, v45
	v_pk_fma_f32 v[74:75], v[56:57], v[46:47], v[74:75] op_sel_hi:[1,0,1]
	v_pk_fma_f32 v[72:73], v[54:55], v[46:47], v[72:73] op_sel_hi:[1,0,1]
	v_fmac_f32_e32 v78, v60, v46
	s_barrier
	s_add_i32 s4, s34, 1
	s_min_i32 s4, s4, 0x200
	s_mul_i32 s5, s4, 0x804
	s_add_i32 s5, s5, s35
	s_add_i32 s6, s5, 0x0
	s_add_i32 s7, s5, 0x101004
	s_add_i32 s8, s5, 0x202008
	s_add_i32 s11, s5, 0x30300c
	s_add_i32 s15, s5, 0x404010
	s_mul_i32 s9, s4, 0x180c
	s_add_i32 s9, s9, s33
	buffer_load_dword v48, v28, s[16:19], s6 offen nt
	buffer_load_dword v49, v28, s[16:19], s7 offen nt
	buffer_load_dword v50, v28, s[16:19], s8 offen nt
	buffer_load_dword v51, v28, s[16:19], s11 offen nt
	buffer_load_dword v52, v28, s[16:19], s15 offen nt
	buffer_load_dwordx3 v[88:90], v27, s[24:27], s9 offen nt
	s_waitcnt vmcnt(12)
	v_mov_b32_dpp v92, v32 wave_shr:1 row_mask:0xf bank_mask:0xf bound_ctrl:1
	v_mov_b32_dpp v93, v33 wave_shr:1 row_mask:0xf bank_mask:0xf bound_ctrl:1
	v_mov_b32_dpp v94, v34 wave_shr:1 row_mask:0xf bank_mask:0xf bound_ctrl:1
	v_mov_b32_dpp v96, v32 wave_shl:1 row_mask:0xf bank_mask:0xf bound_ctrl:1
	v_mov_b32_dpp v97, v33 wave_shl:1 row_mask:0xf bank_mask:0xf bound_ctrl:1
	v_mov_b32_dpp v98, v34 wave_shl:1 row_mask:0xf bank_mask:0xf bound_ctrl:1
	v_mov_b32_dpp v54, v12 wave_shr:1 row_mask:0xf bank_mask:0xf bound_ctrl:1
	v_mov_b32_dpp v55, v13 wave_shr:1 row_mask:0xf bank_mask:0xf bound_ctrl:1
	v_mov_b32_dpp v56, v14 wave_shr:1 row_mask:0xf bank_mask:0xf bound_ctrl:1
	v_mov_b32_dpp v57, v15 wave_shr:1 row_mask:0xf bank_mask:0xf bound_ctrl:1
	v_mov_b32_dpp v102, v16 wave_shr:1 row_mask:0xf bank_mask:0xf bound_ctrl:1
	v_mov_b32_dpp v106, v12 wave_shl:1 row_mask:0xf bank_mask:0xf bound_ctrl:1
	v_mov_b32_dpp v107, v13 wave_shl:1 row_mask:0xf bank_mask:0xf bound_ctrl:1
	v_mov_b32_dpp v60, v14 wave_shl:1 row_mask:0xf bank_mask:0xf bound_ctrl:1
	v_mov_b32_dpp v61, v15 wave_shl:1 row_mask:0xf bank_mask:0xf bound_ctrl:1
	v_mov_b32_dpp v110, v16 wave_shl:1 row_mask:0xf bank_mask:0xf bound_ctrl:1
	v_pk_mul_f32 v[80:81], v[12:13], v[32:33] op_sel_hi:[1,0]
	v_pk_mul_f32 v[114:115], v[14:15], v[32:33] op_sel_hi:[1,0]
	v_mul_f32_e32 v84, v16, v32
	v_pk_mul_f32 v[100:101], v[12:13], v[32:33] op_sel:[0,1]
	v_pk_mul_f32 v[118:119], v[14:15], v[32:33] op_sel:[0,1]
	v_mul_f32_e32 v104, v16, v33
	v_pk_mul_f32 v[108:109], v[12:13], v[34:35] op_sel_hi:[1,0]
	v_pk_mul_f32 v[122:123], v[14:15], v[34:35] op_sel_hi:[1,0]
	v_mul_f32_e32 v112, v16, v34
	v_pk_add_f32 v[116:117], v[12:13], v[54:55]
	v_pk_add_f32 v[126:127], v[14:15], v[56:57]
	v_add_f32_e32 v120, v16, v102
	v_pk_fma_f32 v[80:81], v[54:55], v[92:93], v[80:81] op_sel_hi:[1,0,1]
	v_pk_fma_f32 v[114:115], v[56:57], v[92:93], v[114:115] op_sel_hi:[1,0,1]
	v_fmac_f32_e32 v84, v102, v92
	v_pk_fma_f32 v[100:101], v[54:55], v[92:93], v[100:101] op_sel:[0,1,0]
	v_pk_fma_f32 v[118:119], v[56:57], v[92:93], v[118:119] op_sel:[0,1,0]
	v_fmac_f32_e32 v104, v102, v93
	v_pk_fma_f32 v[108:109], v[54:55], v[94:95], v[108:109] op_sel_hi:[1,0,1]
	v_pk_fma_f32 v[122:123], v[56:57], v[94:95], v[122:123] op_sel_hi:[1,0,1]
	v_fmac_f32_e32 v112, v102, v94
	v_pk_add_f32 v[116:117], v[116:117], v[106:107]
	v_pk_add_f32 v[126:127], v[126:127], v[60:61]
	v_add_f32_e32 v120, v120, v110
	v_pk_fma_f32 v[80:81], v[106:107], v[96:97], v[80:81] op_sel_hi:[1,0,1]
	v_pk_fma_f32 v[114:115], v[60:61], v[96:97], v[114:115] op_sel_hi:[1,0,1]
	v_fmac_f32_e32 v84, v110, v96
	v_pk_fma_f32 v[100:101], v[106:107], v[96:97], v[100:101] op_sel:[0,1,0]
	v_pk_fma_f32 v[118:119], v[60:61], v[96:97], v[118:119] op_sel:[0,1,0]
	v_fmac_f32_e32 v104, v110, v97
	v_pk_fma_f32 v[108:109], v[106:107], v[98:99], v[108:109] op_sel_hi:[1,0,1]
	v_pk_fma_f32 v[122:123], v[60:61], v[98:99], v[122:123] op_sel_hi:[1,0,1]
	v_fmac_f32_e32 v112, v110, v98
	s_barrier
	s_add_i32 s4, s34, 2
	s_min_i32 s4, s4, 0x200
	s_mul_i32 s5, s4, 0x804
	s_add_i32 s5, s5, s35
	s_add_i32 s6, s5, 0x0
	s_add_i32 s7, s5, 0x101004
	s_add_i32 s8, s5, 0x202008
	s_add_i32 s11, s5, 0x30300c
	s_add_i32 s15, s5, 0x404010
	s_mul_i32 s9, s4, 0x180c
	s_add_i32 s9, s9, s33
	buffer_load_dword v54, v28, s[16:19], s6 offen nt
	buffer_load_dword v55, v28, s[16:19], s7 offen nt
	buffer_load_dword v56, v28, s[16:19], s8 offen nt
	buffer_load_dword v57, v28, s[16:19], s11 offen nt
	buffer_load_dword v60, v28, s[16:19], s15 offen nt
	buffer_load_dwordx3 v[128:130], v27, s[24:27], s9 offen nt
	s_waitcnt vmcnt(12)
	v_mov_b32_dpp v132, v36 wave_shr:1 row_mask:0xf bank_mask:0xf bound_ctrl:1
	v_mov_b32_dpp v133, v37 wave_shr:1 row_mask:0xf bank_mask:0xf bound_ctrl:1
	v_mov_b32_dpp v134, v38 wave_shr:1 row_mask:0xf bank_mask:0xf bound_ctrl:1
	v_mov_b32_dpp v136, v36 wave_shl:1 row_mask:0xf bank_mask:0xf bound_ctrl:1
	v_mov_b32_dpp v137, v37 wave_shl:1 row_mask:0xf bank_mask:0xf bound_ctrl:1
	v_mov_b32_dpp v138, v38 wave_shl:1 row_mask:0xf bank_mask:0xf bound_ctrl:1
	v_mov_b32_dpp v102, v20 wave_shr:1 row_mask:0xf bank_mask:0xf bound_ctrl:1
	v_mov_b32_dpp v103, v21 wave_shr:1 row_mask:0xf bank_mask:0xf bound_ctrl:1
	v_mov_b32_dpp v106, v24 wave_shr:1 row_mask:0xf bank_mask:0xf bound_ctrl:1
	v_mov_b32_dpp v107, v25 wave_shr:1 row_mask:0xf bank_mask:0xf bound_ctrl:1
	v_mov_b32_dpp v124, v30 wave_shr:1 row_mask:0xf bank_mask:0xf bound_ctrl:1
	v_mov_b32_dpp v110, v20 wave_shl:1 row_mask:0xf bank_mask:0xf bound_ctrl:1
	v_mov_b32_dpp v111, v21 wave_shl:1 row_mask:0xf bank_mask:0xf bound_ctrl:1
	v_mov_b32_dpp v142, v24 wave_shl:1 row_mask:0xf bank_mask:0xf bound_ctrl:1
	v_mov_b32_dpp v143, v25 wave_shl:1 row_mask:0xf bank_mask:0xf bound_ctrl:1
	v_mov_b32_dpp v140, v30 wave_shl:1 row_mask:0xf bank_mask:0xf bound_ctrl:1
	v_pk_mul_f32 v[144:145], v[20:21], v[36:37] op_sel_hi:[1,0]
	v_pk_mul_f32 v[148:149], v[24:25], v[36:37] op_sel_hi:[1,0]
	v_mul_f32_e32 v146, v30, v36
	v_pk_mul_f32 v[152:153], v[20:21], v[36:37] op_sel:[0,1]
	v_pk_mul_f32 v[156:157], v[24:25], v[36:37] op_sel:[0,1]
	v_mul_f32_e32 v150, v30, v37
	v_pk_mul_f32 v[160:161], v[20:21], v[38:39] op_sel_hi:[1,0]
	v_pk_mul_f32 v[164:165], v[24:25], v[38:39] op_sel_hi:[1,0]
	v_mul_f32_e32 v154, v30, v38
	v_pk_add_f32 v[168:169], v[20:21], v[102:103]
	v_pk_add_f32 v[172:173], v[24:25], v[106:107]
	v_add_f32_e32 v158, v30, v124
	v_pk_fma_f32 v[144:145], v[102:103], v[132:133], v[144:145] op_sel_hi:[1,0,1]
	v_pk_fma_f32 v[148:149], v[106:107], v[132:133], v[148:149] op_sel_hi:[1,0,1]
	v_fmac_f32_e32 v146, v124, v132
	v_pk_fma_f32 v[152:153], v[102:103], v[132:133], v[152:153] op_sel:[0,1,0]
	v_pk_fma_f32 v[156:157], v[106:107], v[132:133], v[156:157] op_sel:[0,1,0]
	v_fmac_f32_e32 v150, v124, v133
	v_pk_fma_f32 v[160:161], v[102:103], v[134:135], v[160:161] op_sel_hi:[1,0,1]
	v_pk_fma_f32 v[164:165], v[106:107], v[134:135], v[164:165] op_sel_hi:[1,0,1]
	v_fmac_f32_e32 v154, v124, v134
	v_pk_add_f32 v[168:169], v[168:169], v[110:111]
	v_pk_add_f32 v[172:173], v[172:173], v[142:143]
	v_add_f32_e32 v158, v158, v140
	v_pk_fma_f32 v[144:145], v[110:111], v[136:137], v[144:145] op_sel_hi:[1,0,1]
	v_pk_fma_f32 v[148:149], v[142:143], v[136:137], v[148:149] op_sel_hi:[1,0,1]
	v_fmac_f32_e32 v146, v140, v136
	v_pk_fma_f32 v[152:153], v[110:111], v[136:137], v[152:153] op_sel:[0,1,0]
	v_pk_fma_f32 v[156:157], v[142:143], v[136:137], v[156:157] op_sel:[0,1,0]
	v_fmac_f32_e32 v150, v140, v137
	v_pk_fma_f32 v[160:161], v[110:111], v[138:139], v[160:161] op_sel_hi:[1,0,1]
	v_pk_fma_f32 v[164:165], v[142:143], v[138:139], v[164:165] op_sel_hi:[1,0,1]
	v_fmac_f32_e32 v154, v140, v138
	s_barrier
	ds_read_b128 v[140:143], v23 offset:0
	ds_read_b128 v[176:179], v23 offset:1024
	ds_read_b128 v[180:183], v23 offset:2048
	v_pk_add_f32 v[124:125], v[116:117], v[168:169]
	v_pk_add_f32 v[102:103], v[82:83], v[124:125]
	v_pk_add_f32 v[82:83], v[126:127], v[172:173]
	v_pk_add_f32 v[106:107], v[76:77], v[82:83]
	v_add_f32_e32 v76, v120, v158
	v_add_f32_e32 v110, v86, v76
	v_pk_add_f32 v[116:117], v[80:81], v[144:145]
	v_pk_add_f32 v[120:121], v[58:59], v[116:117]
	v_pk_add_f32 v[58:59], v[114:115], v[148:149]
	v_pk_add_f32 v[80:81], v[64:65], v[58:59]
	v_add_f32_e32 v64, v84, v146
	v_add_f32_e32 v184, v62, v64
	v_pk_add_f32 v[84:85], v[100:101], v[152:153]
	v_pk_add_f32 v[188:189], v[66:67], v[84:85]
	v_pk_add_f32 v[62:63], v[118:119], v[156:157]
	v_pk_add_f32 v[100:101], v[68:69], v[62:63]
	v_add_f32_e32 v68, v104, v150
	v_add_f32_e32 v192, v70, v68
	v_pk_add_f32 v[104:105], v[108:109], v[160:161]
	v_pk_add_f32 v[196:197], v[74:75], v[104:105]
	v_pk_add_f32 v[66:67], v[122:123], v[164:165]
	v_pk_add_f32 v[108:109], v[72:73], v[66:67]
	v_add_f32_e32 v72, v112, v154
	v_add_f32_e32 v200, v78, v72
	s_waitcnt lgkmcnt(2)
	v_pk_fma_f32 v[120:121], v[140:141], v[102:103], v[120:121] op_sel_hi:[0,1,1] neg_lo:[1,0,0] neg_hi:[1,0,0]
	v_pk_fma_f32 v[80:81], v[140:141], v[106:107], v[80:81] op_sel_hi:[0,1,1] neg_lo:[1,0,0] neg_hi:[1,0,0]
	v_fma_f32 v184, -v140, v110, v184
	v_pk_fma_f32 v[188:189], v[140:141], v[102:103], v[188:189] op_sel:[1,0,0] neg_lo:[1,0,0] neg_hi:[1,0,0]
	v_pk_fma_f32 v[100:101], v[140:141], v[106:107], v[100:101] op_sel:[1,0,0] neg_lo:[1,0,0] neg_hi:[1,0,0]
	v_fma_f32 v192, -v141, v110, v192
	v_pk_fma_f32 v[196:197], v[142:143], v[102:103], v[196:197] op_sel_hi:[0,1,1] neg_lo:[1,0,0] neg_hi:[1,0,0]
	v_pk_fma_f32 v[108:109], v[142:143], v[106:107], v[108:109] op_sel_hi:[0,1,1] neg_lo:[1,0,0] neg_hi:[1,0,0]
	v_fma_f32 v200, -v142, v110, v200
	v_pk_mul_f32 v[70:71], v[142:143], v[120:121] op_sel:[1,0]
	v_pk_mul_f32 v[86:87], v[142:143], v[80:81] op_sel:[1,0]
	v_mul_f32_e32 v122, v143, v184
	s_waitcnt lgkmcnt(1)
	v_pk_mul_f32 v[74:75], v[176:177], v[120:121] op_sel_hi:[0,1]
	v_pk_mul_f32 v[114:115], v[176:177], v[80:81] op_sel_hi:[0,1]
	v_mul_f32_e32 v126, v176, v184
	v_pk_mul_f32 v[78:79], v[176:177], v[120:121] op_sel:[1,0]
	v_pk_mul_f32 v[118:119], v[176:177], v[80:81] op_sel:[1,0]
	v_mul_f32_e32 v162, v177, v184
	v_pk_fma_f32 v[70:71], v[176:177], v[188:189], v[70:71] op_sel_hi:[0,1,1]
	v_pk_fma_f32 v[86:87], v[176:177], v[100:101], v[86:87] op_sel_hi:[0,1,1]
	v_fmac_f32_e32 v122, v176, v192
	v_pk_fma_f32 v[74:75], v[178:179], v[188:189], v[74:75] op_sel_hi:[0,1,1]
	v_pk_fma_f32 v[114:115], v[178:179], v[100:101], v[114:115] op_sel_hi:[0,1,1]
	v_fmac_f32_e32 v126, v178, v192
	v_pk_fma_f32 v[78:79], v[178:179], v[188:189], v[78:79] op_sel:[1,0,0]
	v_pk_fma_f32 v[118:119], v[178:179], v[100:101], v[118:119] op_sel:[1,0,0]
	v_fmac_f32_e32 v162, v179, v192
	v_pk_fma_f32 v[70:71], v[176:177], v[196:197], v[70:71] op_sel:[1,0,0]
	v_pk_fma_f32 v[86:87], v[176:177], v[108:109], v[86:87] op_sel:[1,0,0]
	v_fmac_f32_e32 v122, v177, v200
	v_pk_fma_f32 v[74:75], v[178:179], v[196:197], v[74:75] op_sel:[1,0,0]
	v_pk_fma_f32 v[114:115], v[178:179], v[108:109], v[114:115] op_sel:[1,0,0]
	v_fmac_f32_e32 v126, v179, v200
	s_waitcnt lgkmcnt(0)
	v_pk_fma_f32 v[78:79], v[180:181], v[196:197], v[78:79] op_sel_hi:[0,1,1]
	v_pk_fma_f32 v[118:119], v[180:181], v[108:109], v[118:119] op_sel_hi:[0,1,1]
	v_fmac_f32_e32 v162, v180, v200
	v_pk_mul_f32 v[112:113], v[140:141], v[70:71] op_sel_hi:[0,1]
	v_pk_mul_f32 v[204:205], v[140:141], v[86:87] op_sel_hi:[0,1]
	v_mul_f32_e32 v208, v140, v122
	v_pk_fma_f32 v[112:113], v[140:141], v[74:75], v[112:113] op_sel:[1,0,0]
	v_pk_fma_f32 v[204:205], v[140:141], v[114:115], v[204:205] op_sel:[1,0,0]
	v_fmac_f32_e32 v208, v141, v126
	v_pk_fma_f32 v[112:113], v[142:143], v[78:79], v[112:113] op_sel_hi:[0,1,1]
	v_pk_fma_f32 v[204:205], v[142:143], v[118:119], v[204:205] op_sel_hi:[0,1,1]
	v_fmac_f32_e32 v208, v142, v162
	v_pk_fma_f32 v[112:113], v[180:181], v[102:103], v[112:113] op_sel:[1,0,0] neg_lo:[0,0,1] neg_hi:[0,0,1]
	v_pk_fma_f32 v[204:205], v[180:181], v[106:107], v[204:205] op_sel:[1,0,0] neg_lo:[0,0,1] neg_hi:[0,0,1]
	v_fma_f32 v208, v181, v110, -v208
	s_add_i32 s4, s34, 3
	s_min_i32 s4, s4, 0x200
	s_mul_i32 s5, s4, 0x804
	s_add_i32 s5, s5, s35
	s_add_i32 s6, s5, 0x0
	s_add_i32 s7, s5, 0x101004
	s_add_i32 s8, s5, 0x202008
	s_add_i32 s11, s5, 0x30300c
	s_add_i32 s15, s5, 0x404010
	s_mul_i32 s9, s4, 0x180c
	s_add_i32 s9, s9, s33
	buffer_load_dword v2, v28, s[16:19], s6 offen nt
	buffer_load_dword v3, v28, s[16:19], s7 offen nt
	buffer_load_dword v4, v28, s[16:19], s8 offen nt
	buffer_load_dword v5, v28, s[16:19], s11 offen nt
	buffer_load_dword v6, v28, s[16:19], s15 offen nt
	buffer_load_dwordx3 v[8:10], v27, s[24:27], s9 offen nt
	s_waitcnt vmcnt(12)
	v_mov_b32_dpp v40, v88 wave_shr:1 row_mask:0xf bank_mask:0xf bound_ctrl:1
	v_mov_b32_dpp v41, v89 wave_shr:1 row_mask:0xf bank_mask:0xf bound_ctrl:1
	v_mov_b32_dpp v42, v90 wave_shr:1 row_mask:0xf bank_mask:0xf bound_ctrl:1
	v_mov_b32_dpp v44, v88 wave_shl:1 row_mask:0xf bank_mask:0xf bound_ctrl:1
	v_mov_b32_dpp v45, v89 wave_shl:1 row_mask:0xf bank_mask:0xf bound_ctrl:1
	v_mov_b32_dpp v46, v90 wave_shl:1 row_mask:0xf bank_mask:0xf bound_ctrl:1
	v_mov_b32_dpp v102, v48 wave_shr:1 row_mask:0xf bank_mask:0xf bound_ctrl:1
	v_mov_b32_dpp v103, v49 wave_shr:1 row_mask:0xf bank_mask:0xf bound_ctrl:1
	v_mov_b32_dpp v80, v50 wave_shr:1 row_mask:0xf bank_mask:0xf bound_ctrl:1
	v_mov_b32_dpp v81, v51 wave_shr:1 row_mask:0xf bank_mask:0xf bound_ctrl:1
	v_mov_b32_dpp v106, v52 wave_shr:1 row_mask:0xf bank_mask:0xf bound_ctrl:1
	v_mov_b32_dpp v110, v48 wave_shl:1 row_mask:0xf bank_mask:0xf bound_ctrl:1
	v_mov_b32_dpp v111, v49 wave_shl:1 row_mask:0xf bank_mask:0xf bound_ctrl:1
	v_mov_b32_dpp v100, v50 wave_shl:1 row_mask:0xf bank_mask:0xf bound_ctrl:1
	v_mov_b32_dpp v101, v51 wave_shl:1 row_mask:0xf bank_mask:0xf bound_ctrl:1
	v_mov_b32_dpp v142, v52 wave_shl:1 row_mask:0xf bank_mask:0xf bound_ctrl:1
	v_pk_mul_f32 v[108:109], v[48:49], v[88:89] op_sel_hi:[1,0]
	v_pk_mul_f32 v[166:167], v[50:51], v[88:89] op_sel_hi:[1,0]
	v_mul_f32_e32 v120, v52, v88
	v_pk_mul_f32 v[140:141], v[48:49], v[88:89] op_sel:[0,1]
	v_pk_mul_f32 v[170:171], v[50:51], v[88:89] op_sel:[0,1]
	v_mul_f32_e32 v176, v52, v89
	v_pk_mul_f32 v[180:181], v[48:49], v[90:91] op_sel_hi:[1,0]
	v_pk_mul_f32 v[174:175], v[50:51], v[90:91] op_sel_hi:[1,0]
	v_mul_f32_e32 v184, v52, v90
	v_pk_add_f32 v[188:189], v[48:49], v[102:103]
	v_pk_add_f32 v[178:179], v[50:51], v[80:81]
	v_add_f32_e32 v192, v52, v106
	v_pk_fma_f32 v[108:109], v[102:103], v[40:41], v[108:109] op_sel_hi:[1,0,1]
	v_pk_fma_f32 v[166:167], v[80:81], v[40:41], v[166:167] op_sel_hi:[1,0,1]
	v_fmac_f32_e32 v120, v106, v40
	v_pk_fma_f32 v[140:141], v[102:103], v[40:41], v[140:141] op_sel:[0,1,0]
	v_pk_fma_f32 v[170:171], v[80:81], v[40:41], v[170:171] op_sel:[0,1,0]
	v_fmac_f32_e32 v176, v106, v41
	v_pk_fma_f32 v[180:181], v[102:103], v[42:43], v[180:181] op_sel_hi:[1,0,1]
	v_pk_fma_f32 v[174:175], v[80:81], v[42:43], v[174:175] op_sel_hi:[1,0,1]
	v_fmac_f32_e32 v184, v106, v42
	v_pk_add_f32 v[188:189], v[188:189], v[110:111]
	v_pk_add_f32 v[178:179], v[178:179], v[100:101]
	v_add_f32_e32 v192, v192, v142
	v_pk_fma_f32 v[108:109], v[110:111], v[44:45], v[108:109] op_sel_hi:[1,0,1]
	v_pk_fma_f32 v[166:167], v[100:101], v[44:45], v[166:167] op_sel_hi:[1,0,1]
	v_fmac_f32_e32 v120, v142, v44
	v_pk_fma_f32 v[140:141], v[110:111], v[44:45], v[140:141] op_sel:[0,1,0]
	v_pk_fma_f32 v[170:171], v[100:101], v[44:45], v[170:171] op_sel:[0,1,0]
	v_fmac_f32_e32 v176, v142, v45
	v_pk_fma_f32 v[180:181], v[110:111], v[46:47], v[180:181] op_sel_hi:[1,0,1]
	v_pk_fma_f32 v[174:175], v[100:101], v[46:47], v[174:175] op_sel_hi:[1,0,1]
	v_fmac_f32_e32 v184, v142, v46
	s_barrier
	ds_read_b128 v[100:103], v23 offset:3072
	ds_read_b128 v[196:199], v23 offset:4096
	ds_read_b128 v[200:203], v23 offset:5120
	v_pk_add_f32 v[80:81], v[124:125], v[188:189]
	v_pk_add_f32 v[106:107], v[82:83], v[178:179]
	v_add_f32_e32 v82, v76, v192
	v_pk_add_f32 v[110:111], v[116:117], v[108:109]
	v_pk_add_f32 v[76:77], v[58:59], v[166:167]
	v_add_f32_e32 v116, v64, v120
	v_pk_add_f32 v[58:59], v[84:85], v[140:141]
	v_pk_add_f32 v[64:65], v[62:63], v[170:171]
	v_add_f32_e32 v84, v68, v176
	v_pk_add_f32 v[62:63], v[104:105], v[180:181]
	v_pk_add_f32 v[68:69], v[66:67], v[174:175]
	v_add_f32_e32 v104, v72, v184
	s_waitcnt lgkmcnt(2)
	v_pk_fma_f32 v[110:111], v[100:101], v[80:81], v[110:111] op_sel_hi:[0,1,1] neg_lo:[1,0,0] neg_hi:[1,0,0]
	v_pk_fma_f32 v[76:77], v[100:101], v[106:107], v[76:77] op_sel_hi:[0,1,1] neg_lo:[1,0,0] neg_hi:[1,0,0]
	v_fma_f32 v116, -v100, v82, v116
	v_pk_fma_f32 v[58:59], v[100:101], v[80:81], v[58:59] op_sel:[1,0,0] neg_lo:[1,0,0] neg_hi:[1,0,0]
	v_pk_fma_f32 v[64:65], v[100:101], v[106:107], v[64:65] op_sel:[1,0,0] neg_lo:[1,0,0] neg_hi:[1,0,0]
	v_fma_f32 v84, -v101, v82, v84
	v_pk_fma_f32 v[62:63], v[102:103], v[80:81], v[62:63] op_sel_hi:[0,1,1] neg_lo:[1,0,0] neg_hi:[1,0,0]
	v_pk_fma_f32 v[68:69], v[102:103], v[106:107], v[68:69] op_sel_hi:[0,1,1] neg_lo:[1,0,0] neg_hi:[1,0,0]
	v_fma_f32 v104, -v102, v82, v104
	v_pk_mul_f32 v[72:73], v[102:103], v[110:111] op_sel:[1,0]
	v_pk_mul_f32 v[66:67], v[102:103], v[76:77] op_sel:[1,0]
	v_mul_f32_e32 v186, v103, v116
	s_waitcnt lgkmcnt(1)
	v_pk_mul_f32 v[124:125], v[196:197], v[110:111] op_sel_hi:[0,1]
	v_pk_mul_f32 v[142:143], v[196:197], v[76:77] op_sel_hi:[0,1]
	v_mul_f32_e32 v190, v196, v116
	v_pk_mul_f32 v[212:213], v[196:197], v[110:111] op_sel:[1,0]
	v_pk_mul_f32 v[182:183], v[196:197], v[76:77] op_sel:[1,0]
	v_mul_f32_e32 v194, v197, v116
	v_pk_fma_f32 v[72:73], v[196:197], v[58:59], v[72:73] op_sel_hi:[0,1,1]
	v_pk_fma_f32 v[66:67], v[196:197], v[64:65], v[66:67] op_sel_hi:[0,1,1]
	v_fmac_f32_e32 v186, v196, v84
	v_pk_fma_f32 v[124:125], v[198:199], v[58:59], v[124:125] op_sel_hi:[0,1,1]
	v_pk_fma_f32 v[142:143], v[198:199], v[64:65], v[142:143] op_sel_hi:[0,1,1]
	v_fmac_f32_e32 v190, v198, v84
	v_pk_fma_f32 v[212:213], v[198:199], v[58:59], v[212:213] op_sel:[1,0,0]
	v_pk_fma_f32 v[182:183], v[198:199], v[64:65], v[182:183] op_sel:[1,0,0]
	v_fmac_f32_e32 v194, v199, v84
	v_pk_fma_f32 v[72:73], v[196:197], v[62:63], v[72:73] op_sel:[1,0,0]
	v_pk_fma_f32 v[66:67], v[196:197], v[68:69], v[66:67] op_sel:[1,0,0]
	v_fmac_f32_e32 v186, v197, v104
	v_pk_fma_f32 v[124:125], v[198:199], v[62:63], v[124:125] op_sel:[1,0,0]
	v_pk_fma_f32 v[142:143], v[198:199], v[68:69], v[142:143] op_sel:[1,0,0]
	v_fmac_f32_e32 v190, v199, v104
	s_waitcnt lgkmcnt(0)
	v_pk_fma_f32 v[212:213], v[200:201], v[62:63], v[212:213] op_sel_hi:[0,1,1]
	v_pk_fma_f32 v[182:183], v[200:201], v[68:69], v[182:183] op_sel_hi:[0,1,1]
	v_fmac_f32_e32 v194, v200, v104
	v_pk_mul_f32 v[206:207], v[100:101], v[72:73] op_sel_hi:[0,1]
	v_pk_mul_f32 v[216:217], v[100:101], v[66:67] op_sel_hi:[0,1]
	v_mul_f32_e32 v220, v100, v186
	v_pk_fma_f32 v[206:207], v[100:101], v[124:125], v[206:207] op_sel:[1,0,0]
	v_pk_fma_f32 v[216:217], v[100:101], v[142:143], v[216:217] op_sel:[1,0,0]
	v_fmac_f32_e32 v220, v101, v190
	v_pk_fma_f32 v[206:207], v[102:103], v[212:213], v[206:207] op_sel_hi:[0,1,1]
	v_pk_fma_f32 v[216:217], v[102:103], v[182:183], v[216:217] op_sel_hi:[0,1,1]
	v_fmac_f32_e32 v220, v102, v194
	v_pk_fma_f32 v[206:207], v[200:201], v[80:81], v[206:207] op_sel:[1,0,0] neg_lo:[0,0,1] neg_hi:[0,0,1]
	v_pk_fma_f32 v[216:217], v[200:201], v[106:107], v[216:217] op_sel:[1,0,0] neg_lo:[0,0,1] neg_hi:[0,0,1]
	v_fma_f32 v220, v201, v82, -v220
	s_add_i32 s4, s34, 4
	s_min_i32 s4, s4, 0x200
	s_mul_i32 s5, s4, 0x804
	s_add_i32 s5, s5, s35
	s_add_i32 s6, s5, 0x0
	s_add_i32 s7, s5, 0x101004
	s_add_i32 s8, s5, 0x202008
	s_add_i32 s11, s5, 0x30300c
	s_add_i32 s15, s5, 0x404010
	s_mul_i32 s9, s4, 0x180c
	s_add_i32 s9, s9, s33
	buffer_load_dword v12, v28, s[16:19], s6 offen nt
	buffer_load_dword v13, v28, s[16:19], s7 offen nt
	buffer_load_dword v14, v28, s[16:19], s8 offen nt
	buffer_load_dword v15, v28, s[16:19], s11 offen nt
	buffer_load_dword v16, v28, s[16:19], s15 offen nt
	buffer_load_dwordx3 v[32:34], v27, s[24:27], s9 offen nt
	s_waitcnt vmcnt(12)
	v_mov_b32_dpp v80, v128 wave_shr:1 row_mask:0xf bank_mask:0xf bound_ctrl:1
	v_mov_b32_dpp v81, v129 wave_shr:1 row_mask:0xf bank_mask:0xf bound_ctrl:1
	v_mov_b32_dpp v82, v130 wave_shr:1 row_mask:0xf bank_mask:0xf bound_ctrl:1
	v_mov_b32_dpp v92, v128 wave_shl:1 row_mask:0xf bank_mask:0xf bound_ctrl:1
	v_mov_b32_dpp v93, v129 wave_shl:1 row_mask:0xf bank_mask:0xf bound_ctrl:1
	v_mov_b32_dpp v94, v130 wave_shl:1 row_mask:0xf bank_mask:0xf bound_ctrl:1
	v_mov_b32_dpp v64, v54 wave_shr:1 row_mask:0xf bank_mask:0xf bound_ctrl:1
	v_mov_b32_dpp v65, v55 wave_shr:1 row_mask:0xf bank_mask:0xf bound_ctrl:1
	v_mov_b32_dpp v58, v56 wave_shr:1 row_mask:0xf bank_mask:0xf bound_ctrl:1
	v_mov_b32_dpp v59, v57 wave_shr:1 row_mask:0xf bank_mask:0xf bound_ctrl:1
	v_mov_b32_dpp v62, v60 wave_shr:1 row_mask:0xf bank_mask:0xf bound_ctrl:1
	v_mov_b32_dpp v68, v54 wave_shl:1 row_mask:0xf bank_mask:0xf bound_ctrl:1
	v_mov_b32_dpp v69, v55 wave_shl:1 row_mask:0xf bank_mask:0xf bound_ctrl:1
	v_mov_b32_dpp v98, v56 wave_shl:1 row_mask:0xf bank_mask:0xf bound_ctrl:1
	v_mov_b32_dpp v99, v57 wave_shl:1 row_mask:0xf bank_mask:0xf bound_ctrl:1
	v_mov_b32_dpp v102, v60 wave_shl:1 row_mask:0xf bank_mask:0xf bound_ctrl:1
	v_pk_mul_f32 v[106:107], v[54:55], v[128:129] op_sel_hi:[1,0]
	v_pk_mul_f32 v[76:77], v[56:57], v[128:129] op_sel_hi:[1,0]
	v_mul_f32_e32 v84, v60, v128
	v_pk_mul_f32 v[110:111], v[54:55], v[128:129] op_sel:[0,1]
	v_pk_mul_f32 v[96:97], v[56:57], v[128:129] op_sel:[0,1]
	v_mul_f32_e32 v100, v60, v129
	v_pk_mul_f32 v[198:199], v[54:55], v[130:131] op_sel_hi:[1,0]
	v_pk_mul_f32 v[104:105], v[56:57], v[130:131] op_sel_hi:[1,0]
	v_mul_f32_e32 v116, v60, v130
	v_pk_add_f32 v[202:203], v[54:55], v[64:65]
	v_pk_add_f32 v[196:197], v[56:57], v[58:59]
	v_add_f32_e32 v200, v60, v62
	v_pk_fma_f32 v[106:107], v[64:65], v[80:81], v[106:107] op_sel_hi:[1,0,1]
	v_pk_fma_f32 v[76:77], v[58:59], v[80:81], v[76:77] op_sel_hi:[1,0,1]
	v_fmac_f32_e32 v84, v62, v80
	v_pk_fma_f32 v[110:111], v[64:65], v[80:81], v[110:111] op_sel:[0,1,0]
	v_pk_fma_f32 v[96:97], v[58:59], v[80:81], v[96:97] op_sel:[0,1,0]
	v_fmac_f32_e32 v100, v62, v81
	v_pk_fma_f32 v[198:199], v[64:65], v[82:83], v[198:199] op_sel_hi:[1,0,1]
	v_pk_fma_f32 v[104:105], v[58:59], v[82:83], v[104:105] op_sel_hi:[1,0,1]
	v_fmac_f32_e32 v116, v62, v82
	v_pk_add_f32 v[202:203], v[202:203], v[68:69]
	v_pk_add_f32 v[196:197], v[196:197], v[98:99]
	v_add_f32_e32 v200, v200, v102
	v_pk_fma_f32 v[106:107], v[68:69], v[92:93], v[106:107] op_sel_hi:[1,0,1]
	v_pk_fma_f32 v[76:77], v[98:99], v[92:93], v[76:77] op_sel_hi:[1,0,1]
	v_fmac_f32_e32 v84, v102, v92
	v_pk_fma_f32 v[110:111], v[68:69], v[92:93], v[110:111] op_sel:[0,1,0]
	v_pk_fma_f32 v[96:97], v[98:99], v[92:93], v[96:97] op_sel:[0,1,0]
	v_fmac_f32_e32 v100, v102, v93
	v_pk_fma_f32 v[198:199], v[68:69], v[94:95], v[198:199] op_sel_hi:[1,0,1]
	v_pk_fma_f32 v[104:105], v[98:99], v[94:95], v[104:105] op_sel_hi:[1,0,1]
	v_fmac_f32_e32 v116, v102, v94
	s_barrier
	ds_read_b128 v[224:227], v23 offset:0
	ds_read_b128 v[228:231], v23 offset:1024
	ds_read_b128 v[232:235], v23 offset:2048
	v_pk_add_f32 v[58:59], v[188:189], v[202:203]
	v_pk_add_f32 v[62:63], v[168:169], v[58:59]
	v_pk_add_f32 v[98:99], v[178:179], v[196:197]
	v_pk_add_f32 v[64:65], v[172:173], v[98:99]
	v_add_f32_e32 v68, v192, v200
	v_add_f32_e32 v102, v158, v68
	v_pk_add_f32 v[158:159], v[108:109], v[106:107]
	v_pk_add_f32 v[168:169], v[144:145], v[158:159]
	v_pk_add_f32 v[178:179], v[166:167], v[76:77]
	v_pk_add_f32 v[210:211], v[148:149], v[178:179]
	v_add_f32_e32 v108, v120, v84
	v_add_f32_e32 v144, v146, v108
	v_pk_add_f32 v[146:147], v[140:141], v[110:111]
	v_pk_add_f32 v[120:121], v[152:153], v[146:147]
	v_pk_add_f32 v[166:167], v[170:171], v[96:97]
	v_pk_add_f32 v[214:215], v[156:157], v[166:167]
	v_add_f32_e32 v140, v176, v100
	v_add_f32_e32 v148, v150, v140
	v_pk_add_f32 v[150:151], v[180:181], v[198:199]
	v_pk_add_f32 v[152:153], v[160:161], v[150:151]
	v_pk_add_f32 v[170:171], v[174:175], v[104:105]
	v_pk_add_f32 v[218:219], v[164:165], v[170:171]
	v_add_f32_e32 v156, v184, v116
	v_add_f32_e32 v160, v154, v156
	s_waitcnt lgkmcnt(2)
	v_pk_fma_f32 v[168:169], v[224:225], v[62:63], v[168:169] op_sel_hi:[0,1,1] neg_lo:[1,0,0] neg_hi:[1,0,0]
	v_pk_fma_f32 v[210:211], v[224:225], v[64:65], v[210:211] op_sel_hi:[0,1,1] neg_lo:[1,0,0] neg_hi:[1,0,0]
	v_fma_f32 v144, -v224, v102, v144
	v_pk_fma_f32 v[120:121], v[224:225], v[62:63], v[120:121] op_sel:[1,0,0] neg_lo:[1,0,0] neg_hi:[1,0,0]
	v_pk_fma_f32 v[214:215], v[224:225], v[64:65], v[214:215] op_sel:[1,0,0] neg_lo:[1,0,0] neg_hi:[1,0,0]
	v_fma_f32 v148, -v225, v102, v148
	v_pk_fma_f32 v[152:153], v[226:227], v[62:63], v[152:153] op_sel_hi:[0,1,1] neg_lo:[1,0,0] neg_hi:[1,0,0]
	v_pk_fma_f32 v[218:219], v[226:227], v[64:65], v[218:219] op_sel_hi:[0,1,1] neg_lo:[1,0,0] neg_hi:[1,0,0]
	v_fma_f32 v160, -v226, v102, v160
	v_pk_mul_f32 v[154:155], v[226:227], v[168:169] op_sel:[1,0]
	v_pk_mul_f32 v[164:165], v[226:227], v[210:211] op_sel:[1,0]
	v_mul_f32_e32 v238, v227, v144
	s_waitcnt lgkmcnt(1)
	v_pk_mul_f32 v[174:175], v[228:229], v[168:169] op_sel_hi:[0,1]
	v_pk_mul_f32 v[172:173], v[228:229], v[210:211] op_sel_hi:[0,1]
	v_mul_f32_e32 v242, v228, v144
	v_pk_mul_f32 v[222:223], v[228:229], v[168:169] op_sel:[1,0]
	v_pk_mul_f32 v[176:177], v[228:229], v[210:211] op_sel:[1,0]
	v_mul_f32_e32 v246, v229, v144
	v_pk_fma_f32 v[154:155], v[228:229], v[120:121], v[154:155] op_sel_hi:[0,1,1]
	v_pk_fma_f32 v[164:165], v[228:229], v[214:215], v[164:165] op_sel_hi:[0,1,1]
	v_fmac_f32_e32 v238, v228, v148
	v_pk_fma_f32 v[174:175], v[230:231], v[120:121], v[174:175] op_sel_hi:[0,1,1]
	v_pk_fma_f32 v[172:173], v[230:231], v[214:215], v[172:173] op_sel_hi:[0,1,1]
	v_fmac_f32_e32 v242, v230, v148
	v_pk_fma_f32 v[222:223], v[230:231], v[120:121], v[222:223] op_sel:[1,0,0]
	v_pk_fma_f32 v[176:177], v[230:231], v[214:215], v[176:177] op_sel:[1,0,0]
	v_fmac_f32_e32 v246, v231, v148
	v_pk_fma_f32 v[154:155], v[228:229], v[152:153], v[154:155] op_sel:[1,0,0]
	v_pk_fma_f32 v[164:165], v[228:229], v[218:219], v[164:165] op_sel:[1,0,0]
	v_fmac_f32_e32 v238, v229, v160
	v_pk_fma_f32 v[174:175], v[230:231], v[152:153], v[174:175] op_sel:[1,0,0]
	v_pk_fma_f32 v[172:173], v[230:231], v[218:219], v[172:173] op_sel:[1,0,0]
	v_fmac_f32_e32 v242, v231, v160
	s_waitcnt lgkmcnt(0)
	v_pk_fma_f32 v[222:223], v[232:233], v[152:153], v[222:223] op_sel_hi:[0,1,1]
	v_pk_fma_f32 v[176:177], v[232:233], v[218:219], v[176:177] op_sel_hi:[0,1,1]
	v_fmac_f32_e32 v246, v232, v160
	v_pk_mul_f32 v[180:181], v[224:225], v[154:155] op_sel_hi:[0,1]
	v_pk_mul_f32 v[184:185], v[224:225], v[164:165] op_sel_hi:[0,1]
	v_mul_f32_e32 v188, v224, v238
	v_pk_fma_f32 v[180:181], v[224:225], v[174:175], v[180:181] op_sel:[1,0,0]
	v_pk_fma_f32 v[184:185], v[224:225], v[172:173], v[184:185] op_sel:[1,0,0]
	v_fmac_f32_e32 v188, v225, v242
	v_pk_fma_f32 v[180:181], v[226:227], v[222:223], v[180:181] op_sel_hi:[0,1,1]
	v_pk_fma_f32 v[184:185], v[226:227], v[176:177], v[184:185] op_sel_hi:[0,1,1]
	v_fmac_f32_e32 v188, v226, v246
	v_pk_fma_f32 v[180:181], v[232:233], v[62:63], v[180:181] op_sel:[1,0,0] neg_lo:[0,0,1] neg_hi:[0,0,1]
	v_pk_fma_f32 v[184:185], v[232:233], v[64:65], v[184:185] op_sel:[1,0,0] neg_lo:[0,0,1] neg_hi:[0,0,1]
	v_fma_f32 v188, v233, v102, -v188
	v_cmp_eq_u32_e64 s[10:11], 1, v235
	v_cmp_eq_u32_e64 s[14:15], 2, v235
	v_cmp_eq_u32_e64 s[20:21], 3, v235
	v_cmp_eq_u32_e64 s[22:23], 4, v235
	v_cmp_eq_u32_e64 s[30:31], 5, v235
	v_pk_add_f32 v[64:65], v[72:73], v[154:155]
	v_pk_add_f32 v[62:63], v[70:71], v[64:65]
	v_pk_add_f32 v[72:73], v[66:67], v[164:165]
	v_pk_add_f32 v[70:71], v[86:87], v[72:73]
	v_add_f32_e32 v120, v186, v238
	v_add_f32_e32 v66, v122, v120
	v_pk_add_f32 v[144:145], v[124:125], v[174:175]
	v_pk_add_f32 v[86:87], v[74:75], v[144:145]
	v_pk_add_f32 v[124:125], v[142:143], v[172:173]
	v_pk_add_f32 v[74:75], v[114:115], v[124:125]
	v_add_f32_e32 v148, v190, v242
	v_add_f32_e32 v102, v126, v148
	v_pk_add_f32 v[152:153], v[212:213], v[222:223]
	v_pk_add_f32 v[114:115], v[78:79], v[152:153]
	v_pk_add_f32 v[160:161], v[182:183], v[176:177]
	v_pk_add_f32 v[78:79], v[118:119], v[160:161]
	v_add_f32_e32 v168, v194, v246
	v_add_f32_e32 v118, v162, v168
	v_pk_add_f32 v[122:123], v[206:207], v[180:181]
	v_pk_add_f32 v[192:193], v[112:113], v[122:123]
	v_pk_add_f32 v[126:127], v[216:217], v[184:185]
	v_pk_add_f32 v[112:113], v[204:205], v[126:127]
	v_add_f32_e32 v142, v220, v188
	v_add_f32_e32 v204, v208, v142
	v_pk_fma_f32 v[208:209], v[132:133], v[62:63], v[192:193] op_sel_hi:[0,1,1]
	v_pk_fma_f32 v[212:213], v[132:133], v[70:71], v[112:113] op_sel_hi:[0,1,1]
	v_fma_f32 v216, v132, v66, v204
	v_pk_fma_f32 v[220:221], v[136:137], v[62:63], v[192:193] op_sel_hi:[0,1,1]
	v_pk_fma_f32 v[236:237], v[136:137], v[70:71], v[112:113] op_sel_hi:[0,1,1]
	v_fma_f32 v240, v136, v66, v204
	v_pk_fma_f32 v[208:209], v[132:133], v[86:87], v[208:209] op_sel:[1,0,0]
	v_pk_fma_f32 v[212:213], v[132:133], v[74:75], v[212:213] op_sel:[1,0,0]
	v_fmac_f32_e32 v216, v133, v102
	v_pk_fma_f32 v[220:221], v[136:137], v[86:87], v[220:221] op_sel:[1,0,0]
	v_pk_fma_f32 v[236:237], v[136:137], v[74:75], v[236:237] op_sel:[1,0,0]
	v_fmac_f32_e32 v240, v137, v102
	v_pk_fma_f32 v[208:209], v[134:135], v[114:115], v[208:209] op_sel_hi:[0,1,1]
	v_pk_fma_f32 v[212:213], v[134:135], v[78:79], v[212:213] op_sel_hi:[0,1,1]
	v_fmac_f32_e32 v216, v134, v118
	v_pk_fma_f32 v[220:221], v[138:139], v[114:115], v[220:221] op_sel_hi:[0,1,1]
	v_pk_fma_f32 v[236:237], v[138:139], v[78:79], v[236:237] op_sel_hi:[0,1,1]
	v_fmac_f32_e32 v240, v138, v118
	v_pk_fma_f32 v[192:193], v[36:37], v[62:63], v[192:193] op_sel_hi:[0,1,1]
	v_pk_fma_f32 v[112:113], v[36:37], v[70:71], v[112:113] op_sel_hi:[0,1,1]
	v_fmac_f32_e32 v204, v36, v66
	v_pk_fma_f32 v[192:193], v[36:37], v[86:87], v[192:193] op_sel:[1,0,0]
	v_pk_fma_f32 v[112:113], v[36:37], v[74:75], v[112:113] op_sel:[1,0,0]
	v_fmac_f32_e32 v204, v37, v102
	v_pk_fma_f32 v[192:193], v[38:39], v[114:115], v[192:193] op_sel_hi:[0,1,1]
	v_pk_fma_f32 v[112:113], v[38:39], v[78:79], v[112:113] op_sel_hi:[0,1,1]
	v_fmac_f32_e32 v204, v38, v118
	v_cndmask_b32_e64 v162, 0, v1, s[10:11]
	v_cndmask_b32_e64 v163, 0, v1, s[14:15]
	v_cndmask_b32_e64 v182, 0, v1, s[20:21]
	v_cndmask_b32_e64 v183, 0, v1, s[22:23]
	v_cndmask_b32_e64 v186, 0, v1, s[30:31]
	v_add_f32_dpp v192, v208, v192 wave_shl:1 row_mask:0xf bank_mask:0xf bound_ctrl:1
	v_add_f32_dpp v193, v209, v193 wave_shl:1 row_mask:0xf bank_mask:0xf bound_ctrl:1
	v_add_f32_dpp v112, v212, v112 wave_shl:1 row_mask:0xf bank_mask:0xf bound_ctrl:1
	v_add_f32_dpp v113, v213, v113 wave_shl:1 row_mask:0xf bank_mask:0xf bound_ctrl:1
	v_add_f32_dpp v204, v216, v204 wave_shl:1 row_mask:0xf bank_mask:0xf bound_ctrl:1
	s_add_i32 s4, s34, 0
	s_cmpk_lt_i32 s4, 0x201
	s_cselect_b64 s[12:13], s[0:1], 0
	v_add_f32_dpp v192, v220, v192 wave_shr:1 row_mask:0xf bank_mask:0xf bound_ctrl:1
	v_add_f32_dpp v193, v221, v193 wave_shr:1 row_mask:0xf bank_mask:0xf bound_ctrl:1
	v_add_f32_dpp v112, v236, v112 wave_shr:1 row_mask:0xf bank_mask:0xf bound_ctrl:1
	v_add_f32_dpp v113, v237, v113 wave_shr:1 row_mask:0xf bank_mask:0xf bound_ctrl:1
	v_add_f32_dpp v204, v240, v204 wave_shr:1 row_mask:0xf bank_mask:0xf bound_ctrl:1
	v_pk_fma_f32 v[192:193], v[20:21], v[234:235], v[192:193] op_sel_hi:[1,0,1] neg_lo:[0,0,1] neg_hi:[0,0,1]
	v_pk_fma_f32 v[112:113], v[24:25], v[234:235], v[112:113] op_sel_hi:[1,0,1] neg_lo:[0,0,1] neg_hi:[0,0,1]
	v_fma_f32 v204, v30, v234, -v204
	v_pk_add_f32 v[192:193], v[192:193], v[162:163] neg_lo:[0,1] neg_hi:[0,1]
	v_pk_add_f32 v[112:113], v[112:113], v[182:183] neg_lo:[0,1] neg_hi:[0,1]
	v_sub_f32_e32 v204, v204, v186
	v_pk_mul_f32 v[190:191], v[192:193], v[192:193]
	v_pk_fma_f32 v[190:191], v[112:113], v[112:113], v[190:191]
	v_add_f32_e32 v190, v190, v191
	v_fmac_f32_e32 v190, v204, v204
	v_cndmask_b32_e64 v191, 0, v190, s[12:13]
	v_add_f32_e32 v0, v0, v191
	s_add_i32 s4, s34, 5
	s_min_i32 s4, s4, 0x200
	s_mul_i32 s5, s4, 0x804
	s_add_i32 s5, s5, s35
	s_add_i32 s6, s5, 0x0
	s_add_i32 s7, s5, 0x101004
	s_add_i32 s8, s5, 0x202008
	s_add_i32 s11, s5, 0x30300c
	s_add_i32 s15, s5, 0x404010
	s_mul_i32 s9, s4, 0x180c
	s_add_i32 s9, s9, s33
	buffer_load_dword v20, v28, s[16:19], s6 offen nt
	buffer_load_dword v21, v28, s[16:19], s7 offen nt
	buffer_load_dword v24, v28, s[16:19], s8 offen nt
	buffer_load_dword v25, v28, s[16:19], s11 offen nt
	buffer_load_dword v30, v28, s[16:19], s15 offen nt
	buffer_load_dwordx3 v[36:38], v27, s[24:27], s9 offen nt
	s_waitcnt vmcnt(12)
	v_mov_b32_dpp v112, v8 wave_shr:1 row_mask:0xf bank_mask:0xf bound_ctrl:1
	v_mov_b32_dpp v113, v9 wave_shr:1 row_mask:0xf bank_mask:0xf bound_ctrl:1
	v_mov_b32_dpp v114, v10 wave_shr:1 row_mask:0xf bank_mask:0xf bound_ctrl:1
	v_mov_b32_dpp v132, v8 wave_shl:1 row_mask:0xf bank_mask:0xf bound_ctrl:1
	v_mov_b32_dpp v133, v9 wave_shl:1 row_mask:0xf bank_mask:0xf bound_ctrl:1
	v_mov_b32_dpp v134, v10 wave_shl:1 row_mask:0xf bank_mask:0xf bound_ctrl:1
	v_mov_b32_dpp v136, v2 wave_shr:1 row_mask:0xf bank_mask:0xf bound_ctrl:1
	v_mov_b32_dpp v137, v3 wave_shr:1 row_mask:0xf bank_mask:0xf bound_ctrl:1
	v_mov_b32_dpp v62, v4 wave_shr:1 row_mask:0xf bank_mask:0xf bound_ctrl:1
	v_mov_b32_dpp v63, v5 wave_shr:1 row_mask:0xf bank_mask:0xf bound_ctrl:1
	v_mov_b32_dpp v192, v6 wave_shr:1 row_mask:0xf bank_mask:0xf bound_ctrl:1
	v_mov_b32_dpp v204, v2 wave_shl:1 row_mask:0xf bank_mask:0xf bound_ctrl:1
	v_mov_b32_dpp v205, v3 wave_shl:1 row_mask:0xf bank_mask:0xf bound_ctrl:1
	v_mov_b32_dpp v66, v4 wave_shl:1 row_mask:0xf bank_mask:0xf bound_ctrl:1
	v_mov_b32_dpp v67, v5 wave_shl:1 row_mask:0xf bank_mask:0xf bound_ctrl:1
	v_mov_b32_dpp v208, v6 wave_shl:1 row_mask:0xf bank_mask:0xf bound_ctrl:1
	v_pk_mul_f32 v[70:71], v[2:3], v[8:9] op_sel_hi:[1,0]
	v_pk_mul_f32 v[212:213], v[4:5], v[8:9] op_sel_hi:[1,0]
	v_mul_f32_e32 v74, v6, v8
	v_pk_mul_f32 v[78:79], v[2:3], v[8:9] op_sel:[0,1]
	v_pk_mul_f32 v[216:217], v[4:5], v[8:9] op_sel:[0,1]
	v_mul_f32_e32 v86, v6, v9
	v_pk_mul_f32 v[102:103], v[2:3], v[10:11] op_sel_hi:[1,0]
	v_pk_mul_f32 v[220:221], v[4:5], v[10:11] op_sel_hi:[1,0]
	v_mul_f32_e32 v118, v6, v10
	v_pk_add_f32 v[138:139], v[2:3], v[136:137]
	v_pk_add_f32 v[224:225], v[4:5], v[62:63]
	v_add_f32_e32 v162, v6, v192
	v_pk_fma_f32 v[70:71], v[136:137], v[112:113], v[70:71] op_sel_hi:[1,0,1]
	v_pk_fma_f32 v[212:213], v[62:63], v[112:113], v[212:213] op_sel_hi:[1,0,1]
	v_fmac_f32_e32 v74, v192, v112
	v_pk_fma_f32 v[78:79], v[136:137], v[112:113], v[78:79] op_sel:[0,1,0]
	v_pk_fma_f32 v[216:217], v[62:63], v[112:113], v[216:217] op_sel:[0,1,0]
	v_fmac_f32_e32 v86, v192, v113
	v_pk_fma_f32 v[102:103], v[136:137], v[114:115], v[102:103] op_sel_hi:[1,0,1]
	v_pk_fma_f32 v[220:221], v[62:63], v[114:115], v[220:221] op_sel_hi:[1,0,1]
	v_fmac_f32_e32 v118, v192, v114
	v_pk_add_f32 v[138:139], v[138:139], v[204:205]
	v_pk_add_f32 v[224:225], v[224:225], v[66:67]
	v_add_f32_e32 v162, v162, v208
	v_pk_fma_f32 v[70:71], v[204:205], v[132:133], v[70:71] op_sel_hi:[1,0,1]
	v_pk_fma_f32 v[212:213], v[66:67], v[132:133], v[212:213] op_sel_hi:[1,0,1]
	v_fmac_f32_e32 v74, v208, v132
	v_pk_fma_f32 v[78:79], v[204:205], v[132:133], v[78:79] op_sel:[0,1,0]
	v_pk_fma_f32 v[216:217], v[66:67], v[132:133], v[216:217] op_sel:[0,1,0]
	v_fmac_f32_e32 v86, v208, v133
	v_pk_fma_f32 v[102:103], v[204:205], v[134:135], v[102:103] op_sel_hi:[1,0,1]
	v_pk_fma_f32 v[220:221], v[66:67], v[134:135], v[220:221] op_sel_hi:[1,0,1]
	v_fmac_f32_e32 v118, v208, v134
	s_barrier
	ds_read_b128 v[192:195], v23 offset:3072
	ds_read_b128 v[204:207], v23 offset:4096
	ds_read_b128 v[208:211], v23 offset:5120
	v_pk_add_f32 v[62:63], v[58:59], v[138:139]
	v_pk_add_f32 v[58:59], v[98:99], v[224:225]
	v_add_f32_e32 v66, v68, v162
	v_pk_add_f32 v[68:69], v[158:159], v[70:71]
	v_pk_add_f32 v[136:137], v[178:179], v[212:213]
	v_add_f32_e32 v228, v108, v74
	v_pk_add_f32 v[108:109], v[146:147], v[78:79]
	v_pk_add_f32 v[232:233], v[166:167], v[216:217]
	v_add_f32_e32 v236, v140, v86
	v_pk_add_f32 v[140:141], v[150:151], v[102:103]
	v_pk_add_f32 v[240:241], v[170:171], v[220:221]
	v_add_f32_e32 v244, v156, v118
	s_waitcnt lgkmcnt(2)
	v_pk_fma_f32 v[68:69], v[192:193], v[62:63], v[68:69] op_sel_hi:[0,1,1] neg_lo:[1,0,0] neg_hi:[1,0,0]
	v_pk_fma_f32 v[136:137], v[192:193], v[58:59], v[136:137] op_sel_hi:[0,1,1] neg_lo:[1,0,0] neg_hi:[1,0,0]
	v_fma_f32 v228, -v192, v66, v228
	v_pk_fma_f32 v[108:109], v[192:193], v[62:63], v[108:109] op_sel:[1,0,0] neg_lo:[1,0,0] neg_hi:[1,0,0]
	v_pk_fma_f32 v[232:233], v[192:193], v[58:59], v[232:233] op_sel:[1,0,0] neg_lo:[1,0,0] neg_hi:[1,0,0]
	v_fma_f32 v236, -v193, v66, v236
	v_pk_fma_f32 v[140:141], v[194:195], v[62:63], v[140:141] op_sel_hi:[0,1,1] neg_lo:[1,0,0] neg_hi:[1,0,0]
	v_pk_fma_f32 v[240:241], v[194:195], v[58:59], v[240:241] op_sel_hi:[0,1,1] neg_lo:[1,0,0] neg_hi:[1,0,0]
	v_fma_f32 v244, -v194, v66, v244
	v_pk_mul_f32 v[98:99], v[194:195], v[68:69] op_sel:[1,0]
	v_pk_mul_f32 v[158:159], v[194:195], v[136:137] op_sel:[1,0]
	v_mul_f32_e32 v178, v195, v228
	s_waitcnt lgkmcnt(1)
	v_pk_mul_f32 v[146:147], v[204:205], v[68:69] op_sel_hi:[0,1]
	v_pk_mul_f32 v[166:167], v[204:205], v[136:137] op_sel_hi:[0,1]
	v_mul_f32_e32 v182, v204, v228
	v_pk_mul_f32 v[150:151], v[204:205], v[68:69] op_sel:[1,0]
	v_pk_mul_f32 v[170:171], v[204:205], v[136:137] op_sel:[1,0]
	v_mul_f32_e32 v186, v205, v228
	v_pk_fma_f32 v[98:99], v[204:205], v[108:109], v[98:99] op_sel_hi:[0,1,1]
	v_pk_fma_f32 v[158:159], v[204:205], v[232:233], v[158:159] op_sel_hi:[0,1,1]
	v_fmac_f32_e32 v178, v204, v236
	v_pk_fma_f32 v[146:147], v[206:207], v[108:109], v[146:147] op_sel_hi:[0,1,1]
	v_pk_fma_f32 v[166:167], v[206:207], v[232:233], v[166:167] op_sel_hi:[0,1,1]
	v_fmac_f32_e32 v182, v206, v236
	v_pk_fma_f32 v[150:151], v[206:207], v[108:109], v[150:151] op_sel:[1,0,0]
	v_pk_fma_f32 v[170:171], v[206:207], v[232:233], v[170:171] op_sel:[1,0,0]
	v_fmac_f32_e32 v186, v207, v236
	v_pk_fma_f32 v[98:99], v[204:205], v[140:141], v[98:99] op_sel:[1,0,0]
	v_pk_fma_f32 v[158:159], v[204:205], v[240:241], v[158:159] op_sel:[1,0,0]
	v_fmac_f32_e32 v178, v205, v244
	v_pk_fma_f32 v[146:147], v[206:207], v[140:141], v[146:147] op_sel:[1,0,0]
	v_pk_fma_f32 v[166:167], v[206:207], v[240:241], v[166:167] op_sel:[1,0,0]
	v_fmac_f32_e32 v182, v207, v244
	s_waitcnt lgkmcnt(0)
	v_pk_fma_f32 v[150:151], v[208:209], v[140:141], v[150:151] op_sel_hi:[0,1,1]
	v_pk_fma_f32 v[170:171], v[208:209], v[240:241], v[170:171] op_sel_hi:[0,1,1]
	v_fmac_f32_e32 v186, v208, v244
	v_pk_mul_f32 v[156:157], v[192:193], v[98:99] op_sel_hi:[0,1]
	v_pk_mul_f32 v[248:249], v[192:193], v[158:159] op_sel_hi:[0,1]
	v_mul_f32_e32 v190, v192, v178
	v_pk_fma_f32 v[156:157], v[192:193], v[146:147], v[156:157] op_sel:[1,0,0]
	v_pk_fma_f32 v[248:249], v[192:193], v[166:167], v[248:249] op_sel:[1,0,0]
	v_fmac_f32_e32 v190, v193, v182
	v_pk_fma_f32 v[156:157], v[194:195], v[150:151], v[156:157] op_sel_hi:[0,1,1]
	v_pk_fma_f32 v[248:249], v[194:195], v[170:171], v[248:249] op_sel_hi:[0,1,1]
	v_fmac_f32_e32 v190, v194, v186
	v_pk_fma_f32 v[156:157], v[208:209], v[62:63], v[156:157] op_sel:[1,0,0] neg_lo:[0,0,1] neg_hi:[0,0,1]
	v_pk_fma_f32 v[248:249], v[208:209], v[58:59], v[248:249] op_sel:[1,0,0] neg_lo:[0,0,1] neg_hi:[0,0,1]
	v_fma_f32 v190, v209, v66, -v190
	v_cmp_eq_u32_e64 s[10:11], 1, v211
	v_cmp_eq_u32_e64 s[14:15], 2, v211
	v_cmp_eq_u32_e64 s[20:21], 3, v211
	v_cmp_eq_u32_e64 s[22:23], 4, v211
	v_cmp_eq_u32_e64 s[30:31], 5, v211
	v_pk_add_f32 v[58:59], v[64:65], v[98:99]
	v_pk_add_f32 v[62:63], v[72:73], v[158:159]
	v_add_f32_e32 v64, v120, v178
	v_pk_add_f32 v[66:67], v[144:145], v[146:147]
	v_pk_add_f32 v[68:69], v[124:125], v[166:167]
	v_add_f32_e32 v72, v148, v182
	v_pk_add_f32 v[108:109], v[152:153], v[150:151]
	v_pk_add_f32 v[120:121], v[160:161], v[170:171]
	v_add_f32_e32 v124, v168, v186
	v_pk_add_f32 v[136:137], v[122:123], v[156:157]
	v_pk_add_f32 v[122:123], v[126:127], v[248:249]
	v_add_f32_e32 v126, v142, v190
	v_pk_fma_f32 v[140:141], v[40:41], v[58:59], v[136:137] op_sel_hi:[0,1,1]
	v_pk_fma_f32 v[142:143], v[40:41], v[62:63], v[122:123] op_sel_hi:[0,1,1]
	v_fma_f32 v214, v40, v64, v126
	v_pk_fma_f32 v[144:145], v[44:45], v[58:59], v[136:137] op_sel_hi:[0,1,1]
	v_pk_fma_f32 v[218:219], v[44:45], v[62:63], v[122:123] op_sel_hi:[0,1,1]
	v_fma_f32 v226, v44, v64, v126
	v_pk_fma_f32 v[140:141], v[40:41], v[66:67], v[140:141] op_sel:[1,0,0]
	v_pk_fma_f32 v[142:143], v[40:41], v[68:69], v[142:143] op_sel:[1,0,0]
	v_fmac_f32_e32 v214, v41, v72
	v_pk_fma_f32 v[144:145], v[44:45], v[66:67], v[144:145] op_sel:[1,0,0]
	v_pk_fma_f32 v[218:219], v[44:45], v[68:69], v[218:219] op_sel:[1,0,0]
	v_fmac_f32_e32 v226, v45, v72
	v_pk_fma_f32 v[140:141], v[42:43], v[108:109], v[140:141] op_sel_hi:[0,1,1]
	v_pk_fma_f32 v[142:143], v[42:43], v[120:121], v[142:143] op_sel_hi:[0,1,1]
	v_fmac_f32_e32 v214, v42, v124
	v_pk_fma_f32 v[144:145], v[46:47], v[108:109], v[144:145] op_sel_hi:[0,1,1]
	v_pk_fma_f32 v[218:219], v[46:47], v[120:121], v[218:219] op_sel_hi:[0,1,1]
	v_fmac_f32_e32 v226, v46, v124
	v_pk_fma_f32 v[136:137], v[88:89], v[58:59], v[136:137] op_sel_hi:[0,1,1]
	v_pk_fma_f32 v[122:123], v[88:89], v[62:63], v[122:123] op_sel_hi:[0,1,1]
	v_fmac_f32_e32 v126, v88, v64
	v_pk_fma_f32 v[136:137], v[88:89], v[66:67], v[136:137] op_sel:[1,0,0]
	v_pk_fma_f32 v[122:123], v[88:89], v[68:69], v[122:123] op_sel:[1,0,0]
	v_fmac_f32_e32 v126, v89, v72
	v_pk_fma_f32 v[136:137], v[90:91], v[108:109], v[136:137] op_sel_hi:[0,1,1]
	v_pk_fma_f32 v[122:123], v[90:91], v[120:121], v[122:123] op_sel_hi:[0,1,1]
	v_fmac_f32_e32 v126, v90, v124
	v_cndmask_b32_e64 v230, 0, v1, s[10:11]
	v_cndmask_b32_e64 v231, 0, v1, s[14:15]
	v_cndmask_b32_e64 v148, 0, v1, s[20:21]
	v_cndmask_b32_e64 v149, 0, v1, s[22:23]
	v_cndmask_b32_e64 v152, 0, v1, s[30:31]
	v_add_f32_dpp v136, v140, v136 wave_shl:1 row_mask:0xf bank_mask:0xf bound_ctrl:1
	v_add_f32_dpp v137, v141, v137 wave_shl:1 row_mask:0xf bank_mask:0xf bound_ctrl:1
	v_add_f32_dpp v122, v142, v122 wave_shl:1 row_mask:0xf bank_mask:0xf bound_ctrl:1
	v_add_f32_dpp v123, v143, v123 wave_shl:1 row_mask:0xf bank_mask:0xf bound_ctrl:1
	v_add_f32_dpp v126, v214, v126 wave_shl:1 row_mask:0xf bank_mask:0xf bound_ctrl:1
	s_add_i32 s4, s34, 1
	s_cmpk_lt_i32 s4, 0x201
	s_cselect_b64 s[12:13], s[0:1], 0
	v_add_f32_dpp v136, v144, v136 wave_shr:1 row_mask:0xf bank_mask:0xf bound_ctrl:1
	v_add_f32_dpp v137, v145, v137 wave_shr:1 row_mask:0xf bank_mask:0xf bound_ctrl:1
	v_add_f32_dpp v122, v218, v122 wave_shr:1 row_mask:0xf bank_mask:0xf bound_ctrl:1
	v_add_f32_dpp v123, v219, v123 wave_shr:1 row_mask:0xf bank_mask:0xf bound_ctrl:1
	v_add_f32_dpp v126, v226, v126 wave_shr:1 row_mask:0xf bank_mask:0xf bound_ctrl:1
	v_pk_fma_f32 v[136:137], v[48:49], v[210:211], v[136:137] op_sel_hi:[1,0,1] neg_lo:[0,0,1] neg_hi:[0,0,1]
	v_pk_fma_f32 v[122:123], v[50:51], v[210:211], v[122:123] op_sel_hi:[1,0,1] neg_lo:[0,0,1] neg_hi:[0,0,1]
	v_fma_f32 v126, v52, v210, -v126
	v_pk_add_f32 v[136:137], v[136:137], v[230:231] neg_lo:[0,1] neg_hi:[0,1]
	v_pk_add_f32 v[122:123], v[122:123], v[148:149] neg_lo:[0,1] neg_hi:[0,1]
	v_sub_f32_e32 v126, v126, v152
	v_pk_mul_f32 v[160:161], v[136:137], v[136:137]
	v_pk_fma_f32 v[160:161], v[122:123], v[122:123], v[160:161]
	v_add_f32_e32 v160, v160, v161
	v_fmac_f32_e32 v160, v126, v126
	v_cndmask_b32_e64 v161, 0, v160, s[12:13]
	v_add_f32_e32 v0, v0, v161
	s_add_i32 s4, s34, 6
	s_min_i32 s4, s4, 0x200
	s_mul_i32 s5, s4, 0x804
	s_add_i32 s5, s5, s35
	s_add_i32 s6, s5, 0x0
	s_add_i32 s7, s5, 0x101004
	s_add_i32 s8, s5, 0x202008
	s_add_i32 s11, s5, 0x30300c
	s_add_i32 s15, s5, 0x404010
	s_mul_i32 s9, s4, 0x180c
	s_add_i32 s9, s9, s33
	buffer_load_dword v40, v28, s[16:19], s6 offen nt
	buffer_load_dword v41, v28, s[16:19], s7 offen nt
	buffer_load_dword v42, v28, s[16:19], s8 offen nt
	buffer_load_dword v43, v28, s[16:19], s11 offen nt
	buffer_load_dword v44, v28, s[16:19], s15 offen nt
	buffer_load_dwordx3 v[48:50], v27, s[24:27], s9 offen nt
	s_waitcnt vmcnt(12)
	v_mov_b32_dpp v64, v32 wave_shr:1 row_mask:0xf bank_mask:0xf bound_ctrl:1
	v_mov_b32_dpp v65, v33 wave_shr:1 row_mask:0xf bank_mask:0xf bound_ctrl:1
	v_mov_b32_dpp v66, v34 wave_shr:1 row_mask:0xf bank_mask:0xf bound_ctrl:1
	v_mov_b32_dpp v88, v32 wave_shl:1 row_mask:0xf bank_mask:0xf bound_ctrl:1
	v_mov_b32_dpp v89, v33 wave_shl:1 row_mask:0xf bank_mask:0xf bound_ctrl:1
	v_mov_b32_dpp v90, v34 wave_shl:1 row_mask:0xf bank_mask:0xf bound_ctrl:1
	v_mov_b32_dpp v46, v12 wave_shr:1 row_mask:0xf bank_mask:0xf bound_ctrl:1
	v_mov_b32_dpp v47, v13 wave_shr:1 row_mask:0xf bank_mask:0xf bound_ctrl:1
	v_mov_b32_dpp v52, v14 wave_shr:1 row_mask:0xf bank_mask:0xf bound_ctrl:1
	v_mov_b32_dpp v53, v15 wave_shr:1 row_mask:0xf bank_mask:0xf bound_ctrl:1
	v_mov_b32_dpp v58, v16 wave_shr:1 row_mask:0xf bank_mask:0xf bound_ctrl:1
	v_mov_b32_dpp v62, v12 wave_shl:1 row_mask:0xf bank_mask:0xf bound_ctrl:1
	v_mov_b32_dpp v63, v13 wave_shl:1 row_mask:0xf bank_mask:0xf bound_ctrl:1
	v_mov_b32_dpp v68, v14 wave_shl:1 row_mask:0xf bank_mask:0xf bound_ctrl:1
	v_mov_b32_dpp v69, v15 wave_shl:1 row_mask:0xf bank_mask:0xf bound_ctrl:1
	v_mov_b32_dpp v122, v16 wave_shl:1 row_mask:0xf bank_mask:0xf bound_ctrl:1
	v_pk_mul_f32 v[72:73], v[12:13], v[32:33] op_sel_hi:[1,0]
	v_pk_mul_f32 v[126:127], v[14:15], v[32:33] op_sel_hi:[1,0]
	v_mul_f32_e32 v108, v16, v32
	v_pk_mul_f32 v[120:121], v[12:13], v[32:33] op_sel:[0,1]
	v_pk_mul_f32 v[142:143], v[14:15], v[32:33] op_sel:[0,1]
	v_mul_f32_e32 v124, v16, v33
	v_pk_mul_f32 v[136:137], v[12:13], v[34:35] op_sel_hi:[1,0]
	v_pk_mul_f32 v[194:195], v[14:15], v[34:35] op_sel_hi:[1,0]
	v_mul_f32_e32 v140, v16, v34
	v_pk_add_f32 v[144:145], v[12:13], v[46:47]
	v_pk_add_f32 v[206:207], v[14:15], v[52:53]
	v_add_f32_e32 v148, v16, v58
	v_pk_fma_f32 v[72:73], v[46:47], v[64:65], v[72:73] op_sel_hi:[1,0,1]
	v_pk_fma_f32 v[126:127], v[52:53], v[64:65], v[126:127] op_sel_hi:[1,0,1]
	v_fmac_f32_e32 v108, v58, v64
	v_pk_fma_f32 v[120:121], v[46:47], v[64:65], v[120:121] op_sel:[0,1,0]
	v_pk_fma_f32 v[142:143], v[52:53], v[64:65], v[142:143] op_sel:[0,1,0]
	v_fmac_f32_e32 v124, v58, v65
	v_pk_fma_f32 v[136:137], v[46:47], v[66:67], v[136:137] op_sel_hi:[1,0,1]
	v_pk_fma_f32 v[194:195], v[52:53], v[66:67], v[194:195] op_sel_hi:[1,0,1]
	v_fmac_f32_e32 v140, v58, v66
	v_pk_add_f32 v[144:145], v[144:145], v[62:63]
	v_pk_add_f32 v[206:207], v[206:207], v[68:69]
	v_add_f32_e32 v148, v148, v122
	v_pk_fma_f32 v[72:73], v[62:63], v[88:89], v[72:73] op_sel_hi:[1,0,1]
	v_pk_fma_f32 v[126:127], v[68:69], v[88:89], v[126:127] op_sel_hi:[1,0,1]
	v_fmac_f32_e32 v108, v122, v88
	v_pk_fma_f32 v[120:121], v[62:63], v[88:89], v[120:121] op_sel:[0,1,0]
	v_pk_fma_f32 v[142:143], v[68:69], v[88:89], v[142:143] op_sel:[0,1,0]
	v_fmac_f32_e32 v124, v122, v89
	v_pk_fma_f32 v[136:137], v[62:63], v[90:91], v[136:137] op_sel_hi:[1,0,1]
	v_pk_fma_f32 v[194:195], v[68:69], v[90:91], v[194:195] op_sel_hi:[1,0,1]
	v_fmac_f32_e32 v140, v122, v90
	s_barrier
	ds_read_b128 v[208:211], v23 offset:0
	ds_read_b128 v[228:231], v23 offset:1024
	ds_read_b128 v[232:235], v23 offset:2048
	v_pk_add_f32 v[52:53], v[138:139], v[144:145]
	v_pk_add_f32 v[46:47], v[202:203], v[52:53]
	v_pk_add_f32 v[58:59], v[224:225], v[206:207]
	v_pk_add_f32 v[62:63], v[196:197], v[58:59]
	v_add_f32_e32 v122, v162, v148
	v_add_f32_e32 v68, v200, v122
	v_pk_add_f32 v[152:153], v[70:71], v[72:73]
	v_pk_add_f32 v[160:161], v[106:107], v[152:153]
	v_pk_add_f32 v[70:71], v[212:213], v[126:127]
	v_pk_add_f32 v[168:169], v[76:77], v[70:71]
	v_add_f32_e32 v106, v74, v108
	v_add_f32_e32 v138, v84, v106
	v_pk_add_f32 v[76:77], v[78:79], v[120:121]
	v_pk_add_f32 v[84:85], v[110:111], v[76:77]
	v_pk_add_f32 v[74:75], v[216:217], v[142:143]
	v_pk_add_f32 v[192:193], v[96:97], v[74:75]
	v_add_f32_e32 v78, v86, v124
	v_add_f32_e32 v110, v100, v78
	v_pk_add_f32 v[96:97], v[102:103], v[136:137]
	v_pk_add_f32 v[100:101], v[198:199], v[96:97]
	v_pk_add_f32 v[86:87], v[220:221], v[194:195]
	v_pk_add_f32 v[196:197], v[104:105], v[86:87]
	v_add_f32_e32 v102, v118, v140
	v_add_f32_e32 v162, v116, v102
	s_waitcnt lgkmcnt(2)
	v_pk_fma_f32 v[160:161], v[208:209], v[46:47], v[160:161] op_sel_hi:[0,1,1] neg_lo:[1,0,0] neg_hi:[1,0,0]
	v_pk_fma_f32 v[168:169], v[208:209], v[62:63], v[168:169] op_sel_hi:[0,1,1] neg_lo:[1,0,0] neg_hi:[1,0,0]
	v_fma_f32 v138, -v208, v68, v138
	v_pk_fma_f32 v[84:85], v[208:209], v[46:47], v[84:85] op_sel:[1,0,0] neg_lo:[1,0,0] neg_hi:[1,0,0]
	v_pk_fma_f32 v[192:193], v[208:209], v[62:63], v[192:193] op_sel:[1,0,0] neg_lo:[1,0,0] neg_hi:[1,0,0]
	v_fma_f32 v110, -v209, v68, v110
	v_pk_fma_f32 v[100:101], v[210:211], v[46:47], v[100:101] op_sel_hi:[0,1,1] neg_lo:[1,0,0] neg_hi:[1,0,0]
	v_pk_fma_f32 v[196:197], v[210:211], v[62:63], v[196:197] op_sel_hi:[0,1,1] neg_lo:[1,0,0] neg_hi:[1,0,0]
	v_fma_f32 v162, -v210, v68, v162
	v_pk_mul_f32 v[118:119], v[210:211], v[160:161] op_sel:[1,0]
	v_pk_mul_f32 v[214:215], v[210:211], v[168:169] op_sel:[1,0]
	v_mul_f32_e32 v104, v211, v138
	s_waitcnt lgkmcnt(1)
	v_pk_mul_f32 v[198:199], v[228:229], v[160:161] op_sel_hi:[0,1]
	v_pk_mul_f32 v[218:219], v[228:229], v[168:169] op_sel_hi:[0,1]
	v_mul_f32_e32 v116, v228, v138
	v_pk_mul_f32 v[202:203], v[228:229], v[160:161] op_sel:[1,0]
	v_pk_mul_f32 v[226:227], v[228:229], v[168:169] op_sel:[1,0]
	v_mul_f32_e32 v200, v229, v138
	v_pk_fma_f32 v[118:119], v[228:229], v[84:85], v[118:119] op_sel_hi:[0,1,1]
	v_pk_fma_f32 v[214:215], v[228:229], v[192:193], v[214:215] op_sel_hi:[0,1,1]
	v_fmac_f32_e32 v104, v228, v110
	v_pk_fma_f32 v[198:199], v[230:231], v[84:85], v[198:199] op_sel_hi:[0,1,1]
	v_pk_fma_f32 v[218:219], v[230:231], v[192:193], v[218:219] op_sel_hi:[0,1,1]
	v_fmac_f32_e32 v116, v230, v110
	v_pk_fma_f32 v[202:203], v[230:231], v[84:85], v[202:203] op_sel:[1,0,0]
	v_pk_fma_f32 v[226:227], v[230:231], v[192:193], v[226:227] op_sel:[1,0,0]
	v_fmac_f32_e32 v200, v231, v110
	v_pk_fma_f32 v[118:119], v[228:229], v[100:101], v[118:119] op_sel:[1,0,0]
	v_pk_fma_f32 v[214:215], v[228:229], v[196:197], v[214:215] op_sel:[1,0,0]
	v_fmac_f32_e32 v104, v229, v162
	v_pk_fma_f32 v[198:199], v[230:231], v[100:101], v[198:199] op_sel:[1,0,0]
	v_pk_fma_f32 v[218:219], v[230:231], v[196:197], v[218:219] op_sel:[1,0,0]
	v_fmac_f32_e32 v116, v231, v162
	s_waitcnt lgkmcnt(0)
	v_pk_fma_f32 v[202:203], v[232:233], v[100:101], v[202:203] op_sel_hi:[0,1,1]
	v_pk_fma_f32 v[226:227], v[232:233], v[196:197], v[226:227] op_sel_hi:[0,1,1]
	v_fmac_f32_e32 v200, v232, v162
	v_pk_mul_f32 v[204:205], v[208:209], v[118:119] op_sel_hi:[0,1]
	v_pk_mul_f32 v[212:213], v[208:209], v[214:215] op_sel_hi:[0,1]
	v_mul_f32_e32 v216, v208, v104
	v_pk_fma_f32 v[204:205], v[208:209], v[198:199], v[204:205] op_sel:[1,0,0]
	v_pk_fma_f32 v[212:213], v[208:209], v[218:219], v[212:213] op_sel:[1,0,0]
	v_fmac_f32_e32 v216, v209, v116
	v_pk_fma_f32 v[204:205], v[210:211], v[202:203], v[204:205] op_sel_hi:[0,1,1]
	v_pk_fma_f32 v[212:213], v[210:211], v[226:227], v[212:213] op_sel_hi:[0,1,1]
	v_fmac_f32_e32 v216, v210, v200
	v_pk_fma_f32 v[204:205], v[232:233], v[46:47], v[204:205] op_sel:[1,0,0] neg_lo:[0,0,1] neg_hi:[0,0,1]
	v_pk_fma_f32 v[212:213], v[232:233], v[62:63], v[212:213] op_sel:[1,0,0] neg_lo:[0,0,1] neg_hi:[0,0,1]
	v_fma_f32 v216, v233, v68, -v216
	v_cmp_eq_u32_e64 s[10:11], 1, v235
	v_cmp_eq_u32_e64 s[14:15], 2, v235
	v_cmp_eq_u32_e64 s[20:21], 3, v235
	v_cmp_eq_u32_e64 s[22:23], 4, v235
	v_cmp_eq_u32_e64 s[30:31], 5, v235
	v_pk_add_f32 v[68:69], v[98:99], v[118:119]
	v_pk_add_f32 v[46:47], v[154:155], v[68:69]
	v_pk_add_f32 v[62:63], v[158:159], v[214:215]
	v_pk_add_f32 v[84:85], v[164:165], v[62:63]
	v_add_f32_e32 v100, v178, v104
	v_add_f32_e32 v98, v238, v100
	v_pk_add_f32 v[160:161], v[146:147], v[198:199]
	v_pk_add_f32 v[110:111], v[174:175], v[160:161]
	v_pk_add_f32 v[138:139], v[166:167], v[218:219]
	v_pk_add_f32 v[146:147], v[172:173], v[138:139]
	v_add_f32_e32 v164, v182, v116
	v_add_f32_e32 v154, v242, v164
	v_pk_add_f32 v[168:169], v[150:151], v[202:203]
	v_pk_add_f32 v[158:159], v[222:223], v[168:169]
	v_pk_add_f32 v[150:151], v[170:171], v[226:227]
	v_pk_add_f32 v[162:163], v[176:177], v[150:151]
	v_add_f32_e32 v172, v186, v200
	v_add_f32_e32 v166, v246, v172
	v_pk_add_f32 v[170:171], v[156:157], v[204:205]
	v_pk_add_f32 v[176:177], v[180:181], v[170:171]
	v_pk_add_f32 v[174:175], v[248:249], v[212:213]
	v_pk_add_f32 v[156:157], v[184:185], v[174:175]
	v_add_f32_e32 v178, v190, v216
	v_add_f32_e32 v180, v188, v178
	v_pk_fma_f32 v[184:185], v[80:81], v[46:47], v[176:177] op_sel_hi:[0,1,1]
	v_pk_fma_f32 v[188:189], v[80:81], v[84:85], v[156:157] op_sel_hi:[0,1,1]
	v_fma_f32 v192, v80, v98, v180
	v_pk_fma_f32 v[196:197], v[92:93], v[46:47], v[176:177] op_sel_hi:[0,1,1]
	v_pk_fma_f32 v[220:221], v[92:93], v[84:85], v[156:157] op_sel_hi:[0,1,1]
	v_fma_f32 v224, v92, v98, v180
	v_pk_fma_f32 v[184:185], v[80:81], v[110:111], v[184:185] op_sel:[1,0,0]
	v_pk_fma_f32 v[188:189], v[80:81], v[146:147], v[188:189] op_sel:[1,0,0]
	v_fmac_f32_e32 v192, v81, v154
	v_pk_fma_f32 v[196:197], v[92:93], v[110:111], v[196:197] op_sel:[1,0,0]
	v_pk_fma_f32 v[220:221], v[92:93], v[146:147], v[220:221] op_sel:[1,0,0]
	v_fmac_f32_e32 v224, v93, v154
	v_pk_fma_f32 v[184:185], v[82:83], v[158:159], v[184:185] op_sel_hi:[0,1,1]
	v_pk_fma_f32 v[188:189], v[82:83], v[162:163], v[188:189] op_sel_hi:[0,1,1]
	v_fmac_f32_e32 v192, v82, v166
	v_pk_fma_f32 v[196:197], v[94:95], v[158:159], v[196:197] op_sel_hi:[0,1,1]
	v_pk_fma_f32 v[220:221], v[94:95], v[162:163], v[220:221] op_sel_hi:[0,1,1]
	v_fmac_f32_e32 v224, v94, v166
	v_pk_fma_f32 v[176:177], v[128:129], v[46:47], v[176:177] op_sel_hi:[0,1,1]
	v_pk_fma_f32 v[156:157], v[128:129], v[84:85], v[156:157] op_sel_hi:[0,1,1]
	v_fmac_f32_e32 v180, v128, v98
	v_pk_fma_f32 v[176:177], v[128:129], v[110:111], v[176:177] op_sel:[1,0,0]
	v_pk_fma_f32 v[156:157], v[128:129], v[146:147], v[156:157] op_sel:[1,0,0]
	v_fmac_f32_e32 v180, v129, v154
	v_pk_fma_f32 v[176:177], v[130:131], v[158:159], v[176:177] op_sel_hi:[0,1,1]
	v_pk_fma_f32 v[156:157], v[130:131], v[162:163], v[156:157] op_sel_hi:[0,1,1]
	v_fmac_f32_e32 v180, v130, v166
	v_cndmask_b32_e64 v182, 0, v1, s[10:11]
	v_cndmask_b32_e64 v183, 0, v1, s[14:15]
	v_cndmask_b32_e64 v186, 0, v1, s[20:21]
	v_cndmask_b32_e64 v187, 0, v1, s[22:23]
	v_cndmask_b32_e64 v190, 0, v1, s[30:31]
	v_add_f32_dpp v176, v184, v176 wave_shl:1 row_mask:0xf bank_mask:0xf bound_ctrl:1
	v_add_f32_dpp v177, v185, v177 wave_shl:1 row_mask:0xf bank_mask:0xf bound_ctrl:1
	v_add_f32_dpp v156, v188, v156 wave_shl:1 row_mask:0xf bank_mask:0xf bound_ctrl:1
	v_add_f32_dpp v157, v189, v157 wave_shl:1 row_mask:0xf bank_mask:0xf bound_ctrl:1
	v_add_f32_dpp v180, v192, v180 wave_shl:1 row_mask:0xf bank_mask:0xf bound_ctrl:1
	s_add_i32 s4, s34, 2
	s_cmpk_lt_i32 s4, 0x201
	s_cselect_b64 s[12:13], s[0:1], 0
	v_add_f32_dpp v176, v196, v176 wave_shr:1 row_mask:0xf bank_mask:0xf bound_ctrl:1
	v_add_f32_dpp v177, v197, v177 wave_shr:1 row_mask:0xf bank_mask:0xf bound_ctrl:1
	v_add_f32_dpp v156, v220, v156 wave_shr:1 row_mask:0xf bank_mask:0xf bound_ctrl:1
	v_add_f32_dpp v157, v221, v157 wave_shr:1 row_mask:0xf bank_mask:0xf bound_ctrl:1
	v_add_f32_dpp v180, v224, v180 wave_shr:1 row_mask:0xf bank_mask:0xf bound_ctrl:1
	v_pk_fma_f32 v[176:177], v[54:55], v[234:235], v[176:177] op_sel_hi:[1,0,1] neg_lo:[0,0,1] neg_hi:[0,0,1]
	v_pk_fma_f32 v[156:157], v[56:57], v[234:235], v[156:157] op_sel_hi:[1,0,1] neg_lo:[0,0,1] neg_hi:[0,0,1]
	v_fma_f32 v180, v60, v234, -v180
	v_pk_add_f32 v[176:177], v[176:177], v[182:183] neg_lo:[0,1] neg_hi:[0,1]
	v_pk_add_f32 v[156:157], v[156:157], v[186:187] neg_lo:[0,1] neg_hi:[0,1]
	v_sub_f32_e32 v180, v180, v190
	v_pk_mul_f32 v[222:223], v[176:177], v[176:177]
	v_pk_fma_f32 v[222:223], v[156:157], v[156:157], v[222:223]
	v_add_f32_e32 v222, v222, v223
	v_fmac_f32_e32 v222, v180, v180
	v_cndmask_b32_e64 v223, 0, v222, s[12:13]
	v_add_f32_e32 v0, v0, v223
	s_add_i32 s4, s34, 7
	s_min_i32 s4, s4, 0x200
	s_mul_i32 s5, s4, 0x804
	s_add_i32 s5, s5, s35
	s_add_i32 s6, s5, 0x0
	s_add_i32 s7, s5, 0x101004
	s_add_i32 s8, s5, 0x202008
	s_add_i32 s11, s5, 0x30300c
	s_add_i32 s15, s5, 0x404010
	s_mul_i32 s9, s4, 0x180c
	s_add_i32 s9, s9, s33
	buffer_load_dword v46, v28, s[16:19], s6 offen nt
	buffer_load_dword v47, v28, s[16:19], s7 offen nt
	buffer_load_dword v54, v28, s[16:19], s8 offen nt
	buffer_load_dword v55, v28, s[16:19], s11 offen nt
	buffer_load_dword v56, v28, s[16:19], s15 offen nt
	buffer_load_dwordx3 v[80:82], v27, s[24:27], s9 offen nt
	s_waitcnt vmcnt(12)
	v_mov_b32_dpp v92, v36 wave_shr:1 row_mask:0xf bank_mask:0xf bound_ctrl:1
	v_mov_b32_dpp v93, v37 wave_shr:1 row_mask:0xf bank_mask:0xf bound_ctrl:1
	v_mov_b32_dpp v94, v38 wave_shr:1 row_mask:0xf bank_mask:0xf bound_ctrl:1
	v_mov_b32_dpp v128, v36 wave_shl:1 row_mask:0xf bank_mask:0xf bound_ctrl:1
	v_mov_b32_dpp v129, v37 wave_shl:1 row_mask:0xf bank_mask:0xf bound_ctrl:1
	v_mov_b32_dpp v130, v38 wave_shl:1 row_mask:0xf bank_mask:0xf bound_ctrl:1
	v_mov_b32_dpp v98, v20 wave_shr:1 row_mask:0xf bank_mask:0xf bound_ctrl:1
	v_mov_b32_dpp v99, v21 wave_shr:1 row_mask:0xf bank_mask:0xf bound_ctrl:1
	v_mov_b32_dpp v110, v24 wave_shr:1 row_mask:0xf bank_mask:0xf bound_ctrl:1
	v_mov_b32_dpp v111, v25 wave_shr:1 row_mask:0xf bank_mask:0xf bound_ctrl:1
	v_mov_b32_dpp v60, v30 wave_shr:1 row_mask:0xf bank_mask:0xf bound_ctrl:1
	v_mov_b32_dpp v146, v20 wave_shl:1 row_mask:0xf bank_mask:0xf bound_ctrl:1
	v_mov_b32_dpp v147, v21 wave_shl:1 row_mask:0xf bank_mask:0xf bound_ctrl:1
	v_mov_b32_dpp v154, v24 wave_shl:1 row_mask:0xf bank_mask:0xf bound_ctrl:1
	v_mov_b32_dpp v155, v25 wave_shl:1 row_mask:0xf bank_mask:0xf bound_ctrl:1
	v_mov_b32_dpp v84, v30 wave_shl:1 row_mask:0xf bank_mask:0xf bound_ctrl:1
	v_pk_mul_f32 v[156:157], v[20:21], v[36:37] op_sel_hi:[1,0]
	v_pk_mul_f32 v[176:177], v[24:25], v[36:37] op_sel_hi:[1,0]
	v_mul_f32_e32 v158, v30, v36
	v_pk_mul_f32 v[180:181], v[20:21], v[36:37] op_sel:[0,1]
	v_pk_mul_f32 v[184:185], v[24:25], v[36:37] op_sel:[0,1]
	v_mul_f32_e32 v162, v30, v37
	v_pk_mul_f32 v[188:189], v[20:21], v[38:39] op_sel_hi:[1,0]
	v_pk_mul_f32 v[192:193], v[24:25], v[38:39] op_sel_hi:[1,0]
	v_mul_f32_e32 v166, v30, v38
	v_pk_add_f32 v[196:197], v[20:21], v[98:99]
	v_pk_add_f32 v[208:209], v[24:25], v[110:111]
	v_add_f32_e32 v182, v30, v60
	v_pk_fma_f32 v[156:157], v[98:99], v[92:93], v[156:157] op_sel_hi:[1,0,1]
	v_pk_fma_f32 v[176:177], v[110:111], v[92:93], v[176:177] op_sel_hi:[1,0,1]
	v_fmac_f32_e32 v158, v60, v92
	v_pk_fma_f32 v[180:181], v[98:99], v[92:93], v[180:181] op_sel:[0,1,0]
	v_pk_fma_f32 v[184:185], v[110:111], v[92:93], v[184:185] op_sel:[0,1,0]
	v_fmac_f32_e32 v162, v60, v93
	v_pk_fma_f32 v[188:189], v[98:99], v[94:95], v[188:189] op_sel_hi:[1,0,1]
	v_pk_fma_f32 v[192:193], v[110:111], v[94:95], v[192:193] op_sel_hi:[1,0,1]
	v_fmac_f32_e32 v166, v60, v94
	v_pk_add_f32 v[196:197], v[196:197], v[146:147]
	v_pk_add_f32 v[208:209], v[208:209], v[154:155]
	v_add_f32_e32 v182, v182, v84
	v_pk_fma_f32 v[156:157], v[146:147], v[128:129], v[156:157] op_sel_hi:[1,0,1]
	v_pk_fma_f32 v[176:177], v[154:155], v[128:129], v[176:177] op_sel_hi:[1,0,1]
	v_fmac_f32_e32 v158, v84, v128
	v_pk_fma_f32 v[180:181], v[146:147], v[128:129], v[180:181] op_sel:[0,1,0]
	v_pk_fma_f32 v[184:185], v[154:155], v[128:129], v[184:185] op_sel:[0,1,0]
	v_fmac_f32_e32 v162, v84, v129
	v_pk_fma_f32 v[188:189], v[146:147], v[130:131], v[188:189] op_sel_hi:[1,0,1]
	v_pk_fma_f32 v[192:193], v[154:155], v[130:131], v[192:193] op_sel_hi:[1,0,1]
	v_fmac_f32_e32 v166, v84, v130
	s_barrier
	ds_read_b128 v[220:223], v23 offset:3072
	ds_read_b128 v[228:231], v23 offset:4096
	ds_read_b128 v[232:235], v23 offset:5120
	v_pk_add_f32 v[60:61], v[52:53], v[196:197]
	v_pk_add_f32 v[52:53], v[58:59], v[208:209]
	v_add_f32_e32 v58, v122, v182
	v_pk_add_f32 v[98:99], v[152:153], v[156:157]
	v_pk_add_f32 v[110:111], v[70:71], v[176:177]
	v_add_f32_e32 v84, v106, v158
	v_pk_add_f32 v[70:71], v[76:77], v[180:181]
	v_pk_add_f32 v[106:107], v[74:75], v[184:185]
	v_add_f32_e32 v76, v78, v162
	v_pk_add_f32 v[74:75], v[96:97], v[188:189]
	v_pk_add_f32 v[78:79], v[86:87], v[192:193]
	v_add_f32_e32 v96, v102, v166
	s_waitcnt lgkmcnt(2)
	v_pk_fma_f32 v[98:99], v[220:221], v[60:61], v[98:99] op_sel_hi:[0,1,1] neg_lo:[1,0,0] neg_hi:[1,0,0]
	v_pk_fma_f32 v[110:111], v[220:221], v[52:53], v[110:111] op_sel_hi:[0,1,1] neg_lo:[1,0,0] neg_hi:[1,0,0]
	v_fma_f32 v84, -v220, v58, v84
	v_pk_fma_f32 v[70:71], v[220:221], v[60:61], v[70:71] op_sel:[1,0,0] neg_lo:[1,0,0] neg_hi:[1,0,0]
	v_pk_fma_f32 v[106:107], v[220:221], v[52:53], v[106:107] op_sel:[1,0,0] neg_lo:[1,0,0] neg_hi:[1,0,0]
	v_fma_f32 v76, -v221, v58, v76
	v_pk_fma_f32 v[74:75], v[222:223], v[60:61], v[74:75] op_sel_hi:[0,1,1] neg_lo:[1,0,0] neg_hi:[1,0,0]
	v_pk_fma_f32 v[78:79], v[222:223], v[52:53], v[78:79] op_sel_hi:[0,1,1] neg_lo:[1,0,0] neg_hi:[1,0,0]
	v_fma_f32 v96, -v222, v58, v96
	v_pk_mul_f32 v[152:153], v[222:223], v[98:99] op_sel:[1,0]
	v_pk_mul_f32 v[240:241], v[222:223], v[110:111] op_sel:[1,0]
	v_mul_f32_e32 v86, v223, v84
	s_waitcnt lgkmcnt(1)
	v_pk_mul_f32 v[224:225], v[228:229], v[98:99] op_sel_hi:[0,1]
	v_pk_mul_f32 v[244:245], v[228:229], v[110:111] op_sel_hi:[0,1]
	v_mul_f32_e32 v102, v228, v84
	v_pk_mul_f32 v[236:237], v[228:229], v[98:99] op_sel:[1,0]
	v_pk_mul_f32 v[248:249], v[228:229], v[110:111] op_sel:[1,0]
	v_mul_f32_e32 v122, v229, v84
	v_pk_fma_f32 v[152:153], v[228:229], v[70:71], v[152:153] op_sel_hi:[0,1,1]
	v_pk_fma_f32 v[240:241], v[228:229], v[106:107], v[240:241] op_sel_hi:[0,1,1]
	v_fmac_f32_e32 v86, v228, v76
	v_pk_fma_f32 v[224:225], v[230:231], v[70:71], v[224:225] op_sel_hi:[0,1,1]
	v_pk_fma_f32 v[244:245], v[230:231], v[106:107], v[244:245] op_sel_hi:[0,1,1]
	v_fmac_f32_e32 v102, v230, v76
	v_pk_fma_f32 v[236:237], v[230:231], v[70:71], v[236:237] op_sel:[1,0,0]
	v_pk_fma_f32 v[248:249], v[230:231], v[106:107], v[248:249] op_sel:[1,0,0]
	v_fmac_f32_e32 v122, v231, v76
	v_pk_fma_f32 v[152:153], v[228:229], v[74:75], v[152:153] op_sel:[1,0,0]
	v_pk_fma_f32 v[240:241], v[228:229], v[78:79], v[240:241] op_sel:[1,0,0]
	v_fmac_f32_e32 v86, v229, v96
	v_pk_fma_f32 v[224:225], v[230:231], v[74:75], v[224:225] op_sel:[1,0,0]
	v_pk_fma_f32 v[244:245], v[230:231], v[78:79], v[244:245] op_sel:[1,0,0]
	v_fmac_f32_e32 v102, v231, v96
	s_waitcnt lgkmcnt(0)
	v_pk_fma_f32 v[236:237], v[232:233], v[74:75], v[236:237] op_sel_hi:[0,1,1]
	v_pk_fma_f32 v[248:249], v[232:233], v[78:79], v[248:249] op_sel_hi:[0,1,1]
	v_fmac_f32_e32 v122, v232, v96
	v_pk_mul_f32 v[146:147], v[220:221], v[152:153] op_sel_hi:[0,1]
	v_pk_mul_f32 v[154:155], v[220:221], v[240:241] op_sel_hi:[0,1]
	v_mul_f32_e32 v186, v220, v86
	v_pk_fma_f32 v[146:147], v[220:221], v[224:225], v[146:147] op_sel:[1,0,0]
	v_pk_fma_f32 v[154:155], v[220:221], v[244:245], v[154:155] op_sel:[1,0,0]
	v_fmac_f32_e32 v186, v221, v102
	v_pk_fma_f32 v[146:147], v[222:223], v[236:237], v[146:147] op_sel_hi:[0,1,1]
	v_pk_fma_f32 v[154:155], v[222:223], v[248:249], v[154:155] op_sel_hi:[0,1,1]
	v_fmac_f32_e32 v186, v222, v122
	v_pk_fma_f32 v[146:147], v[232:233], v[60:61], v[146:147] op_sel:[1,0,0] neg_lo:[0,0,1] neg_hi:[0,0,1]
	v_pk_fma_f32 v[154:155], v[232:233], v[52:53], v[154:155] op_sel:[1,0,0] neg_lo:[0,0,1] neg_hi:[0,0,1]
	v_fma_f32 v186, v233, v58, -v186
	v_cmp_eq_u32_e64 s[10:11], 1, v235
	v_cmp_eq_u32_e64 s[14:15], 2, v235
	v_cmp_eq_u32_e64 s[20:21], 3, v235
	v_cmp_eq_u32_e64 s[22:23], 4, v235
	v_cmp_eq_u32_e64 s[30:31], 5, v235
	v_pk_add_f32 v[52:53], v[68:69], v[152:153]
	v_pk_add_f32 v[58:59], v[62:63], v[240:241]
	v_add_f32_e32 v60, v100, v86
	v_pk_add_f32 v[62:63], v[160:161], v[224:225]
	v_pk_add_f32 v[68:69], v[138:139], v[244:245]
	v_add_f32_e32 v70, v164, v102
	v_pk_add_f32 v[74:75], v[168:169], v[236:237]
	v_pk_add_f32 v[76:77], v[150:151], v[248:249]
	v_add_f32_e32 v78, v172, v122
	v_pk_add_f32 v[84:85], v[170:171], v[146:147]
	v_pk_add_f32 v[98:99], v[174:175], v[154:155]
	v_add_f32_e32 v96, v178, v186
	v_pk_fma_f32 v[100:101], v[112:113], v[52:53], v[84:85] op_sel_hi:[0,1,1]
	v_pk_fma_f32 v[106:107], v[112:113], v[58:59], v[98:99] op_sel_hi:[0,1,1]
	v_fma_f32 v160, v112, v60, v96
	v_pk_fma_f32 v[164:165], v[132:133], v[52:53], v[84:85] op_sel_hi:[0,1,1]
	v_pk_fma_f32 v[110:111], v[132:133], v[58:59], v[98:99] op_sel_hi:[0,1,1]
	v_fma_f32 v168, v132, v60, v96
	v_pk_fma_f32 v[100:101], v[112:113], v[62:63], v[100:101] op_sel:[1,0,0]
	v_pk_fma_f32 v[106:107], v[112:113], v[68:69], v[106:107] op_sel:[1,0,0]
	v_fmac_f32_e32 v160, v113, v70
	v_pk_fma_f32 v[164:165], v[132:133], v[62:63], v[164:165] op_sel:[1,0,0]
	v_pk_fma_f32 v[110:111], v[132:133], v[68:69], v[110:111] op_sel:[1,0,0]
	v_fmac_f32_e32 v168, v133, v70
	v_pk_fma_f32 v[100:101], v[114:115], v[74:75], v[100:101] op_sel_hi:[0,1,1]
	v_pk_fma_f32 v[106:107], v[114:115], v[76:77], v[106:107] op_sel_hi:[0,1,1]
	v_fmac_f32_e32 v160, v114, v78
	v_pk_fma_f32 v[164:165], v[134:135], v[74:75], v[164:165] op_sel_hi:[0,1,1]
	v_pk_fma_f32 v[110:111], v[134:135], v[76:77], v[110:111] op_sel_hi:[0,1,1]
	v_fmac_f32_e32 v168, v134, v78
	v_pk_fma_f32 v[84:85], v[8:9], v[52:53], v[84:85] op_sel_hi:[0,1,1]
	v_pk_fma_f32 v[98:99], v[8:9], v[58:59], v[98:99] op_sel_hi:[0,1,1]
	v_fmac_f32_e32 v96, v8, v60
	v_pk_fma_f32 v[84:85], v[8:9], v[62:63], v[84:85] op_sel:[1,0,0]
	v_pk_fma_f32 v[98:99], v[8:9], v[68:69], v[98:99] op_sel:[1,0,0]
	v_fmac_f32_e32 v96, v9, v70
	v_pk_fma_f32 v[84:85], v[10:11], v[74:75], v[84:85] op_sel_hi:[0,1,1]
	v_pk_fma_f32 v[98:99], v[10:11], v[76:77], v[98:99] op_sel_hi:[0,1,1]
	v_fmac_f32_e32 v96, v10, v78
	v_cndmask_b32_e64 v138, 0, v1, s[10:11]
	v_cndmask_b32_e64 v139, 0, v1, s[14:15]
	v_cndmask_b32_e64 v172, 0, v1, s[20:21]
	v_cndmask_b32_e64 v173, 0, v1, s[22:23]
	v_cndmask_b32_e64 v150, 0, v1, s[30:31]
	v_add_f32_dpp v84, v100, v84 wave_shl:1 row_mask:0xf bank_mask:0xf bound_ctrl:1
	v_add_f32_dpp v85, v101, v85 wave_shl:1 row_mask:0xf bank_mask:0xf bound_ctrl:1
	v_add_f32_dpp v98, v106, v98 wave_shl:1 row_mask:0xf bank_mask:0xf bound_ctrl:1
	v_add_f32_dpp v99, v107, v99 wave_shl:1 row_mask:0xf bank_mask:0xf bound_ctrl:1
	v_add_f32_dpp v96, v160, v96 wave_shl:1 row_mask:0xf bank_mask:0xf bound_ctrl:1
	s_add_i32 s4, s34, 3
	s_cmpk_lt_i32 s4, 0x201
	s_cselect_b64 s[12:13], s[0:1], 0
	v_add_f32_dpp v84, v164, v84 wave_shr:1 row_mask:0xf bank_mask:0xf bound_ctrl:1
	v_add_f32_dpp v85, v165, v85 wave_shr:1 row_mask:0xf bank_mask:0xf bound_ctrl:1
	v_add_f32_dpp v98, v110, v98 wave_shr:1 row_mask:0xf bank_mask:0xf bound_ctrl:1
	v_add_f32_dpp v99, v111, v99 wave_shr:1 row_mask:0xf bank_mask:0xf bound_ctrl:1
	v_add_f32_dpp v96, v168, v96 wave_shr:1 row_mask:0xf bank_mask:0xf bound_ctrl:1
	v_pk_fma_f32 v[84:85], v[2:3], v[234:235], v[84:85] op_sel_hi:[1,0,1] neg_lo:[0,0,1] neg_hi:[0,0,1]
	v_pk_fma_f32 v[98:99], v[4:5], v[234:235], v[98:99] op_sel_hi:[1,0,1] neg_lo:[0,0,1] neg_hi:[0,0,1]
	v_fma_f32 v96, v6, v234, -v96
	v_pk_add_f32 v[84:85], v[84:85], v[138:139] neg_lo:[0,1] neg_hi:[0,1]
	v_pk_add_f32 v[98:99], v[98:99], v[172:173] neg_lo:[0,1] neg_hi:[0,1]
	v_sub_f32_e32 v96, v96, v150
	v_pk_mul_f32 v[170:171], v[84:85], v[84:85]
	v_pk_fma_f32 v[170:171], v[98:99], v[98:99], v[170:171]
	v_add_f32_e32 v170, v170, v171
	v_fmac_f32_e32 v170, v96, v96
	v_cndmask_b32_e64 v171, 0, v170, s[12:13]
	v_add_f32_e32 v0, v0, v171
	s_add_i32 s4, s34, 8
	s_min_i32 s4, s4, 0x200
	s_mul_i32 s5, s4, 0x804
	s_add_i32 s5, s5, s35
	s_add_i32 s6, s5, 0x0
	s_add_i32 s7, s5, 0x101004
	s_add_i32 s8, s5, 0x202008
	s_add_i32 s11, s5, 0x30300c
	s_add_i32 s15, s5, 0x404010
	s_mul_i32 s9, s4, 0x180c
	s_add_i32 s9, s9, s33
	buffer_load_dword v2, v28, s[16:19], s6 offen nt
	buffer_load_dword v3, v28, s[16:19], s7 offen nt
	buffer_load_dword v4, v28, s[16:19], s8 offen nt
	buffer_load_dword v5, v28, s[16:19], s11 offen nt
	buffer_load_dword v6, v28, s[16:19], s15 offen nt
	buffer_load_dwordx3 v[8:10], v27, s[24:27], s9 offen nt
	s_waitcnt vmcnt(12)
	v_mov_b32_dpp v60, v48 wave_shr:1 row_mask:0xf bank_mask:0xf bound_ctrl:1
	v_mov_b32_dpp v61, v49 wave_shr:1 row_mask:0xf bank_mask:0xf bound_ctrl:1
	v_mov_b32_dpp v62, v50 wave_shr:1 row_mask:0xf bank_mask:0xf bound_ctrl:1
	v_mov_b32_dpp v68, v48 wave_shl:1 row_mask:0xf bank_mask:0xf bound_ctrl:1
	v_mov_b32_dpp v69, v49 wave_shl:1 row_mask:0xf bank_mask:0xf bound_ctrl:1
	v_mov_b32_dpp v70, v50 wave_shl:1 row_mask:0xf bank_mask:0xf bound_ctrl:1
	v_mov_b32_dpp v58, v40 wave_shr:1 row_mask:0xf bank_mask:0xf bound_ctrl:1
	v_mov_b32_dpp v59, v41 wave_shr:1 row_mask:0xf bank_mask:0xf bound_ctrl:1
	v_mov_b32_dpp v52, v42 wave_shr:1 row_mask:0xf bank_mask:0xf bound_ctrl:1
	v_mov_b32_dpp v53, v43 wave_shr:1 row_mask:0xf bank_mask:0xf bound_ctrl:1
	v_mov_b32_dpp v74, v44 wave_shr:1 row_mask:0xf bank_mask:0xf bound_ctrl:1
	v_mov_b32_dpp v78, v40 wave_shl:1 row_mask:0xf bank_mask:0xf bound_ctrl:1
	v_mov_b32_dpp v79, v41 wave_shl:1 row_mask:0xf bank_mask:0xf bound_ctrl:1
	v_mov_b32_dpp v76, v42 wave_shl:1 row_mask:0xf bank_mask:0xf bound_ctrl:1
	v_mov_b32_dpp v77, v43 wave_shl:1 row_mask:0xf bank_mask:0xf bound_ctrl:1
	v_mov_b32_dpp v98, v44 wave_shl:1 row_mask:0xf bank_mask:0xf bound_ctrl:1
	v_pk_mul_f32 v[84:85], v[40:41], v[48:49] op_sel_hi:[1,0]
	v_pk_mul_f32 v[106:107], v[42:43], v[48:49] op_sel_hi:[1,0]
	v_mul_f32_e32 v96, v44, v48
	v_pk_mul_f32 v[100:101], v[40:41], v[48:49] op_sel:[0,1]
	v_pk_mul_f32 v[110:111], v[42:43], v[48:49] op_sel:[0,1]
	v_mul_f32_e32 v112, v44, v49
	v_pk_mul_f32 v[132:133], v[40:41], v[50:51] op_sel_hi:[1,0]
	v_pk_mul_f32 v[114:115], v[42:43], v[50:51] op_sel_hi:[1,0]
	v_mul_f32_e32 v160, v44, v50
	v_pk_add_f32 v[164:165], v[40:41], v[58:59]
	v_pk_add_f32 v[134:135], v[42:43], v[52:53]
	v_add_f32_e32 v168, v44, v74
	v_pk_fma_f32 v[84:85], v[58:59], v[60:61], v[84:85] op_sel_hi:[1,0,1]
	v_pk_fma_f32 v[106:107], v[52:53], v[60:61], v[106:107] op_sel_hi:[1,0,1]
	v_fmac_f32_e32 v96, v74, v60
	v_pk_fma_f32 v[100:101], v[58:59], v[60:61], v[100:101] op_sel:[0,1,0]
	v_pk_fma_f32 v[110:111], v[52:53], v[60:61], v[110:111] op_sel:[0,1,0]
	v_fmac_f32_e32 v112, v74, v61
	v_pk_fma_f32 v[132:133], v[58:59], v[62:63], v[132:133] op_sel_hi:[1,0,1]
	v_pk_fma_f32 v[114:115], v[52:53], v[62:63], v[114:115] op_sel_hi:[1,0,1]
	v_fmac_f32_e32 v160, v74, v62
	v_pk_add_f32 v[164:165], v[164:165], v[78:79]
	v_pk_add_f32 v[134:135], v[134:135], v[76:77]
	v_add_f32_e32 v168, v168, v98
	v_pk_fma_f32 v[84:85], v[78:79], v[68:69], v[84:85] op_sel_hi:[1,0,1]
	v_pk_fma_f32 v[106:107], v[76:77], v[68:69], v[106:107] op_sel_hi:[1,0,1]
	v_fmac_f32_e32 v96, v98, v68
	v_pk_fma_f32 v[100:101], v[78:79], v[68:69], v[100:101] op_sel:[0,1,0]
	v_pk_fma_f32 v[110:111], v[76:77], v[68:69], v[110:111] op_sel:[0,1,0]
	v_fmac_f32_e32 v112, v98, v69
	v_pk_fma_f32 v[132:133], v[78:79], v[70:71], v[132:133] op_sel_hi:[1,0,1]
	v_pk_fma_f32 v[114:115], v[76:77], v[70:71], v[114:115] op_sel_hi:[1,0,1]
	v_fmac_f32_e32 v160, v98, v70
	s_barrier
	ds_read_b128 v[76:79], v23 offset:0
	ds_read_b128 v[172:175], v23 offset:1024
	ds_read_b128 v[220:223], v23 offset:2048
	v_pk_add_f32 v[58:59], v[196:197], v[164:165]
	v_pk_add_f32 v[52:53], v[144:145], v[58:59]
	v_pk_add_f32 v[144:145], v[208:209], v[134:135]
	v_pk_add_f32 v[74:75], v[206:207], v[144:145]
	v_add_f32_e32 v98, v182, v168
	v_add_f32_e32 v138, v148, v98
	v_pk_add_f32 v[150:151], v[156:157], v[84:85]
	v_pk_add_f32 v[170:171], v[72:73], v[150:151]
	v_pk_add_f32 v[72:73], v[176:177], v[106:107]
	v_pk_add_f32 v[148:149], v[126:127], v[72:73]
	v_add_f32_e32 v126, v158, v96
	v_add_f32_e32 v156, v108, v126
	v_pk_add_f32 v[158:159], v[180:181], v[100:101]
	v_pk_add_f32 v[178:179], v[120:121], v[158:159]
	v_pk_add_f32 v[108:109], v[184:185], v[110:111]
	v_pk_add_f32 v[120:121], v[142:143], v[108:109]
	v_add_f32_e32 v142, v162, v112
	v_add_f32_e32 v176, v124, v142
	v_pk_add_f32 v[162:163], v[188:189], v[132:133]
	v_pk_add_f32 v[182:183], v[136:137], v[162:163]
	v_pk_add_f32 v[124:125], v[192:193], v[114:115]
	v_pk_add_f32 v[136:137], v[194:195], v[124:125]
	v_add_f32_e32 v190, v166, v160
	v_add_f32_e32 v180, v140, v190
	s_waitcnt lgkmcnt(2)
	v_pk_fma_f32 v[170:171], v[76:77], v[52:53], v[170:171] op_sel_hi:[0,1,1] neg_lo:[1,0,0] neg_hi:[1,0,0]
	v_pk_fma_f32 v[148:149], v[76:77], v[74:75], v[148:149] op_sel_hi:[0,1,1] neg_lo:[1,0,0] neg_hi:[1,0,0]
	v_fma_f32 v156, -v76, v138, v156
	v_pk_fma_f32 v[178:179], v[76:77], v[52:53], v[178:179] op_sel:[1,0,0] neg_lo:[1,0,0] neg_hi:[1,0,0]
	v_pk_fma_f32 v[120:121], v[76:77], v[74:75], v[120:121] op_sel:[1,0,0] neg_lo:[1,0,0] neg_hi:[1,0,0]
	v_fma_f32 v176, -v77, v138, v176
	v_pk_fma_f32 v[182:183], v[78:79], v[52:53], v[182:183] op_sel_hi:[0,1,1] neg_lo:[1,0,0] neg_hi:[1,0,0]
	v_pk_fma_f32 v[136:137], v[78:79], v[74:75], v[136:137] op_sel_hi:[0,1,1] neg_lo:[1,0,0] neg_hi:[1,0,0]
	v_fma_f32 v180, -v78, v138, v180
	v_pk_mul_f32 v[140:141], v[78:79], v[170:171] op_sel:[1,0]
	v_pk_mul_f32 v[166:167], v[78:79], v[148:149] op_sel:[1,0]
	v_mul_f32_e32 v210, v79, v156
	s_waitcnt lgkmcnt(1)
	v_pk_mul_f32 v[184:185], v[172:173], v[170:171] op_sel_hi:[0,1]
	v_pk_mul_f32 v[194:195], v[172:173], v[148:149] op_sel_hi:[0,1]
	v_mul_f32_e32 v230, v172, v156
	v_pk_mul_f32 v[188:189], v[172:173], v[170:171] op_sel:[1,0]
	v_pk_mul_f32 v[206:207], v[172:173], v[148:149] op_sel:[1,0]
	v_mul_f32_e32 v234, v173, v156
	v_pk_fma_f32 v[140:141], v[172:173], v[178:179], v[140:141] op_sel_hi:[0,1,1]
	v_pk_fma_f32 v[166:167], v[172:173], v[120:121], v[166:167] op_sel_hi:[0,1,1]
	v_fmac_f32_e32 v210, v172, v176
	v_pk_fma_f32 v[184:185], v[174:175], v[178:179], v[184:185] op_sel_hi:[0,1,1]
	v_pk_fma_f32 v[194:195], v[174:175], v[120:121], v[194:195] op_sel_hi:[0,1,1]
	v_fmac_f32_e32 v230, v174, v176
	v_pk_fma_f32 v[188:189], v[174:175], v[178:179], v[188:189] op_sel:[1,0,0]
	v_pk_fma_f32 v[206:207], v[174:175], v[120:121], v[206:207] op_sel:[1,0,0]
	v_fmac_f32_e32 v234, v175, v176
	v_pk_fma_f32 v[140:141], v[172:173], v[182:183], v[140:141] op_sel:[1,0,0]
	v_pk_fma_f32 v[166:167], v[172:173], v[136:137], v[166:167] op_sel:[1,0,0]
	v_fmac_f32_e32 v210, v173, v180
	v_pk_fma_f32 v[184:185], v[174:175], v[182:183], v[184:185] op_sel:[1,0,0]
	v_pk_fma_f32 v[194:195], v[174:175], v[136:137], v[194:195] op_sel:[1,0,0]
	v_fmac_f32_e32 v230, v175, v180
	s_waitcnt lgkmcnt(0)
	v_pk_fma_f32 v[188:189], v[220:221], v[182:183], v[188:189] op_sel_hi:[0,1,1]
	v_pk_fma_f32 v[206:207], v[220:221], v[136:137], v[206:207] op_sel_hi:[0,1,1]
	v_fmac_f32_e32 v234, v220, v180
	v_pk_mul_f32 v[238:239], v[76:77], v[140:141] op_sel_hi:[0,1]
	v_pk_mul_f32 v[192:193], v[76:77], v[166:167] op_sel_hi:[0,1]
	v_mul_f32_e32 v196, v76, v210
	v_pk_fma_f32 v[238:239], v[76:77], v[184:185], v[238:239] op_sel:[1,0,0]
	v_pk_fma_f32 v[192:193], v[76:77], v[194:195], v[192:193] op_sel:[1,0,0]
	v_fmac_f32_e32 v196, v77, v230
	v_pk_fma_f32 v[238:239], v[78:79], v[188:189], v[238:239] op_sel_hi:[0,1,1]
	v_pk_fma_f32 v[192:193], v[78:79], v[206:207], v[192:193] op_sel_hi:[0,1,1]
	v_fmac_f32_e32 v196, v78, v234
	v_pk_fma_f32 v[238:239], v[220:221], v[52:53], v[238:239] op_sel:[1,0,0] neg_lo:[0,0,1] neg_hi:[0,0,1]
	v_pk_fma_f32 v[192:193], v[220:221], v[74:75], v[192:193] op_sel:[1,0,0] neg_lo:[0,0,1] neg_hi:[0,0,1]
	v_fma_f32 v196, v221, v138, -v196
	v_cmp_eq_u32_e64 s[10:11], 1, v223
	v_cmp_eq_u32_e64 s[14:15], 2, v223
	v_cmp_eq_u32_e64 s[20:21], 3, v223
	v_cmp_eq_u32_e64 s[22:23], 4, v223
	v_cmp_eq_u32_e64 s[30:31], 5, v223
	v_pk_add_f32 v[52:53], v[152:153], v[140:141]
	v_pk_add_f32 v[74:75], v[118:119], v[52:53]
	v_pk_add_f32 v[120:121], v[240:241], v[166:167]
	v_pk_add_f32 v[118:119], v[214:215], v[120:121]
	v_add_f32_e32 v138, v86, v210
	v_add_f32_e32 v136, v104, v138
	v_pk_add_f32 v[104:105], v[224:225], v[184:185]
	v_pk_add_f32 v[86:87], v[198:199], v[104:105]
	v_pk_add_f32 v[148:149], v[244:245], v[194:195]
	v_pk_add_f32 v[152:153], v[218:219], v[148:149]
	v_add_f32_e32 v170, v102, v230
	v_add_f32_e32 v156, v116, v170
	v_pk_add_f32 v[116:117], v[236:237], v[188:189]
	v_pk_add_f32 v[102:103], v[202:203], v[116:117]
	v_pk_add_f32 v[176:177], v[248:249], v[206:207]
	v_pk_add_f32 v[178:179], v[226:227], v[176:177]
	v_add_f32_e32 v182, v122, v234
	v_add_f32_e32 v180, v200, v182
	v_pk_add_f32 v[122:123], v[146:147], v[238:239]
	v_pk_add_f32 v[200:201], v[204:205], v[122:123]
	v_pk_add_f32 v[146:147], v[154:155], v[192:193]
	v_pk_add_f32 v[204:205], v[212:213], v[146:147]
	v_add_f32_e32 v154, v186, v196
	v_add_f32_e32 v198, v216, v154
	v_pk_fma_f32 v[208:209], v[64:65], v[74:75], v[200:201] op_sel_hi:[0,1,1]
	v_pk_fma_f32 v[212:213], v[64:65], v[118:119], v[204:205] op_sel_hi:[0,1,1]
	v_fma_f32 v186, v64, v136, v198
	v_pk_fma_f32 v[216:217], v[88:89], v[74:75], v[200:201] op_sel_hi:[0,1,1]
	v_pk_fma_f32 v[224:225], v[88:89], v[118:119], v[204:205] op_sel_hi:[0,1,1]
	v_fma_f32 v202, v88, v136, v198
	v_pk_fma_f32 v[208:209], v[64:65], v[86:87], v[208:209] op_sel:[1,0,0]
	v_pk_fma_f32 v[212:213], v[64:65], v[152:153], v[212:213] op_sel:[1,0,0]
	v_fmac_f32_e32 v186, v65, v156
	v_pk_fma_f32 v[216:217], v[88:89], v[86:87], v[216:217] op_sel:[1,0,0]
	v_pk_fma_f32 v[224:225], v[88:89], v[152:153], v[224:225] op_sel:[1,0,0]
	v_fmac_f32_e32 v202, v89, v156
	v_pk_fma_f32 v[208:209], v[66:67], v[102:103], v[208:209] op_sel_hi:[0,1,1]
	v_pk_fma_f32 v[212:213], v[66:67], v[178:179], v[212:213] op_sel_hi:[0,1,1]
	v_fmac_f32_e32 v186, v66, v180
	v_pk_fma_f32 v[216:217], v[90:91], v[102:103], v[216:217] op_sel_hi:[0,1,1]
	v_pk_fma_f32 v[224:225], v[90:91], v[178:179], v[224:225] op_sel_hi:[0,1,1]
	v_fmac_f32_e32 v202, v90, v180
	v_pk_fma_f32 v[200:201], v[32:33], v[74:75], v[200:201] op_sel_hi:[0,1,1]
	v_pk_fma_f32 v[204:205], v[32:33], v[118:119], v[204:205] op_sel_hi:[0,1,1]
	v_fmac_f32_e32 v198, v32, v136
	v_pk_fma_f32 v[200:201], v[32:33], v[86:87], v[200:201] op_sel:[1,0,0]
	v_pk_fma_f32 v[204:205], v[32:33], v[152:153], v[204:205] op_sel:[1,0,0]
	v_fmac_f32_e32 v198, v33, v156
	v_pk_fma_f32 v[200:201], v[34:35], v[102:103], v[200:201] op_sel_hi:[0,1,1]
	v_pk_fma_f32 v[204:205], v[34:35], v[178:179], v[204:205] op_sel_hi:[0,1,1]
	v_fmac_f32_e32 v198, v34, v180
	v_cndmask_b32_e64 v214, 0, v1, s[10:11]
	v_cndmask_b32_e64 v215, 0, v1, s[14:15]
	v_cndmask_b32_e64 v218, 0, v1, s[20:21]
	v_cndmask_b32_e64 v219, 0, v1, s[22:23]
	v_cndmask_b32_e64 v228, 0, v1, s[30:31]
	v_add_f32_dpp v200, v208, v200 wave_shl:1 row_mask:0xf bank_mask:0xf bound_ctrl:1
	v_add_f32_dpp v201, v209, v201 wave_shl:1 row_mask:0xf bank_mask:0xf bound_ctrl:1
	v_add_f32_dpp v204, v212, v204 wave_shl:1 row_mask:0xf bank_mask:0xf bound_ctrl:1
	v_add_f32_dpp v205, v213, v205 wave_shl:1 row_mask:0xf bank_mask:0xf bound_ctrl:1
	v_add_f32_dpp v198, v186, v198 wave_shl:1 row_mask:0xf bank_mask:0xf bound_ctrl:1
	s_add_i32 s4, s34, 4
	s_cmpk_lt_i32 s4, 0x201
	s_cselect_b64 s[12:13], s[0:1], 0
	v_add_f32_dpp v200, v216, v200 wave_shr:1 row_mask:0xf bank_mask:0xf bound_ctrl:1
	v_add_f32_dpp v201, v217, v201 wave_shr:1 row_mask:0xf bank_mask:0xf bound_ctrl:1
	v_add_f32_dpp v204, v224, v204 wave_shr:1 row_mask:0xf bank_mask:0xf bound_ctrl:1
	v_add_f32_dpp v205, v225, v205 wave_shr:1 row_mask:0xf bank_mask:0xf bound_ctrl:1
	v_add_f32_dpp v198, v202, v198 wave_shr:1 row_mask:0xf bank_mask:0xf bound_ctrl:1
	v_pk_fma_f32 v[200:201], v[12:13], v[222:223], v[200:201] op_sel_hi:[1,0,1] neg_lo:[0,0,1] neg_hi:[0,0,1]
	v_pk_fma_f32 v[204:205], v[14:15], v[222:223], v[204:205] op_sel_hi:[1,0,1] neg_lo:[0,0,1] neg_hi:[0,0,1]
	v_fma_f32 v198, v16, v222, -v198
	v_pk_add_f32 v[200:201], v[200:201], v[214:215] neg_lo:[0,1] neg_hi:[0,1]
	v_pk_add_f32 v[204:205], v[204:205], v[218:219] neg_lo:[0,1] neg_hi:[0,1]
	v_sub_f32_e32 v198, v198, v228
	v_pk_mul_f32 v[226:227], v[200:201], v[200:201]
	v_pk_fma_f32 v[226:227], v[204:205], v[204:205], v[226:227]
	v_add_f32_e32 v226, v226, v227
	v_fmac_f32_e32 v226, v198, v198
	v_cndmask_b32_e64 v227, 0, v226, s[12:13]
	v_add_f32_e32 v0, v0, v227
	s_add_i32 s4, s34, 9
	s_min_i32 s4, s4, 0x200
	s_mul_i32 s5, s4, 0x804
	s_add_i32 s5, s5, s35
	s_add_i32 s6, s5, 0x0
	s_add_i32 s7, s5, 0x101004
	s_add_i32 s8, s5, 0x202008
	s_add_i32 s11, s5, 0x30300c
	s_add_i32 s15, s5, 0x404010
	s_mul_i32 s9, s4, 0x180c
	s_add_i32 s9, s9, s33
	buffer_load_dword v12, v28, s[16:19], s6 offen nt
	buffer_load_dword v13, v28, s[16:19], s7 offen nt
	buffer_load_dword v14, v28, s[16:19], s8 offen nt
	buffer_load_dword v15, v28, s[16:19], s11 offen nt
	buffer_load_dword v16, v28, s[16:19], s15 offen nt
	buffer_load_dwordx3 v[32:34], v27, s[24:27], s9 offen nt
	s_waitcnt vmcnt(12)
	v_mov_b32_dpp v64, v80 wave_shr:1 row_mask:0xf bank_mask:0xf bound_ctrl:1
	v_mov_b32_dpp v65, v81 wave_shr:1 row_mask:0xf bank_mask:0xf bound_ctrl:1
	v_mov_b32_dpp v66, v82 wave_shr:1 row_mask:0xf bank_mask:0xf bound_ctrl:1
	v_mov_b32_dpp v76, v80 wave_shl:1 row_mask:0xf bank_mask:0xf bound_ctrl:1
	v_mov_b32_dpp v77, v81 wave_shl:1 row_mask:0xf bank_mask:0xf bound_ctrl:1
	v_mov_b32_dpp v78, v82 wave_shl:1 row_mask:0xf bank_mask:0xf bound_ctrl:1
	v_mov_b32_dpp v88, v46 wave_shr:1 row_mask:0xf bank_mask:0xf bound_ctrl:1
	v_mov_b32_dpp v89, v47 wave_shr:1 row_mask:0xf bank_mask:0xf bound_ctrl:1
	v_mov_b32_dpp v136, v54 wave_shr:1 row_mask:0xf bank_mask:0xf bound_ctrl:1
	v_mov_b32_dpp v137, v55 wave_shr:1 row_mask:0xf bank_mask:0xf bound_ctrl:1
	v_mov_b32_dpp v74, v56 wave_shr:1 row_mask:0xf bank_mask:0xf bound_ctrl:1
	v_mov_b32_dpp v152, v46 wave_shl:1 row_mask:0xf bank_mask:0xf bound_ctrl:1
	v_mov_b32_dpp v153, v47 wave_shl:1 row_mask:0xf bank_mask:0xf bound_ctrl:1
	v_mov_b32_dpp v156, v54 wave_shl:1 row_mask:0xf bank_mask:0xf bound_ctrl:1
	v_mov_b32_dpp v157, v55 wave_shl:1 row_mask:0xf bank_mask:0xf bound_ctrl:1
	v_mov_b32_dpp v86, v56 wave_shl:1 row_mask:0xf bank_mask:0xf bound_ctrl:1
	v_pk_mul_f32 v[90:91], v[46:47], v[80:81] op_sel_hi:[1,0]
	v_pk_mul_f32 v[102:103], v[54:55], v[80:81] op_sel_hi:[1,0]
	v_mul_f32_e32 v172, v56, v80
	v_pk_mul_f32 v[118:119], v[46:47], v[80:81] op_sel:[0,1]
	v_pk_mul_f32 v[174:175], v[54:55], v[80:81] op_sel:[0,1]
	v_mul_f32_e32 v180, v56, v81
	v_pk_mul_f32 v[178:179], v[46:47], v[82:83] op_sel_hi:[1,0]
	v_pk_mul_f32 v[186:187], v[54:55], v[82:83] op_sel_hi:[1,0]
	v_mul_f32_e32 v200, v56, v82
	v_pk_add_f32 v[198:199], v[46:47], v[88:89]
	v_pk_add_f32 v[202:203], v[54:55], v[136:137]
	v_add_f32_e32 v204, v56, v74
	v_pk_fma_f32 v[90:91], v[88:89], v[64:65], v[90:91] op_sel_hi:[1,0,1]
	v_pk_fma_f32 v[102:103], v[136:137], v[64:65], v[102:103] op_sel_hi:[1,0,1]
	v_fmac_f32_e32 v172, v74, v64
	v_pk_fma_f32 v[118:119], v[88:89], v[64:65], v[118:119] op_sel:[0,1,0]
	v_pk_fma_f32 v[174:175], v[136:137], v[64:65], v[174:175] op_sel:[0,1,0]
	v_fmac_f32_e32 v180, v74, v65
	v_pk_fma_f32 v[178:179], v[88:89], v[66:67], v[178:179] op_sel_hi:[1,0,1]
	v_pk_fma_f32 v[186:187], v[136:137], v[66:67], v[186:187] op_sel_hi:[1,0,1]
	v_fmac_f32_e32 v200, v74, v66
	v_pk_add_f32 v[198:199], v[198:199], v[152:153]
	v_pk_add_f32 v[202:203], v[202:203], v[156:157]
	v_add_f32_e32 v204, v204, v86
	v_pk_fma_f32 v[90:91], v[152:153], v[76:77], v[90:91] op_sel_hi:[1,0,1]
	v_pk_fma_f32 v[102:103], v[156:157], v[76:77], v[102:103] op_sel_hi:[1,0,1]
	v_fmac_f32_e32 v172, v86, v76
	v_pk_fma_f32 v[118:119], v[152:153], v[76:77], v[118:119] op_sel:[0,1,0]
	v_pk_fma_f32 v[174:175], v[156:157], v[76:77], v[174:175] op_sel:[0,1,0]
	v_fmac_f32_e32 v180, v86, v77
	v_pk_fma_f32 v[178:179], v[152:153], v[78:79], v[178:179] op_sel_hi:[1,0,1]
	v_pk_fma_f32 v[186:187], v[156:157], v[78:79], v[186:187] op_sel_hi:[1,0,1]
	v_fmac_f32_e32 v200, v86, v78
	s_barrier
	ds_read_b128 v[212:215], v23 offset:3072
	ds_read_b128 v[216:219], v23 offset:4096
	ds_read_b128 v[220:223], v23 offset:5120
	v_pk_add_f32 v[74:75], v[58:59], v[198:199]
	v_pk_add_f32 v[58:59], v[144:145], v[202:203]
	v_add_f32_e32 v86, v98, v204
	v_pk_add_f32 v[88:89], v[150:151], v[90:91]
	v_pk_add_f32 v[136:137], v[72:73], v[102:103]
	v_add_f32_e32 v72, v126, v172
	v_pk_add_f32 v[144:145], v[158:159], v[118:119]
	v_pk_add_f32 v[152:153], v[108:109], v[174:175]
	v_add_f32_e32 v108, v142, v180
	v_pk_add_f32 v[156:157], v[162:163], v[178:179]
	v_pk_add_f32 v[208:209], v[124:125], v[186:187]
	v_add_f32_e32 v124, v190, v200
	s_waitcnt lgkmcnt(2)
	v_pk_fma_f32 v[88:89], v[212:213], v[74:75], v[88:89] op_sel_hi:[0,1,1] neg_lo:[1,0,0] neg_hi:[1,0,0]
	v_pk_fma_f32 v[136:137], v[212:213], v[58:59], v[136:137] op_sel_hi:[0,1,1] neg_lo:[1,0,0] neg_hi:[1,0,0]
	v_fma_f32 v72, -v212, v86, v72
	v_pk_fma_f32 v[144:145], v[212:213], v[74:75], v[144:145] op_sel:[1,0,0] neg_lo:[1,0,0] neg_hi:[1,0,0]
	v_pk_fma_f32 v[152:153], v[212:213], v[58:59], v[152:153] op_sel:[1,0,0] neg_lo:[1,0,0] neg_hi:[1,0,0]
	v_fma_f32 v108, -v213, v86, v108
	v_pk_fma_f32 v[156:157], v[214:215], v[74:75], v[156:157] op_sel_hi:[0,1,1] neg_lo:[1,0,0] neg_hi:[1,0,0]
	v_pk_fma_f32 v[208:209], v[214:215], v[58:59], v[208:209] op_sel_hi:[0,1,1] neg_lo:[1,0,0] neg_hi:[1,0,0]
	v_fma_f32 v124, -v214, v86, v124
	v_pk_mul_f32 v[98:99], v[214:215], v[88:89] op_sel:[1,0]
	v_pk_mul_f32 v[150:151], v[214:215], v[136:137] op_sel:[1,0]
	v_mul_f32_e32 v190, v215, v72
	s_waitcnt lgkmcnt(1)
	v_pk_mul_f32 v[126:127], v[216:217], v[88:89] op_sel_hi:[0,1]
	v_pk_mul_f32 v[158:159], v[216:217], v[136:137] op_sel_hi:[0,1]
	v_mul_f32_e32 v226, v216, v72
	v_pk_mul_f32 v[142:143], v[216:217], v[88:89] op_sel:[1,0]
	v_pk_mul_f32 v[162:163], v[216:217], v[136:137] op_sel:[1,0]
	v_mul_f32_e32 v242, v217, v72
	v_pk_fma_f32 v[98:99], v[216:217], v[144:145], v[98:99] op_sel_hi:[0,1,1]
	v_pk_fma_f32 v[150:151], v[216:217], v[152:153], v[150:151] op_sel_hi:[0,1,1]
	v_fmac_f32_e32 v190, v216, v108
	v_pk_fma_f32 v[126:127], v[218:219], v[144:145], v[126:127] op_sel_hi:[0,1,1]
	v_pk_fma_f32 v[158:159], v[218:219], v[152:153], v[158:159] op_sel_hi:[0,1,1]
	v_fmac_f32_e32 v226, v218, v108
	v_pk_fma_f32 v[142:143], v[218:219], v[144:145], v[142:143] op_sel:[1,0,0]
	v_pk_fma_f32 v[162:163], v[218:219], v[152:153], v[162:163] op_sel:[1,0,0]
	v_fmac_f32_e32 v242, v219, v108
	v_pk_fma_f32 v[98:99], v[216:217], v[156:157], v[98:99] op_sel:[1,0,0]
	v_pk_fma_f32 v[150:151], v[216:217], v[208:209], v[150:151] op_sel:[1,0,0]
	v_fmac_f32_e32 v190, v217, v124
	v_pk_fma_f32 v[126:127], v[218:219], v[156:157], v[126:127] op_sel:[1,0,0]
	v_pk_fma_f32 v[158:159], v[218:219], v[208:209], v[158:159] op_sel:[1,0,0]
	v_fmac_f32_e32 v226, v219, v124
	s_waitcnt lgkmcnt(0)
	v_pk_fma_f32 v[142:143], v[220:221], v[156:157], v[142:143] op_sel_hi:[0,1,1]
	v_pk_fma_f32 v[162:163], v[220:221], v[208:209], v[162:163] op_sel_hi:[0,1,1]
	v_fmac_f32_e32 v242, v220, v124
	v_pk_mul_f32 v[224:225], v[212:213], v[98:99] op_sel_hi:[0,1]
	v_pk_mul_f32 v[228:229], v[212:213], v[150:151] op_sel_hi:[0,1]
	v_mul_f32_e32 v232, v212, v190
	v_pk_fma_f32 v[224:225], v[212:213], v[126:127], v[224:225] op_sel:[1,0,0]
	v_pk_fma_f32 v[228:229], v[212:213], v[158:159], v[228:229] op_sel:[1,0,0]
	v_fmac_f32_e32 v232, v213, v226
	v_pk_fma_f32 v[224:225], v[214:215], v[142:143], v[224:225] op_sel_hi:[0,1,1]
	v_pk_fma_f32 v[228:229], v[214:215], v[162:163], v[228:229] op_sel_hi:[0,1,1]
	v_fmac_f32_e32 v232, v214, v242
	v_pk_fma_f32 v[224:225], v[220:221], v[74:75], v[224:225] op_sel:[1,0,0] neg_lo:[0,0,1] neg_hi:[0,0,1]
	v_pk_fma_f32 v[228:229], v[220:221], v[58:59], v[228:229] op_sel:[1,0,0] neg_lo:[0,0,1] neg_hi:[0,0,1]
	v_fma_f32 v232, v221, v86, -v232
	v_cmp_eq_u32_e64 s[10:11], 1, v223
	v_cmp_eq_u32_e64 s[14:15], 2, v223
	v_cmp_eq_u32_e64 s[20:21], 3, v223
	v_cmp_eq_u32_e64 s[22:23], 4, v223
	v_cmp_eq_u32_e64 s[30:31], 5, v223
	v_pk_add_f32 v[58:59], v[52:53], v[98:99]
	v_pk_add_f32 v[52:53], v[120:121], v[150:151]
	v_add_f32_e32 v72, v138, v190
	v_pk_add_f32 v[74:75], v[104:105], v[126:127]
	v_pk_add_f32 v[86:87], v[148:149], v[158:159]
	v_add_f32_e32 v88, v170, v226
	v_pk_add_f32 v[104:105], v[116:117], v[142:143]
	v_pk_add_f32 v[108:109], v[176:177], v[162:163]
	v_add_f32_e32 v116, v182, v242
	v_pk_add_f32 v[120:121], v[122:123], v[224:225]
	v_pk_add_f32 v[122:123], v[146:147], v[228:229]
	v_add_f32_e32 v138, v154, v232
	v_pk_fma_f32 v[124:125], v[92:93], v[58:59], v[120:121] op_sel_hi:[0,1,1]
	v_pk_fma_f32 v[146:147], v[92:93], v[52:53], v[122:123] op_sel_hi:[0,1,1]
	v_fma_f32 v154, v92, v72, v138
	v_pk_fma_f32 v[136:137], v[128:129], v[58:59], v[120:121] op_sel_hi:[0,1,1]
	v_pk_fma_f32 v[170:171], v[128:129], v[52:53], v[122:123] op_sel_hi:[0,1,1]
	v_fma_f32 v182, v128, v72, v138
	v_pk_fma_f32 v[124:125], v[92:93], v[74:75], v[124:125] op_sel:[1,0,0]
	v_pk_fma_f32 v[146:147], v[92:93], v[86:87], v[146:147] op_sel:[1,0,0]
	v_fmac_f32_e32 v154, v93, v88
	v_pk_fma_f32 v[136:137], v[128:129], v[74:75], v[136:137] op_sel:[1,0,0]
	v_pk_fma_f32 v[170:171], v[128:129], v[86:87], v[170:171] op_sel:[1,0,0]
	v_fmac_f32_e32 v182, v129, v88
	v_pk_fma_f32 v[124:125], v[94:95], v[104:105], v[124:125] op_sel_hi:[0,1,1]
	v_pk_fma_f32 v[146:147], v[94:95], v[108:109], v[146:147] op_sel_hi:[0,1,1]
	v_fmac_f32_e32 v154, v94, v116
	v_pk_fma_f32 v[136:137], v[130:131], v[104:105], v[136:137] op_sel_hi:[0,1,1]
	v_pk_fma_f32 v[170:171], v[130:131], v[108:109], v[170:171] op_sel_hi:[0,1,1]
	v_fmac_f32_e32 v182, v130, v116
	v_pk_fma_f32 v[120:121], v[36:37], v[58:59], v[120:121] op_sel_hi:[0,1,1]
	v_pk_fma_f32 v[122:123], v[36:37], v[52:53], v[122:123] op_sel_hi:[0,1,1]
	v_fmac_f32_e32 v138, v36, v72
	v_pk_fma_f32 v[120:121], v[36:37], v[74:75], v[120:121] op_sel:[1,0,0]
	v_pk_fma_f32 v[122:123], v[36:37], v[86:87], v[122:123] op_sel:[1,0,0]
	v_fmac_f32_e32 v138, v37, v88
	v_pk_fma_f32 v[120:121], v[38:39], v[104:105], v[120:121] op_sel_hi:[0,1,1]
	v_pk_fma_f32 v[122:123], v[38:39], v[108:109], v[122:123] op_sel_hi:[0,1,1]
	v_fmac_f32_e32 v138, v38, v116
	v_cndmask_b32_e64 v246, 0, v1, s[10:11]
	v_cndmask_b32_e64 v247, 0, v1, s[14:15]
	v_cndmask_b32_e64 v144, 0, v1, s[20:21]
	v_cndmask_b32_e64 v145, 0, v1, s[22:23]
	v_cndmask_b32_e64 v148, 0, v1, s[30:31]
	v_add_f32_dpp v120, v124, v120 wave_shl:1 row_mask:0xf bank_mask:0xf bound_ctrl:1
	v_add_f32_dpp v121, v125, v121 wave_shl:1 row_mask:0xf bank_mask:0xf bound_ctrl:1
	v_add_f32_dpp v122, v146, v122 wave_shl:1 row_mask:0xf bank_mask:0xf bound_ctrl:1
	v_add_f32_dpp v123, v147, v123 wave_shl:1 row_mask:0xf bank_mask:0xf bound_ctrl:1
	v_add_f32_dpp v138, v154, v138 wave_shl:1 row_mask:0xf bank_mask:0xf bound_ctrl:1
	s_add_i32 s4, s34, 5
	s_cmpk_lt_i32 s4, 0x201
	s_cselect_b64 s[12:13], s[0:1], 0
	v_add_f32_dpp v120, v136, v120 wave_shr:1 row_mask:0xf bank_mask:0xf bound_ctrl:1
	v_add_f32_dpp v121, v137, v121 wave_shr:1 row_mask:0xf bank_mask:0xf bound_ctrl:1
	v_add_f32_dpp v122, v170, v122 wave_shr:1 row_mask:0xf bank_mask:0xf bound_ctrl:1
	v_add_f32_dpp v123, v171, v123 wave_shr:1 row_mask:0xf bank_mask:0xf bound_ctrl:1
	v_add_f32_dpp v138, v182, v138 wave_shr:1 row_mask:0xf bank_mask:0xf bound_ctrl:1
	v_pk_fma_f32 v[120:121], v[20:21], v[222:223], v[120:121] op_sel_hi:[1,0,1] neg_lo:[0,0,1] neg_hi:[0,0,1]
	v_pk_fma_f32 v[122:123], v[24:25], v[222:223], v[122:123] op_sel_hi:[1,0,1] neg_lo:[0,0,1] neg_hi:[0,0,1]
	v_fma_f32 v138, v30, v222, -v138
	v_pk_add_f32 v[120:121], v[120:121], v[246:247] neg_lo:[0,1] neg_hi:[0,1]
	v_pk_add_f32 v[122:123], v[122:123], v[144:145] neg_lo:[0,1] neg_hi:[0,1]
	v_sub_f32_e32 v138, v138, v148
	v_pk_mul_f32 v[152:153], v[120:121], v[120:121]
	v_pk_fma_f32 v[152:153], v[122:123], v[122:123], v[152:153]
	v_add_f32_e32 v152, v152, v153
	v_fmac_f32_e32 v152, v138, v138
	v_cndmask_b32_e64 v153, 0, v152, s[12:13]
	v_add_f32_e32 v0, v0, v153
	s_add_i32 s4, s34, 10
	s_min_i32 s4, s4, 0x200
	s_mul_i32 s5, s4, 0x804
	s_add_i32 s5, s5, s35
	s_add_i32 s6, s5, 0x0
	s_add_i32 s7, s5, 0x101004
	s_add_i32 s8, s5, 0x202008
	s_add_i32 s11, s5, 0x30300c
	s_add_i32 s15, s5, 0x404010
	s_mul_i32 s9, s4, 0x180c
	s_add_i32 s9, s9, s33
	buffer_load_dword v20, v28, s[16:19], s6 offen nt
	buffer_load_dword v21, v28, s[16:19], s7 offen nt
	buffer_load_dword v24, v28, s[16:19], s8 offen nt
	buffer_load_dword v25, v28, s[16:19], s11 offen nt
	buffer_load_dword v30, v28, s[16:19], s15 offen nt
	buffer_load_dwordx3 v[36:38], v27, s[24:27], s9 offen nt
	s_waitcnt vmcnt(12)
	v_mov_b32_dpp v72, v8 wave_shr:1 row_mask:0xf bank_mask:0xf bound_ctrl:1
	v_mov_b32_dpp v73, v9 wave_shr:1 row_mask:0xf bank_mask:0xf bound_ctrl:1
	v_mov_b32_dpp v74, v10 wave_shr:1 row_mask:0xf bank_mask:0xf bound_ctrl:1
	v_mov_b32_dpp v92, v8 wave_shl:1 row_mask:0xf bank_mask:0xf bound_ctrl:1
	v_mov_b32_dpp v93, v9 wave_shl:1 row_mask:0xf bank_mask:0xf bound_ctrl:1
	v_mov_b32_dpp v94, v10 wave_shl:1 row_mask:0xf bank_mask:0xf bound_ctrl:1
	v_mov_b32_dpp v52, v2 wave_shr:1 row_mask:0xf bank_mask:0xf bound_ctrl:1
	v_mov_b32_dpp v53, v3 wave_shr:1 row_mask:0xf bank_mask:0xf bound_ctrl:1
	v_mov_b32_dpp v58, v4 wave_shr:1 row_mask:0xf bank_mask:0xf bound_ctrl:1
	v_mov_b32_dpp v59, v5 wave_shr:1 row_mask:0xf bank_mask:0xf bound_ctrl:1
	v_mov_b32_dpp v88, v6 wave_shr:1 row_mask:0xf bank_mask:0xf bound_ctrl:1
	v_mov_b32_dpp v104, v2 wave_shl:1 row_mask:0xf bank_mask:0xf bound_ctrl:1
	v_mov_b32_dpp v105, v3 wave_shl:1 row_mask:0xf bank_mask:0xf bound_ctrl:1
	v_mov_b32_dpp v86, v4 wave_shl:1 row_mask:0xf bank_mask:0xf bound_ctrl:1
	v_mov_b32_dpp v87, v5 wave_shl:1 row_mask:0xf bank_mask:0xf bound_ctrl:1
	v_mov_b32_dpp v108, v6 wave_shl:1 row_mask:0xf bank_mask:0xf bound_ctrl:1
	v_pk_mul_f32 v[122:123], v[2:3], v[8:9] op_sel_hi:[1,0]
	v_pk_mul_f32 v[116:117], v[4:5], v[8:9] op_sel_hi:[1,0]
	v_mul_f32_e32 v130, v6, v8
	v_pk_mul_f32 v[138:139], v[2:3], v[8:9] op_sel:[0,1]
	v_pk_mul_f32 v[120:121], v[4:5], v[8:9] op_sel:[0,1]
	v_mul_f32_e32 v146, v6, v9
	v_pk_mul_f32 v[154:155], v[2:3], v[10:11] op_sel_hi:[1,0]
	v_pk_mul_f32 v[124:125], v[4:5], v[10:11] op_sel_hi:[1,0]
	v_mul_f32_e32 v170, v6, v10
	v_pk_add_f32 v[182:183], v[2:3], v[52:53]
	v_pk_add_f32 v[128:129], v[4:5], v[58:59]
	v_add_f32_e32 v214, v6, v88
	v_pk_fma_f32 v[122:123], v[52:53], v[72:73], v[122:123] op_sel_hi:[1,0,1]
	v_pk_fma_f32 v[116:117], v[58:59], v[72:73], v[116:117] op_sel_hi:[1,0,1]
	v_fmac_f32_e32 v130, v88, v72
	v_pk_fma_f32 v[138:139], v[52:53], v[72:73], v[138:139] op_sel:[0,1,0]
	v_pk_fma_f32 v[120:121], v[58:59], v[72:73], v[120:121] op_sel:[0,1,0]
	v_fmac_f32_e32 v146, v88, v73
	v_pk_fma_f32 v[154:155], v[52:53], v[74:75], v[154:155] op_sel_hi:[1,0,1]
	v_pk_fma_f32 v[124:125], v[58:59], v[74:75], v[124:125] op_sel_hi:[1,0,1]
	v_fmac_f32_e32 v170, v88, v74
	v_pk_add_f32 v[182:183], v[182:183], v[104:105]
	v_pk_add_f32 v[128:129], v[128:129], v[86:87]
	v_add_f32_e32 v214, v214, v108
	v_pk_fma_f32 v[122:123], v[104:105], v[92:93], v[122:123] op_sel_hi:[1,0,1]
	v_pk_fma_f32 v[116:117], v[86:87], v[92:93], v[116:117] op_sel_hi:[1,0,1]
	v_fmac_f32_e32 v130, v108, v92
	v_pk_fma_f32 v[138:139], v[104:105], v[92:93], v[138:139] op_sel:[0,1,0]
	v_pk_fma_f32 v[120:121], v[86:87], v[92:93], v[120:121] op_sel:[0,1,0]
	v_fmac_f32_e32 v146, v108, v93
	v_pk_fma_f32 v[154:155], v[104:105], v[94:95], v[154:155] op_sel_hi:[1,0,1]
	v_pk_fma_f32 v[124:125], v[86:87], v[94:95], v[124:125] op_sel_hi:[1,0,1]
	v_fmac_f32_e32 v170, v108, v94
	s_barrier
	ds_read_b128 v[216:219], v23 offset:0
	ds_read_b128 v[220:223], v23 offset:1024
	ds_read_b128 v[244:247], v23 offset:2048
	v_pk_add_f32 v[58:59], v[198:199], v[182:183]
	v_pk_add_f32 v[52:53], v[164:165], v[58:59]
	v_pk_add_f32 v[88:89], v[202:203], v[128:129]
	v_pk_add_f32 v[86:87], v[134:135], v[88:89]
	v_add_f32_e32 v134, v204, v214
	v_add_f32_e32 v104, v168, v134
	v_pk_add_f32 v[198:199], v[90:91], v[122:123]
	v_pk_add_f32 v[202:203], v[84:85], v[198:199]
	v_pk_add_f32 v[84:85], v[102:103], v[116:117]
	v_pk_add_f32 v[108:109], v[106:107], v[84:85]
	v_add_f32_e32 v90, v172, v130
	v_add_f32_e32 v102, v96, v90
	v_pk_add_f32 v[106:107], v[118:119], v[138:139]
	v_pk_add_f32 v[96:97], v[100:101], v[106:107]
	v_pk_add_f32 v[100:101], v[174:175], v[120:121]
	v_pk_add_f32 v[136:137], v[110:111], v[100:101]
	v_add_f32_e32 v110, v180, v146
	v_add_f32_e32 v118, v112, v110
	v_pk_add_f32 v[174:175], v[178:179], v[154:155]
	v_pk_add_f32 v[112:113], v[132:133], v[174:175]
	v_pk_add_f32 v[132:133], v[186:187], v[124:125]
	v_pk_add_f32 v[144:145], v[114:115], v[132:133]
	v_add_f32_e32 v114, v200, v170
	v_add_f32_e32 v178, v160, v114
	s_waitcnt lgkmcnt(2)
	v_pk_fma_f32 v[202:203], v[216:217], v[52:53], v[202:203] op_sel_hi:[0,1,1] neg_lo:[1,0,0] neg_hi:[1,0,0]
	v_pk_fma_f32 v[108:109], v[216:217], v[86:87], v[108:109] op_sel_hi:[0,1,1] neg_lo:[1,0,0] neg_hi:[1,0,0]
	v_fma_f32 v102, -v216, v104, v102
	v_pk_fma_f32 v[96:97], v[216:217], v[52:53], v[96:97] op_sel:[1,0,0] neg_lo:[1,0,0] neg_hi:[1,0,0]
	v_pk_fma_f32 v[136:137], v[216:217], v[86:87], v[136:137] op_sel:[1,0,0] neg_lo:[1,0,0] neg_hi:[1,0,0]
	v_fma_f32 v118, -v217, v104, v118
	v_pk_fma_f32 v[112:113], v[218:219], v[52:53], v[112:113] op_sel_hi:[0,1,1] neg_lo:[1,0,0] neg_hi:[1,0,0]
	v_pk_fma_f32 v[144:145], v[218:219], v[86:87], v[144:145] op_sel_hi:[0,1,1] neg_lo:[1,0,0] neg_hi:[1,0,0]
	v_fma_f32 v178, -v218, v104, v178
	v_pk_mul_f32 v[186:187], v[218:219], v[202:203] op_sel:[1,0]
	v_pk_mul_f32 v[156:157], v[218:219], v[108:109] op_sel:[1,0]
	v_mul_f32_e32 v168, v219, v102
	s_waitcnt lgkmcnt(1)
	v_pk_mul_f32 v[148:149], v[220:221], v[202:203] op_sel_hi:[0,1]
	v_pk_mul_f32 v[160:161], v[220:221], v[108:109] op_sel_hi:[0,1]
	v_mul_f32_e32 v172, v220, v102
	v_pk_mul_f32 v[152:153], v[220:221], v[202:203] op_sel:[1,0]
	v_pk_mul_f32 v[164:165], v[220:221], v[108:109] op_sel:[1,0]
	v_mul_f32_e32 v176, v221, v102
	v_pk_fma_f32 v[186:187], v[220:221], v[96:97], v[186:187] op_sel_hi:[0,1,1]
	v_pk_fma_f32 v[156:157], v[220:221], v[136:137], v[156:157] op_sel_hi:[0,1,1]
	v_fmac_f32_e32 v168, v220, v118
	v_pk_fma_f32 v[148:149], v[222:223], v[96:97], v[148:149] op_sel_hi:[0,1,1]
	v_pk_fma_f32 v[160:161], v[222:223], v[136:137], v[160:161] op_sel_hi:[0,1,1]
	v_fmac_f32_e32 v172, v222, v118
	v_pk_fma_f32 v[152:153], v[222:223], v[96:97], v[152:153] op_sel:[1,0,0]
	v_pk_fma_f32 v[164:165], v[222:223], v[136:137], v[164:165] op_sel:[1,0,0]
	v_fmac_f32_e32 v176, v223, v118
	v_pk_fma_f32 v[186:187], v[220:221], v[112:113], v[186:187] op_sel:[1,0,0]
	v_pk_fma_f32 v[156:157], v[220:221], v[144:145], v[156:157] op_sel:[1,0,0]
	v_fmac_f32_e32 v168, v221, v178
	v_pk_fma_f32 v[148:149], v[222:223], v[112:113], v[148:149] op_sel:[1,0,0]
	v_pk_fma_f32 v[160:161], v[222:223], v[144:145], v[160:161] op_sel:[1,0,0]
	v_fmac_f32_e32 v172, v223, v178
	s_waitcnt lgkmcnt(0)
	v_pk_fma_f32 v[152:153], v[244:245], v[112:113], v[152:153] op_sel_hi:[0,1,1]
	v_pk_fma_f32 v[164:165], v[244:245], v[144:145], v[164:165] op_sel_hi:[0,1,1]
	v_fmac_f32_e32 v176, v244, v178
	v_pk_mul_f32 v[180:181], v[216:217], v[186:187] op_sel_hi:[0,1]
	v_pk_mul_f32 v[200:201], v[216:217], v[156:157] op_sel_hi:[0,1]
	v_mul_f32_e32 v204, v216, v168
	v_pk_fma_f32 v[180:181], v[216:217], v[148:149], v[180:181] op_sel:[1,0,0]
	v_pk_fma_f32 v[200:201], v[216:217], v[160:161], v[200:201] op_sel:[1,0,0]
	v_fmac_f32_e32 v204, v217, v172
	v_pk_fma_f32 v[180:181], v[218:219], v[152:153], v[180:181] op_sel_hi:[0,1,1]
	v_pk_fma_f32 v[200:201], v[218:219], v[164:165], v[200:201] op_sel_hi:[0,1,1]
	v_fmac_f32_e32 v204, v218, v176
	v_pk_fma_f32 v[180:181], v[244:245], v[52:53], v[180:181] op_sel:[1,0,0] neg_lo:[0,0,1] neg_hi:[0,0,1]
	v_pk_fma_f32 v[200:201], v[244:245], v[86:87], v[200:201] op_sel:[1,0,0] neg_lo:[0,0,1] neg_hi:[0,0,1]
	v_fma_f32 v204, v245, v104, -v204
	v_cmp_eq_u32_e64 s[10:11], 1, v247
	v_cmp_eq_u32_e64 s[14:15], 2, v247
	v_cmp_eq_u32_e64 s[20:21], 3, v247
	v_cmp_eq_u32_e64 s[22:23], 4, v247
	v_cmp_eq_u32_e64 s[30:31], 5, v247
	v_pk_add_f32 v[86:87], v[98:99], v[186:187]
	v_pk_add_f32 v[52:53], v[140:141], v[86:87]
	v_pk_add_f32 v[96:97], v[150:151], v[156:157]
	v_pk_add_f32 v[98:99], v[166:167], v[96:97]
	v_add_f32_e32 v104, v190, v168
	v_add_f32_e32 v102, v210, v104
	v_pk_add_f32 v[118:119], v[126:127], v[148:149]
	v_pk_add_f32 v[108:109], v[184:185], v[118:119]
	v_pk_add_f32 v[112:113], v[158:159], v[160:161]
	v_pk_add_f32 v[126:127], v[194:195], v[112:113]
	v_add_f32_e32 v136, v226, v172
	v_add_f32_e32 v140, v230, v136
	v_pk_add_f32 v[150:151], v[142:143], v[152:153]
	v_pk_add_f32 v[144:145], v[188:189], v[150:151]
	v_pk_add_f32 v[184:185], v[162:163], v[164:165]
	v_pk_add_f32 v[142:143], v[206:207], v[184:185]
	v_add_f32_e32 v188, v242, v176
	v_add_f32_e32 v158, v234, v188
	v_pk_add_f32 v[208:209], v[224:225], v[180:181]
	v_pk_add_f32 v[162:163], v[238:239], v[208:209]
	v_pk_add_f32 v[166:167], v[228:229], v[200:201]
	v_pk_add_f32 v[212:213], v[192:193], v[166:167]
	v_add_f32_e32 v178, v232, v204
	v_add_f32_e32 v192, v196, v178
	v_pk_fma_f32 v[190:191], v[60:61], v[52:53], v[162:163] op_sel_hi:[0,1,1]
	v_pk_fma_f32 v[196:197], v[60:61], v[98:99], v[212:213] op_sel_hi:[0,1,1]
	v_fma_f32 v224, v60, v102, v192
	v_pk_fma_f32 v[194:195], v[68:69], v[52:53], v[162:163] op_sel_hi:[0,1,1]
	v_pk_fma_f32 v[228:229], v[68:69], v[98:99], v[212:213] op_sel_hi:[0,1,1]
	v_fma_f32 v232, v68, v102, v192
	v_pk_fma_f32 v[190:191], v[60:61], v[108:109], v[190:191] op_sel:[1,0,0]
	v_pk_fma_f32 v[196:197], v[60:61], v[126:127], v[196:197] op_sel:[1,0,0]
	v_fmac_f32_e32 v224, v61, v140
	v_pk_fma_f32 v[194:195], v[68:69], v[108:109], v[194:195] op_sel:[1,0,0]
	v_pk_fma_f32 v[228:229], v[68:69], v[126:127], v[228:229] op_sel:[1,0,0]
	v_fmac_f32_e32 v232, v69, v140
	v_pk_fma_f32 v[190:191], v[62:63], v[144:145], v[190:191] op_sel_hi:[0,1,1]
	v_pk_fma_f32 v[196:197], v[62:63], v[142:143], v[196:197] op_sel_hi:[0,1,1]
	v_fmac_f32_e32 v224, v62, v158
	v_pk_fma_f32 v[194:195], v[70:71], v[144:145], v[194:195] op_sel_hi:[0,1,1]
	v_pk_fma_f32 v[228:229], v[70:71], v[142:143], v[228:229] op_sel_hi:[0,1,1]
	v_fmac_f32_e32 v232, v70, v158
	v_pk_fma_f32 v[162:163], v[48:49], v[52:53], v[162:163] op_sel_hi:[0,1,1]
	v_pk_fma_f32 v[212:213], v[48:49], v[98:99], v[212:213] op_sel_hi:[0,1,1]
	v_fmac_f32_e32 v192, v48, v102
	v_pk_fma_f32 v[162:163], v[48:49], v[108:109], v[162:163] op_sel:[1,0,0]
	v_pk_fma_f32 v[212:213], v[48:49], v[126:127], v[212:213] op_sel:[1,0,0]
	v_fmac_f32_e32 v192, v49, v140
	v_pk_fma_f32 v[162:163], v[50:51], v[144:145], v[162:163] op_sel_hi:[0,1,1]
	v_pk_fma_f32 v[212:213], v[50:51], v[142:143], v[212:213] op_sel_hi:[0,1,1]
	v_fmac_f32_e32 v192, v50, v158
	v_cndmask_b32_e64 v236, 0, v1, s[10:11]
	v_cndmask_b32_e64 v237, 0, v1, s[14:15]
	v_cndmask_b32_e64 v202, 0, v1, s[20:21]
	v_cndmask_b32_e64 v203, 0, v1, s[22:23]
	v_cndmask_b32_e64 v206, 0, v1, s[30:31]
	v_add_f32_dpp v162, v190, v162 wave_shl:1 row_mask:0xf bank_mask:0xf bound_ctrl:1
	v_add_f32_dpp v163, v191, v163 wave_shl:1 row_mask:0xf bank_mask:0xf bound_ctrl:1
	v_add_f32_dpp v212, v196, v212 wave_shl:1 row_mask:0xf bank_mask:0xf bound_ctrl:1
	v_add_f32_dpp v213, v197, v213 wave_shl:1 row_mask:0xf bank_mask:0xf bound_ctrl:1
	v_add_f32_dpp v192, v224, v192 wave_shl:1 row_mask:0xf bank_mask:0xf bound_ctrl:1
	s_add_i32 s4, s34, 6
	s_cmpk_lt_i32 s4, 0x201
	s_cselect_b64 s[12:13], s[0:1], 0
	v_add_f32_dpp v162, v194, v162 wave_shr:1 row_mask:0xf bank_mask:0xf bound_ctrl:1
	v_add_f32_dpp v163, v195, v163 wave_shr:1 row_mask:0xf bank_mask:0xf bound_ctrl:1
	v_add_f32_dpp v212, v228, v212 wave_shr:1 row_mask:0xf bank_mask:0xf bound_ctrl:1
	v_add_f32_dpp v213, v229, v213 wave_shr:1 row_mask:0xf bank_mask:0xf bound_ctrl:1
	v_add_f32_dpp v192, v232, v192 wave_shr:1 row_mask:0xf bank_mask:0xf bound_ctrl:1
	v_pk_fma_f32 v[162:163], v[40:41], v[246:247], v[162:163] op_sel_hi:[1,0,1] neg_lo:[0,0,1] neg_hi:[0,0,1]
	v_pk_fma_f32 v[212:213], v[42:43], v[246:247], v[212:213] op_sel_hi:[1,0,1] neg_lo:[0,0,1] neg_hi:[0,0,1]
	v_fma_f32 v192, v44, v246, -v192
	v_pk_add_f32 v[162:163], v[162:163], v[236:237] neg_lo:[0,1] neg_hi:[0,1]
	v_pk_add_f32 v[212:213], v[212:213], v[202:203] neg_lo:[0,1] neg_hi:[0,1]
	v_sub_f32_e32 v192, v192, v206
	v_pk_mul_f32 v[210:211], v[162:163], v[162:163]
	v_pk_fma_f32 v[210:211], v[212:213], v[212:213], v[210:211]
	v_add_f32_e32 v210, v210, v211
	v_fmac_f32_e32 v210, v192, v192
	v_cndmask_b32_e64 v211, 0, v210, s[12:13]
	v_add_f32_e32 v0, v0, v211
	s_add_i32 s4, s34, 11
	s_min_i32 s4, s4, 0x200
	s_mul_i32 s5, s4, 0x804
	s_add_i32 s5, s5, s35
	s_add_i32 s6, s5, 0x0
	s_add_i32 s7, s5, 0x101004
	s_add_i32 s8, s5, 0x202008
	s_add_i32 s11, s5, 0x30300c
	s_add_i32 s15, s5, 0x404010
	s_mul_i32 s9, s4, 0x180c
	s_add_i32 s9, s9, s33
	buffer_load_dword v40, v28, s[16:19], s6 offen nt
	buffer_load_dword v41, v28, s[16:19], s7 offen nt
	buffer_load_dword v42, v28, s[16:19], s8 offen nt
	buffer_load_dword v43, v28, s[16:19], s11 offen nt
	buffer_load_dword v44, v28, s[16:19], s15 offen nt
	buffer_load_dwordx3 v[48:50], v27, s[24:27], s9 offen nt
	s_waitcnt vmcnt(12)
	v_mov_b32_dpp v60, v32 wave_shr:1 row_mask:0xf bank_mask:0xf bound_ctrl:1
	v_mov_b32_dpp v61, v33 wave_shr:1 row_mask:0xf bank_mask:0xf bound_ctrl:1
	v_mov_b32_dpp v62, v34 wave_shr:1 row_mask:0xf bank_mask:0xf bound_ctrl:1
	v_mov_b32_dpp v68, v32 wave_shl:1 row_mask:0xf bank_mask:0xf bound_ctrl:1
	v_mov_b32_dpp v69, v33 wave_shl:1 row_mask:0xf bank_mask:0xf bound_ctrl:1
	v_mov_b32_dpp v70, v34 wave_shl:1 row_mask:0xf bank_mask:0xf bound_ctrl:1
	v_mov_b32_dpp v98, v12 wave_shr:1 row_mask:0xf bank_mask:0xf bound_ctrl:1
	v_mov_b32_dpp v99, v13 wave_shr:1 row_mask:0xf bank_mask:0xf bound_ctrl:1
	v_mov_b32_dpp v52, v14 wave_shr:1 row_mask:0xf bank_mask:0xf bound_ctrl:1
	v_mov_b32_dpp v53, v15 wave_shr:1 row_mask:0xf bank_mask:0xf bound_ctrl:1
	v_mov_b32_dpp v102, v16 wave_shr:1 row_mask:0xf bank_mask:0xf bound_ctrl:1
	v_mov_b32_dpp v126, v12 wave_shl:1 row_mask:0xf bank_mask:0xf bound_ctrl:1
	v_mov_b32_dpp v127, v13 wave_shl:1 row_mask:0xf bank_mask:0xf bound_ctrl:1
	v_mov_b32_dpp v108, v14 wave_shl:1 row_mask:0xf bank_mask:0xf bound_ctrl:1
	v_mov_b32_dpp v109, v15 wave_shl:1 row_mask:0xf bank_mask:0xf bound_ctrl:1
	v_mov_b32_dpp v142, v16 wave_shl:1 row_mask:0xf bank_mask:0xf bound_ctrl:1
	v_pk_mul_f32 v[140:141], v[12:13], v[32:33] op_sel_hi:[1,0]
	v_pk_mul_f32 v[158:159], v[14:15], v[32:33] op_sel_hi:[1,0]
	v_mul_f32_e32 v144, v16, v32
	v_pk_mul_f32 v[192:193], v[12:13], v[32:33] op_sel:[0,1]
	v_pk_mul_f32 v[162:163], v[14:15], v[32:33] op_sel:[0,1]
	v_mul_f32_e32 v196, v16, v33
	v_pk_mul_f32 v[212:213], v[12:13], v[34:35] op_sel_hi:[1,0]
	v_pk_mul_f32 v[190:191], v[14:15], v[34:35] op_sel_hi:[1,0]
	v_mul_f32_e32 v216, v16, v34
	v_pk_add_f32 v[220:221], v[12:13], v[98:99]
	v_pk_add_f32 v[194:195], v[14:15], v[52:53]
	v_add_f32_e32 v224, v16, v102
	v_pk_fma_f32 v[140:141], v[98:99], v[60:61], v[140:141] op_sel_hi:[1,0,1]
	v_pk_fma_f32 v[158:159], v[52:53], v[60:61], v[158:159] op_sel_hi:[1,0,1]
	v_fmac_f32_e32 v144, v102, v60
	v_pk_fma_f32 v[192:193], v[98:99], v[60:61], v[192:193] op_sel:[0,1,0]
	v_pk_fma_f32 v[162:163], v[52:53], v[60:61], v[162:163] op_sel:[0,1,0]
	v_fmac_f32_e32 v196, v102, v61
	v_pk_fma_f32 v[212:213], v[98:99], v[62:63], v[212:213] op_sel_hi:[1,0,1]
	v_pk_fma_f32 v[190:191], v[52:53], v[62:63], v[190:191] op_sel_hi:[1,0,1]
	v_fmac_f32_e32 v216, v102, v62
	v_pk_add_f32 v[220:221], v[220:221], v[126:127]
	v_pk_add_f32 v[194:195], v[194:195], v[108:109]
	v_add_f32_e32 v224, v224, v142
	v_pk_fma_f32 v[140:141], v[126:127], v[68:69], v[140:141] op_sel_hi:[1,0,1]
	v_pk_fma_f32 v[158:159], v[108:109], v[68:69], v[158:159] op_sel_hi:[1,0,1]
	v_fmac_f32_e32 v144, v142, v68
	v_pk_fma_f32 v[192:193], v[126:127], v[68:69], v[192:193] op_sel:[0,1,0]
	v_pk_fma_f32 v[162:163], v[108:109], v[68:69], v[162:163] op_sel:[0,1,0]
	v_fmac_f32_e32 v196, v142, v69
	v_pk_fma_f32 v[212:213], v[126:127], v[70:71], v[212:213] op_sel_hi:[1,0,1]
	v_pk_fma_f32 v[190:191], v[108:109], v[70:71], v[190:191] op_sel_hi:[1,0,1]
	v_fmac_f32_e32 v216, v142, v70
	s_barrier
	ds_read_b128 v[228:231], v23 offset:3072
	ds_read_b128 v[232:235], v23 offset:4096
	ds_read_b128 v[236:239], v23 offset:5120
	v_pk_add_f32 v[52:53], v[58:59], v[220:221]
	v_pk_add_f32 v[58:59], v[88:89], v[194:195]
	v_add_f32_e32 v88, v134, v224
	v_pk_add_f32 v[98:99], v[198:199], v[140:141]
	v_pk_add_f32 v[108:109], v[84:85], v[158:159]
	v_add_f32_e32 v102, v90, v144
	v_pk_add_f32 v[90:91], v[106:107], v[192:193]
	v_pk_add_f32 v[84:85], v[100:101], v[162:163]
	v_add_f32_e32 v106, v110, v196
	v_pk_add_f32 v[110:111], v[174:175], v[212:213]
	v_pk_add_f32 v[100:101], v[132:133], v[190:191]
	v_add_f32_e32 v126, v114, v216
	s_waitcnt lgkmcnt(2)
	v_pk_fma_f32 v[98:99], v[228:229], v[52:53], v[98:99] op_sel_hi:[0,1,1] neg_lo:[1,0,0] neg_hi:[1,0,0]
	v_pk_fma_f32 v[108:109], v[228:229], v[58:59], v[108:109] op_sel_hi:[0,1,1] neg_lo:[1,0,0] neg_hi:[1,0,0]
	v_fma_f32 v102, -v228, v88, v102
	v_pk_fma_f32 v[90:91], v[228:229], v[52:53], v[90:91] op_sel:[1,0,0] neg_lo:[1,0,0] neg_hi:[1,0,0]
	v_pk_fma_f32 v[84:85], v[228:229], v[58:59], v[84:85] op_sel:[1,0,0] neg_lo:[1,0,0] neg_hi:[1,0,0]
	v_fma_f32 v106, -v229, v88, v106
	v_pk_fma_f32 v[110:111], v[230:231], v[52:53], v[110:111] op_sel_hi:[0,1,1] neg_lo:[1,0,0] neg_hi:[1,0,0]
	v_pk_fma_f32 v[100:101], v[230:231], v[58:59], v[100:101] op_sel_hi:[0,1,1] neg_lo:[1,0,0] neg_hi:[1,0,0]
	v_fma_f32 v126, -v230, v88, v126
	v_pk_mul_f32 v[132:133], v[230:231], v[98:99] op_sel:[1,0]
	v_pk_mul_f32 v[114:115], v[230:231], v[108:109] op_sel:[1,0]
	v_mul_f32_e32 v248, v231, v102
	s_waitcnt lgkmcnt(1)
	v_pk_mul_f32 v[240:241], v[232:233], v[98:99] op_sel_hi:[0,1]
	v_pk_mul_f32 v[134:135], v[232:233], v[108:109] op_sel_hi:[0,1]
	v_mul_f32_e32 v174, v232, v102
	v_pk_mul_f32 v[244:245], v[232:233], v[98:99] op_sel:[1,0]
	v_pk_mul_f32 v[142:143], v[232:233], v[108:109] op_sel:[1,0]
	v_mul_f32_e32 v198, v233, v102
	v_pk_fma_f32 v[132:133], v[232:233], v[90:91], v[132:133] op_sel_hi:[0,1,1]
	v_pk_fma_f32 v[114:115], v[232:233], v[84:85], v[114:115] op_sel_hi:[0,1,1]
	v_fmac_f32_e32 v248, v232, v106
	v_pk_fma_f32 v[240:241], v[234:235], v[90:91], v[240:241] op_sel_hi:[0,1,1]
	v_pk_fma_f32 v[134:135], v[234:235], v[84:85], v[134:135] op_sel_hi:[0,1,1]
	v_fmac_f32_e32 v174, v234, v106
	v_pk_fma_f32 v[244:245], v[234:235], v[90:91], v[244:245] op_sel:[1,0,0]
	v_pk_fma_f32 v[142:143], v[234:235], v[84:85], v[142:143] op_sel:[1,0,0]
	v_fmac_f32_e32 v198, v235, v106
	v_pk_fma_f32 v[132:133], v[232:233], v[110:111], v[132:133] op_sel:[1,0,0]
	v_pk_fma_f32 v[114:115], v[232:233], v[100:101], v[114:115] op_sel:[1,0,0]
	v_fmac_f32_e32 v248, v233, v126
	v_pk_fma_f32 v[240:241], v[234:235], v[110:111], v[240:241] op_sel:[1,0,0]
	v_pk_fma_f32 v[134:135], v[234:235], v[100:101], v[134:135] op_sel:[1,0,0]
	v_fmac_f32_e32 v174, v235, v126
	s_waitcnt lgkmcnt(0)
	v_pk_fma_f32 v[244:245], v[236:237], v[110:111], v[244:245] op_sel_hi:[0,1,1]
	v_pk_fma_f32 v[142:143], v[236:237], v[100:101], v[142:143] op_sel_hi:[0,1,1]
	v_fmac_f32_e32 v198, v236, v126
	v_pk_mul_f32 v[202:203], v[228:229], v[132:133] op_sel_hi:[0,1]
	v_pk_mul_f32 v[206:207], v[228:229], v[114:115] op_sel_hi:[0,1]
	v_mul_f32_e32 v210, v228, v248
	v_pk_fma_f32 v[202:203], v[228:229], v[240:241], v[202:203] op_sel:[1,0,0]
	v_pk_fma_f32 v[206:207], v[228:229], v[134:135], v[206:207] op_sel:[1,0,0]
	v_fmac_f32_e32 v210, v229, v174
	v_pk_fma_f32 v[202:203], v[230:231], v[244:245], v[202:203] op_sel_hi:[0,1,1]
	v_pk_fma_f32 v[206:207], v[230:231], v[142:143], v[206:207] op_sel_hi:[0,1,1]
	v_fmac_f32_e32 v210, v230, v198
	v_pk_fma_f32 v[202:203], v[236:237], v[52:53], v[202:203] op_sel:[1,0,0] neg_lo:[0,0,1] neg_hi:[0,0,1]
	v_pk_fma_f32 v[206:207], v[236:237], v[58:59], v[206:207] op_sel:[1,0,0] neg_lo:[0,0,1] neg_hi:[0,0,1]
	v_fma_f32 v210, v237, v88, -v210
	v_cmp_eq_u32_e64 s[10:11], 1, v239
	v_cmp_eq_u32_e64 s[14:15], 2, v239
	v_cmp_eq_u32_e64 s[20:21], 3, v239
	v_cmp_eq_u32_e64 s[22:23], 4, v239
	v_cmp_eq_u32_e64 s[30:31], 5, v239
	v_pk_add_f32 v[52:53], v[86:87], v[132:133]
	v_pk_add_f32 v[58:59], v[96:97], v[114:115]
	v_add_f32_e32 v84, v104, v248
	v_pk_add_f32 v[86:87], v[118:119], v[240:241]
	v_pk_add_f32 v[88:89], v[112:113], v[134:135]
	v_add_f32_e32 v90, v136, v174
	v_pk_add_f32 v[96:97], v[150:151], v[244:245]
	v_pk_add_f32 v[98:99], v[184:185], v[142:143]
	v_add_f32_e32 v100, v188, v198
	v_pk_add_f32 v[102:103], v[208:209], v[202:203]
	v_pk_add_f32 v[104:105], v[166:167], v[206:207]
	v_add_f32_e32 v106, v178, v210
	v_pk_fma_f32 v[110:111], v[64:65], v[52:53], v[102:103] op_sel_hi:[0,1,1]
	v_pk_fma_f32 v[108:109], v[64:65], v[58:59], v[104:105] op_sel_hi:[0,1,1]
	v_fma_f32 v118, v64, v84, v106
	v_pk_fma_f32 v[126:127], v[76:77], v[52:53], v[102:103] op_sel_hi:[0,1,1]
	v_pk_fma_f32 v[112:113], v[76:77], v[58:59], v[104:105] op_sel_hi:[0,1,1]
	v_fma_f32 v150, v76, v84, v106
	v_pk_fma_f32 v[110:111], v[64:65], v[86:87], v[110:111] op_sel:[1,0,0]
	v_pk_fma_f32 v[108:109], v[64:65], v[88:89], v[108:109] op_sel:[1,0,0]
	v_fmac_f32_e32 v118, v65, v90
	v_pk_fma_f32 v[126:127], v[76:77], v[86:87], v[126:127] op_sel:[1,0,0]
	v_pk_fma_f32 v[112:113], v[76:77], v[88:89], v[112:113] op_sel:[1,0,0]
	v_fmac_f32_e32 v150, v77, v90
	v_pk_fma_f32 v[110:111], v[66:67], v[96:97], v[110:111] op_sel_hi:[0,1,1]
	v_pk_fma_f32 v[108:109], v[66:67], v[98:99], v[108:109] op_sel_hi:[0,1,1]
	v_fmac_f32_e32 v118, v66, v100
	v_pk_fma_f32 v[126:127], v[78:79], v[96:97], v[126:127] op_sel_hi:[0,1,1]
	v_pk_fma_f32 v[112:113], v[78:79], v[98:99], v[112:113] op_sel_hi:[0,1,1]
	v_fmac_f32_e32 v150, v78, v100
	v_pk_fma_f32 v[102:103], v[80:81], v[52:53], v[102:103] op_sel_hi:[0,1,1]
	v_pk_fma_f32 v[104:105], v[80:81], v[58:59], v[104:105] op_sel_hi:[0,1,1]
	v_fmac_f32_e32 v106, v80, v84
	v_pk_fma_f32 v[102:103], v[80:81], v[86:87], v[102:103] op_sel:[1,0,0]
	v_pk_fma_f32 v[104:105], v[80:81], v[88:89], v[104:105] op_sel:[1,0,0]
	v_fmac_f32_e32 v106, v81, v90
	v_pk_fma_f32 v[102:103], v[82:83], v[96:97], v[102:103] op_sel_hi:[0,1,1]
	v_pk_fma_f32 v[104:105], v[82:83], v[98:99], v[104:105] op_sel_hi:[0,1,1]
	v_fmac_f32_e32 v106, v82, v100
	v_cndmask_b32_e64 v136, 0, v1, s[10:11]
	v_cndmask_b32_e64 v137, 0, v1, s[14:15]
	v_cndmask_b32_e64 v166, 0, v1, s[20:21]
	v_cndmask_b32_e64 v167, 0, v1, s[22:23]
	v_cndmask_b32_e64 v184, 0, v1, s[30:31]
	v_add_f32_dpp v102, v110, v102 wave_shl:1 row_mask:0xf bank_mask:0xf bound_ctrl:1
	v_add_f32_dpp v103, v111, v103 wave_shl:1 row_mask:0xf bank_mask:0xf bound_ctrl:1
	v_add_f32_dpp v104, v108, v104 wave_shl:1 row_mask:0xf bank_mask:0xf bound_ctrl:1
	v_add_f32_dpp v105, v109, v105 wave_shl:1 row_mask:0xf bank_mask:0xf bound_ctrl:1
	v_add_f32_dpp v106, v118, v106 wave_shl:1 row_mask:0xf bank_mask:0xf bound_ctrl:1
	s_add_i32 s4, s34, 7
	s_cmpk_lt_i32 s4, 0x201
	s_cselect_b64 s[12:13], s[0:1], 0
	v_add_f32_dpp v102, v126, v102 wave_shr:1 row_mask:0xf bank_mask:0xf bound_ctrl:1
	v_add_f32_dpp v103, v127, v103 wave_shr:1 row_mask:0xf bank_mask:0xf bound_ctrl:1
	v_add_f32_dpp v104, v112, v104 wave_shr:1 row_mask:0xf bank_mask:0xf bound_ctrl:1
	v_add_f32_dpp v105, v113, v105 wave_shr:1 row_mask:0xf bank_mask:0xf bound_ctrl:1
	v_add_f32_dpp v106, v150, v106 wave_shr:1 row_mask:0xf bank_mask:0xf bound_ctrl:1
	v_pk_fma_f32 v[102:103], v[46:47], v[238:239], v[102:103] op_sel_hi:[1,0,1] neg_lo:[0,0,1] neg_hi:[0,0,1]
	v_pk_fma_f32 v[104:105], v[54:55], v[238:239], v[104:105] op_sel_hi:[1,0,1] neg_lo:[0,0,1] neg_hi:[0,0,1]
	v_fma_f32 v106, v56, v238, -v106
	v_pk_add_f32 v[102:103], v[102:103], v[136:137] neg_lo:[0,1] neg_hi:[0,1]
	v_pk_add_f32 v[104:105], v[104:105], v[166:167] neg_lo:[0,1] neg_hi:[0,1]
	v_sub_f32_e32 v106, v106, v184
	v_pk_mul_f32 v[178:179], v[102:103], v[102:103]
	v_pk_fma_f32 v[178:179], v[104:105], v[104:105], v[178:179]
	v_add_f32_e32 v178, v178, v179
	v_fmac_f32_e32 v178, v106, v106
	v_cndmask_b32_e64 v179, 0, v178, s[12:13]
	v_add_f32_e32 v0, v0, v179
	s_waitcnt vmcnt(6)
	v_mov_b32_dpp v52, v36 wave_shr:1 row_mask:0xf bank_mask:0xf bound_ctrl:1
	v_mov_b32_dpp v53, v37 wave_shr:1 row_mask:0xf bank_mask:0xf bound_ctrl:1
	v_mov_b32_dpp v54, v38 wave_shr:1 row_mask:0xf bank_mask:0xf bound_ctrl:1
	v_mov_b32_dpp v56, v36 wave_shl:1 row_mask:0xf bank_mask:0xf bound_ctrl:1
	v_mov_b32_dpp v57, v37 wave_shl:1 row_mask:0xf bank_mask:0xf bound_ctrl:1
	v_mov_b32_dpp v58, v38 wave_shl:1 row_mask:0xf bank_mask:0xf bound_ctrl:1
	v_mov_b32_dpp v46, v20 wave_shr:1 row_mask:0xf bank_mask:0xf bound_ctrl:1
	v_mov_b32_dpp v47, v21 wave_shr:1 row_mask:0xf bank_mask:0xf bound_ctrl:1
	v_mov_b32_dpp v66, v24 wave_shr:1 row_mask:0xf bank_mask:0xf bound_ctrl:1
	v_mov_b32_dpp v67, v25 wave_shr:1 row_mask:0xf bank_mask:0xf bound_ctrl:1
	v_mov_b32_dpp v64, v30 wave_shr:1 row_mask:0xf bank_mask:0xf bound_ctrl:1
	v_mov_b32_dpp v78, v20 wave_shl:1 row_mask:0xf bank_mask:0xf bound_ctrl:1
	v_mov_b32_dpp v79, v21 wave_shl:1 row_mask:0xf bank_mask:0xf bound_ctrl:1
	v_mov_b32_dpp v82, v24 wave_shl:1 row_mask:0xf bank_mask:0xf bound_ctrl:1
	v_mov_b32_dpp v83, v25 wave_shl:1 row_mask:0xf bank_mask:0xf bound_ctrl:1
	v_mov_b32_dpp v76, v30 wave_shl:1 row_mask:0xf bank_mask:0xf bound_ctrl:1
	v_pk_mul_f32 v[80:81], v[20:21], v[36:37] op_sel_hi:[1,0]
	v_pk_mul_f32 v[84:85], v[24:25], v[36:37] op_sel_hi:[1,0]
	v_mul_f32_e32 v86, v30, v36
	v_pk_mul_f32 v[88:89], v[20:21], v[36:37] op_sel:[0,1]
	v_pk_mul_f32 v[96:97], v[24:25], v[36:37] op_sel:[0,1]
	v_mul_f32_e32 v90, v30, v37
	v_pk_mul_f32 v[100:101], v[20:21], v[38:39] op_sel_hi:[1,0]
	v_pk_mul_f32 v[104:105], v[24:25], v[38:39] op_sel_hi:[1,0]
	v_mul_f32_e32 v98, v30, v38
	v_pk_add_f32 v[108:109], v[20:21], v[46:47]
	v_pk_add_f32 v[112:113], v[24:25], v[66:67]
	v_add_f32_e32 v102, v30, v64
	v_pk_fma_f32 v[80:81], v[46:47], v[52:53], v[80:81] op_sel_hi:[1,0,1]
	v_pk_fma_f32 v[84:85], v[66:67], v[52:53], v[84:85] op_sel_hi:[1,0,1]
	v_fmac_f32_e32 v86, v64, v52
	v_pk_fma_f32 v[88:89], v[46:47], v[52:53], v[88:89] op_sel:[0,1,0]
	v_pk_fma_f32 v[96:97], v[66:67], v[52:53], v[96:97] op_sel:[0,1,0]
	v_fmac_f32_e32 v90, v64, v53
	v_pk_fma_f32 v[100:101], v[46:47], v[54:55], v[100:101] op_sel_hi:[1,0,1]
	v_pk_fma_f32 v[104:105], v[66:67], v[54:55], v[104:105] op_sel_hi:[1,0,1]
	v_fmac_f32_e32 v98, v64, v54
	v_pk_add_f32 v[108:109], v[108:109], v[78:79]
	v_pk_add_f32 v[112:113], v[112:113], v[82:83]
	v_add_f32_e32 v102, v102, v76
	v_pk_fma_f32 v[80:81], v[78:79], v[56:57], v[80:81] op_sel_hi:[1,0,1]
	v_pk_fma_f32 v[84:85], v[82:83], v[56:57], v[84:85] op_sel_hi:[1,0,1]
	v_fmac_f32_e32 v86, v76, v56
	v_pk_fma_f32 v[88:89], v[78:79], v[56:57], v[88:89] op_sel:[0,1,0]
	v_pk_fma_f32 v[96:97], v[82:83], v[56:57], v[96:97] op_sel:[0,1,0]
	v_fmac_f32_e32 v90, v76, v57
	v_pk_fma_f32 v[100:101], v[78:79], v[58:59], v[100:101] op_sel_hi:[1,0,1]
	v_pk_fma_f32 v[104:105], v[82:83], v[58:59], v[104:105] op_sel_hi:[1,0,1]
	v_fmac_f32_e32 v98, v76, v58
	s_barrier
	ds_read_b128 v[64:67], v23 offset:0
	ds_read_b128 v[76:79], v23 offset:1024
	ds_read_b128 v[228:231], v23 offset:2048
	v_pk_add_f32 v[136:137], v[220:221], v[108:109]
	v_pk_add_f32 v[46:47], v[182:183], v[136:137]
	v_pk_add_f32 v[82:83], v[194:195], v[112:113]
	v_pk_add_f32 v[106:107], v[128:129], v[82:83]
	v_add_f32_e32 v128, v224, v102
	v_add_f32_e32 v110, v214, v128
	v_pk_add_f32 v[184:185], v[140:141], v[80:81]
	v_pk_add_f32 v[188:189], v[122:123], v[184:185]
	v_pk_add_f32 v[118:119], v[158:159], v[84:85]
	v_pk_add_f32 v[140:141], v[116:117], v[118:119]
	v_add_f32_e32 v116, v144, v86
	v_add_f32_e32 v208, v130, v116
	v_pk_add_f32 v[144:145], v[192:193], v[88:89]
	v_pk_add_f32 v[220:221], v[138:139], v[144:145]
	v_pk_add_f32 v[122:123], v[162:163], v[96:97]
	v_pk_add_f32 v[192:193], v[120:121], v[122:123]
	v_add_f32_e32 v120, v196, v90
	v_add_f32_e32 v224, v146, v120
	v_pk_add_f32 v[196:197], v[212:213], v[100:101]
	v_pk_add_f32 v[232:233], v[154:155], v[196:197]
	v_pk_add_f32 v[126:127], v[190:191], v[104:105]
	v_pk_add_f32 v[212:213], v[124:125], v[126:127]
	v_add_f32_e32 v124, v216, v98
	v_add_f32_e32 v236, v170, v124
	s_waitcnt lgkmcnt(2)
	v_pk_fma_f32 v[188:189], v[64:65], v[46:47], v[188:189] op_sel_hi:[0,1,1] neg_lo:[1,0,0] neg_hi:[1,0,0]
	v_pk_fma_f32 v[140:141], v[64:65], v[106:107], v[140:141] op_sel_hi:[0,1,1] neg_lo:[1,0,0] neg_hi:[1,0,0]
	v_fma_f32 v208, -v64, v110, v208
	v_pk_fma_f32 v[220:221], v[64:65], v[46:47], v[220:221] op_sel:[1,0,0] neg_lo:[1,0,0] neg_hi:[1,0,0]
	v_pk_fma_f32 v[192:193], v[64:65], v[106:107], v[192:193] op_sel:[1,0,0] neg_lo:[1,0,0] neg_hi:[1,0,0]
	v_fma_f32 v224, -v65, v110, v224
	v_pk_fma_f32 v[232:233], v[66:67], v[46:47], v[232:233] op_sel_hi:[0,1,1] neg_lo:[1,0,0] neg_hi:[1,0,0]
	v_pk_fma_f32 v[212:213], v[66:67], v[106:107], v[212:213] op_sel_hi:[0,1,1] neg_lo:[1,0,0] neg_hi:[1,0,0]
	v_fma_f32 v236, -v66, v110, v236
	v_pk_mul_f32 v[130:131], v[66:67], v[188:189] op_sel:[1,0]
	v_pk_mul_f32 v[150:151], v[66:67], v[140:141] op_sel:[1,0]
	v_mul_f32_e32 v162, v67, v208
	s_waitcnt lgkmcnt(1)
	v_pk_mul_f32 v[138:139], v[76:77], v[188:189] op_sel_hi:[0,1]
	v_pk_mul_f32 v[154:155], v[76:77], v[140:141] op_sel_hi:[0,1]
	v_mul_f32_e32 v166, v76, v208
	v_pk_mul_f32 v[146:147], v[76:77], v[188:189] op_sel:[1,0]
	v_pk_mul_f32 v[158:159], v[76:77], v[140:141] op_sel:[1,0]
	v_mul_f32_e32 v170, v77, v208
	v_pk_fma_f32 v[130:131], v[76:77], v[220:221], v[130:131] op_sel_hi:[0,1,1]
	v_pk_fma_f32 v[150:151], v[76:77], v[192:193], v[150:151] op_sel_hi:[0,1,1]
	v_fmac_f32_e32 v162, v76, v224
	v_pk_fma_f32 v[138:139], v[78:79], v[220:221], v[138:139] op_sel_hi:[0,1,1]
	v_pk_fma_f32 v[154:155], v[78:79], v[192:193], v[154:155] op_sel_hi:[0,1,1]
	v_fmac_f32_e32 v166, v78, v224
	v_pk_fma_f32 v[146:147], v[78:79], v[220:221], v[146:147] op_sel:[1,0,0]
	v_pk_fma_f32 v[158:159], v[78:79], v[192:193], v[158:159] op_sel:[1,0,0]
	v_fmac_f32_e32 v170, v79, v224
	v_pk_fma_f32 v[130:131], v[76:77], v[232:233], v[130:131] op_sel:[1,0,0]
	v_pk_fma_f32 v[150:151], v[76:77], v[212:213], v[150:151] op_sel:[1,0,0]
	v_fmac_f32_e32 v162, v77, v236
	v_pk_fma_f32 v[138:139], v[78:79], v[232:233], v[138:139] op_sel:[1,0,0]
	v_pk_fma_f32 v[154:155], v[78:79], v[212:213], v[154:155] op_sel:[1,0,0]
	v_fmac_f32_e32 v166, v79, v236
	s_waitcnt lgkmcnt(0)
	v_pk_fma_f32 v[146:147], v[228:229], v[232:233], v[146:147] op_sel_hi:[0,1,1]
	v_pk_fma_f32 v[158:159], v[228:229], v[212:213], v[158:159] op_sel_hi:[0,1,1]
	v_fmac_f32_e32 v170, v228, v236
	v_pk_mul_f32 v[216:217], v[64:65], v[130:131] op_sel_hi:[0,1]
	v_pk_mul_f32 v[178:179], v[64:65], v[150:151] op_sel_hi:[0,1]
	v_mul_f32_e32 v182, v64, v162
	v_pk_fma_f32 v[216:217], v[64:65], v[138:139], v[216:217] op_sel:[1,0,0]
	v_pk_fma_f32 v[178:179], v[64:65], v[154:155], v[178:179] op_sel:[1,0,0]
	v_fmac_f32_e32 v182, v65, v166
	v_pk_fma_f32 v[216:217], v[66:67], v[146:147], v[216:217] op_sel_hi:[0,1,1]
	v_pk_fma_f32 v[178:179], v[66:67], v[158:159], v[178:179] op_sel_hi:[0,1,1]
	v_fmac_f32_e32 v182, v66, v170
	v_pk_fma_f32 v[216:217], v[228:229], v[46:47], v[216:217] op_sel:[1,0,0] neg_lo:[0,0,1] neg_hi:[0,0,1]
	v_pk_fma_f32 v[178:179], v[228:229], v[106:107], v[178:179] op_sel:[1,0,0] neg_lo:[0,0,1] neg_hi:[0,0,1]
	v_fma_f32 v182, v229, v110, -v182
	v_cmp_eq_u32_e64 s[10:11], 1, v231
	v_cmp_eq_u32_e64 s[14:15], 2, v231
	v_cmp_eq_u32_e64 s[20:21], 3, v231
	v_cmp_eq_u32_e64 s[22:23], 4, v231
	v_cmp_eq_u32_e64 s[30:31], 5, v231
	v_pk_add_f32 v[140:141], v[132:133], v[130:131]
	v_pk_add_f32 v[46:47], v[186:187], v[140:141]
	v_pk_add_f32 v[106:107], v[114:115], v[150:151]
	v_pk_add_f32 v[110:111], v[156:157], v[106:107]
	v_add_f32_e32 v114, v248, v162
	v_add_f32_e32 v132, v168, v114
	v_pk_add_f32 v[186:187], v[240:241], v[138:139]
	v_pk_add_f32 v[156:157], v[148:149], v[186:187]
	v_pk_add_f32 v[190:191], v[134:135], v[154:155]
	v_pk_add_f32 v[148:149], v[160:161], v[190:191]
	v_add_f32_e32 v134, v174, v166
	v_add_f32_e32 v160, v172, v134
	v_pk_add_f32 v[174:175], v[244:245], v[146:147]
	v_pk_add_f32 v[168:169], v[152:153], v[174:175]
	v_pk_add_f32 v[194:195], v[142:143], v[158:159]
	v_pk_add_f32 v[152:153], v[164:165], v[194:195]
	v_add_f32_e32 v142, v198, v170
	v_add_f32_e32 v164, v176, v142
	v_pk_add_f32 v[198:199], v[202:203], v[216:217]
	v_pk_add_f32 v[214:215], v[180:181], v[198:199]
	v_pk_add_f32 v[202:203], v[206:207], v[178:179]
	v_pk_add_f32 v[218:219], v[200:201], v[202:203]
	v_add_f32_e32 v206, v210, v182
	v_add_f32_e32 v222, v204, v206
	v_pk_fma_f32 v[210:211], v[72:73], v[46:47], v[214:215] op_sel_hi:[0,1,1]
	v_pk_fma_f32 v[226:227], v[72:73], v[110:111], v[218:219] op_sel_hi:[0,1,1]
	v_fma_f32 v234, v72, v132, v222
	v_pk_fma_f32 v[238:239], v[92:93], v[46:47], v[214:215] op_sel_hi:[0,1,1]
	v_pk_fma_f32 v[242:243], v[92:93], v[110:111], v[218:219] op_sel_hi:[0,1,1]
	v_fma_f32 v246, v92, v132, v222
	v_pk_fma_f32 v[210:211], v[72:73], v[156:157], v[210:211] op_sel:[1,0,0]
	v_pk_fma_f32 v[226:227], v[72:73], v[148:149], v[226:227] op_sel:[1,0,0]
	v_fmac_f32_e32 v234, v73, v160
	v_pk_fma_f32 v[238:239], v[92:93], v[156:157], v[238:239] op_sel:[1,0,0]
	v_pk_fma_f32 v[242:243], v[92:93], v[148:149], v[242:243] op_sel:[1,0,0]
	v_fmac_f32_e32 v246, v93, v160
	v_pk_fma_f32 v[210:211], v[74:75], v[168:169], v[210:211] op_sel_hi:[0,1,1]
	v_pk_fma_f32 v[226:227], v[74:75], v[152:153], v[226:227] op_sel_hi:[0,1,1]
	v_fmac_f32_e32 v234, v74, v164
	v_pk_fma_f32 v[238:239], v[94:95], v[168:169], v[238:239] op_sel_hi:[0,1,1]
	v_pk_fma_f32 v[242:243], v[94:95], v[152:153], v[242:243] op_sel_hi:[0,1,1]
	v_fmac_f32_e32 v246, v94, v164
	v_pk_fma_f32 v[214:215], v[8:9], v[46:47], v[214:215] op_sel_hi:[0,1,1]
	v_pk_fma_f32 v[218:219], v[8:9], v[110:111], v[218:219] op_sel_hi:[0,1,1]
	v_fmac_f32_e32 v222, v8, v132
	v_pk_fma_f32 v[214:215], v[8:9], v[156:157], v[214:215] op_sel:[1,0,0]
	v_pk_fma_f32 v[218:219], v[8:9], v[148:149], v[218:219] op_sel:[1,0,0]
	v_fmac_f32_e32 v222, v9, v160
	v_pk_fma_f32 v[214:215], v[10:11], v[168:169], v[214:215] op_sel_hi:[0,1,1]
	v_pk_fma_f32 v[218:219], v[10:11], v[152:153], v[218:219] op_sel_hi:[0,1,1]
	v_fmac_f32_e32 v222, v10, v164
	v_cndmask_b32_e64 v172, 0, v1, s[10:11]
	v_cndmask_b32_e64 v173, 0, v1, s[14:15]
	v_cndmask_b32_e64 v176, 0, v1, s[20:21]
	v_cndmask_b32_e64 v177, 0, v1, s[22:23]
	v_cndmask_b32_e64 v180, 0, v1, s[30:31]
	v_add_f32_dpp v214, v210, v214 wave_shl:1 row_mask:0xf bank_mask:0xf bound_ctrl:1
	v_add_f32_dpp v215, v211, v215 wave_shl:1 row_mask:0xf bank_mask:0xf bound_ctrl:1
	v_add_f32_dpp v218, v226, v218 wave_shl:1 row_mask:0xf bank_mask:0xf bound_ctrl:1
	v_add_f32_dpp v219, v227, v219 wave_shl:1 row_mask:0xf bank_mask:0xf bound_ctrl:1
	v_add_f32_dpp v222, v234, v222 wave_shl:1 row_mask:0xf bank_mask:0xf bound_ctrl:1
	s_add_i32 s4, s34, 8
	s_cmpk_lt_i32 s4, 0x201
	s_cselect_b64 s[12:13], s[0:1], 0
	v_add_f32_dpp v214, v238, v214 wave_shr:1 row_mask:0xf bank_mask:0xf bound_ctrl:1
	v_add_f32_dpp v215, v239, v215 wave_shr:1 row_mask:0xf bank_mask:0xf bound_ctrl:1
	v_add_f32_dpp v218, v242, v218 wave_shr:1 row_mask:0xf bank_mask:0xf bound_ctrl:1
	v_add_f32_dpp v219, v243, v219 wave_shr:1 row_mask:0xf bank_mask:0xf bound_ctrl:1
	v_add_f32_dpp v222, v246, v222 wave_shr:1 row_mask:0xf bank_mask:0xf bound_ctrl:1
	v_pk_fma_f32 v[214:215], v[2:3], v[230:231], v[214:215] op_sel_hi:[1,0,1] neg_lo:[0,0,1] neg_hi:[0,0,1]
	v_pk_fma_f32 v[218:219], v[4:5], v[230:231], v[218:219] op_sel_hi:[1,0,1] neg_lo:[0,0,1] neg_hi:[0,0,1]
	v_fma_f32 v222, v6, v230, -v222
	v_pk_add_f32 v[214:215], v[214:215], v[172:173] neg_lo:[0,1] neg_hi:[0,1]
	v_pk_add_f32 v[218:219], v[218:219], v[176:177] neg_lo:[0,1] neg_hi:[0,1]
	v_sub_f32_e32 v222, v222, v180
	v_pk_mul_f32 v[188:189], v[214:215], v[214:215]
	v_pk_fma_f32 v[188:189], v[218:219], v[218:219], v[188:189]
	v_add_f32_e32 v188, v188, v189
	v_fmac_f32_e32 v188, v222, v222
	v_cndmask_b32_e64 v189, 0, v188, s[12:13]
	v_add_f32_e32 v0, v0, v189
	s_waitcnt vmcnt(0)
	v_mov_b32_dpp v4, v48 wave_shr:1 row_mask:0xf bank_mask:0xf bound_ctrl:1
	v_mov_b32_dpp v5, v49 wave_shr:1 row_mask:0xf bank_mask:0xf bound_ctrl:1
	v_mov_b32_dpp v6, v50 wave_shr:1 row_mask:0xf bank_mask:0xf bound_ctrl:1
	v_mov_b32_dpp v8, v48 wave_shl:1 row_mask:0xf bank_mask:0xf bound_ctrl:1
	v_mov_b32_dpp v9, v49 wave_shl:1 row_mask:0xf bank_mask:0xf bound_ctrl:1
	v_mov_b32_dpp v10, v50 wave_shl:1 row_mask:0xf bank_mask:0xf bound_ctrl:1
	v_mov_b32_dpp v2, v40 wave_shr:1 row_mask:0xf bank_mask:0xf bound_ctrl:1
	v_mov_b32_dpp v3, v41 wave_shr:1 row_mask:0xf bank_mask:0xf bound_ctrl:1
	v_mov_b32_dpp v64, v42 wave_shr:1 row_mask:0xf bank_mask:0xf bound_ctrl:1
	v_mov_b32_dpp v65, v43 wave_shr:1 row_mask:0xf bank_mask:0xf bound_ctrl:1
	v_mov_b32_dpp v46, v44 wave_shr:1 row_mask:0xf bank_mask:0xf bound_ctrl:1
	v_mov_b32_dpp v66, v40 wave_shl:1 row_mask:0xf bank_mask:0xf bound_ctrl:1
	v_mov_b32_dpp v67, v41 wave_shl:1 row_mask:0xf bank_mask:0xf bound_ctrl:1
	v_mov_b32_dpp v72, v42 wave_shl:1 row_mask:0xf bank_mask:0xf bound_ctrl:1
	v_mov_b32_dpp v73, v43 wave_shl:1 row_mask:0xf bank_mask:0xf bound_ctrl:1
	v_mov_b32_dpp v74, v44 wave_shl:1 row_mask:0xf bank_mask:0xf bound_ctrl:1
	v_pk_mul_f32 v[76:77], v[40:41], v[48:49] op_sel_hi:[1,0]
	v_pk_mul_f32 v[78:79], v[42:43], v[48:49] op_sel_hi:[1,0]
	v_mul_f32_e32 v92, v44, v48
	v_pk_mul_f32 v[132:133], v[40:41], v[48:49] op_sel:[0,1]
	v_pk_mul_f32 v[94:95], v[42:43], v[48:49] op_sel:[0,1]
	v_mul_f32_e32 v148, v44, v49
	v_pk_mul_f32 v[152:153], v[40:41], v[50:51] op_sel_hi:[1,0]
	v_pk_mul_f32 v[110:111], v[42:43], v[50:51] op_sel_hi:[1,0]
	v_mul_f32_e32 v156, v44, v50
	v_pk_add_f32 v[160:161], v[40:41], v[2:3]
	v_pk_add_f32 v[210:211], v[42:43], v[64:65]
	v_add_f32_e32 v164, v44, v46
	v_pk_fma_f32 v[76:77], v[2:3], v[4:5], v[76:77] op_sel_hi:[1,0,1]
	v_pk_fma_f32 v[78:79], v[64:65], v[4:5], v[78:79] op_sel_hi:[1,0,1]
	v_fmac_f32_e32 v92, v46, v4
	v_pk_fma_f32 v[132:133], v[2:3], v[4:5], v[132:133] op_sel:[0,1,0]
	v_pk_fma_f32 v[94:95], v[64:65], v[4:5], v[94:95] op_sel:[0,1,0]
	v_fmac_f32_e32 v148, v46, v5
	v_pk_fma_f32 v[152:153], v[2:3], v[6:7], v[152:153] op_sel_hi:[1,0,1]
	v_pk_fma_f32 v[110:111], v[64:65], v[6:7], v[110:111] op_sel_hi:[1,0,1]
	v_fmac_f32_e32 v156, v46, v6
	v_pk_add_f32 v[160:161], v[160:161], v[66:67]
	v_pk_add_f32 v[210:211], v[210:211], v[72:73]
	v_add_f32_e32 v164, v164, v74
	v_pk_fma_f32 v[76:77], v[66:67], v[8:9], v[76:77] op_sel_hi:[1,0,1]
	v_pk_fma_f32 v[78:79], v[72:73], v[8:9], v[78:79] op_sel_hi:[1,0,1]
	v_fmac_f32_e32 v92, v74, v8
	v_pk_fma_f32 v[132:133], v[66:67], v[8:9], v[132:133] op_sel:[0,1,0]
	v_pk_fma_f32 v[94:95], v[72:73], v[8:9], v[94:95] op_sel:[0,1,0]
	v_fmac_f32_e32 v148, v74, v9
	v_pk_fma_f32 v[152:153], v[66:67], v[10:11], v[152:153] op_sel_hi:[1,0,1]
	v_pk_fma_f32 v[110:111], v[72:73], v[10:11], v[110:111] op_sel_hi:[1,0,1]
	v_fmac_f32_e32 v156, v74, v10
	s_barrier
	ds_read_b128 v[64:67], v23 offset:3072
	ds_read_b128 v[72:75], v23 offset:4096
	ds_read_b128 v[212:215], v23 offset:5120
	v_pk_add_f32 v[2:3], v[136:137], v[160:161]
	v_pk_add_f32 v[46:47], v[82:83], v[210:211]
	v_add_f32_e32 v82, v128, v164
	v_pk_add_f32 v[128:129], v[184:185], v[76:77]
	v_pk_add_f32 v[136:137], v[118:119], v[78:79]
	v_add_f32_e32 v168, v116, v92
	v_pk_add_f32 v[116:117], v[144:145], v[132:133]
	v_pk_add_f32 v[144:145], v[122:123], v[94:95]
	v_add_f32_e32 v172, v120, v148
	v_pk_add_f32 v[120:121], v[196:197], v[152:153]
	v_pk_add_f32 v[176:177], v[126:127], v[110:111]
	v_add_f32_e32 v180, v124, v156
	s_waitcnt lgkmcnt(2)
	v_pk_fma_f32 v[128:129], v[64:65], v[2:3], v[128:129] op_sel_hi:[0,1,1] neg_lo:[1,0,0] neg_hi:[1,0,0]
	v_pk_fma_f32 v[136:137], v[64:65], v[46:47], v[136:137] op_sel_hi:[0,1,1] neg_lo:[1,0,0] neg_hi:[1,0,0]
	v_fma_f32 v168, -v64, v82, v168
	v_pk_fma_f32 v[116:117], v[64:65], v[2:3], v[116:117] op_sel:[1,0,0] neg_lo:[1,0,0] neg_hi:[1,0,0]
	v_pk_fma_f32 v[144:145], v[64:65], v[46:47], v[144:145] op_sel:[1,0,0] neg_lo:[1,0,0] neg_hi:[1,0,0]
	v_fma_f32 v172, -v65, v82, v172
	v_pk_fma_f32 v[120:121], v[66:67], v[2:3], v[120:121] op_sel_hi:[0,1,1] neg_lo:[1,0,0] neg_hi:[1,0,0]
	v_pk_fma_f32 v[176:177], v[66:67], v[46:47], v[176:177] op_sel_hi:[0,1,1] neg_lo:[1,0,0] neg_hi:[1,0,0]
	v_fma_f32 v180, -v66, v82, v180
	v_pk_mul_f32 v[118:119], v[66:67], v[128:129] op_sel:[1,0]
	v_pk_mul_f32 v[218:219], v[66:67], v[136:137] op_sel:[1,0]
	v_mul_f32_e32 v230, v67, v168
	s_waitcnt lgkmcnt(1)
	v_pk_mul_f32 v[122:123], v[72:73], v[128:129] op_sel_hi:[0,1]
	v_pk_mul_f32 v[222:223], v[72:73], v[136:137] op_sel_hi:[0,1]
	v_mul_f32_e32 v234, v72, v168
	v_pk_mul_f32 v[126:127], v[72:73], v[128:129] op_sel:[1,0]
	v_pk_mul_f32 v[226:227], v[72:73], v[136:137] op_sel:[1,0]
	v_mul_f32_e32 v238, v73, v168
	v_pk_fma_f32 v[118:119], v[72:73], v[116:117], v[118:119] op_sel_hi:[0,1,1]
	v_pk_fma_f32 v[218:219], v[72:73], v[144:145], v[218:219] op_sel_hi:[0,1,1]
	v_fmac_f32_e32 v230, v72, v172
	v_pk_fma_f32 v[122:123], v[74:75], v[116:117], v[122:123] op_sel_hi:[0,1,1]
	v_pk_fma_f32 v[222:223], v[74:75], v[144:145], v[222:223] op_sel_hi:[0,1,1]
	v_fmac_f32_e32 v234, v74, v172
	v_pk_fma_f32 v[126:127], v[74:75], v[116:117], v[126:127] op_sel:[1,0,0]
	v_pk_fma_f32 v[226:227], v[74:75], v[144:145], v[226:227] op_sel:[1,0,0]
	v_fmac_f32_e32 v238, v75, v172
	v_pk_fma_f32 v[118:119], v[72:73], v[120:121], v[118:119] op_sel:[1,0,0]
	v_pk_fma_f32 v[218:219], v[72:73], v[176:177], v[218:219] op_sel:[1,0,0]
	v_fmac_f32_e32 v230, v73, v180
	v_pk_fma_f32 v[122:123], v[74:75], v[120:121], v[122:123] op_sel:[1,0,0]
	v_pk_fma_f32 v[222:223], v[74:75], v[176:177], v[222:223] op_sel:[1,0,0]
	v_fmac_f32_e32 v234, v75, v180
	s_waitcnt lgkmcnt(0)
	v_pk_fma_f32 v[126:127], v[212:213], v[120:121], v[126:127] op_sel_hi:[0,1,1]
	v_pk_fma_f32 v[226:227], v[212:213], v[176:177], v[226:227] op_sel_hi:[0,1,1]
	v_fmac_f32_e32 v238, v212, v180
	v_pk_mul_f32 v[124:125], v[64:65], v[118:119] op_sel_hi:[0,1]
	v_pk_mul_f32 v[184:185], v[64:65], v[218:219] op_sel_hi:[0,1]
	v_mul_f32_e32 v188, v64, v230
	v_pk_fma_f32 v[124:125], v[64:65], v[122:123], v[124:125] op_sel:[1,0,0]
	v_pk_fma_f32 v[184:185], v[64:65], v[222:223], v[184:185] op_sel:[1,0,0]
	v_fmac_f32_e32 v188, v65, v234
	v_pk_fma_f32 v[124:125], v[66:67], v[126:127], v[124:125] op_sel_hi:[0,1,1]
	v_pk_fma_f32 v[184:185], v[66:67], v[226:227], v[184:185] op_sel_hi:[0,1,1]
	v_fmac_f32_e32 v188, v66, v238
	v_pk_fma_f32 v[124:125], v[212:213], v[2:3], v[124:125] op_sel:[1,0,0] neg_lo:[0,0,1] neg_hi:[0,0,1]
	v_pk_fma_f32 v[184:185], v[212:213], v[46:47], v[184:185] op_sel:[1,0,0] neg_lo:[0,0,1] neg_hi:[0,0,1]
	v_fma_f32 v188, v213, v82, -v188
	v_cmp_eq_u32_e64 s[10:11], 1, v215
	v_cmp_eq_u32_e64 s[14:15], 2, v215
	v_cmp_eq_u32_e64 s[20:21], 3, v215
	v_cmp_eq_u32_e64 s[22:23], 4, v215
	v_cmp_eq_u32_e64 s[30:31], 5, v215
	v_pk_add_f32 v[2:3], v[140:141], v[118:119]
	v_pk_add_f32 v[46:47], v[106:107], v[218:219]
	v_add_f32_e32 v82, v114, v230
	v_pk_add_f32 v[106:107], v[186:187], v[122:123]
	v_pk_add_f32 v[114:115], v[190:191], v[222:223]
	v_add_f32_e32 v116, v134, v234
	v_pk_add_f32 v[120:121], v[174:175], v[126:127]
	v_pk_add_f32 v[128:129], v[194:195], v[226:227]
	v_add_f32_e32 v134, v142, v238
	v_pk_add_f32 v[136:137], v[198:199], v[124:125]
	v_pk_add_f32 v[140:141], v[202:203], v[184:185]
	v_add_f32_e32 v144, v206, v188
	v_pk_fma_f32 v[168:169], v[60:61], v[2:3], v[136:137] op_sel_hi:[0,1,1]
	v_pk_fma_f32 v[172:173], v[60:61], v[46:47], v[140:141] op_sel_hi:[0,1,1]
	v_fma_f32 v176, v60, v82, v144
	v_pk_fma_f32 v[180:181], v[68:69], v[2:3], v[136:137] op_sel_hi:[0,1,1]
	v_pk_fma_f32 v[192:193], v[68:69], v[46:47], v[140:141] op_sel_hi:[0,1,1]
	v_fma_f32 v196, v68, v82, v144
	v_pk_fma_f32 v[168:169], v[60:61], v[106:107], v[168:169] op_sel:[1,0,0]
	v_pk_fma_f32 v[172:173], v[60:61], v[114:115], v[172:173] op_sel:[1,0,0]
	v_fmac_f32_e32 v176, v61, v116
	v_pk_fma_f32 v[180:181], v[68:69], v[106:107], v[180:181] op_sel:[1,0,0]
	v_pk_fma_f32 v[192:193], v[68:69], v[114:115], v[192:193] op_sel:[1,0,0]
	v_fmac_f32_e32 v196, v69, v116
	v_pk_fma_f32 v[168:169], v[62:63], v[120:121], v[168:169] op_sel_hi:[0,1,1]
	v_pk_fma_f32 v[172:173], v[62:63], v[128:129], v[172:173] op_sel_hi:[0,1,1]
	v_fmac_f32_e32 v176, v62, v134
	v_pk_fma_f32 v[180:181], v[70:71], v[120:121], v[180:181] op_sel_hi:[0,1,1]
	v_pk_fma_f32 v[192:193], v[70:71], v[128:129], v[192:193] op_sel_hi:[0,1,1]
	v_fmac_f32_e32 v196, v70, v134
	v_pk_fma_f32 v[136:137], v[32:33], v[2:3], v[136:137] op_sel_hi:[0,1,1]
	v_pk_fma_f32 v[140:141], v[32:33], v[46:47], v[140:141] op_sel_hi:[0,1,1]
	v_fmac_f32_e32 v144, v32, v82
	v_pk_fma_f32 v[136:137], v[32:33], v[106:107], v[136:137] op_sel:[1,0,0]
	v_pk_fma_f32 v[140:141], v[32:33], v[114:115], v[140:141] op_sel:[1,0,0]
	v_fmac_f32_e32 v144, v33, v116
	v_pk_fma_f32 v[136:137], v[34:35], v[120:121], v[136:137] op_sel_hi:[0,1,1]
	v_pk_fma_f32 v[140:141], v[34:35], v[128:129], v[140:141] op_sel_hi:[0,1,1]
	v_fmac_f32_e32 v144, v34, v134
	v_cndmask_b32_e64 v142, 0, v1, s[10:11]
	v_cndmask_b32_e64 v143, 0, v1, s[14:15]
	v_cndmask_b32_e64 v174, 0, v1, s[20:21]
	v_cndmask_b32_e64 v175, 0, v1, s[22:23]
	v_cndmask_b32_e64 v186, 0, v1, s[30:31]
	v_add_f32_dpp v136, v168, v136 wave_shl:1 row_mask:0xf bank_mask:0xf bound_ctrl:1
	v_add_f32_dpp v137, v169, v137 wave_shl:1 row_mask:0xf bank_mask:0xf bound_ctrl:1
	v_add_f32_dpp v140, v172, v140 wave_shl:1 row_mask:0xf bank_mask:0xf bound_ctrl:1
	v_add_f32_dpp v141, v173, v141 wave_shl:1 row_mask:0xf bank_mask:0xf bound_ctrl:1
	v_add_f32_dpp v144, v176, v144 wave_shl:1 row_mask:0xf bank_mask:0xf bound_ctrl:1
	s_add_i32 s4, s34, 9
	s_cmpk_lt_i32 s4, 0x201
	s_cselect_b64 s[12:13], s[0:1], 0
	v_add_f32_dpp v136, v180, v136 wave_shr:1 row_mask:0xf bank_mask:0xf bound_ctrl:1
	v_add_f32_dpp v137, v181, v137 wave_shr:1 row_mask:0xf bank_mask:0xf bound_ctrl:1
	v_add_f32_dpp v140, v192, v140 wave_shr:1 row_mask:0xf bank_mask:0xf bound_ctrl:1
	v_add_f32_dpp v141, v193, v141 wave_shr:1 row_mask:0xf bank_mask:0xf bound_ctrl:1
	v_add_f32_dpp v144, v196, v144 wave_shr:1 row_mask:0xf bank_mask:0xf bound_ctrl:1
	v_pk_fma_f32 v[136:137], v[12:13], v[214:215], v[136:137] op_sel_hi:[1,0,1] neg_lo:[0,0,1] neg_hi:[0,0,1]
	v_pk_fma_f32 v[140:141], v[14:15], v[214:215], v[140:141] op_sel_hi:[1,0,1] neg_lo:[0,0,1] neg_hi:[0,0,1]
	v_fma_f32 v144, v16, v214, -v144
	v_pk_add_f32 v[136:137], v[136:137], v[142:143] neg_lo:[0,1] neg_hi:[0,1]
	v_pk_add_f32 v[140:141], v[140:141], v[174:175] neg_lo:[0,1] neg_hi:[0,1]
	v_sub_f32_e32 v144, v144, v186
	v_pk_mul_f32 v[190:191], v[136:137], v[136:137]
	v_pk_fma_f32 v[190:191], v[140:141], v[140:141], v[190:191]
	v_add_f32_e32 v190, v190, v191
	v_fmac_f32_e32 v190, v144, v144
	v_cndmask_b32_e64 v191, 0, v190, s[12:13]
	v_add_f32_e32 v0, v0, v191

	.amdhsa_kernel _Z16closed_form_mainPKfS0_PKiPf
		.amdhsa_group_segment_fixed_size 6144
		.amdhsa_private_segment_fixed_size 0
		.amdhsa_kernarg_size 32
		.amdhsa_user_sgpr_count 2
		.amdhsa_user_sgpr_dispatch_ptr 0
		.amdhsa_user_sgpr_queue_ptr 0
		.amdhsa_user_sgpr_kernarg_segment_ptr 1
		.amdhsa_user_sgpr_dispatch_id 0
		.amdhsa_user_sgpr_kernarg_preload_length 0
		.amdhsa_user_sgpr_kernarg_preload_offset 0
		.amdhsa_user_sgpr_private_segment_size 0
		.amdhsa_uses_dynamic_stack 0
		.amdhsa_enable_private_segment 0
		.amdhsa_system_sgpr_workgroup_id_x 1
		.amdhsa_system_sgpr_workgroup_id_y 0
		.amdhsa_system_sgpr_workgroup_id_z 0
		.amdhsa_system_sgpr_workgroup_info 0
		.amdhsa_system_vgpr_workitem_id 0
		.amdhsa_next_free_vgpr 250
		.amdhsa_next_free_sgpr 48
		.amdhsa_accum_offset 252
		.amdhsa_reserve_vcc 1
		.amdhsa_float_round_mode_32 0
		.amdhsa_float_round_mode_16_64 0
		.amdhsa_float_denorm_mode_32 3
		.amdhsa_float_denorm_mode_16_64 3
		.amdhsa_dx10_clamp 1
		.amdhsa_ieee_mode 1
		.amdhsa_fp16_overflow 0
		.amdhsa_tg_split 0
		.amdhsa_exception_fp_ieee_invalid_op 0
		.amdhsa_exception_fp_denorm_src 0
		.amdhsa_exception_fp_ieee_div_zero 0
		.amdhsa_exception_fp_ieee_overflow 0
		.amdhsa_exception_fp_ieee_underflow 0
		.amdhsa_exception_fp_ieee_inexact 0
		.amdhsa_exception_int_div_zero 0
	.end_amdhsa_kernel

amdhsa.kernels:
  - .agpr_count:     0
    .args:
      - .address_space:  global
        .offset:         0
        .size:           8
        .value_kind:     global_buffer
      - .address_space:  global
        .offset:         8
        .size:           8
        .value_kind:     global_buffer
      - .address_space:  global
        .offset:         16
        .size:           8
        .value_kind:     global_buffer
      - .address_space:  global
        .offset:         24
        .size:           8
        .value_kind:     global_buffer
    .group_segment_fixed_size: 6144
    .kernarg_segment_align: 8
    .kernarg_segment_size: 32
    .language:       OpenCL C
    .language_version:
      - 2
      - 0
    .max_flat_workgroup_size: 128
    .name:           _Z16closed_form_mainPKfS0_PKiPf
    .private_segment_fixed_size: 0
    .sgpr_count:     54
    .sgpr_spill_count: 0
    .symbol:         _Z16closed_form_mainPKfS0_PKiPf.kd
    .uniform_work_group_size: 1
    .uses_dynamic_stack: false
    .vgpr_count:     250
    .vgpr_spill_count: 0
    .wavefront_size: 64
  - .agpr_count:     0
    .args:
      - .actual_access:  read_only
        .address_space:  global
        .offset:         0
        .size:           8
        .value_kind:     global_buffer
      - .actual_access:  write_only
        .address_space:  global
        .offset:         8
        .size:           8
        .value_kind:     global_buffer
    .group_segment_fixed_size: 0
    .kernarg_segment_align: 8
    .kernarg_segment_size: 16
    .language:       OpenCL C
    .language_version:
      - 2
      - 0
    .max_flat_workgroup_size: 64
    .name:           _Z17closed_form_finalPK15HIP_vector_typeIfLj4EEPf
    .private_segment_fixed_size: 0
    .sgpr_count:     10
    .sgpr_spill_count: 0
    .symbol:         _Z17closed_form_finalPK15HIP_vector_typeIfLj4EEPf.kd
    .uniform_work_group_size: 1
    .uses_dynamic_stack: false
    .vgpr_count:     36
    .vgpr_spill_count: 0
    .wavefront_size: 64
